# B3 router phase: window-sum Z/X loads (compiler had serialized ~80 load->wait round trips per row pair) batched 2-6 deep into spare VGPRs with recomputed counted vmcnt waits; MoE expert-count loads is
# speedup vs baseline: 1.0438x; 1.0219x over previous
.LBB0_594:
	s_or_b64 exec, exec, s[0:1]
	v_and_or_b32 v14, v0, 15, s9
	v_ashrrev_i32_e32 v0, 1, v0
	v_and_b32_e32 v0, -8, v0
	s_add_i32 s0, 0, 0x22100
	v_add_u32_e32 v8, s24, v0
	v_lshl_add_u32 v0, v14, 4, s0
	s_waitcnt lgkmcnt(0)
	s_barrier
	s_waitcnt lgkmcnt(0)
	ds_read_b128 v[0:3], v0
	s_or_b32 s20, s16, s12
	s_mov_b32 s21, s17
	v_ashrrev_i32_e32 v15, 31, v14
	v_ashrrev_i32_e32 v9, 31, v8
	s_waitcnt lgkmcnt(0)
	v_mov_b32_e32 v4, v1
	v_mov_b32_e32 v5, v2
	v_mov_b32_e32 v1, v3
	v_pk_add_f32 v[0:1], v[4:5], v[0:1]
	v_readlane_b32 s2, v252, 19
	v_add_f32_e32 v0, v0, v1
	v_fmamk_f32 v0, v0, 0x3b000000, v189
	v_rsq_f32_e32 v20, v0
	v_lshl_add_u64 v[0:1], s[20:21], 0, v[14:15]
	v_lshlrev_b64 v[2:3], 12, v[0:1]
	v_lshlrev_b64 v[0:1], 13, v[0:1]
	v_lshl_add_u64 v[0:1], s[66:67], 0, v[0:1]
	v_lshlrev_b64 v[10:11], 1, v[8:9]
	v_readlane_b32 s3, v252, 20
	v_lshl_add_u64 v[16:17], v[0:1], 0, v[10:11]
	v_lshl_add_u64 v[18:19], s[34:35], 0, v[2:3]
	v_lshl_add_u64 v[12:13], v[8:9], 2, s[2:3]
	s_nop 0
	s_nop 0
	global_load_dwordx4 v[212:215], v[16:17], off
	global_load_dwordx4 v[224:227], v[12:13], off offset:16
	global_load_dwordx4 v[228:231], v[12:13], off
	global_load_dwordx4 v[216:219], v[16:17], off offset:256
	global_load_dwordx4 v[232:235], v[12:13], off offset:528
	global_load_dwordx4 v[236:239], v[12:13], off offset:512
	global_load_dwordx4 v[174:177], v[16:17], off offset:512
	global_load_dwordx4 v[240:243], v[12:13], off offset:1040
	global_load_dwordx4 v[244:247], v[12:13], off offset:1024
	global_load_dwordx4 v[178:181], v[16:17], off offset:768
	global_load_dwordx4 v[204:207], v[12:13], off offset:1552
	global_load_dwordx4 v[208:211], v[12:13], off offset:1536
	v_mul_f32_e32 v28, v156, v20
	v_mul_f32_e32 v132, v132, v20
	s_and_b64 vcc, exec, s[18:19]
	s_waitcnt vmcnt(9)
	v_lshlrev_b32_e32 v15, 16, v212
	s_nop 0
	v_mul_f32_e32 v4, v228, v28
	v_mul_f32_e32 v4, v4, v15
	v_mul_f32_e32 v15, 0xbfb8aa3b, v15
	v_exp_f32_e32 v15, v15
	v_lshlrev_b32_e32 v26, 16, v214
	v_and_b32_e32 v21, 0xffff0000, v212
	v_and_b32_e32 v24, 0xffff0000, v214
	v_add_f32_e32 v15, 1.0, v15
	v_rcp_f32_e32 v15, v15
	v_lshlrev_b32_e32 v22, 16, v213
	v_lshlrev_b32_e32 v27, 16, v215
	v_and_b32_e32 v23, 0xffff0000, v213
	v_mul_f32_e32 v4, v15, v4
	v_mul_f32_e32 v15, v152, v20
	v_mul_f32_e32 v0, v224, v15
	v_mul_f32_e32 v15, 0xbfb8aa3b, v26
	v_exp_f32_e32 v15, v15
	v_mul_f32_e32 v0, v0, v26
	v_and_b32_e32 v25, 0xffff0000, v215
	v_add_f32_e32 v15, 1.0, v15
	v_rcp_f32_e32 v15, v15
	s_nop 0
	v_mul_f32_e32 v15, v15, v0
	v_mul_f32_e32 v0, v157, v20
	v_mul_f32_e32 v0, v229, v0
	v_mul_f32_e32 v5, 0xbfb8aa3b, v21
	v_exp_f32_e32 v5, v5
	v_mul_f32_e32 v0, v0, v21
	v_add_f32_e32 v5, 1.0, v5
	v_rcp_f32_e32 v5, v5
	s_nop 0
	v_mul_f32_e32 v5, v5, v0
	v_mul_f32_e32 v0, v153, v20
	v_mul_f32_e32 v0, v225, v0
	v_mul_f32_e32 v1, 0xbfb8aa3b, v24
	v_exp_f32_e32 v1, v1
	v_mul_f32_e32 v0, v0, v24
	v_add_f32_e32 v1, 1.0, v1
	v_rcp_f32_e32 v1, v1
	s_nop 0
	v_mul_f32_e32 v21, v1, v0
	v_mul_f32_e32 v1, 0xbfb8aa3b, v22
	v_exp_f32_e32 v1, v1
	v_mul_f32_e32 v0, v158, v20
	v_mul_f32_e32 v0, v230, v0
	v_mul_f32_e32 v0, v0, v22
	v_add_f32_e32 v1, 1.0, v1
	v_rcp_f32_e32 v1, v1
	v_mul_f32_e32 v6, 0xbfb8aa3b, v23
	v_exp_f32_e32 v6, v6
	v_mul_f32_e32 v1, v1, v0
	v_mul_f32_e32 v0, v154, v20
	v_mul_f32_e32 v0, v226, v0
	v_mul_f32_e32 v2, 0xbfb8aa3b, v27
	v_exp_f32_e32 v2, v2
	v_add_f32_e32 v6, 1.0, v6
	v_mul_f32_e32 v0, v0, v27
	v_rcp_f32_e32 v6, v6
	v_add_f32_e32 v2, 1.0, v2
	v_rcp_f32_e32 v2, v2
	s_nop 0
	v_mul_f32_e32 v2, v2, v0
	v_mul_f32_e32 v0, v159, v20
	v_mul_f32_e32 v0, v231, v0
	v_mul_f32_e32 v0, v0, v23
	v_mul_f32_e32 v6, v6, v0
	v_mul_f32_e32 v0, v155, v20
	v_mul_f32_e32 v0, v227, v0
	v_mul_f32_e32 v3, 0xbfb8aa3b, v25
	v_exp_f32_e32 v3, v3
	v_mul_f32_e32 v0, v0, v25
	v_add_f32_e32 v3, 1.0, v3
	v_rcp_f32_e32 v3, v3
	s_nop 0
	v_mul_f32_e32 v3, v3, v0
	v_mov_b32_e32 v0, 0
	v_cvt_pk_fp8_f32 v0, v4, v5
	v_cvt_pk_fp8_f32 v0, v1, v6 op_sel:[0,0,1]
	v_mov_b32_e32 v1, 0
	v_cvt_pk_fp8_f32 v1, v15, v21
	v_lshl_add_u64 v[6:7], v[18:19], 0, v[8:9]
	v_cvt_pk_fp8_f32 v1, v2, v3 op_sel:[0,0,1]
	global_store_dwordx2 v[6:7], v[0:1], off
	s_nop 0
	v_add_u32_e32 v0, 0x80, v8
	v_ashrrev_i32_e32 v1, 31, v0
	v_lshl_add_u64 v[0:1], v[0:1], 2, s[2:3]
	s_nop 0
	s_nop 0
	s_waitcnt vmcnt(7)
	v_lshlrev_b32_e32 v15, 16, v216
	v_lshlrev_b32_e32 v30, 16, v219
	v_and_b32_e32 v31, 0xffff0000, v219
	v_mul_f32_e32 v5, 0xbfb8aa3b, v15
	v_exp_f32_e32 v5, v5
	v_lshlrev_b32_e32 v19, 16, v218
	v_and_b32_e32 v21, 0xffff0000, v218
	v_mul_f32_e32 v4, v148, v20
	v_add_f32_e32 v5, 1.0, v5
	v_rcp_f32_e32 v5, v5
	s_nop 0
	v_mul_f32_e32 v4, v4, v236
	v_mul_f32_e32 v4, v4, v15
	v_and_b32_e32 v2, 0xffff0000, v216
	v_mul_f32_e32 v26, v4, v5
	v_mul_f32_e32 v5, 0xbfb8aa3b, v19
	v_exp_f32_e32 v5, v5
	v_mul_f32_e32 v4, v144, v20
	v_mul_f32_e32 v4, v4, v232
	v_mul_f32_e32 v4, v4, v19
	v_add_f32_e32 v5, 1.0, v5
	v_rcp_f32_e32 v5, v5
	v_lshlrev_b32_e32 v18, 16, v217
	v_mul_f32_e32 v15, 0xbfb8aa3b, v18
	v_exp_f32_e32 v15, v15
	v_mul_f32_e32 v4, v4, v5
	v_mul_f32_e32 v5, v149, v20
	v_mul_f32_e32 v5, v5, v237
	v_mul_f32_e32 v5, v5, v2
	v_mul_f32_e32 v2, 0xbfb8aa3b, v2
	v_exp_f32_e32 v2, v2
	v_add_f32_e32 v15, 1.0, v15
	v_rcp_f32_e32 v15, v15
	v_and_b32_e32 v3, 0xffff0000, v217
	v_add_f32_e32 v2, 1.0, v2
	v_rcp_f32_e32 v2, v2
	s_nop 0
	v_mul_f32_e32 v19, v5, v2
	v_mul_f32_e32 v5, 0xbfb8aa3b, v21
	v_exp_f32_e32 v5, v5
	v_mul_f32_e32 v2, v145, v20
	v_mul_f32_e32 v2, v2, v233
	v_mul_f32_e32 v2, v2, v21
	v_add_f32_e32 v5, 1.0, v5
	v_rcp_f32_e32 v5, v5
	s_nop 0
	v_mul_f32_e32 v5, v2, v5
	v_mul_f32_e32 v2, v150, v20
	v_mul_f32_e32 v2, v2, v238
	v_mul_f32_e32 v2, v2, v18
	v_mul_f32_e32 v21, v2, v15
	v_mul_f32_e32 v15, 0xbfb8aa3b, v30
	v_exp_f32_e32 v15, v15
	v_mul_f32_e32 v2, v146, v20
	v_mul_f32_e32 v2, v2, v234
	v_mul_f32_e32 v2, v2, v30
	v_add_f32_e32 v15, 1.0, v15
	v_rcp_f32_e32 v15, v15
	v_mul_f32_e32 v18, 0xbfb8aa3b, v31
	v_exp_f32_e32 v18, v18
	v_mul_f32_e32 v15, v2, v15
	v_mul_f32_e32 v2, v151, v20
	v_mul_f32_e32 v2, v2, v239
	v_mul_f32_e32 v2, v2, v3
	v_mul_f32_e32 v3, 0xbfb8aa3b, v3
	v_exp_f32_e32 v3, v3
	v_add_f32_e32 v18, 1.0, v18
	v_rcp_f32_e32 v18, v18
	v_add_f32_e32 v3, 1.0, v3
	v_rcp_f32_e32 v3, v3
	s_nop 0
	v_mul_f32_e32 v3, v2, v3
	v_mul_f32_e32 v2, v147, v20
	v_mul_f32_e32 v2, v2, v235
	v_mul_f32_e32 v2, v2, v31
	v_mul_f32_e32 v18, v2, v18
	v_mov_b32_e32 v2, 0
	v_cvt_pk_fp8_f32 v2, v26, v19
	v_cvt_pk_fp8_f32 v2, v21, v3 op_sel:[0,0,1]
	v_mov_b32_e32 v3, 0
	v_cvt_pk_fp8_f32 v3, v4, v5
	v_cvt_pk_fp8_f32 v3, v15, v18 op_sel:[0,0,1]
	global_store_dwordx2 v[6:7], v[2:3], off offset:128
	v_add_u32_e32 v2, 0x100, v8
	v_ashrrev_i32_e32 v3, 31, v2
	s_nop 0
	v_lshl_add_u64 v[2:3], v[2:3], 2, s[2:3]
	s_nop 0
	s_nop 0
	s_waitcnt vmcnt(5)
	v_lshlrev_b32_e32 v15, 16, v176
	v_and_b32_e32 v18, 0xffff0000, v176
	v_mul_f32_e32 v24, v140, v20
	v_lshlrev_b32_e32 v4, 16, v174
	s_nop 0
	v_mul_f32_e32 v24, v24, v244
	v_mul_f32_e32 v24, v24, v4
	v_mul_f32_e32 v4, 0xbfb8aa3b, v4
	v_exp_f32_e32 v4, v4
	v_and_b32_e32 v5, 0xffff0000, v174
	v_lshlrev_b32_e32 v19, 16, v175
	v_lshlrev_b32_e32 v22, 16, v177
	v_add_f32_e32 v4, 1.0, v4
	v_rcp_f32_e32 v4, v4
	v_and_b32_e32 v21, 0xffff0000, v175
	v_and_b32_e32 v23, 0xffff0000, v177
	v_mul_f32_e32 v24, v24, v4
	v_mul_f32_e32 v4, v136, v20
	v_mul_f32_e32 v4, v4, v240
	v_mul_f32_e32 v4, v4, v15
	v_mul_f32_e32 v15, 0xbfb8aa3b, v15
	v_exp_f32_e32 v15, v15
	s_nop 0
	v_add_f32_e32 v15, 1.0, v15
	v_rcp_f32_e32 v15, v15
	s_nop 0
	v_mul_f32_e32 v15, v4, v15
	v_mul_f32_e32 v4, v141, v20
	v_mul_f32_e32 v4, v4, v245
	v_mul_f32_e32 v4, v4, v5
	v_mul_f32_e32 v5, 0xbfb8aa3b, v5
	v_exp_f32_e32 v5, v5
	s_nop 0
	v_add_f32_e32 v5, 1.0, v5
	v_rcp_f32_e32 v5, v5
	s_nop 0
	v_mul_f32_e32 v5, v4, v5
	v_mul_f32_e32 v4, v137, v20
	v_mul_f32_e32 v4, v4, v241
	v_mul_f32_e32 v4, v4, v18
	v_mul_f32_e32 v18, 0xbfb8aa3b, v18
	v_exp_f32_e32 v18, v18
	s_nop 0
	v_add_f32_e32 v18, 1.0, v18
	v_rcp_f32_e32 v18, v18
	s_nop 0
	v_mul_f32_e32 v18, v4, v18
	v_mul_f32_e32 v4, v142, v20
	v_mul_f32_e32 v4, v4, v246
	v_mul_f32_e32 v4, v4, v19
	v_mul_f32_e32 v19, 0xbfb8aa3b, v19
	v_exp_f32_e32 v19, v19
	s_nop 0
	v_add_f32_e32 v19, 1.0, v19
	v_rcp_f32_e32 v19, v19
	s_nop 0
	v_mul_f32_e32 v25, v4, v19
	v_mul_f32_e32 v19, 0xbfb8aa3b, v22
	v_exp_f32_e32 v19, v19
	v_mul_f32_e32 v4, v138, v20
	v_mul_f32_e32 v4, v4, v242
	v_mul_f32_e32 v4, v4, v22
	v_add_f32_e32 v19, 1.0, v19
	v_rcp_f32_e32 v19, v19
	s_nop 0
	v_mul_f32_e32 v19, v4, v19
	v_mul_f32_e32 v4, v143, v20
	v_mul_f32_e32 v4, v4, v247
	v_mul_f32_e32 v4, v4, v21
	v_mul_f32_e32 v21, 0xbfb8aa3b, v21
	v_exp_f32_e32 v21, v21
	s_nop 0
	v_add_f32_e32 v21, 1.0, v21
	v_rcp_f32_e32 v21, v21
	s_nop 0
	v_mul_f32_e32 v22, v4, v21
	v_mul_f32_e32 v21, 0xbfb8aa3b, v23
	v_exp_f32_e32 v21, v21
	v_mul_f32_e32 v4, v139, v20
	v_mul_f32_e32 v4, v4, v243
	v_mul_f32_e32 v4, v4, v23
	v_add_f32_e32 v21, 1.0, v21
	v_rcp_f32_e32 v21, v21
	s_nop 0
	v_mul_f32_e32 v21, v4, v21
	v_mov_b32_e32 v4, 0
	v_cvt_pk_fp8_f32 v4, v24, v5
	v_mov_b32_e32 v5, 0
	v_cvt_pk_fp8_f32 v5, v15, v18
	v_cvt_pk_fp8_f32 v4, v25, v22 op_sel:[0,0,1]
	v_cvt_pk_fp8_f32 v5, v19, v21 op_sel:[0,0,1]
	global_store_dwordx2 v[6:7], v[4:5], off offset:256
	v_add_u32_e32 v4, 0x180, v8
	v_ashrrev_i32_e32 v5, 31, v4
	v_lshl_add_u64 v[4:5], v[4:5], 2, s[2:3]
	s_nop 0
	s_nop 0
	s_nop 0
	s_nop 0
	s_waitcnt vmcnt(3)
	v_lshlrev_b32_e32 v15, 16, v178
	s_nop 0
	v_mul_f32_e32 v26, v132, v208
	v_mul_f32_e32 v26, v26, v15
	v_mul_f32_e32 v15, 0xbfb8aa3b, v15
	v_exp_f32_e32 v15, v15
	v_lshlrev_b32_e32 v30, 16, v180
	v_and_b32_e32 v16, 0xffff0000, v178
	v_and_b32_e32 v18, 0xffff0000, v180
	v_add_f32_e32 v15, 1.0, v15
	v_rcp_f32_e32 v15, v15
	v_lshlrev_b32_e32 v21, 16, v179
	v_lshlrev_b32_e32 v31, 16, v181
	v_and_b32_e32 v17, 0xffff0000, v179
	v_mul_f32_e32 v15, v26, v15
	v_mul_f32_e32 v26, v128, v20
	v_mul_f32_e32 v22, v26, v204
	v_mul_f32_e32 v26, 0xbfb8aa3b, v30
	v_exp_f32_e32 v26, v26
	v_mul_f32_e32 v22, v22, v30
	v_and_b32_e32 v19, 0xffff0000, v181
	v_add_f32_e32 v26, 1.0, v26
	v_rcp_f32_e32 v26, v26
	s_nop 0
	v_mul_f32_e32 v22, v22, v26
	v_mul_f32_e32 v26, v133, v20
	v_mul_f32_e32 v26, v26, v209
	v_mul_f32_e32 v26, v26, v16
	v_mul_f32_e32 v16, 0xbfb8aa3b, v16
	v_exp_f32_e32 v16, v16
	s_nop 0
	v_add_f32_e32 v16, 1.0, v16
	v_rcp_f32_e32 v16, v16
	s_nop 0
	v_mul_f32_e32 v26, v26, v16
	v_mul_f32_e32 v16, v129, v20
	v_mul_f32_e32 v16, v16, v205
	v_mul_f32_e32 v16, v16, v18
	v_mul_f32_e32 v18, 0xbfb8aa3b, v18
	v_exp_f32_e32 v18, v18
	v_mul_f32_e32 v23, 0xbfb8aa3b, v31
	v_exp_f32_e32 v23, v23
	v_add_f32_e32 v18, 1.0, v18
	v_rcp_f32_e32 v18, v18
	v_add_f32_e32 v23, 1.0, v23
	v_rcp_f32_e32 v23, v23
	v_mul_f32_e32 v18, v16, v18
	v_mul_f32_e32 v16, v134, v20
	v_mul_f32_e32 v16, v16, v210
	v_mul_f32_e32 v16, v16, v21
	v_mul_f32_e32 v21, 0xbfb8aa3b, v21
	v_exp_f32_e32 v21, v21
	s_nop 0
	v_add_f32_e32 v21, 1.0, v21
	v_rcp_f32_e32 v21, v21
	s_nop 0
	v_mul_f32_e32 v21, v16, v21
	v_mul_f32_e32 v16, v130, v20
	v_mul_f32_e32 v16, v16, v206
	v_mul_f32_e32 v16, v16, v31
	v_mul_f32_e32 v23, v16, v23
	v_mul_f32_e32 v16, v135, v20
	v_mul_f32_e32 v16, v16, v211
	v_mul_f32_e32 v16, v16, v17
	v_mul_f32_e32 v17, 0xbfb8aa3b, v17
	v_exp_f32_e32 v17, v17
	s_nop 0
	v_add_f32_e32 v17, 1.0, v17
	v_rcp_f32_e32 v17, v17
	s_nop 0
	v_mul_f32_e32 v17, v16, v17
	v_mul_f32_e32 v16, v131, v20
	v_mul_f32_e32 v16, v16, v207
	v_mul_f32_e32 v16, v16, v19
	v_mul_f32_e32 v19, 0xbfb8aa3b, v19
	v_exp_f32_e32 v19, v19
	s_nop 0
	v_add_f32_e32 v19, 1.0, v19
	v_rcp_f32_e32 v19, v19
	s_nop 0
	v_mul_f32_e32 v19, v16, v19
	v_mov_b32_e32 v16, 0
	v_cvt_pk_fp8_f32 v16, v15, v26
	v_cvt_pk_fp8_f32 v16, v21, v17 op_sel:[0,0,1]
	v_mov_b32_e32 v17, 0
	v_cvt_pk_fp8_f32 v17, v22, v18
	v_cvt_pk_fp8_f32 v17, v23, v19 op_sel:[0,0,1]
	global_store_dwordx2 v[6:7], v[16:17], off offset:384
	v_or_b32_e32 v6, 16, v14
	v_lshl_add_u32 v7, v6, 4, s0
	ds_read_b128 v[16:19], v7
	s_waitcnt lgkmcnt(0)
	v_mov_b32_e32 v20, v17
	v_mov_b32_e32 v21, v18
	v_mov_b32_e32 v17, v19
	v_pk_add_f32 v[16:17], v[20:21], v[16:17]
	s_nop 0
	v_add_f32_e32 v7, v16, v17
	v_fmamk_f32 v7, v7, 0x3b000000, v189
	v_rsq_f32_e32 v15, v7
	v_ashrrev_i32_e32 v7, 31, v6
	v_lshl_add_u64 v[16:17], s[20:21], 0, v[6:7]
	v_lshlrev_b64 v[6:7], 12, v[16:17]
	v_lshlrev_b64 v[16:17], 13, v[16:17]
	v_lshl_add_u64 v[18:19], s[66:67], 0, v[16:17]
	v_lshl_add_u64 v[16:17], s[34:35], 0, v[6:7]
	v_lshl_add_u64 v[6:7], v[18:19], 0, v[10:11]
	global_load_dwordx4 v[212:215], v[6:7], off
	global_load_dwordx4 v[216:219], v[6:7], off offset:256
	global_load_dwordx4 v[174:177], v[6:7], off offset:512
	global_load_dwordx4 v[178:181], v[6:7], off offset:768
	s_nop 0
	s_nop 0
	v_lshl_add_u64 v[16:17], v[16:17], 0, v[8:9]
	v_mul_f32_e32 v100, v100, v15
	s_waitcnt vmcnt(3)
	v_lshlrev_b32_e32 v30, 16, v212
	v_lshlrev_b32_e32 v130, 16, v215
	v_and_b32_e32 v131, 0xffff0000, v215
	v_mul_f32_e32 v21, 0xbfb8aa3b, v30
	v_exp_f32_e32 v21, v21
	v_lshlrev_b32_e32 v128, 16, v214
	v_and_b32_e32 v129, 0xffff0000, v214
	v_mul_f32_e32 v20, v124, v15
	v_add_f32_e32 v21, 1.0, v21
	v_rcp_f32_e32 v21, v21
	s_nop 0
	v_mul_f32_e32 v20, v228, v20
	v_mul_f32_e32 v20, v20, v30
	v_and_b32_e32 v18, 0xffff0000, v212
	v_mul_f32_e32 v26, v21, v20
	v_mul_f32_e32 v21, 0xbfb8aa3b, v128
	v_exp_f32_e32 v21, v21
	v_mul_f32_e32 v20, v120, v15
	v_mul_f32_e32 v20, v224, v20
	v_mul_f32_e32 v20, v20, v128
	v_add_f32_e32 v21, 1.0, v21
	v_rcp_f32_e32 v21, v21
	v_lshlrev_b32_e32 v31, 16, v213
	v_mul_f32_e32 v22, 0xbfb8aa3b, v31
	v_exp_f32_e32 v22, v22
	v_mul_f32_e32 v20, v21, v20
	v_mul_f32_e32 v21, v125, v15
	v_mul_f32_e32 v21, v229, v21
	v_mul_f32_e32 v21, v21, v18
	v_mul_f32_e32 v18, 0xbfb8aa3b, v18
	v_exp_f32_e32 v18, v18
	v_add_f32_e32 v22, 1.0, v22
	v_rcp_f32_e32 v22, v22
	v_and_b32_e32 v19, 0xffff0000, v213
	v_add_f32_e32 v18, 1.0, v18
	v_rcp_f32_e32 v18, v18
	s_nop 0
	v_mul_f32_e32 v27, v18, v21
	v_mul_f32_e32 v21, 0xbfb8aa3b, v129
	v_exp_f32_e32 v21, v21
	v_mul_f32_e32 v18, v121, v15
	v_mul_f32_e32 v18, v225, v18
	v_mul_f32_e32 v18, v18, v129
	v_add_f32_e32 v21, 1.0, v21
	v_rcp_f32_e32 v21, v21
	v_mul_f32_e32 v23, 0xbfb8aa3b, v131
	v_exp_f32_e32 v23, v23
	v_mul_f32_e32 v21, v21, v18
	v_mul_f32_e32 v18, v126, v15
	v_mul_f32_e32 v18, v230, v18
	v_mul_f32_e32 v18, v18, v31
	v_mul_f32_e32 v28, v22, v18
	v_mul_f32_e32 v22, 0xbfb8aa3b, v130
	v_exp_f32_e32 v22, v22
	v_mul_f32_e32 v18, v122, v15
	v_mul_f32_e32 v18, v226, v18
	v_mul_f32_e32 v18, v18, v130
	v_add_f32_e32 v22, 1.0, v22
	v_rcp_f32_e32 v22, v22
	v_add_f32_e32 v23, 1.0, v23
	v_rcp_f32_e32 v23, v23
	v_mul_f32_e32 v22, v22, v18
	v_mul_f32_e32 v18, v127, v15
	v_mul_f32_e32 v18, v231, v18
	v_mul_f32_e32 v18, v18, v19
	v_mul_f32_e32 v19, 0xbfb8aa3b, v19
	v_exp_f32_e32 v19, v19
	s_nop 0
	v_add_f32_e32 v19, 1.0, v19
	v_rcp_f32_e32 v19, v19
	s_nop 0
	v_mul_f32_e32 v19, v19, v18
	v_mul_f32_e32 v18, v123, v15
	v_mul_f32_e32 v18, v227, v18
	v_mul_f32_e32 v18, v18, v131
	v_mul_f32_e32 v23, v23, v18
	v_mov_b32_e32 v18, 0
	v_cvt_pk_fp8_f32 v18, v26, v27
	v_cvt_pk_fp8_f32 v18, v28, v19 op_sel:[0,0,1]
	v_mov_b32_e32 v19, 0
	v_cvt_pk_fp8_f32 v19, v20, v21
	v_cvt_pk_fp8_f32 v19, v22, v23 op_sel:[0,0,1]
	global_store_dwordx2 v[16:17], v[18:19], off
	s_nop 0
	s_nop 0
	s_nop 0
	s_nop 0
	s_waitcnt vmcnt(3)
	v_lshlrev_b32_e32 v30, 16, v216
	v_lshlrev_b32_e32 v122, 16, v219
	v_and_b32_e32 v123, 0xffff0000, v219
	v_mul_f32_e32 v21, 0xbfb8aa3b, v30
	v_exp_f32_e32 v21, v21
	v_lshlrev_b32_e32 v120, 16, v218
	v_and_b32_e32 v121, 0xffff0000, v218
	v_mul_f32_e32 v20, v116, v15
	v_add_f32_e32 v21, 1.0, v21
	v_rcp_f32_e32 v21, v21
	s_nop 0
	v_mul_f32_e32 v20, v20, v236
	v_mul_f32_e32 v20, v20, v30
	v_and_b32_e32 v18, 0xffff0000, v216
	v_mul_f32_e32 v26, v20, v21
	v_mul_f32_e32 v21, 0xbfb8aa3b, v120
	v_exp_f32_e32 v21, v21
	v_mul_f32_e32 v20, v112, v15
	v_mul_f32_e32 v20, v20, v232
	v_mul_f32_e32 v20, v20, v120
	v_add_f32_e32 v21, 1.0, v21
	v_rcp_f32_e32 v21, v21
	v_lshlrev_b32_e32 v31, 16, v217
	v_mul_f32_e32 v22, 0xbfb8aa3b, v31
	v_exp_f32_e32 v22, v22
	v_mul_f32_e32 v20, v20, v21
	v_mul_f32_e32 v21, v117, v15
	v_mul_f32_e32 v21, v21, v237
	v_mul_f32_e32 v21, v21, v18
	v_mul_f32_e32 v18, 0xbfb8aa3b, v18
	v_exp_f32_e32 v18, v18
	v_add_f32_e32 v22, 1.0, v22
	v_rcp_f32_e32 v22, v22
	v_and_b32_e32 v19, 0xffff0000, v217
	v_add_f32_e32 v18, 1.0, v18
	v_rcp_f32_e32 v18, v18
	s_nop 0
	v_mul_f32_e32 v27, v21, v18
	v_mul_f32_e32 v21, 0xbfb8aa3b, v121
	v_exp_f32_e32 v21, v21
	v_mul_f32_e32 v18, v113, v15
	v_mul_f32_e32 v18, v18, v233
	v_mul_f32_e32 v18, v18, v121
	v_add_f32_e32 v21, 1.0, v21
	v_rcp_f32_e32 v21, v21
	v_mul_f32_e32 v23, 0xbfb8aa3b, v123
	v_exp_f32_e32 v23, v23
	v_mul_f32_e32 v21, v18, v21
	v_mul_f32_e32 v18, v118, v15
	v_mul_f32_e32 v18, v18, v238
	v_mul_f32_e32 v18, v18, v31
	v_mul_f32_e32 v28, v18, v22
	v_mul_f32_e32 v22, 0xbfb8aa3b, v122
	v_exp_f32_e32 v22, v22
	v_mul_f32_e32 v18, v114, v15
	v_mul_f32_e32 v18, v18, v234
	v_mul_f32_e32 v18, v18, v122
	v_add_f32_e32 v22, 1.0, v22
	v_rcp_f32_e32 v22, v22
	v_add_f32_e32 v23, 1.0, v23
	v_rcp_f32_e32 v23, v23
	v_mul_f32_e32 v22, v18, v22
	v_mul_f32_e32 v18, v119, v15
	v_mul_f32_e32 v18, v18, v239
	v_mul_f32_e32 v18, v18, v19
	v_mul_f32_e32 v19, 0xbfb8aa3b, v19
	v_exp_f32_e32 v19, v19
	s_nop 0
	v_add_f32_e32 v19, 1.0, v19
	v_rcp_f32_e32 v19, v19
	s_nop 0
	v_mul_f32_e32 v19, v18, v19
	v_mul_f32_e32 v18, v115, v15
	v_mul_f32_e32 v18, v18, v235
	v_mul_f32_e32 v18, v18, v123
	v_mul_f32_e32 v23, v18, v23
	v_mov_b32_e32 v18, 0
	v_cvt_pk_fp8_f32 v18, v26, v27
	v_cvt_pk_fp8_f32 v18, v28, v19 op_sel:[0,0,1]
	v_mov_b32_e32 v19, 0
	v_cvt_pk_fp8_f32 v19, v20, v21
	v_cvt_pk_fp8_f32 v19, v22, v23 op_sel:[0,0,1]
	global_store_dwordx2 v[16:17], v[18:19], off offset:128
	s_nop 0
	s_nop 0
	s_nop 0
	s_nop 0
	s_waitcnt vmcnt(3)
	v_lshlrev_b32_e32 v30, 16, v174
	v_lshlrev_b32_e32 v114, 16, v177
	v_and_b32_e32 v115, 0xffff0000, v177
	v_mul_f32_e32 v21, 0xbfb8aa3b, v30
	v_exp_f32_e32 v21, v21
	v_lshlrev_b32_e32 v112, 16, v176
	v_and_b32_e32 v113, 0xffff0000, v176
	v_mul_f32_e32 v20, v108, v15
	v_add_f32_e32 v21, 1.0, v21
	v_rcp_f32_e32 v21, v21
	s_nop 0
	v_mul_f32_e32 v20, v20, v244
	v_mul_f32_e32 v20, v20, v30
	v_and_b32_e32 v18, 0xffff0000, v174
	v_mul_f32_e32 v26, v20, v21
	v_mul_f32_e32 v21, 0xbfb8aa3b, v112
	v_exp_f32_e32 v21, v21
	v_mul_f32_e32 v20, v104, v15
	v_mul_f32_e32 v20, v20, v240
	v_mul_f32_e32 v20, v20, v112
	v_add_f32_e32 v21, 1.0, v21
	v_rcp_f32_e32 v21, v21
	v_lshlrev_b32_e32 v31, 16, v175
	v_mul_f32_e32 v22, 0xbfb8aa3b, v31
	v_exp_f32_e32 v22, v22
	v_mul_f32_e32 v20, v20, v21
	v_mul_f32_e32 v21, v109, v15
	v_mul_f32_e32 v21, v21, v245
	v_mul_f32_e32 v21, v21, v18
	v_mul_f32_e32 v18, 0xbfb8aa3b, v18
	v_exp_f32_e32 v18, v18
	v_add_f32_e32 v22, 1.0, v22
	v_rcp_f32_e32 v22, v22
	v_and_b32_e32 v19, 0xffff0000, v175
	v_add_f32_e32 v18, 1.0, v18
	v_rcp_f32_e32 v18, v18
	s_nop 0
	v_mul_f32_e32 v27, v21, v18
	v_mul_f32_e32 v21, 0xbfb8aa3b, v113
	v_exp_f32_e32 v21, v21
	v_mul_f32_e32 v18, v105, v15
	v_mul_f32_e32 v18, v18, v241
	v_mul_f32_e32 v18, v18, v113
	v_add_f32_e32 v21, 1.0, v21
	v_rcp_f32_e32 v21, v21
	v_mul_f32_e32 v23, 0xbfb8aa3b, v115
	v_exp_f32_e32 v23, v23
	v_mul_f32_e32 v21, v18, v21
	v_mul_f32_e32 v18, v110, v15
	v_mul_f32_e32 v18, v18, v246
	v_mul_f32_e32 v18, v18, v31
	v_mul_f32_e32 v28, v18, v22
	v_mul_f32_e32 v22, 0xbfb8aa3b, v114
	v_exp_f32_e32 v22, v22
	v_mul_f32_e32 v18, v106, v15
	v_mul_f32_e32 v18, v18, v242
	v_mul_f32_e32 v18, v18, v114
	v_add_f32_e32 v22, 1.0, v22
	v_rcp_f32_e32 v22, v22
	v_add_f32_e32 v23, 1.0, v23
	v_rcp_f32_e32 v23, v23
	v_mul_f32_e32 v22, v18, v22
	v_mul_f32_e32 v18, v111, v15
	v_mul_f32_e32 v18, v18, v247
	v_mul_f32_e32 v18, v18, v19
	v_mul_f32_e32 v19, 0xbfb8aa3b, v19
	v_exp_f32_e32 v19, v19
	s_nop 0
	v_add_f32_e32 v19, 1.0, v19
	v_rcp_f32_e32 v19, v19
	s_nop 0
	v_mul_f32_e32 v19, v18, v19
	v_mul_f32_e32 v18, v107, v15
	v_mul_f32_e32 v18, v18, v243
	v_mul_f32_e32 v18, v18, v115
	v_mul_f32_e32 v23, v18, v23
	v_mov_b32_e32 v18, 0
	v_cvt_pk_fp8_f32 v18, v26, v27
	v_cvt_pk_fp8_f32 v18, v28, v19 op_sel:[0,0,1]
	v_mov_b32_e32 v19, 0
	v_cvt_pk_fp8_f32 v19, v20, v21
	v_cvt_pk_fp8_f32 v19, v22, v23 op_sel:[0,0,1]
	global_store_dwordx2 v[16:17], v[18:19], off offset:256
	s_nop 0
	s_nop 0
	s_nop 0
	s_nop 0
	s_waitcnt vmcnt(3)
	v_lshlrev_b32_e32 v6, 16, v178
	v_lshlrev_b32_e32 v30, 16, v180
	s_nop 0
	v_mul_f32_e32 v26, v100, v208
	v_mul_f32_e32 v26, v26, v6
	v_mul_f32_e32 v6, 0xbfb8aa3b, v6
	v_exp_f32_e32 v6, v6
	v_and_b32_e32 v7, 0xffff0000, v178
	v_and_b32_e32 v20, 0xffff0000, v180
	v_lshlrev_b32_e32 v18, 16, v179
	v_add_f32_e32 v6, 1.0, v6
	v_rcp_f32_e32 v6, v6
	v_lshlrev_b32_e32 v31, 16, v181
	v_and_b32_e32 v19, 0xffff0000, v179
	v_and_b32_e32 v21, 0xffff0000, v181
	v_mul_f32_e32 v26, v26, v6
	v_mul_f32_e32 v6, v96, v15
	v_mul_f32_e32 v6, v6, v204
	v_mul_f32_e32 v22, 0xbfb8aa3b, v30
	v_exp_f32_e32 v22, v22
	v_mul_f32_e32 v6, v6, v30
	v_add_f32_e32 v22, 1.0, v22
	v_rcp_f32_e32 v22, v22
	s_nop 0
	v_mul_f32_e32 v22, v6, v22
	v_mul_f32_e32 v6, v101, v15
	v_mul_f32_e32 v6, v6, v209
	v_mul_f32_e32 v6, v6, v7
	v_mul_f32_e32 v7, 0xbfb8aa3b, v7
	v_exp_f32_e32 v7, v7
	s_nop 0
	v_add_f32_e32 v7, 1.0, v7
	v_rcp_f32_e32 v7, v7
	s_nop 0
	v_mul_f32_e32 v7, v6, v7
	v_mul_f32_e32 v6, v97, v15
	v_mul_f32_e32 v6, v6, v205
	v_mul_f32_e32 v6, v6, v20
	v_mul_f32_e32 v20, 0xbfb8aa3b, v20
	v_exp_f32_e32 v20, v20
	v_mul_f32_e32 v23, 0xbfb8aa3b, v31
	v_exp_f32_e32 v23, v23
	v_add_f32_e32 v20, 1.0, v20
	v_rcp_f32_e32 v20, v20
	v_add_f32_e32 v23, 1.0, v23
	v_rcp_f32_e32 v23, v23
	v_mul_f32_e32 v20, v6, v20
	v_mul_f32_e32 v6, v102, v15
	v_mul_f32_e32 v6, v6, v210
	v_mul_f32_e32 v6, v6, v18
	v_mul_f32_e32 v18, 0xbfb8aa3b, v18
	v_exp_f32_e32 v18, v18
	s_nop 0
	v_add_f32_e32 v18, 1.0, v18
	v_rcp_f32_e32 v18, v18
	s_nop 0
	v_mul_f32_e32 v18, v6, v18
	v_mul_f32_e32 v6, v98, v15
	v_mul_f32_e32 v6, v6, v206
	v_mul_f32_e32 v6, v6, v31
	v_mul_f32_e32 v23, v6, v23
	v_mul_f32_e32 v6, v103, v15
	v_mul_f32_e32 v6, v6, v211
	v_mul_f32_e32 v6, v6, v19
	v_mul_f32_e32 v19, 0xbfb8aa3b, v19
	v_exp_f32_e32 v19, v19
	s_nop 0
	v_add_f32_e32 v19, 1.0, v19
	v_rcp_f32_e32 v19, v19
	s_nop 0
	v_mul_f32_e32 v19, v6, v19
	v_mul_f32_e32 v6, v99, v15
	v_mul_f32_e32 v15, 0xbfb8aa3b, v21
	v_exp_f32_e32 v15, v15
	v_mul_f32_e32 v6, v6, v207
	v_mul_f32_e32 v6, v6, v21
	v_add_f32_e32 v15, 1.0, v15
	v_rcp_f32_e32 v15, v15
	s_nop 0
	v_mul_f32_e32 v15, v6, v15
	v_mov_b32_e32 v6, 0
	v_cvt_pk_fp8_f32 v6, v26, v7
	v_mov_b32_e32 v7, 0
	v_cvt_pk_fp8_f32 v7, v22, v20
	v_cvt_pk_fp8_f32 v6, v18, v19 op_sel:[0,0,1]
	v_cvt_pk_fp8_f32 v7, v23, v15 op_sel:[0,0,1]
	global_store_dwordx2 v[16:17], v[6:7], off offset:384
	v_or_b32_e32 v6, 32, v14
	v_lshl_add_u32 v7, v6, 4, s0
	ds_read_b128 v[16:19], v7
	s_waitcnt lgkmcnt(0)
	v_mov_b32_e32 v20, v17
	v_mov_b32_e32 v21, v18
	v_mov_b32_e32 v17, v19
	v_pk_add_f32 v[16:17], v[20:21], v[16:17]
	s_nop 0
	v_add_f32_e32 v7, v16, v17
	v_fmamk_f32 v7, v7, 0x3b000000, v189
	v_rsq_f32_e32 v15, v7
	v_ashrrev_i32_e32 v7, 31, v6
	v_lshl_add_u64 v[16:17], s[20:21], 0, v[6:7]
	v_lshlrev_b64 v[6:7], 12, v[16:17]
	v_lshlrev_b64 v[16:17], 13, v[16:17]
	v_lshl_add_u64 v[18:19], s[66:67], 0, v[16:17]
	v_lshl_add_u64 v[16:17], s[34:35], 0, v[6:7]
	v_lshl_add_u64 v[6:7], v[18:19], 0, v[10:11]
	global_load_dwordx4 v[212:215], v[6:7], off
	global_load_dwordx4 v[216:219], v[6:7], off offset:256
	global_load_dwordx4 v[174:177], v[6:7], off offset:512
	global_load_dwordx4 v[178:181], v[6:7], off offset:768
	s_nop 0
	s_nop 0
	v_lshl_add_u64 v[16:17], v[16:17], 0, v[8:9]
	v_mul_f32_e32 v68, v68, v15
	s_waitcnt vmcnt(3)
	v_lshlrev_b32_e32 v30, 16, v212
	v_lshlrev_b32_e32 v98, 16, v215
	v_and_b32_e32 v99, 0xffff0000, v215
	v_mul_f32_e32 v21, 0xbfb8aa3b, v30
	v_exp_f32_e32 v21, v21
	v_lshlrev_b32_e32 v96, 16, v214
	v_and_b32_e32 v97, 0xffff0000, v214
	v_mul_f32_e32 v20, v92, v15
	v_add_f32_e32 v21, 1.0, v21
	v_rcp_f32_e32 v21, v21
	s_nop 0
	v_mul_f32_e32 v20, v228, v20
	v_mul_f32_e32 v20, v20, v30
	v_and_b32_e32 v18, 0xffff0000, v212
	v_mul_f32_e32 v26, v21, v20
	v_mul_f32_e32 v21, 0xbfb8aa3b, v96
	v_exp_f32_e32 v21, v21
	v_mul_f32_e32 v20, v88, v15
	v_mul_f32_e32 v20, v224, v20
	v_mul_f32_e32 v20, v20, v96
	v_add_f32_e32 v21, 1.0, v21
	v_rcp_f32_e32 v21, v21
	v_lshlrev_b32_e32 v31, 16, v213
	v_mul_f32_e32 v22, 0xbfb8aa3b, v31
	v_exp_f32_e32 v22, v22
	v_mul_f32_e32 v20, v21, v20
	v_mul_f32_e32 v21, v93, v15
	v_mul_f32_e32 v21, v229, v21
	v_mul_f32_e32 v21, v21, v18
	v_mul_f32_e32 v18, 0xbfb8aa3b, v18
	v_exp_f32_e32 v18, v18
	v_add_f32_e32 v22, 1.0, v22
	v_rcp_f32_e32 v22, v22
	v_and_b32_e32 v19, 0xffff0000, v213
	v_add_f32_e32 v18, 1.0, v18
	v_rcp_f32_e32 v18, v18
	s_nop 0
	v_mul_f32_e32 v27, v18, v21
	v_mul_f32_e32 v21, 0xbfb8aa3b, v97
	v_exp_f32_e32 v21, v21
	v_mul_f32_e32 v18, v89, v15
	v_mul_f32_e32 v18, v225, v18
	v_mul_f32_e32 v18, v18, v97
	v_add_f32_e32 v21, 1.0, v21
	v_rcp_f32_e32 v21, v21
	v_mul_f32_e32 v23, 0xbfb8aa3b, v99
	v_exp_f32_e32 v23, v23
	v_mul_f32_e32 v21, v21, v18
	v_mul_f32_e32 v18, v94, v15
	v_mul_f32_e32 v18, v230, v18
	v_mul_f32_e32 v18, v18, v31
	v_mul_f32_e32 v28, v22, v18
	v_mul_f32_e32 v22, 0xbfb8aa3b, v98
	v_exp_f32_e32 v22, v22
	v_mul_f32_e32 v18, v90, v15
	v_mul_f32_e32 v18, v226, v18
	v_mul_f32_e32 v18, v18, v98
	v_add_f32_e32 v22, 1.0, v22
	v_rcp_f32_e32 v22, v22
	v_add_f32_e32 v23, 1.0, v23
	v_rcp_f32_e32 v23, v23
	v_mul_f32_e32 v22, v22, v18
	v_mul_f32_e32 v18, v95, v15
	v_mul_f32_e32 v18, v231, v18
	v_mul_f32_e32 v18, v18, v19
	v_mul_f32_e32 v19, 0xbfb8aa3b, v19
	v_exp_f32_e32 v19, v19
	s_nop 0
	v_add_f32_e32 v19, 1.0, v19
	v_rcp_f32_e32 v19, v19
	s_nop 0
	v_mul_f32_e32 v19, v19, v18
	v_mul_f32_e32 v18, v91, v15
	v_mul_f32_e32 v18, v227, v18
	v_mul_f32_e32 v18, v18, v99
	v_mul_f32_e32 v23, v23, v18
	v_mov_b32_e32 v18, 0
	v_cvt_pk_fp8_f32 v18, v26, v27
	v_cvt_pk_fp8_f32 v18, v28, v19 op_sel:[0,0,1]
	v_mov_b32_e32 v19, 0
	v_cvt_pk_fp8_f32 v19, v20, v21
	v_cvt_pk_fp8_f32 v19, v22, v23 op_sel:[0,0,1]
	global_store_dwordx2 v[16:17], v[18:19], off
	s_nop 0
	s_nop 0
	s_nop 0
	s_nop 0
	s_waitcnt vmcnt(3)
	v_lshlrev_b32_e32 v30, 16, v216
	v_lshlrev_b32_e32 v90, 16, v219
	v_and_b32_e32 v91, 0xffff0000, v219
	v_mul_f32_e32 v21, 0xbfb8aa3b, v30
	v_exp_f32_e32 v21, v21
	v_lshlrev_b32_e32 v88, 16, v218
	v_and_b32_e32 v89, 0xffff0000, v218
	v_mul_f32_e32 v20, v84, v15
	v_add_f32_e32 v21, 1.0, v21
	v_rcp_f32_e32 v21, v21
	s_nop 0
	v_mul_f32_e32 v20, v20, v236
	v_mul_f32_e32 v20, v20, v30
	v_and_b32_e32 v18, 0xffff0000, v216
	v_mul_f32_e32 v26, v20, v21
	v_mul_f32_e32 v21, 0xbfb8aa3b, v88
	v_exp_f32_e32 v21, v21
	v_mul_f32_e32 v20, v80, v15
	v_mul_f32_e32 v20, v20, v232
	v_mul_f32_e32 v20, v20, v88
	v_add_f32_e32 v21, 1.0, v21
	v_rcp_f32_e32 v21, v21
	v_lshlrev_b32_e32 v31, 16, v217
	v_mul_f32_e32 v22, 0xbfb8aa3b, v31
	v_exp_f32_e32 v22, v22
	v_mul_f32_e32 v20, v20, v21
	v_mul_f32_e32 v21, v85, v15
	v_mul_f32_e32 v21, v21, v237
	v_mul_f32_e32 v21, v21, v18
	v_mul_f32_e32 v18, 0xbfb8aa3b, v18
	v_exp_f32_e32 v18, v18
	v_add_f32_e32 v22, 1.0, v22
	v_rcp_f32_e32 v22, v22
	v_and_b32_e32 v19, 0xffff0000, v217
	v_add_f32_e32 v18, 1.0, v18
	v_rcp_f32_e32 v18, v18
	s_nop 0
	v_mul_f32_e32 v27, v21, v18
	v_mul_f32_e32 v21, 0xbfb8aa3b, v89
	v_exp_f32_e32 v21, v21
	v_mul_f32_e32 v18, v81, v15
	v_mul_f32_e32 v18, v18, v233
	v_mul_f32_e32 v18, v18, v89
	v_add_f32_e32 v21, 1.0, v21
	v_rcp_f32_e32 v21, v21
	v_mul_f32_e32 v23, 0xbfb8aa3b, v91
	v_exp_f32_e32 v23, v23
	v_mul_f32_e32 v21, v18, v21
	v_mul_f32_e32 v18, v86, v15
	v_mul_f32_e32 v18, v18, v238
	v_mul_f32_e32 v18, v18, v31
	v_mul_f32_e32 v28, v18, v22
	v_mul_f32_e32 v22, 0xbfb8aa3b, v90
	v_exp_f32_e32 v22, v22
	v_mul_f32_e32 v18, v82, v15
	v_mul_f32_e32 v18, v18, v234
	v_mul_f32_e32 v18, v18, v90
	v_add_f32_e32 v22, 1.0, v22
	v_rcp_f32_e32 v22, v22
	v_add_f32_e32 v23, 1.0, v23
	v_rcp_f32_e32 v23, v23
	v_mul_f32_e32 v22, v18, v22
	v_mul_f32_e32 v18, v87, v15
	v_mul_f32_e32 v18, v18, v239
	v_mul_f32_e32 v18, v18, v19
	v_mul_f32_e32 v19, 0xbfb8aa3b, v19
	v_exp_f32_e32 v19, v19
	s_nop 0
	v_add_f32_e32 v19, 1.0, v19
	v_rcp_f32_e32 v19, v19
	s_nop 0
	v_mul_f32_e32 v19, v18, v19
	v_mul_f32_e32 v18, v83, v15
	v_mul_f32_e32 v18, v18, v235
	v_mul_f32_e32 v18, v18, v91
	v_mul_f32_e32 v23, v18, v23
	v_mov_b32_e32 v18, 0
	v_cvt_pk_fp8_f32 v18, v26, v27
	v_cvt_pk_fp8_f32 v18, v28, v19 op_sel:[0,0,1]
	v_mov_b32_e32 v19, 0
	v_cvt_pk_fp8_f32 v19, v20, v21
	v_cvt_pk_fp8_f32 v19, v22, v23 op_sel:[0,0,1]
	global_store_dwordx2 v[16:17], v[18:19], off offset:128
	s_nop 0
	s_nop 0
	s_nop 0
	s_nop 0
	s_waitcnt vmcnt(3)
	v_lshlrev_b32_e32 v30, 16, v174
	v_lshlrev_b32_e32 v82, 16, v177
	v_and_b32_e32 v83, 0xffff0000, v177
	v_mul_f32_e32 v21, 0xbfb8aa3b, v30
	v_exp_f32_e32 v21, v21
	v_lshlrev_b32_e32 v80, 16, v176
	v_and_b32_e32 v81, 0xffff0000, v176
	v_mul_f32_e32 v20, v76, v15
	v_add_f32_e32 v21, 1.0, v21
	v_rcp_f32_e32 v21, v21
	s_nop 0
	v_mul_f32_e32 v20, v20, v244
	v_mul_f32_e32 v20, v20, v30
	v_and_b32_e32 v18, 0xffff0000, v174
	v_mul_f32_e32 v26, v20, v21
	v_mul_f32_e32 v21, 0xbfb8aa3b, v80
	v_exp_f32_e32 v21, v21
	v_mul_f32_e32 v20, v72, v15
	v_mul_f32_e32 v20, v20, v240
	v_mul_f32_e32 v20, v20, v80
	v_add_f32_e32 v21, 1.0, v21
	v_rcp_f32_e32 v21, v21
	v_lshlrev_b32_e32 v31, 16, v175
	v_mul_f32_e32 v22, 0xbfb8aa3b, v31
	v_exp_f32_e32 v22, v22
	v_mul_f32_e32 v20, v20, v21
	v_mul_f32_e32 v21, v77, v15
	v_mul_f32_e32 v21, v21, v245
	v_mul_f32_e32 v21, v21, v18
	v_mul_f32_e32 v18, 0xbfb8aa3b, v18
	v_exp_f32_e32 v18, v18
	v_add_f32_e32 v22, 1.0, v22
	v_rcp_f32_e32 v22, v22
	v_and_b32_e32 v19, 0xffff0000, v175
	v_add_f32_e32 v18, 1.0, v18
	v_rcp_f32_e32 v18, v18
	s_nop 0
	v_mul_f32_e32 v27, v21, v18
	v_mul_f32_e32 v21, 0xbfb8aa3b, v81
	v_exp_f32_e32 v21, v21
	v_mul_f32_e32 v18, v73, v15
	v_mul_f32_e32 v18, v18, v241
	v_mul_f32_e32 v18, v18, v81
	v_add_f32_e32 v21, 1.0, v21
	v_rcp_f32_e32 v21, v21
	v_mul_f32_e32 v23, 0xbfb8aa3b, v83
	v_exp_f32_e32 v23, v23
	v_mul_f32_e32 v21, v18, v21
	v_mul_f32_e32 v18, v78, v15
	v_mul_f32_e32 v18, v18, v246
	v_mul_f32_e32 v18, v18, v31
	v_mul_f32_e32 v28, v18, v22
	v_mul_f32_e32 v22, 0xbfb8aa3b, v82
	v_exp_f32_e32 v22, v22
	v_mul_f32_e32 v18, v74, v15
	v_mul_f32_e32 v18, v18, v242
	v_mul_f32_e32 v18, v18, v82
	v_add_f32_e32 v22, 1.0, v22
	v_rcp_f32_e32 v22, v22
	v_add_f32_e32 v23, 1.0, v23
	v_rcp_f32_e32 v23, v23
	v_mul_f32_e32 v22, v18, v22
	v_mul_f32_e32 v18, v79, v15
	v_mul_f32_e32 v18, v18, v247
	v_mul_f32_e32 v18, v18, v19
	v_mul_f32_e32 v19, 0xbfb8aa3b, v19
	v_exp_f32_e32 v19, v19
	s_nop 0
	v_add_f32_e32 v19, 1.0, v19
	v_rcp_f32_e32 v19, v19
	s_nop 0
	v_mul_f32_e32 v19, v18, v19
	v_mul_f32_e32 v18, v75, v15
	v_mul_f32_e32 v18, v18, v243
	v_mul_f32_e32 v18, v18, v83
	v_mul_f32_e32 v23, v18, v23
	v_mov_b32_e32 v18, 0
	v_cvt_pk_fp8_f32 v18, v26, v27
	v_cvt_pk_fp8_f32 v18, v28, v19 op_sel:[0,0,1]
	v_mov_b32_e32 v19, 0
	v_cvt_pk_fp8_f32 v19, v20, v21
	v_cvt_pk_fp8_f32 v19, v22, v23 op_sel:[0,0,1]
	global_store_dwordx2 v[16:17], v[18:19], off offset:256
	s_nop 0
	s_nop 0
	s_nop 0
	s_nop 0
	s_waitcnt vmcnt(3)
	v_lshlrev_b32_e32 v6, 16, v178
	v_lshlrev_b32_e32 v30, 16, v180
	s_nop 0
	v_mul_f32_e32 v26, v68, v208
	v_mul_f32_e32 v26, v26, v6
	v_mul_f32_e32 v6, 0xbfb8aa3b, v6
	v_exp_f32_e32 v6, v6
	v_and_b32_e32 v7, 0xffff0000, v178
	v_and_b32_e32 v20, 0xffff0000, v180
	v_lshlrev_b32_e32 v18, 16, v179
	v_add_f32_e32 v6, 1.0, v6
	v_rcp_f32_e32 v6, v6
	v_lshlrev_b32_e32 v31, 16, v181
	v_and_b32_e32 v19, 0xffff0000, v179
	v_and_b32_e32 v21, 0xffff0000, v181
	v_mul_f32_e32 v26, v26, v6
	v_mul_f32_e32 v6, v64, v15
	v_mul_f32_e32 v6, v6, v204
	v_mul_f32_e32 v22, 0xbfb8aa3b, v30
	v_exp_f32_e32 v22, v22
	v_mul_f32_e32 v6, v6, v30
	v_add_f32_e32 v22, 1.0, v22
	v_rcp_f32_e32 v22, v22
	s_nop 0
	v_mul_f32_e32 v22, v6, v22
	v_mul_f32_e32 v6, v69, v15
	v_mul_f32_e32 v6, v6, v209
	v_mul_f32_e32 v6, v6, v7
	v_mul_f32_e32 v7, 0xbfb8aa3b, v7
	v_exp_f32_e32 v7, v7
	s_nop 0
	v_add_f32_e32 v7, 1.0, v7
	v_rcp_f32_e32 v7, v7
	s_nop 0
	v_mul_f32_e32 v7, v6, v7
	v_mul_f32_e32 v6, v65, v15
	v_mul_f32_e32 v6, v6, v205
	v_mul_f32_e32 v6, v6, v20
	v_mul_f32_e32 v20, 0xbfb8aa3b, v20
	v_exp_f32_e32 v20, v20
	v_mul_f32_e32 v23, 0xbfb8aa3b, v31
	v_exp_f32_e32 v23, v23
	v_add_f32_e32 v20, 1.0, v20
	v_rcp_f32_e32 v20, v20
	v_add_f32_e32 v23, 1.0, v23
	v_rcp_f32_e32 v23, v23
	v_mul_f32_e32 v20, v6, v20
	v_mul_f32_e32 v6, v70, v15
	v_mul_f32_e32 v6, v6, v210
	v_mul_f32_e32 v6, v6, v18
	v_mul_f32_e32 v18, 0xbfb8aa3b, v18
	v_exp_f32_e32 v18, v18
	s_nop 0
	v_add_f32_e32 v18, 1.0, v18
	v_rcp_f32_e32 v18, v18
	s_nop 0
	v_mul_f32_e32 v18, v6, v18
	v_mul_f32_e32 v6, v66, v15
	v_mul_f32_e32 v6, v6, v206
	v_mul_f32_e32 v6, v6, v31
	v_mul_f32_e32 v23, v6, v23
	v_mul_f32_e32 v6, v71, v15
	v_mul_f32_e32 v6, v6, v211
	v_mul_f32_e32 v6, v6, v19
	v_mul_f32_e32 v19, 0xbfb8aa3b, v19
	v_exp_f32_e32 v19, v19
	s_nop 0
	v_add_f32_e32 v19, 1.0, v19
	v_rcp_f32_e32 v19, v19
	s_nop 0
	v_mul_f32_e32 v19, v6, v19
	v_mul_f32_e32 v6, v67, v15
	v_mul_f32_e32 v15, 0xbfb8aa3b, v21
	v_exp_f32_e32 v15, v15
	v_mul_f32_e32 v6, v6, v207
	v_mul_f32_e32 v6, v6, v21
	v_add_f32_e32 v15, 1.0, v15
	v_rcp_f32_e32 v15, v15
	s_nop 0
	v_mul_f32_e32 v15, v6, v15
	v_mov_b32_e32 v6, 0
	v_cvt_pk_fp8_f32 v6, v26, v7
	v_mov_b32_e32 v7, 0
	v_cvt_pk_fp8_f32 v7, v22, v20
	v_cvt_pk_fp8_f32 v6, v18, v19 op_sel:[0,0,1]
	v_cvt_pk_fp8_f32 v7, v23, v15 op_sel:[0,0,1]
	global_store_dwordx2 v[16:17], v[6:7], off offset:384
	v_or_b32_e32 v6, 48, v14
	v_lshl_add_u32 v7, v6, 4, s0
	ds_read_b128 v[14:17], v7
	s_mov_b64 s[0:1], 0
	s_waitcnt lgkmcnt(0)
	v_mov_b32_e32 v18, v15
	v_mov_b32_e32 v19, v16
	v_mov_b32_e32 v15, v17
	v_pk_add_f32 v[14:15], v[18:19], v[14:15]
	s_nop 0
	v_add_f32_e32 v7, v14, v15
	v_fmamk_f32 v7, v7, 0x3b000000, v189
	v_rsq_f32_e32 v16, v7
	v_ashrrev_i32_e32 v7, 31, v6
	v_lshl_add_u64 v[14:15], s[20:21], 0, v[6:7]
	v_lshlrev_b64 v[6:7], 12, v[14:15]
	v_lshlrev_b64 v[14:15], 13, v[14:15]
	v_lshl_add_u64 v[18:19], s[66:67], 0, v[14:15]
	v_lshl_add_u64 v[14:15], s[34:35], 0, v[6:7]
	v_lshl_add_u64 v[6:7], v[18:19], 0, v[10:11]
	global_load_dwordx4 v[212:215], v[6:7], off
	global_load_dwordx4 v[216:219], v[6:7], off offset:256
	global_load_dwordx4 v[174:177], v[6:7], off offset:512
	global_load_dwordx4 v[178:181], v[6:7], off offset:768
	s_nop 0
	s_nop 0
	v_lshl_add_u64 v[8:9], v[14:15], 0, v[8:9]
	s_waitcnt vmcnt(3)
	v_lshlrev_b32_e32 v10, 16, v212
	v_and_b32_e32 v11, 0xffff0000, v212
	v_lshlrev_b32_e32 v17, 16, v213
	v_and_b32_e32 v18, 0xffff0000, v213
	v_lshlrev_b32_e32 v12, 16, v214
	v_and_b32_e32 v13, 0xffff0000, v214
	v_lshlrev_b32_e32 v19, 16, v215
	v_and_b32_e32 v20, 0xffff0000, v215
	v_mul_f32_e32 v21, v60, v16
	s_nop 0
	v_mul_f32_e32 v21, v228, v21
	v_mul_f32_e32 v21, v21, v10
	v_mul_f32_e32 v10, 0xbfb8aa3b, v10
	v_exp_f32_e32 v10, v10
	s_nop 0
	v_add_f32_e32 v10, 1.0, v10
	v_rcp_f32_e32 v10, v10
	s_nop 0
	v_mul_f32_e32 v21, v10, v21
	v_mul_f32_e32 v10, v56, v16
	v_mul_f32_e32 v10, v224, v10
	v_mul_f32_e32 v10, v10, v12
	v_mul_f32_e32 v12, 0xbfb8aa3b, v12
	v_exp_f32_e32 v12, v12
	s_nop 0
	v_add_f32_e32 v12, 1.0, v12
	v_rcp_f32_e32 v12, v12
	s_nop 0
	v_mul_f32_e32 v12, v12, v10
	v_mul_f32_e32 v10, v61, v16
	v_mul_f32_e32 v10, v229, v10
	v_mul_f32_e32 v10, v10, v11
	v_mul_f32_e32 v11, 0xbfb8aa3b, v11
	v_exp_f32_e32 v11, v11
	s_nop 0
	v_add_f32_e32 v11, 1.0, v11
	v_rcp_f32_e32 v11, v11
	s_nop 0
	v_mul_f32_e32 v11, v11, v10
	v_mul_f32_e32 v10, v57, v16
	v_mul_f32_e32 v10, v225, v10
	v_mul_f32_e32 v10, v10, v13
	v_mul_f32_e32 v13, 0xbfb8aa3b, v13
	v_exp_f32_e32 v13, v13
	s_nop 0
	v_add_f32_e32 v13, 1.0, v13
	v_rcp_f32_e32 v13, v13
	s_nop 0
	v_mul_f32_e32 v13, v13, v10
	v_mul_f32_e32 v10, v62, v16
	v_mul_f32_e32 v10, v230, v10
	v_mul_f32_e32 v10, v10, v17
	v_mul_f32_e32 v17, 0xbfb8aa3b, v17
	v_exp_f32_e32 v17, v17
	s_nop 0
	v_add_f32_e32 v17, 1.0, v17
	v_rcp_f32_e32 v17, v17
	s_nop 0
	v_mul_f32_e32 v22, v17, v10
	v_mul_f32_e32 v17, 0xbfb8aa3b, v19
	v_exp_f32_e32 v17, v17
	v_mul_f32_e32 v10, v58, v16
	v_mul_f32_e32 v10, v226, v10
	v_mul_f32_e32 v10, v10, v19
	v_add_f32_e32 v17, 1.0, v17
	v_rcp_f32_e32 v17, v17
	s_nop 0
	v_mul_f32_e32 v17, v17, v10
	v_mul_f32_e32 v10, v63, v16
	v_mul_f32_e32 v10, v231, v10
	v_mul_f32_e32 v10, v10, v18
	v_mul_f32_e32 v18, 0xbfb8aa3b, v18
	v_exp_f32_e32 v18, v18
	s_nop 0
	v_add_f32_e32 v18, 1.0, v18
	v_rcp_f32_e32 v18, v18
	s_nop 0
	v_mul_f32_e32 v19, v18, v10
	v_mul_f32_e32 v18, 0xbfb8aa3b, v20
	v_exp_f32_e32 v18, v18
	v_mul_f32_e32 v10, v59, v16
	v_mul_f32_e32 v10, v227, v10
	v_mul_f32_e32 v10, v10, v20
	v_add_f32_e32 v18, 1.0, v18
	v_rcp_f32_e32 v18, v18
	s_nop 0
	v_mul_f32_e32 v18, v18, v10
	v_mov_b32_e32 v10, 0
	v_cvt_pk_fp8_f32 v10, v21, v11
	v_mov_b32_e32 v11, 0
	v_cvt_pk_fp8_f32 v11, v12, v13
	v_cvt_pk_fp8_f32 v10, v22, v19 op_sel:[0,0,1]
	v_cvt_pk_fp8_f32 v11, v17, v18 op_sel:[0,0,1]
	v_mul_f32_e32 v17, v52, v16
	global_store_dwordx2 v[8:9], v[10:11], off
	s_nop 0
	s_nop 0
	s_nop 0
	s_nop 0
	s_waitcnt vmcnt(3)
	v_lshlrev_b32_e32 v0, 16, v216
	v_and_b32_e32 v1, 0xffff0000, v216
	s_nop 0
	v_mul_f32_e32 v17, v17, v236
	v_mul_f32_e32 v17, v17, v0
	v_mul_f32_e32 v0, 0xbfb8aa3b, v0
	v_exp_f32_e32 v0, v0
	v_lshlrev_b32_e32 v10, 16, v218
	v_lshlrev_b32_e32 v14, 16, v217
	v_and_b32_e32 v15, 0xffff0000, v217
	v_add_f32_e32 v0, 1.0, v0
	v_rcp_f32_e32 v0, v0
	v_and_b32_e32 v11, 0xffff0000, v218
	v_lshlrev_b32_e32 v12, 16, v219
	v_and_b32_e32 v13, 0xffff0000, v219
	v_mul_f32_e32 v17, v17, v0
	v_mul_f32_e32 v0, v48, v16
	v_mul_f32_e32 v0, v0, v232
	v_mul_f32_e32 v0, v0, v10
	v_mul_f32_e32 v10, 0xbfb8aa3b, v10
	v_exp_f32_e32 v10, v10
	s_nop 0
	v_add_f32_e32 v10, 1.0, v10
	v_rcp_f32_e32 v10, v10
	s_nop 0
	v_mul_f32_e32 v10, v0, v10
	v_mul_f32_e32 v0, v53, v16
	v_mul_f32_e32 v0, v0, v237
	v_mul_f32_e32 v0, v0, v1
	v_mul_f32_e32 v1, 0xbfb8aa3b, v1
	v_exp_f32_e32 v1, v1
	s_nop 0
	v_add_f32_e32 v1, 1.0, v1
	v_rcp_f32_e32 v1, v1
	s_nop 0
	v_mul_f32_e32 v1, v0, v1
	v_mul_f32_e32 v0, v49, v16
	v_mul_f32_e32 v0, v0, v233
	v_mul_f32_e32 v0, v0, v11
	v_mul_f32_e32 v11, 0xbfb8aa3b, v11
	v_exp_f32_e32 v11, v11
	s_nop 0
	v_add_f32_e32 v11, 1.0, v11
	v_rcp_f32_e32 v11, v11
	s_nop 0
	v_mul_f32_e32 v11, v0, v11
	v_mul_f32_e32 v0, v54, v16
	v_mul_f32_e32 v0, v0, v238
	v_mul_f32_e32 v0, v0, v14
	v_mul_f32_e32 v14, 0xbfb8aa3b, v14
	v_exp_f32_e32 v14, v14
	s_nop 0
	v_add_f32_e32 v14, 1.0, v14
	v_rcp_f32_e32 v14, v14
	s_nop 0
	v_mul_f32_e32 v14, v0, v14
	v_mul_f32_e32 v0, v50, v16
	v_mul_f32_e32 v0, v0, v234
	v_mul_f32_e32 v0, v0, v12
	v_mul_f32_e32 v12, 0xbfb8aa3b, v12
	v_exp_f32_e32 v12, v12
	s_nop 0
	v_add_f32_e32 v12, 1.0, v12
	v_rcp_f32_e32 v12, v12
	s_nop 0
	v_mul_f32_e32 v12, v0, v12
	v_mul_f32_e32 v0, v55, v16
	v_mul_f32_e32 v0, v0, v239
	v_mul_f32_e32 v0, v0, v15
	v_mul_f32_e32 v15, 0xbfb8aa3b, v15
	v_exp_f32_e32 v15, v15
	s_nop 0
	v_add_f32_e32 v15, 1.0, v15
	v_rcp_f32_e32 v15, v15
	s_nop 0
	v_mul_f32_e32 v15, v0, v15
	v_mul_f32_e32 v0, v51, v16
	v_mul_f32_e32 v0, v0, v235
	v_mul_f32_e32 v0, v0, v13
	v_mul_f32_e32 v13, 0xbfb8aa3b, v13
	v_exp_f32_e32 v13, v13
	s_nop 0
	v_add_f32_e32 v13, 1.0, v13
	v_rcp_f32_e32 v13, v13
	s_nop 0
	v_mul_f32_e32 v13, v0, v13
	v_mov_b32_e32 v0, 0
	v_cvt_pk_fp8_f32 v0, v17, v1
	v_mov_b32_e32 v1, 0
	v_cvt_pk_fp8_f32 v1, v10, v11
	v_cvt_pk_fp8_f32 v0, v14, v15 op_sel:[0,0,1]
	v_mul_f32_e32 v14, v44, v16
	v_cvt_pk_fp8_f32 v1, v12, v13 op_sel:[0,0,1]
	global_store_dwordx2 v[8:9], v[0:1], off offset:128
	s_nop 0
	s_nop 0
	s_nop 0
	s_waitcnt vmcnt(3)
	v_lshlrev_b32_e32 v0, 16, v174
	v_lshlrev_b32_e32 v2, 16, v176
	s_nop 0
	v_mul_f32_e32 v14, v14, v244
	v_mul_f32_e32 v14, v14, v0
	v_mul_f32_e32 v0, 0xbfb8aa3b, v0
	v_exp_f32_e32 v0, v0
	v_and_b32_e32 v1, 0xffff0000, v174
	v_and_b32_e32 v3, 0xffff0000, v176
	v_lshlrev_b32_e32 v10, 16, v175
	v_add_f32_e32 v0, 1.0, v0
	v_rcp_f32_e32 v0, v0
	v_lshlrev_b32_e32 v12, 16, v177
	v_and_b32_e32 v11, 0xffff0000, v175
	v_and_b32_e32 v13, 0xffff0000, v177
	v_mul_f32_e32 v14, v14, v0
	v_mul_f32_e32 v0, v40, v16
	v_mul_f32_e32 v0, v0, v240
	v_mul_f32_e32 v0, v0, v2
	v_mul_f32_e32 v2, 0xbfb8aa3b, v2
	v_exp_f32_e32 v2, v2
	s_nop 0
	v_add_f32_e32 v2, 1.0, v2
	v_rcp_f32_e32 v2, v2
	s_nop 0
	v_mul_f32_e32 v2, v0, v2
	v_mul_f32_e32 v0, v45, v16
	v_mul_f32_e32 v0, v0, v245
	v_mul_f32_e32 v0, v0, v1
	v_mul_f32_e32 v1, 0xbfb8aa3b, v1
	v_exp_f32_e32 v1, v1
	s_nop 0
	v_add_f32_e32 v1, 1.0, v1
	v_rcp_f32_e32 v1, v1
	s_nop 0
	v_mul_f32_e32 v1, v0, v1
	v_mul_f32_e32 v0, v41, v16
	v_mul_f32_e32 v0, v0, v241
	v_mul_f32_e32 v0, v0, v3
	v_mul_f32_e32 v3, 0xbfb8aa3b, v3
	v_exp_f32_e32 v3, v3
	s_nop 0
	v_add_f32_e32 v3, 1.0, v3
	v_rcp_f32_e32 v3, v3
	s_nop 0
	v_mul_f32_e32 v3, v0, v3
	v_mul_f32_e32 v0, v46, v16
	v_mul_f32_e32 v0, v0, v246
	v_mul_f32_e32 v0, v0, v10
	v_mul_f32_e32 v10, 0xbfb8aa3b, v10
	v_exp_f32_e32 v10, v10
	s_nop 0
	v_add_f32_e32 v10, 1.0, v10
	v_rcp_f32_e32 v10, v10
	s_nop 0
	v_mul_f32_e32 v15, v0, v10
	v_mul_f32_e32 v10, 0xbfb8aa3b, v12
	v_exp_f32_e32 v10, v10
	v_mul_f32_e32 v0, v42, v16
	v_mul_f32_e32 v0, v0, v242
	v_mul_f32_e32 v0, v0, v12
	v_add_f32_e32 v10, 1.0, v10
	v_rcp_f32_e32 v10, v10
	s_nop 0
	v_mul_f32_e32 v10, v0, v10
	v_mul_f32_e32 v0, v47, v16
	v_mul_f32_e32 v0, v0, v247
	v_mul_f32_e32 v0, v0, v11
	v_mul_f32_e32 v11, 0xbfb8aa3b, v11
	v_exp_f32_e32 v11, v11
	s_nop 0
	v_add_f32_e32 v11, 1.0, v11
	v_rcp_f32_e32 v11, v11
	s_nop 0
	v_mul_f32_e32 v12, v0, v11
	v_mul_f32_e32 v11, 0xbfb8aa3b, v13
	v_exp_f32_e32 v11, v11
	v_mul_f32_e32 v0, v43, v16
	v_mul_f32_e32 v0, v0, v243
	v_mul_f32_e32 v0, v0, v13
	v_add_f32_e32 v11, 1.0, v11
	v_rcp_f32_e32 v11, v11
	s_nop 0
	v_mul_f32_e32 v11, v0, v11
	v_mov_b32_e32 v0, 0
	v_cvt_pk_fp8_f32 v0, v14, v1
	v_mov_b32_e32 v1, 0
	v_cvt_pk_fp8_f32 v1, v2, v3
	v_cvt_pk_fp8_f32 v0, v15, v12 op_sel:[0,0,1]
	v_cvt_pk_fp8_f32 v1, v10, v11 op_sel:[0,0,1]
	global_store_dwordx2 v[8:9], v[0:1], off offset:256
	s_nop 0
	s_nop 0
	s_nop 0
	s_nop 0
	s_nop 0
	s_waitcnt vmcnt(3)
	v_lshlrev_b32_e32 v14, 16, v178
	v_lshlrev_b32_e32 v19, 16, v181
	v_and_b32_e32 v20, 0xffff0000, v181
	v_mul_f32_e32 v3, 0xbfb8aa3b, v14
	v_exp_f32_e32 v3, v3
	v_lshlrev_b32_e32 v17, 16, v180
	v_and_b32_e32 v18, 0xffff0000, v180
	v_mul_f32_e32 v2, v36, v16
	v_add_f32_e32 v3, 1.0, v3
	v_rcp_f32_e32 v3, v3
	s_nop 0
	v_mul_f32_e32 v2, v2, v208
	v_mul_f32_e32 v2, v2, v14
	v_and_b32_e32 v0, 0xffff0000, v178
	v_mul_f32_e32 v14, v2, v3
	v_mul_f32_e32 v3, 0xbfb8aa3b, v17
	v_exp_f32_e32 v3, v3
	v_mul_f32_e32 v2, v32, v16
	v_mul_f32_e32 v2, v2, v204
	v_mul_f32_e32 v2, v2, v17
	v_add_f32_e32 v3, 1.0, v3
	v_rcp_f32_e32 v3, v3
	v_lshlrev_b32_e32 v15, 16, v179
	v_mul_f32_e32 v4, 0xbfb8aa3b, v15
	v_exp_f32_e32 v4, v4
	v_mul_f32_e32 v2, v2, v3
	v_mul_f32_e32 v3, v37, v16
	v_mul_f32_e32 v3, v3, v209
	v_mul_f32_e32 v3, v3, v0
	v_mul_f32_e32 v0, 0xbfb8aa3b, v0
	v_exp_f32_e32 v0, v0
	v_add_f32_e32 v4, 1.0, v4
	v_rcp_f32_e32 v4, v4
	v_and_b32_e32 v1, 0xffff0000, v179
	v_add_f32_e32 v0, 1.0, v0
	v_rcp_f32_e32 v0, v0
	v_mul_f32_e32 v5, 0xbfb8aa3b, v20
	v_exp_f32_e32 v5, v5
	v_mul_f32_e32 v10, v3, v0
	v_mul_f32_e32 v3, 0xbfb8aa3b, v18
	v_exp_f32_e32 v3, v3
	v_mul_f32_e32 v0, v33, v16
	v_mul_f32_e32 v0, v0, v205
	v_mul_f32_e32 v0, v0, v18
	v_add_f32_e32 v3, 1.0, v3
	v_rcp_f32_e32 v3, v3
	v_add_f32_e32 v5, 1.0, v5
	v_rcp_f32_e32 v5, v5
	v_mul_f32_e32 v3, v0, v3
	v_mul_f32_e32 v0, v38, v16
	v_mul_f32_e32 v0, v0, v210
	v_mul_f32_e32 v0, v0, v15
	v_mul_f32_e32 v6, v0, v4
	v_mul_f32_e32 v4, 0xbfb8aa3b, v19
	v_exp_f32_e32 v4, v4
	v_mul_f32_e32 v0, v34, v16
	v_mul_f32_e32 v0, v0, v206
	v_mul_f32_e32 v0, v0, v19
	v_add_f32_e32 v4, 1.0, v4
	v_rcp_f32_e32 v4, v4
	s_nop 0
	v_mul_f32_e32 v4, v0, v4
	v_mul_f32_e32 v0, v39, v16
	v_mul_f32_e32 v0, v0, v211
	v_mul_f32_e32 v0, v0, v1
	v_mul_f32_e32 v1, 0xbfb8aa3b, v1
	v_exp_f32_e32 v1, v1
	s_nop 0
	v_add_f32_e32 v1, 1.0, v1
	v_rcp_f32_e32 v1, v1
	s_nop 0
	v_mul_f32_e32 v1, v0, v1
	v_mul_f32_e32 v0, v35, v16
	v_mul_f32_e32 v0, v0, v207
	v_mul_f32_e32 v0, v0, v20
	v_mul_f32_e32 v5, v0, v5
	v_mov_b32_e32 v0, 0
	v_cvt_pk_fp8_f32 v0, v14, v10
	v_cvt_pk_fp8_f32 v0, v6, v1 op_sel:[0,0,1]
	v_mov_b32_e32 v1, 0
	v_cvt_pk_fp8_f32 v1, v2, v3
	v_cvt_pk_fp8_f32 v1, v4, v5 op_sel:[0,0,1]
	global_store_dwordx2 v[8:9], v[0:1], off offset:384
	s_waitcnt vmcnt(0)
	s_barrier
	s_cbranch_vccnz .LBB0_592

.LBB0_1336:
	s_add_i32 s18, s2, s65
	s_max_i32 s13, s18, 4
	s_add_i32 s14, s13, -4
	s_mov_b32 s15, s60
	s_max_i32 s13, s18, 3
	s_lshl_b64 s[36:37], s[14:15], 12
	s_add_i32 s14, s13, -3
	s_max_i32 s13, s18, 2
	s_lshl_b64 s[52:53], s[14:15], 12
	s_add_i32 s14, s13, -2
	s_max_i32 s13, s18, 1
	s_lshl_b64 s[50:51], s[14:15], 12
	s_add_i32 s14, s13, -1
	s_and_b32 s12, s18, 0x7fc
	s_lshl_b64 s[26:27], s[14:15], 12
	s_max_i32 s14, s18, 0
	s_max_i32 s13, s18, -1
	s_lshl_b64 s[24:25], s[14:15], 12
	s_add_i32 s14, s13, 1
	s_min_u32 s13, s12, 15
	s_add_i32 s13, s13, 1
	s_lshl_b64 s[78:79], s[14:15], 12
	s_min_u32 s14, s12, 14
	v_cvt_f32_ubyte0_e32 v0, s13
	s_add_i32 s16, s14, 2
	v_div_scale_f32 v1, s[14:15], v0, v0, 1.0
	v_rcp_f32_e32 v2, v1
	s_min_u32 s13, s12, 7
	s_add_i32 s13, s13, 1
	s_waitcnt lgkmcnt(0)
	v_fma_f32 v3, -v1, v2, 1.0
	v_fmac_f32_e32 v2, v3, v2
	v_div_scale_f32 v3, vcc, 1.0, v0, 1.0
	v_mul_f32_e32 v4, v3, v2
	v_fma_f32 v5, -v1, v4, v3
	v_fmac_f32_e32 v4, v5, v2
	v_fma_f32 v1, -v1, v4, v3
	v_div_fmas_f32 v1, v1, v2, v4
	v_div_fixup_f32 v92, v1, v0, 1.0
	v_cvt_f32_ubyte0_e32 v0, s16
	v_div_scale_f32 v1, s[14:15], v0, v0, 1.0
	v_rcp_f32_e32 v2, v1
	s_min_u32 s14, s12, 6
	s_add_i32 s16, s14, 2
	s_waitcnt lgkmcnt(0)
	v_fma_f32 v3, -v1, v2, 1.0
	v_fmac_f32_e32 v2, v3, v2
	v_div_scale_f32 v3, vcc, 1.0, v0, 1.0
	v_mul_f32_e32 v4, v3, v2
	v_fma_f32 v5, -v1, v4, v3
	v_fmac_f32_e32 v4, v5, v2
	v_fma_f32 v1, -v1, v4, v3
	v_div_fmas_f32 v1, v1, v2, v4
	v_div_fixup_f32 v94, v1, v0, 1.0
	v_cvt_f32_ubyte0_e32 v0, s13
	v_div_scale_f32 v1, s[14:15], v0, v0, 1.0
	v_rcp_f32_e32 v2, v1
	s_min_u32 s13, s12, 3
	s_add_i32 s13, s13, 1
	s_barrier
	v_fma_f32 v3, -v1, v2, 1.0
	v_fmac_f32_e32 v2, v3, v2
	v_div_scale_f32 v3, vcc, 1.0, v0, 1.0
	v_mul_f32_e32 v4, v3, v2
	v_fma_f32 v5, -v1, v4, v3
	v_fmac_f32_e32 v4, v5, v2
	v_fma_f32 v1, -v1, v4, v3
	v_div_fmas_f32 v1, v1, v2, v4
	v_div_fixup_f32 v8, v1, v0, 1.0
	v_cvt_f32_ubyte0_e32 v0, s16
	v_div_scale_f32 v1, s[14:15], v0, v0, 1.0
	v_rcp_f32_e32 v2, v1
	s_min_u32 s14, s12, 2
	s_add_i32 s16, s14, 2
	v_fma_f32 v3, -v1, v2, 1.0
	v_fmac_f32_e32 v2, v3, v2
	v_div_scale_f32 v3, vcc, 1.0, v0, 1.0
	v_mul_f32_e32 v4, v3, v2
	v_fma_f32 v5, -v1, v4, v3
	v_fmac_f32_e32 v4, v5, v2
	v_fma_f32 v1, -v1, v4, v3
	v_div_fmas_f32 v1, v1, v2, v4
	v_div_fixup_f32 v10, v1, v0, 1.0
	v_cvt_f32_ubyte0_e32 v0, s13
	v_div_scale_f32 v1, s[14:15], v0, v0, 1.0
	v_rcp_f32_e32 v2, v1
	v_mov_b32_e32 v27, s7
	s_max_i32 s0, s18, 15
	s_add_i32 s0, s0, -15
	v_fma_f32 v3, -v1, v2, 1.0
	v_fmac_f32_e32 v2, v3, v2
	v_div_scale_f32 v3, vcc, 1.0, v0, 1.0
	v_mul_f32_e32 v4, v3, v2
	v_fma_f32 v5, -v1, v4, v3
	v_fmac_f32_e32 v4, v5, v2
	v_fma_f32 v1, -v1, v4, v3
	v_div_fmas_f32 v1, v1, v2, v4
	v_div_fixup_f32 v4, v1, v0, 1.0
	v_cvt_f32_ubyte0_e32 v0, s16
	v_div_scale_f32 v1, s[14:15], v0, v0, 1.0
	v_rcp_f32_e32 v2, v1
	s_mov_b32 s1, s60
	s_lshl_b64 s[76:77], s[0:1], 12
	s_max_i32 s0, s18, 14
	v_fma_f32 v3, -v1, v2, 1.0
	v_fmac_f32_e32 v2, v3, v2
	v_div_scale_f32 v3, vcc, 1.0, v0, 1.0
	v_mul_f32_e32 v5, v3, v2
	v_fma_f32 v6, -v1, v5, v3
	v_fmac_f32_e32 v5, v6, v2
	v_fma_f32 v1, -v1, v5, v3
	v_div_fmas_f32 v1, v1, v2, v5
	v_mov_b32_e32 v5, v21
	v_div_fixup_f32 v6, v1, v0, 1.0
	ds_read_b64 v[2:3], v27 offset:56
	ds_read_b32 v12, v27 offset:64
	v_lshlrev_b32_e32 v0, 2, v5
	v_ashrrev_i32_e32 v1, 31, v0
	v_lshlrev_b64 v[84:85], 1, v[0:1]
	v_lshl_add_u64 v[0:1], s[92:93], 0, v[84:85]
	v_lshl_add_u64 v[236:237], v[0:1], 0, s[78:79]
	global_load_dwordx2 v[236:237], v[236:237], off
	v_lshl_add_u64 v[238:239], v[0:1], 0, s[26:27]
	global_load_dwordx2 v[238:239], v[238:239], off
	v_lshl_add_u64 v[240:241], v[0:1], 0, s[24:25]
	global_load_dwordx2 v[240:241], v[240:241], off
	s_nop 0
	s_nop 0
	s_nop 0
	s_nop 0
	s_nop 0
	s_add_i32 s0, s0, -14
	s_nop 0
	s_lshl_b64 s[10:11], s[0:1], 12
	s_max_i32 s0, s18, 13
	s_add_i32 s0, s0, -13
	s_lshl_b64 s[8:9], s[0:1], 12
	s_max_i32 s0, s18, 12
	s_add_i32 s0, s0, -12
	s_lshl_b64 s[44:45], s[0:1], 12
	s_max_i32 s0, s18, 11
	s_add_i32 s0, s0, -11
	s_lshl_b64 s[48:49], s[0:1], 12
	s_max_i32 s0, s18, 10
	s_add_i32 s0, s0, -10
	s_lshl_b64 s[46:47], s[0:1], 12
	s_max_i32 s0, s18, 9
	s_add_i32 s0, s0, -9
	s_lshl_b64 s[30:31], s[0:1], 12
	s_max_i32 s0, s18, 8
	s_max_i32 s2, s18, 6
	s_add_i32 s0, s0, -8
	s_add_i32 s2, s2, -6
	s_mov_b32 s3, s60
	s_lshl_b64 s[28:29], s[0:1], 12
	s_max_i32 s0, s18, 7
	s_lshl_b64 s[42:43], s[2:3], 12
	s_max_i32 s2, s18, 5
	s_add_i32 s0, s0, -7
	s_add_i32 s2, s2, -5
	s_lshl_b64 s[0:1], s[0:1], 12
	s_lshl_b64 s[2:3], s[2:3], 12
	s_cmp_eq_u32 s12, 0
	s_cselect_b32 s54, 1.0, 0.5
	s_ashr_i32 s19, s18, 31
	s_lshl_b64 s[12:13], s[18:19], 12
	s_add_u32 s22, s4, s12
	s_addc_u32 s23, s5, s13
	s_or_b32 s16, s18, 1
	s_ashr_i32 s17, s16, 31
	s_lshl_b64 s[12:13], s[16:17], 12
	s_add_u32 s20, s4, s12
	s_addc_u32 s21, s5, s13
	s_add_i32 s17, 0, 0x12000
	s_add_u32 vcc_lo, s92, s78
	s_addc_u32 vcc_hi, s93, s79
	s_add_u32 s26, s92, s26
	s_addc_u32 s27, s93, s27
	s_add_u32 s24, s92, s24
	s_addc_u32 s25, s93, s25
	s_add_u32 s52, s92, s52
	s_addc_u32 s53, s93, s53
	s_add_u32 s50, s92, s50
	s_addc_u32 s51, s93, s51
	s_nop 0
	s_waitcnt vmcnt(2)
	v_lshlrev_b32_e32 v80, 16, v236
	v_and_b32_e32 v81, 0xffff0000, v236
	s_nop 0
	s_waitcnt vmcnt(1)
	v_lshlrev_b32_e32 v90, 16, v238
	v_and_b32_e32 v91, 0xffff0000, v238
	v_lshlrev_b32_e32 v88, 16, v239
	v_and_b32_e32 v89, 0xffff0000, v239
	s_waitcnt lgkmcnt(1)
	v_pk_fma_f32 v[96:97], v[2:3], v[90:91], 0 op_sel_hi:[0,1,0]
	v_pk_fma_f32 v[98:99], v[2:3], v[88:89], 0 op_sel_hi:[0,1,0]
	s_nop 0
	s_waitcnt vmcnt(0)
	v_lshlrev_b32_e32 v100, 16, v240
	v_and_b32_e32 v101, 0xffff0000, v240
	v_lshlrev_b32_e32 v0, 16, v241
	v_and_b32_e32 v1, 0xffff0000, v241
	v_pk_mul_f32 v[102:103], v[2:3], v[0:1] op_sel:[1,0]
	v_pk_fma_f32 v[0:1], v[2:3], v[0:1], v[98:99] op_sel:[1,0,0]
	v_pk_fma_f32 v[96:97], v[2:3], v[100:101], v[96:97] op_sel:[1,0,0]
	v_lshlrev_b32_e32 v14, 16, v237
	v_and_b32_e32 v15, 0xffff0000, v237
	v_pk_mul_f32 v[104:105], v[2:3], v[100:101] op_sel:[1,0]
	v_pk_fma_f32 v[90:91], v[2:3], v[90:91], v[96:97] op_sel_hi:[0,1,1] neg_lo:[1,0,0] neg_hi:[1,0,0]
	v_pk_fma_f32 v[2:3], v[2:3], v[88:89], v[0:1] op_sel_hi:[0,1,1] neg_lo:[1,0,0] neg_hi:[1,0,0]
	s_waitcnt lgkmcnt(0)
	v_pk_mul_f32 v[82:83], v[12:13], v[14:15] op_sel_hi:[0,1]
	v_pk_mul_f32 v[86:87], v[12:13], v[80:81] op_sel_hi:[0,1]
	v_pk_fma_f32 v[2:3], v[12:13], v[14:15], v[2:3] op_sel_hi:[0,1,1]
	v_pk_fma_f32 v[12:13], v[12:13], v[80:81], v[90:91] op_sel_hi:[0,1,1]
	v_lshl_add_u64 v[236:237], s[22:23], 0, v[84:85]
	global_load_dwordx2 v[236:237], v[236:237], off
	v_lshl_add_u64 v[238:239], s[20:21], 0, v[84:85]
	global_load_dwordx2 v[238:239], v[238:239], off
	v_lshl_add_u64 v[88:89], s[22:23], 0, v[84:85]
	v_pk_fma_f32 v[12:13], v[12:13], 0.5, v[86:87] op_sel_hi:[1,0,1] neg_lo:[0,0,1] neg_hi:[0,0,1]
	s_nop 0
	v_pk_fma_f32 v[80:81], s[54:55], v[0:1], v[102:103] op_sel_hi:[0,1,1] neg_lo:[0,0,1] neg_hi:[0,0,1]
	v_lshl_add_u32 v0, v5, 4, s17
	v_pk_fma_f32 v[14:15], v[2:3], 0.5, v[82:83] op_sel_hi:[1,0,1] neg_lo:[0,0,1] neg_hi:[0,0,1]
	ds_read_b128 v[0:3], v0
	v_pk_fma_f32 v[82:83], s[54:55], v[96:97], v[104:105] op_sel_hi:[0,1,1] neg_lo:[0,0,1] neg_hi:[0,0,1]
	s_nop 0
	s_waitcnt vmcnt(1)
	v_lshlrev_b32_e32 v90, 16, v236
	v_and_b32_e32 v91, 0xffff0000, v236
	s_waitcnt lgkmcnt(0)
	v_pk_fma_f32 v[82:83], v[0:1], v[82:83], v[90:91]
	v_lshl_add_u64 v[90:91], s[20:21], 0, v[84:85]
	s_nop 0
	v_lshlrev_b32_e32 v86, 16, v237
	v_and_b32_e32 v87, 0xffff0000, v237
	v_pk_fma_f32 v[80:81], v[2:3], v[80:81], v[86:87]
	s_nop 0
	s_waitcnt vmcnt(0)
	v_lshlrev_b32_e32 v86, 16, v238
	v_and_b32_e32 v87, 0xffff0000, v238
	v_lshlrev_b32_e32 v84, 16, v239
	v_and_b32_e32 v85, 0xffff0000, v239
	v_pk_fma_f32 v[86:87], v[0:1], v[12:13], v[86:87]
	v_cvt_pk_bf16_f32 v0, v82, v83
	v_cvt_pk_bf16_f32 v1, v80, v81
	v_pk_fma_f32 v[84:85], v[2:3], v[14:15], v[84:85]
	v_cvt_pk_bf16_f32 v2, v86, v87
	s_nop 0
	v_cvt_pk_bf16_f32 v3, v84, v85
	global_store_dwordx2 v[88:89], v[0:1], off
	global_store_dwordx2 v[90:91], v[2:3], off
	v_mov_b32_e32 v0, v21
	ds_read_b64 v[2:3], v27 offset:56
	ds_read_b32 v12, v27 offset:64
	v_lshlrev_b32_e32 v88, 2, v0
	v_add_u32_e32 v0, 0x100, v88
	v_ashrrev_i32_e32 v1, 31, v0
	v_lshlrev_b64 v[14:15], 1, v[0:1]
	v_lshl_add_u64 v[236:237], vcc, 0, v[14:15]
	global_load_dwordx2 v[236:237], v[236:237], off
	v_lshl_add_u64 v[238:239], s[26:27], 0, v[14:15]
	global_load_dwordx2 v[238:239], v[238:239], off
	v_lshl_add_u64 v[240:241], s[24:25], 0, v[14:15]
	global_load_dwordx2 v[240:241], v[240:241], off
	s_nop 0
	s_nop 0
	s_nop 0
	s_nop 0
	s_nop 0
	v_ashrrev_i32_e32 v89, 31, v88
	s_nop 0
	v_lshl_add_u32 v0, v0, 2, s17
	s_nop 0
	s_waitcnt vmcnt(2)
	v_lshlrev_b32_e32 v96, 16, v236
	v_and_b32_e32 v97, 0xffff0000, v236
	s_nop 0
	s_waitcnt vmcnt(1)
	v_lshlrev_b32_e32 v104, 16, v238
	v_and_b32_e32 v105, 0xffff0000, v238
	v_lshlrev_b32_e32 v102, 16, v239
	v_and_b32_e32 v103, 0xffff0000, v239
	s_waitcnt lgkmcnt(1)
	v_pk_fma_f32 v[106:107], v[2:3], v[104:105], 0 op_sel_hi:[0,1,0]
	v_pk_fma_f32 v[108:109], v[2:3], v[102:103], 0 op_sel_hi:[0,1,0]
	s_nop 0
	s_waitcnt vmcnt(0)
	v_lshlrev_b32_e32 v110, 16, v240
	v_and_b32_e32 v111, 0xffff0000, v240
	v_lshlrev_b32_e32 v14, 16, v241
	v_and_b32_e32 v15, 0xffff0000, v241
	v_pk_fma_f32 v[108:109], v[2:3], v[14:15], v[108:109] op_sel:[1,0,0]
	v_pk_fma_f32 v[106:107], v[2:3], v[110:111], v[106:107] op_sel:[1,0,0]
	v_lshlrev_b32_e32 v90, 16, v237
	v_and_b32_e32 v91, 0xffff0000, v237
	v_pk_mul_f32 v[112:113], v[2:3], v[14:15] op_sel:[1,0]
	v_pk_mul_f32 v[114:115], v[2:3], v[110:111] op_sel:[1,0]
	v_pk_fma_f32 v[14:15], v[2:3], v[104:105], v[106:107] op_sel_hi:[0,1,1] neg_lo:[1,0,0] neg_hi:[1,0,0]
	v_pk_fma_f32 v[2:3], v[2:3], v[102:103], v[108:109] op_sel_hi:[0,1,1] neg_lo:[1,0,0] neg_hi:[1,0,0]
	s_waitcnt lgkmcnt(0)
	v_pk_mul_f32 v[98:99], v[12:13], v[90:91] op_sel_hi:[0,1]
	v_pk_fma_f32 v[2:3], v[12:13], v[90:91], v[2:3] op_sel_hi:[0,1,1]
	v_pk_mul_f32 v[100:101], v[12:13], v[96:97] op_sel_hi:[0,1]
	v_pk_fma_f32 v[12:13], v[12:13], v[96:97], v[14:15] op_sel_hi:[0,1,1]
	v_pk_fma_f32 v[14:15], v[2:3], 0.5, v[98:99] op_sel_hi:[1,0,1] neg_lo:[0,0,1] neg_hi:[0,0,1]
	v_lshlrev_b64 v[98:99], 1, v[88:89]
	v_pk_fma_f32 v[12:13], v[12:13], 0.5, v[100:101] op_sel_hi:[1,0,1] neg_lo:[0,0,1] neg_hi:[0,0,1]
	v_lshl_add_u64 v[236:237], s[22:23], 0, v[98:99]
	global_load_dwordx2 v[236:237], v[236:237], off offset:512
	v_lshl_add_u64 v[238:239], s[20:21], 0, v[98:99]
	global_load_dwordx2 v[238:239], v[238:239], off offset:512
	v_lshl_add_u64 v[100:101], s[22:23], 0, v[98:99]
	s_nop 0
	ds_read_b128 v[0:3], v0
	v_pk_fma_f32 v[90:91], s[54:55], v[106:107], v[114:115] op_sel_hi:[0,1,1] neg_lo:[0,0,1] neg_hi:[0,0,1]
	v_pk_fma_f32 v[96:97], s[54:55], v[108:109], v[112:113] op_sel_hi:[0,1,1] neg_lo:[0,0,1] neg_hi:[0,0,1]
	s_nop 0
	s_waitcnt vmcnt(1)
	v_lshlrev_b32_e32 v102, 16, v236
	v_and_b32_e32 v103, 0xffff0000, v236
	v_lshlrev_b32_e32 v88, 16, v237
	v_and_b32_e32 v89, 0xffff0000, v237
	s_waitcnt lgkmcnt(0)
	v_pk_fma_f32 v[90:91], v[0:1], v[90:91], v[102:103]
	v_lshl_add_u64 v[102:103], s[20:21], 0, v[98:99]
	v_pk_fma_f32 v[88:89], v[2:3], v[96:97], v[88:89]
	s_nop 0
	s_nop 0
	s_waitcnt vmcnt(0)
	v_lshlrev_b32_e32 v98, 16, v238
	v_and_b32_e32 v99, 0xffff0000, v238
	v_lshlrev_b32_e32 v96, 16, v239
	v_and_b32_e32 v97, 0xffff0000, v239
	v_pk_fma_f32 v[98:99], v[0:1], v[12:13], v[98:99]
	v_cvt_pk_bf16_f32 v0, v90, v91
	v_cvt_pk_bf16_f32 v1, v88, v89
	v_pk_fma_f32 v[96:97], v[2:3], v[14:15], v[96:97]
	v_cvt_pk_bf16_f32 v2, v98, v99
	s_nop 0
	v_cvt_pk_bf16_f32 v3, v96, v97
	global_store_dwordx2 v[100:101], v[0:1], off offset:512
	global_store_dwordx2 v[102:103], v[2:3], off offset:512
	v_mov_b32_e32 v0, v21
	s_nop 0
	v_lshlrev_b32_e32 v100, 2, v0
	v_add_u32_e32 v102, 0x200, v100
	v_ashrrev_i32_e32 v103, 31, v102
	v_lshlrev_b64 v[14:15], 1, v[102:103]
	v_lshl_add_u64 v[236:237], vcc, 0, v[14:15]
	global_load_dwordx2 v[236:237], v[236:237], off
	v_lshl_add_u64 v[238:239], s[52:53], 0, v[14:15]
	global_load_dwordx2 v[238:239], v[238:239], off
	v_lshl_add_u64 v[240:241], s[50:51], 0, v[14:15]
	global_load_dwordx2 v[240:241], v[240:241], off
	v_lshl_add_u64 v[242:243], s[26:27], 0, v[14:15]
	global_load_dwordx2 v[242:243], v[242:243], off
	v_lshl_add_u64 v[244:245], s[24:25], 0, v[14:15]
	global_load_dwordx2 v[244:245], v[244:245], off
	s_nop 0
	s_nop 0
	ds_read_b128 v[0:3], v27 offset:48
	ds_read_b32 v12, v27 offset:64
	s_nop 0
	s_nop 0
	s_nop 0
	v_ashrrev_i32_e32 v101, 31, v100
	s_nop 0
	s_nop 0
	s_waitcnt vmcnt(3)
	v_lshlrev_b32_e32 v114, 16, v238
	v_and_b32_e32 v115, 0xffff0000, v238
	v_lshlrev_b32_e32 v112, 16, v239
	v_and_b32_e32 v113, 0xffff0000, v239
	s_waitcnt lgkmcnt(1)
	v_pk_fma_f32 v[118:119], v[0:1], v[112:113], 0 op_sel_hi:[0,1,0]
	s_nop 0
	s_waitcnt vmcnt(2)
	v_lshlrev_b32_e32 v122, 16, v240
	v_and_b32_e32 v123, 0xffff0000, v240
	v_lshlrev_b32_e32 v120, 16, v241
	v_and_b32_e32 v121, 0xffff0000, v241
	v_pk_fma_f32 v[118:119], v[0:1], v[120:121], v[118:119] op_sel:[1,0,0]
	s_nop 0
	s_nop 0
	s_nop 0
	s_nop 0
	v_pk_fma_f32 v[116:117], v[0:1], v[114:115], 0 op_sel_hi:[0,1,0]
	v_pk_fma_f32 v[116:117], v[0:1], v[122:123], v[116:117] op_sel:[1,0,0]
	v_lshlrev_b32_e32 v106, 16, v236
	v_and_b32_e32 v107, 0xffff0000, v236
	v_lshlrev_b32_e32 v104, 16, v237
	v_and_b32_e32 v105, 0xffff0000, v237
	s_waitcnt lgkmcnt(0)
	v_pk_mul_f32 v[108:109], v[12:13], v[104:105] op_sel_hi:[0,1]
	v_pk_mul_f32 v[110:111], v[12:13], v[106:107] op_sel_hi:[0,1]
	s_nop 0
	s_waitcnt vmcnt(1)
	v_lshlrev_b32_e32 v122, 16, v242
	v_and_b32_e32 v123, 0xffff0000, v242
	v_lshlrev_b32_e32 v120, 16, v243
	v_and_b32_e32 v121, 0xffff0000, v243
	v_pk_fma_f32 v[116:117], v[2:3], v[122:123], v[116:117] op_sel_hi:[0,1,1]
	v_pk_fma_f32 v[118:119], v[2:3], v[120:121], v[118:119] op_sel_hi:[0,1,1]
	s_nop 0
	s_waitcnt vmcnt(0)
	v_lshlrev_b32_e32 v120, 16, v244
	v_and_b32_e32 v121, 0xffff0000, v244
	v_lshlrev_b32_e32 v14, 16, v245
	v_and_b32_e32 v15, 0xffff0000, v245
	v_mov_b32_e32 v2, v3
	v_pk_mul_f32 v[122:123], v[2:3], v[14:15] op_sel_hi:[0,1]
	v_pk_mul_f32 v[124:125], v[2:3], v[120:121] op_sel_hi:[0,1]
	v_pk_fma_f32 v[118:119], v[2:3], v[14:15], v[118:119] op_sel_hi:[0,1,1]
	v_pk_fma_f32 v[2:3], v[2:3], v[120:121], v[116:117] op_sel_hi:[0,1,1]
	v_pk_fma_f32 v[14:15], v[0:1], v[114:115], v[2:3] op_sel_hi:[0,1,1] neg_lo:[1,0,0] neg_hi:[1,0,0]
	v_pk_fma_f32 v[0:1], v[0:1], v[112:113], v[118:119] op_sel_hi:[0,1,1] neg_lo:[1,0,0] neg_hi:[1,0,0]
	v_pk_fma_f32 v[0:1], v[12:13], v[104:105], v[0:1] op_sel_hi:[0,1,1]
	v_pk_fma_f32 v[12:13], v[12:13], v[106:107], v[14:15] op_sel_hi:[0,1,1]
	v_pk_fma_f32 v[12:13], v[6:7], v[12:13], v[110:111] op_sel_hi:[0,1,1] neg_lo:[0,0,1] neg_hi:[0,0,1]
	v_lshlrev_b64 v[110:111], 1, v[100:101]
	v_pk_fma_f32 v[14:15], v[6:7], v[0:1], v[108:109] op_sel_hi:[0,1,1] neg_lo:[0,0,1] neg_hi:[0,0,1]
	v_lshl_add_u64 v[108:109], s[22:23], 0, v[110:111]
	global_load_dwordx2 v[100:101], v[108:109], off offset:1024
	v_lshl_add_u32 v0, v102, 2, s17
	v_pk_fma_f32 v[104:105], v[4:5], v[2:3], v[124:125] op_sel_hi:[0,1,1] neg_lo:[0,0,1] neg_hi:[0,0,1]
	ds_read_b128 v[0:3], v0
	v_lshl_add_u64 v[110:111], s[20:21], 0, v[110:111]
	v_pk_fma_f32 v[106:107], v[4:5], v[118:119], v[122:123] op_sel_hi:[0,1,1] neg_lo:[0,0,1] neg_hi:[0,0,1]
	s_nop 0
	s_waitcnt vmcnt(0)
	v_lshlrev_b32_e32 v102, 16, v100
	v_and_b32_e32 v103, 0xffff0000, v100
	s_waitcnt lgkmcnt(0)
	v_pk_fma_f32 v[102:103], v[0:1], v[104:105], v[102:103]
	global_load_dwordx2 v[104:105], v[110:111], off offset:1024
	v_lshlrev_b32_e32 v100, 16, v101
	v_and_b32_e32 v101, 0xffff0000, v101
	v_pk_fma_f32 v[100:101], v[2:3], v[106:107], v[100:101]
	s_nop 0
	s_waitcnt vmcnt(0)
	v_lshlrev_b32_e32 v106, 16, v104
	v_and_b32_e32 v107, 0xffff0000, v104
	v_lshlrev_b32_e32 v104, 16, v105
	v_and_b32_e32 v105, 0xffff0000, v105
	v_pk_fma_f32 v[106:107], v[0:1], v[12:13], v[106:107]
	v_cvt_pk_bf16_f32 v0, v102, v103
	v_cvt_pk_bf16_f32 v1, v100, v101
	v_pk_fma_f32 v[104:105], v[2:3], v[14:15], v[104:105]
	v_cvt_pk_bf16_f32 v2, v106, v107
	s_nop 0
	v_cvt_pk_bf16_f32 v3, v104, v105
	global_store_dwordx2 v[108:109], v[0:1], off offset:1024
	global_store_dwordx2 v[110:111], v[2:3], off offset:1024
	v_mov_b32_e32 v0, v21
	s_nop 0
	v_lshlrev_b32_e32 v14, 2, v0
	v_add_u32_e32 v108, 0x300, v14
	v_ashrrev_i32_e32 v109, 31, v108
	v_lshlrev_b64 v[110:111], 1, v[108:109]
	v_lshl_add_u64 v[236:237], vcc, 0, v[110:111]
	global_load_dwordx2 v[236:237], v[236:237], off
	v_lshl_add_u64 v[238:239], s[52:53], 0, v[110:111]
	global_load_dwordx2 v[238:239], v[238:239], off
	v_lshl_add_u64 v[240:241], s[50:51], 0, v[110:111]
	global_load_dwordx2 v[240:241], v[240:241], off
	v_lshl_add_u64 v[242:243], s[26:27], 0, v[110:111]
	global_load_dwordx2 v[242:243], v[242:243], off
	v_lshl_add_u64 v[244:245], s[24:25], 0, v[110:111]
	global_load_dwordx2 v[244:245], v[244:245], off
	s_nop 0
	s_nop 0
	ds_read_b128 v[0:3], v27 offset:48
	ds_read_b32 v12, v27 offset:64
	s_nop 0
	s_nop 0
	s_nop 0
	v_ashrrev_i32_e32 v15, 31, v14
	s_nop 0
	v_lshlrev_b64 v[14:15], 1, v[14:15]
	s_nop 0
	s_waitcnt vmcnt(3)
	v_lshlrev_b32_e32 v122, 16, v238
	v_and_b32_e32 v123, 0xffff0000, v238
	v_lshlrev_b32_e32 v120, 16, v239
	v_and_b32_e32 v121, 0xffff0000, v239
	s_waitcnt lgkmcnt(1)
	v_pk_fma_f32 v[126:127], v[0:1], v[120:121], 0 op_sel_hi:[0,1,0]
	s_nop 0
	s_waitcnt vmcnt(2)
	v_lshlrev_b32_e32 v130, 16, v240
	v_and_b32_e32 v131, 0xffff0000, v240
	v_lshlrev_b32_e32 v128, 16, v241
	v_and_b32_e32 v129, 0xffff0000, v241
	v_pk_fma_f32 v[126:127], v[0:1], v[128:129], v[126:127] op_sel:[1,0,0]
	s_nop 0
	s_nop 0
	s_nop 0
	s_nop 0
	v_pk_fma_f32 v[124:125], v[0:1], v[122:123], 0 op_sel_hi:[0,1,0]
	v_pk_fma_f32 v[124:125], v[0:1], v[130:131], v[124:125] op_sel:[1,0,0]
	v_lshlrev_b32_e32 v114, 16, v236
	v_and_b32_e32 v115, 0xffff0000, v236
	v_lshlrev_b32_e32 v112, 16, v237
	v_and_b32_e32 v113, 0xffff0000, v237
	s_waitcnt lgkmcnt(0)
	v_pk_mul_f32 v[116:117], v[12:13], v[112:113] op_sel_hi:[0,1]
	v_pk_mul_f32 v[118:119], v[12:13], v[114:115] op_sel_hi:[0,1]
	s_nop 0
	s_waitcnt vmcnt(1)
	v_lshlrev_b32_e32 v130, 16, v242
	v_and_b32_e32 v131, 0xffff0000, v242
	v_lshlrev_b32_e32 v128, 16, v243
	v_and_b32_e32 v129, 0xffff0000, v243
	v_pk_fma_f32 v[124:125], v[2:3], v[130:131], v[124:125] op_sel_hi:[0,1,1]
	v_pk_fma_f32 v[126:127], v[2:3], v[128:129], v[126:127] op_sel_hi:[0,1,1]
	s_nop 0
	s_waitcnt vmcnt(0)
	v_lshlrev_b32_e32 v128, 16, v244
	v_and_b32_e32 v129, 0xffff0000, v244
	v_lshlrev_b32_e32 v110, 16, v245
	v_and_b32_e32 v111, 0xffff0000, v245
	v_mov_b32_e32 v2, v3
	v_pk_mul_f32 v[130:131], v[2:3], v[110:111] op_sel_hi:[0,1]
	v_pk_mul_f32 v[132:133], v[2:3], v[128:129] op_sel_hi:[0,1]
	v_pk_fma_f32 v[110:111], v[2:3], v[110:111], v[126:127] op_sel_hi:[0,1,1]
	v_pk_fma_f32 v[2:3], v[2:3], v[128:129], v[124:125] op_sel_hi:[0,1,1]
	v_pk_fma_f32 v[122:123], v[0:1], v[122:123], v[2:3] op_sel_hi:[0,1,1] neg_lo:[1,0,0] neg_hi:[1,0,0]
	v_pk_fma_f32 v[0:1], v[0:1], v[120:121], v[110:111] op_sel_hi:[0,1,1] neg_lo:[1,0,0] neg_hi:[1,0,0]
	v_pk_fma_f32 v[0:1], v[12:13], v[112:113], v[0:1] op_sel_hi:[0,1,1]
	v_pk_fma_f32 v[12:13], v[12:13], v[114:115], v[122:123] op_sel_hi:[0,1,1]
	v_pk_fma_f32 v[112:113], v[4:5], v[2:3], v[132:133] op_sel_hi:[0,1,1] neg_lo:[0,0,1] neg_hi:[0,0,1]
	v_pk_fma_f32 v[110:111], v[4:5], v[110:111], v[130:131] op_sel_hi:[0,1,1] neg_lo:[0,0,1] neg_hi:[0,0,1]
	v_lshl_add_u64 v[4:5], s[22:23], 0, v[14:15]
	v_pk_fma_f32 v[12:13], v[6:7], v[12:13], v[118:119] op_sel_hi:[0,1,1] neg_lo:[0,0,1] neg_hi:[0,0,1]
	v_pk_fma_f32 v[6:7], v[6:7], v[0:1], v[116:117] op_sel_hi:[0,1,1] neg_lo:[0,0,1] neg_hi:[0,0,1]
	v_lshl_add_u32 v0, v108, 2, s17
	global_load_dwordx2 v[108:109], v[4:5], off offset:1536
	ds_read_b128 v[0:3], v0
	v_lshl_add_u64 v[14:15], s[20:21], 0, v[14:15]
	s_nop 0
	s_waitcnt vmcnt(0)
	v_lshlrev_b32_e32 v114, 16, v108
	v_and_b32_e32 v115, 0xffff0000, v108
	v_lshlrev_b32_e32 v108, 16, v109
	v_and_b32_e32 v109, 0xffff0000, v109
	s_waitcnt lgkmcnt(0)
	v_pk_fma_f32 v[108:109], v[2:3], v[110:111], v[108:109]
	v_pk_fma_f32 v[110:111], v[0:1], v[112:113], v[114:115]
	global_load_dwordx2 v[112:113], v[14:15], off offset:1536
	s_nop 0
	s_waitcnt vmcnt(0)
	v_lshlrev_b32_e32 v114, 16, v112
	v_and_b32_e32 v115, 0xffff0000, v112
	v_lshlrev_b32_e32 v112, 16, v113
	v_and_b32_e32 v113, 0xffff0000, v113
	v_pk_fma_f32 v[114:115], v[0:1], v[12:13], v[114:115]
	v_cvt_pk_bf16_f32 v0, v110, v111
	v_cvt_pk_bf16_f32 v1, v108, v109
	v_pk_fma_f32 v[112:113], v[2:3], v[6:7], v[112:113]
	v_cvt_pk_bf16_f32 v2, v114, v115
	s_nop 0
	v_cvt_pk_bf16_f32 v3, v112, v113
	global_store_dwordx2 v[4:5], v[0:1], off offset:1536
	global_store_dwordx2 v[14:15], v[2:3], off offset:1536
	v_mov_b32_e32 v0, v21
	s_add_u32 s0, s92, s0
	v_lshlrev_b32_e32 v12, 2, v0
	v_add_u32_e32 v14, 0x400, v12
	v_ashrrev_i32_e32 v15, 31, v14
	s_addc_u32 s1, s93, s1
	v_lshlrev_b64 v[126:127], 1, v[14:15]
	s_add_u32 s42, s92, s42
	v_lshl_add_u64 v[128:129], s[0:1], 0, v[126:127]
	s_addc_u32 s43, s93, s43
	ds_read_b128 v[0:3], v27 offset:32
	ds_read_b128 v[4:7], v27 offset:48
	ds_read_b32 v116, v27 offset:64
	global_load_dwordx2 v[130:131], v[128:129], off
	v_lshl_add_u64 v[238:239], s[42:43], 0, v[126:127]
	global_load_dwordx2 v[238:239], v[238:239], off
	v_lshl_add_u64 v[240:241], vcc, 0, v[126:127]
	global_load_dwordx2 v[240:241], v[240:241], off
	s_nop 0
	s_nop 0
	s_add_u32 s2, s92, s2
	s_addc_u32 s3, s93, s3
	s_add_u32 s36, s92, s36
	s_addc_u32 s37, s93, s37
	v_lshl_add_u64 v[118:119], vcc, 0, v[126:127]
	s_nop 0
	v_ashrrev_i32_e32 v13, 31, v12
	s_add_u32 s76, s92, s76
	s_addc_u32 s77, s93, s77
	s_add_u32 s10, s92, s10
	s_addc_u32 s11, s93, s11
	s_add_u32 s8, s92, s8
	s_addc_u32 s9, s93, s9
	s_add_u32 s44, s92, s44
	s_addc_u32 s45, s93, s45
	s_add_u32 s48, s92, s48
	s_addc_u32 s49, s93, s49
	s_add_u32 s46, s92, s46
	s_addc_u32 s47, s93, s47
	s_add_u32 s30, s92, s30
	s_addc_u32 s31, s93, s31
	s_add_u32 s28, s92, s28
	s_addc_u32 s29, s93, s29
	s_nop 0
	s_waitcnt vmcnt(2)
	v_lshlrev_b32_e32 v128, 16, v130
	v_and_b32_e32 v129, 0xffff0000, v130
	v_lshlrev_b32_e32 v130, 16, v131
	v_and_b32_e32 v131, 0xffff0000, v131
	s_waitcnt lgkmcnt(2)
	v_pk_fma_f32 v[134:135], v[0:1], v[130:131], 0 op_sel_hi:[0,1,0]
	s_nop 0
	s_waitcnt vmcnt(1)
	v_lshlrev_b32_e32 v138, 16, v238
	v_and_b32_e32 v139, 0xffff0000, v238
	v_lshlrev_b32_e32 v136, 16, v239
	v_and_b32_e32 v137, 0xffff0000, v239
	v_pk_fma_f32 v[134:135], v[0:1], v[136:137], v[134:135] op_sel:[1,0,0]
	v_lshl_add_u64 v[236:237], s[2:3], 0, v[126:127]
	global_load_dwordx2 v[236:237], v[236:237], off
	v_lshl_add_u64 v[238:239], s[36:37], 0, v[126:127]
	global_load_dwordx2 v[238:239], v[238:239], off
	v_lshl_add_u64 v[242:243], s[52:53], 0, v[126:127]
	global_load_dwordx2 v[242:243], v[242:243], off
	v_lshl_add_u64 v[244:245], s[50:51], 0, v[126:127]
	global_load_dwordx2 v[244:245], v[244:245], off
	v_lshl_add_u64 v[246:247], s[24:25], 0, v[126:127]
	global_load_dwordx2 v[246:247], v[246:247], off
	s_nop 0
	s_nop 0
	v_pk_fma_f32 v[132:133], v[0:1], v[128:129], 0 op_sel_hi:[0,1,0]
	v_pk_fma_f32 v[132:133], v[0:1], v[138:139], v[132:133] op_sel:[1,0,0]
	s_nop 0
	s_waitcnt vmcnt(4)
	v_lshlrev_b32_e32 v138, 16, v236
	v_and_b32_e32 v139, 0xffff0000, v236
	v_lshlrev_b32_e32 v136, 16, v237
	v_and_b32_e32 v137, 0xffff0000, v237
	v_pk_fma_f32 v[134:135], v[2:3], v[136:137], v[134:135] op_sel_hi:[0,1,1]
	s_nop 0
	s_nop 0
	v_pk_fma_f32 v[132:133], v[2:3], v[138:139], v[132:133] op_sel_hi:[0,1,1]
	v_mov_b32_e32 v2, v3
	s_nop 0
	s_waitcnt vmcnt(3)
	v_lshlrev_b32_e32 v138, 16, v238
	v_and_b32_e32 v139, 0xffff0000, v238
	v_lshlrev_b32_e32 v136, 16, v239
	v_and_b32_e32 v137, 0xffff0000, v239
	v_pk_fma_f32 v[134:135], v[2:3], v[136:137], v[134:135] op_sel_hi:[0,1,1]
	v_pk_fma_f32 v[2:3], v[2:3], v[138:139], v[132:133] op_sel_hi:[0,1,1]
	s_nop 0
	s_nop 0
	s_nop 0
	s_waitcnt vmcnt(2)
	v_lshlrev_b32_e32 v136, 16, v242
	v_and_b32_e32 v137, 0xffff0000, v242
	v_lshlrev_b32_e32 v132, 16, v243
	v_and_b32_e32 v133, 0xffff0000, v243
	s_waitcnt lgkmcnt(1)
	v_pk_fma_f32 v[132:133], v[4:5], v[132:133], v[134:135] op_sel_hi:[0,1,1]
	s_nop 0
	s_nop 0
	v_pk_fma_f32 v[2:3], v[4:5], v[136:137], v[2:3] op_sel_hi:[0,1,1]
	s_nop 0
	s_waitcnt vmcnt(1)
	v_lshlrev_b32_e32 v136, 16, v244
	v_and_b32_e32 v137, 0xffff0000, v244
	v_lshlrev_b32_e32 v134, 16, v245
	v_and_b32_e32 v135, 0xffff0000, v245
	v_pk_fma_f32 v[132:133], v[4:5], v[134:135], v[132:133] op_sel:[1,0,0]
	v_pk_fma_f32 v[2:3], v[4:5], v[136:137], v[2:3] op_sel:[1,0,0]
	v_lshl_add_u64 v[4:5], s[26:27], 0, v[126:127]
	s_nop 0
	s_nop 0
	s_nop 0
	global_load_dwordx2 v[4:5], v[4:5], off
	v_lshlrev_b32_e32 v122, 16, v241
	v_and_b32_e32 v123, 0xffff0000, v241
	v_lshlrev_b32_e32 v118, 16, v240
	v_and_b32_e32 v119, 0xffff0000, v240
	s_waitcnt lgkmcnt(0)
	v_pk_mul_f32 v[120:121], v[116:117], v[122:123] op_sel_hi:[0,1]
	v_pk_mul_f32 v[124:125], v[116:117], v[118:119] op_sel_hi:[0,1]
	s_nop 0
	s_waitcnt vmcnt(0)
	v_lshlrev_b32_e32 v134, 16, v4
	v_and_b32_e32 v135, 0xffff0000, v4
	v_lshlrev_b32_e32 v4, 16, v5
	v_and_b32_e32 v5, 0xffff0000, v5
	v_pk_fma_f32 v[2:3], v[6:7], v[134:135], v[2:3] op_sel_hi:[0,1,1]
	v_pk_fma_f32 v[4:5], v[6:7], v[4:5], v[132:133] op_sel_hi:[0,1,1]
	v_lshlrev_b32_e32 v132, 16, v246
	v_and_b32_e32 v133, 0xffff0000, v246
	v_lshlrev_b32_e32 v126, 16, v247
	v_and_b32_e32 v127, 0xffff0000, v247
	v_mov_b32_e32 v6, v7
	v_pk_mul_f32 v[134:135], v[6:7], v[126:127] op_sel_hi:[0,1]
	v_pk_fma_f32 v[126:127], v[6:7], v[126:127], v[4:5] op_sel_hi:[0,1,1]
	v_pk_fma_f32 v[2:3], v[6:7], v[132:133], v[2:3] op_sel_hi:[0,1,1]
	v_pk_fma_f32 v[4:5], v[0:1], v[128:129], v[2:3] op_sel_hi:[0,1,1] neg_lo:[1,0,0] neg_hi:[1,0,0]
	v_pk_fma_f32 v[0:1], v[0:1], v[130:131], v[126:127] op_sel_hi:[0,1,1] neg_lo:[1,0,0] neg_hi:[1,0,0]
	v_pk_fma_f32 v[0:1], v[116:117], v[122:123], v[0:1] op_sel_hi:[0,1,1]
	v_pk_mul_f32 v[136:137], v[6:7], v[132:133] op_sel_hi:[0,1]
	v_pk_fma_f32 v[6:7], v[10:11], v[0:1], v[120:121] op_sel_hi:[0,1,1] neg_lo:[0,0,1] neg_hi:[0,0,1]
	v_lshl_add_u32 v0, v14, 2, s17
	v_lshlrev_b64 v[14:15], 1, v[12:13]
	v_lshl_add_u64 v[12:13], s[22:23], 0, v[14:15]
	global_load_dwordx2 v[120:121], v[12:13], off offset:2048
	v_pk_fma_f32 v[4:5], v[116:117], v[118:119], v[4:5] op_sel_hi:[0,1,1]
	v_pk_fma_f32 v[118:119], v[8:9], v[2:3], v[136:137] op_sel_hi:[0,1,1] neg_lo:[0,0,1] neg_hi:[0,0,1]
	ds_read_b128 v[0:3], v0
	v_pk_fma_f32 v[116:117], v[8:9], v[126:127], v[134:135] op_sel_hi:[0,1,1] neg_lo:[0,0,1] neg_hi:[0,0,1]
	v_lshl_add_u64 v[14:15], s[20:21], 0, v[14:15]
	v_pk_fma_f32 v[4:5], v[10:11], v[4:5], v[124:125] op_sel_hi:[0,1,1] neg_lo:[0,0,1] neg_hi:[0,0,1]
	s_nop 0
	s_waitcnt vmcnt(0)
	v_lshlrev_b32_e32 v122, 16, v120
	v_and_b32_e32 v123, 0xffff0000, v120
	v_lshlrev_b32_e32 v120, 16, v121
	v_and_b32_e32 v121, 0xffff0000, v121
	s_waitcnt lgkmcnt(0)
	v_pk_fma_f32 v[116:117], v[2:3], v[116:117], v[120:121]
	global_load_dwordx2 v[120:121], v[14:15], off offset:2048
	v_pk_fma_f32 v[118:119], v[0:1], v[118:119], v[122:123]
	s_nop 0
	s_waitcnt vmcnt(0)
	v_lshlrev_b32_e32 v122, 16, v120
	v_and_b32_e32 v123, 0xffff0000, v120
	v_lshlrev_b32_e32 v120, 16, v121
	v_and_b32_e32 v121, 0xffff0000, v121
	v_pk_fma_f32 v[122:123], v[0:1], v[4:5], v[122:123]
	v_cvt_pk_bf16_f32 v0, v118, v119
	v_cvt_pk_bf16_f32 v1, v116, v117
	v_pk_fma_f32 v[120:121], v[2:3], v[6:7], v[120:121]
	v_cvt_pk_bf16_f32 v2, v122, v123
	s_nop 0
	v_cvt_pk_bf16_f32 v3, v120, v121
	global_store_dwordx2 v[12:13], v[0:1], off offset:2048
	global_store_dwordx2 v[14:15], v[2:3], off offset:2048
	v_mov_b32_e32 v0, v21
	s_nop 0
	v_lshlrev_b32_e32 v12, 2, v0
	v_add_u32_e32 v14, 0x500, v12
	v_ashrrev_i32_e32 v15, 31, v14
	v_lshlrev_b64 v[134:135], 1, v[14:15]
	v_lshl_add_u64 v[236:237], s[0:1], 0, v[134:135]
	global_load_dwordx2 v[236:237], v[236:237], off
	v_lshl_add_u64 v[238:239], s[42:43], 0, v[134:135]
	global_load_dwordx2 v[238:239], v[238:239], off
	v_lshl_add_u64 v[240:241], vcc, 0, v[134:135]
	global_load_dwordx2 v[240:241], v[240:241], off
	v_lshl_add_u64 v[242:243], s[2:3], 0, v[134:135]
	global_load_dwordx2 v[242:243], v[242:243], off
	v_lshl_add_u64 v[244:245], s[36:37], 0, v[134:135]
	global_load_dwordx2 v[244:245], v[244:245], off
	v_lshl_add_u64 v[246:247], s[52:53], 0, v[134:135]
	global_load_dwordx2 v[246:247], v[246:247], off
	v_lshl_add_u64 v[136:137], s[0:1], 0, v[134:135]
	ds_read_b128 v[0:3], v27 offset:32
	ds_read_b128 v[4:7], v27 offset:48
	ds_read_b32 v124, v27 offset:64
	s_nop 0
	s_nop 0
	s_nop 0
	v_lshl_add_u64 v[126:127], vcc, 0, v[134:135]
	s_nop 0
	v_ashrrev_i32_e32 v13, 31, v12
	v_lshlrev_b64 v[12:13], 1, v[12:13]
	s_nop 0
	s_waitcnt vmcnt(5)
	v_lshlrev_b32_e32 v136, 16, v236
	v_and_b32_e32 v137, 0xffff0000, v236
	v_lshlrev_b32_e32 v138, 16, v237
	v_and_b32_e32 v139, 0xffff0000, v237
	s_waitcnt lgkmcnt(2)
	v_pk_fma_f32 v[142:143], v[0:1], v[138:139], 0 op_sel_hi:[0,1,0]
	s_nop 0
	s_waitcnt vmcnt(4)
	v_lshlrev_b32_e32 v146, 16, v238
	v_and_b32_e32 v147, 0xffff0000, v238
	v_lshlrev_b32_e32 v144, 16, v239
	v_and_b32_e32 v145, 0xffff0000, v239
	v_pk_fma_f32 v[142:143], v[0:1], v[144:145], v[142:143] op_sel:[1,0,0]
	s_nop 0
	s_nop 0
	v_pk_fma_f32 v[140:141], v[0:1], v[136:137], 0 op_sel_hi:[0,1,0]
	v_pk_fma_f32 v[140:141], v[0:1], v[146:147], v[140:141] op_sel:[1,0,0]
	s_nop 0
	s_waitcnt vmcnt(2)
	v_lshlrev_b32_e32 v146, 16, v242
	v_and_b32_e32 v147, 0xffff0000, v242
	v_lshlrev_b32_e32 v144, 16, v243
	v_and_b32_e32 v145, 0xffff0000, v243
	v_pk_fma_f32 v[142:143], v[2:3], v[144:145], v[142:143] op_sel_hi:[0,1,1]
	s_nop 0
	s_nop 0
	v_pk_fma_f32 v[140:141], v[2:3], v[146:147], v[140:141] op_sel_hi:[0,1,1]
	v_mov_b32_e32 v2, v3
	s_nop 0
	s_waitcnt vmcnt(1)
	v_lshlrev_b32_e32 v146, 16, v244
	v_and_b32_e32 v147, 0xffff0000, v244
	v_lshlrev_b32_e32 v144, 16, v245
	v_and_b32_e32 v145, 0xffff0000, v245
	v_pk_fma_f32 v[142:143], v[2:3], v[144:145], v[142:143] op_sel_hi:[0,1,1]
	v_pk_fma_f32 v[2:3], v[2:3], v[146:147], v[140:141] op_sel_hi:[0,1,1]
	s_nop 0
	s_nop 0
	s_nop 0
	s_waitcnt vmcnt(0)
	v_lshlrev_b32_e32 v144, 16, v246
	v_and_b32_e32 v145, 0xffff0000, v246
	v_lshlrev_b32_e32 v140, 16, v247
	v_and_b32_e32 v141, 0xffff0000, v247
	s_waitcnt lgkmcnt(1)
	v_pk_fma_f32 v[140:141], v[4:5], v[140:141], v[142:143] op_sel_hi:[0,1,1]
	v_lshl_add_u64 v[236:237], s[50:51], 0, v[134:135]
	global_load_dwordx2 v[236:237], v[236:237], off
	v_lshl_add_u64 v[238:239], s[24:25], 0, v[134:135]
	global_load_dwordx2 v[238:239], v[238:239], off
	v_lshl_add_u64 v[242:243], s[26:27], 0, v[134:135]
	global_load_dwordx2 v[242:243], v[242:243], off
	v_lshl_add_u64 v[244:245], s[22:23], 0, v[12:13]
	global_load_dwordx2 v[244:245], v[244:245], off offset:2560
	v_lshl_add_u64 v[246:247], s[20:21], 0, v[12:13]
	global_load_dwordx2 v[246:247], v[246:247], off offset:2560
	s_nop 0
	s_nop 0
	v_pk_fma_f32 v[2:3], v[4:5], v[144:145], v[2:3] op_sel_hi:[0,1,1]
	s_nop 0
	s_waitcnt vmcnt(4)
	v_lshlrev_b32_e32 v144, 16, v236
	v_and_b32_e32 v145, 0xffff0000, v236
	v_lshlrev_b32_e32 v142, 16, v237
	v_and_b32_e32 v143, 0xffff0000, v237
	v_pk_fma_f32 v[140:141], v[4:5], v[142:143], v[140:141] op_sel:[1,0,0]
	v_pk_fma_f32 v[2:3], v[4:5], v[144:145], v[2:3] op_sel:[1,0,0]
	s_nop 0
	s_nop 0
	s_nop 0
	s_nop 0
	s_nop 0
	v_lshlrev_b32_e32 v126, 16, v240
	v_and_b32_e32 v127, 0xffff0000, v240
	v_lshlrev_b32_e32 v130, 16, v241
	v_and_b32_e32 v131, 0xffff0000, v241
	s_waitcnt lgkmcnt(0)
	v_pk_mul_f32 v[128:129], v[124:125], v[130:131] op_sel_hi:[0,1]
	v_pk_mul_f32 v[132:133], v[124:125], v[126:127] op_sel_hi:[0,1]
	s_nop 0
	s_waitcnt vmcnt(2)
	v_lshlrev_b32_e32 v142, 16, v242
	v_and_b32_e32 v143, 0xffff0000, v242
	v_lshlrev_b32_e32 v4, 16, v243
	v_and_b32_e32 v5, 0xffff0000, v243
	v_pk_fma_f32 v[2:3], v[6:7], v[142:143], v[2:3] op_sel_hi:[0,1,1]
	v_pk_fma_f32 v[4:5], v[6:7], v[4:5], v[140:141] op_sel_hi:[0,1,1]
	v_lshlrev_b32_e32 v140, 16, v238
	v_and_b32_e32 v141, 0xffff0000, v238
	v_lshlrev_b32_e32 v134, 16, v239
	v_and_b32_e32 v135, 0xffff0000, v239
	v_mov_b32_e32 v6, v7
	v_pk_mul_f32 v[142:143], v[6:7], v[134:135] op_sel_hi:[0,1]
	v_pk_fma_f32 v[134:135], v[6:7], v[134:135], v[4:5] op_sel_hi:[0,1,1]
	v_pk_fma_f32 v[2:3], v[6:7], v[140:141], v[2:3] op_sel_hi:[0,1,1]
	v_pk_fma_f32 v[4:5], v[0:1], v[136:137], v[2:3] op_sel_hi:[0,1,1] neg_lo:[1,0,0] neg_hi:[1,0,0]
	v_pk_fma_f32 v[0:1], v[0:1], v[138:139], v[134:135] op_sel_hi:[0,1,1] neg_lo:[1,0,0] neg_hi:[1,0,0]
	v_pk_mul_f32 v[144:145], v[6:7], v[140:141] op_sel_hi:[0,1]
	v_pk_fma_f32 v[0:1], v[124:125], v[130:131], v[0:1] op_sel_hi:[0,1,1]
	v_pk_fma_f32 v[4:5], v[124:125], v[126:127], v[4:5] op_sel_hi:[0,1,1]
	v_pk_fma_f32 v[4:5], v[10:11], v[4:5], v[132:133] op_sel_hi:[0,1,1] neg_lo:[0,0,1] neg_hi:[0,0,1]
	v_pk_fma_f32 v[6:7], v[10:11], v[0:1], v[128:129] op_sel_hi:[0,1,1] neg_lo:[0,0,1] neg_hi:[0,0,1]
	v_pk_fma_f32 v[10:11], v[8:9], v[2:3], v[144:145] op_sel_hi:[0,1,1] neg_lo:[0,0,1] neg_hi:[0,0,1]
	v_pk_fma_f32 v[124:125], v[8:9], v[134:135], v[142:143] op_sel_hi:[0,1,1] neg_lo:[0,0,1] neg_hi:[0,0,1]
	v_lshl_add_u64 v[8:9], s[22:23], 0, v[12:13]
	v_lshl_add_u32 v0, v14, 2, s17
	s_nop 0
	ds_read_b128 v[0:3], v0
	s_nop 0
	s_waitcnt vmcnt(1)
	v_lshlrev_b32_e32 v126, 16, v244
	v_and_b32_e32 v127, 0xffff0000, v244
	s_waitcnt lgkmcnt(0)
	v_pk_fma_f32 v[126:127], v[0:1], v[10:11], v[126:127]
	v_lshl_add_u64 v[10:11], s[20:21], 0, v[12:13]
	s_nop 0
	v_lshlrev_b32_e32 v14, 16, v245
	v_and_b32_e32 v15, 0xffff0000, v245
	v_pk_fma_f32 v[124:125], v[2:3], v[124:125], v[14:15]
	s_nop 0
	s_waitcnt vmcnt(0)
	v_lshlrev_b32_e32 v14, 16, v246
	v_and_b32_e32 v15, 0xffff0000, v246
	v_lshlrev_b32_e32 v12, 16, v247
	v_and_b32_e32 v13, 0xffff0000, v247
	v_pk_fma_f32 v[130:131], v[0:1], v[4:5], v[14:15]
	v_cvt_pk_bf16_f32 v0, v126, v127
	v_cvt_pk_bf16_f32 v1, v124, v125
	v_pk_fma_f32 v[128:129], v[2:3], v[6:7], v[12:13]
	v_cvt_pk_bf16_f32 v2, v130, v131
	s_nop 0
	v_cvt_pk_bf16_f32 v3, v128, v129
	global_store_dwordx2 v[8:9], v[0:1], off offset:2560
	global_store_dwordx2 v[10:11], v[2:3], off offset:2560
	v_mov_b32_e32 v0, v21
	ds_read_b32 v136, v27 offset:64
	v_lshlrev_b32_e32 v132, 2, v0
	v_add_u32_e32 v134, 0x600, v132
	v_ashrrev_i32_e32 v135, 31, v134
	v_lshlrev_b64 v[146:147], 1, v[134:135]
	v_lshl_add_u64 v[0:1], vcc, 0, v[146:147]
	global_load_dwordx2 v[0:1], v[0:1], off
	v_lshl_add_u64 v[148:149], s[76:77], 0, v[146:147]
	v_lshl_add_u64 v[156:157], s[10:11], 0, v[146:147]
	v_ashrrev_i32_e32 v133, 31, v132
	s_nop 0
	s_waitcnt vmcnt(0)
	v_lshlrev_b32_e32 v138, 16, v0
	v_and_b32_e32 v139, 0xffff0000, v0
	v_lshlrev_b32_e32 v142, 16, v1
	v_and_b32_e32 v143, 0xffff0000, v1
	ds_read_b128 v[0:3], v27
	ds_read_b128 v[12:15], v27 offset:16
	ds_read_b128 v[8:11], v27 offset:32
	ds_read_b128 v[4:7], v27 offset:48
	global_load_dwordx2 v[150:151], v[148:149], off
	s_waitcnt lgkmcnt(4)
	v_pk_mul_f32 v[140:141], v[136:137], v[142:143] op_sel_hi:[0,1]
	global_load_dwordx2 v[156:157], v[156:157], off
	v_pk_mul_f32 v[144:145], v[136:137], v[138:139] op_sel_hi:[0,1]
	s_nop 0
	s_waitcnt vmcnt(1)
	v_lshlrev_b32_e32 v148, 16, v150
	v_and_b32_e32 v149, 0xffff0000, v150
	v_lshlrev_b32_e32 v150, 16, v151
	v_and_b32_e32 v151, 0xffff0000, v151
	s_waitcnt lgkmcnt(3)
	v_pk_fma_f32 v[154:155], v[0:1], v[150:151], 0 op_sel_hi:[0,1,0]
	s_nop 0
	s_waitcnt vmcnt(0)
	v_lshlrev_b32_e32 v158, 16, v156
	v_and_b32_e32 v159, 0xffff0000, v156
	v_lshlrev_b32_e32 v156, 16, v157
	v_and_b32_e32 v157, 0xffff0000, v157
	v_pk_fma_f32 v[154:155], v[0:1], v[156:157], v[154:155] op_sel:[1,0,0]
	v_lshl_add_u64 v[236:237], s[8:9], 0, v[146:147]
	global_load_dwordx2 v[236:237], v[236:237], off
	v_lshl_add_u64 v[238:239], s[44:45], 0, v[146:147]
	global_load_dwordx2 v[238:239], v[238:239], off
	v_lshl_add_u64 v[240:241], s[48:49], 0, v[146:147]
	global_load_dwordx2 v[240:241], v[240:241], off
	v_lshl_add_u64 v[242:243], s[46:47], 0, v[146:147]
	global_load_dwordx2 v[242:243], v[242:243], off
	v_lshl_add_u64 v[244:245], s[30:31], 0, v[146:147]
	global_load_dwordx2 v[244:245], v[244:245], off
	v_lshl_add_u64 v[246:247], s[28:29], 0, v[146:147]
	global_load_dwordx2 v[246:247], v[246:247], off
	s_nop 0
	s_nop 0
	v_pk_fma_f32 v[152:153], v[0:1], v[148:149], 0 op_sel_hi:[0,1,0]
	v_pk_fma_f32 v[152:153], v[0:1], v[158:159], v[152:153] op_sel:[1,0,0]
	s_nop 0
	s_waitcnt vmcnt(5)
	v_lshlrev_b32_e32 v158, 16, v236
	v_and_b32_e32 v159, 0xffff0000, v236
	v_lshlrev_b32_e32 v156, 16, v237
	v_and_b32_e32 v157, 0xffff0000, v237
	v_pk_fma_f32 v[154:155], v[2:3], v[156:157], v[154:155] op_sel_hi:[0,1,1]
	s_nop 0
	s_nop 0
	v_pk_fma_f32 v[152:153], v[2:3], v[158:159], v[152:153] op_sel_hi:[0,1,1]
	v_mov_b32_e32 v2, v3
	s_nop 0
	s_waitcnt vmcnt(4)
	v_lshlrev_b32_e32 v158, 16, v238
	v_and_b32_e32 v159, 0xffff0000, v238
	v_lshlrev_b32_e32 v156, 16, v239
	v_and_b32_e32 v157, 0xffff0000, v239
	v_pk_fma_f32 v[154:155], v[2:3], v[156:157], v[154:155] op_sel_hi:[0,1,1]
	v_pk_fma_f32 v[2:3], v[2:3], v[158:159], v[152:153] op_sel_hi:[0,1,1]
	s_nop 0
	s_nop 0
	s_nop 0
	s_waitcnt vmcnt(3)
	v_lshlrev_b32_e32 v156, 16, v240
	v_and_b32_e32 v157, 0xffff0000, v240
	v_lshlrev_b32_e32 v152, 16, v241
	v_and_b32_e32 v153, 0xffff0000, v241
	s_waitcnt lgkmcnt(2)
	v_pk_fma_f32 v[152:153], v[12:13], v[152:153], v[154:155] op_sel_hi:[0,1,1]
	s_nop 0
	s_nop 0
	v_pk_fma_f32 v[2:3], v[12:13], v[156:157], v[2:3] op_sel_hi:[0,1,1]
	s_nop 0
	s_waitcnt vmcnt(2)
	v_lshlrev_b32_e32 v156, 16, v242
	v_and_b32_e32 v157, 0xffff0000, v242
	v_lshlrev_b32_e32 v154, 16, v243
	v_and_b32_e32 v155, 0xffff0000, v243
	v_pk_fma_f32 v[152:153], v[12:13], v[154:155], v[152:153] op_sel:[1,0,0]
	v_pk_fma_f32 v[2:3], v[12:13], v[156:157], v[2:3] op_sel:[1,0,0]
	s_nop 0
	s_nop 0
	s_nop 0
	s_waitcnt vmcnt(1)
	v_lshlrev_b32_e32 v154, 16, v244
	v_and_b32_e32 v155, 0xffff0000, v244
	v_lshlrev_b32_e32 v12, 16, v245
	v_and_b32_e32 v13, 0xffff0000, v245
	v_pk_fma_f32 v[12:13], v[14:15], v[12:13], v[152:153] op_sel_hi:[0,1,1]
	s_nop 0
	s_nop 0
	v_pk_fma_f32 v[2:3], v[14:15], v[154:155], v[2:3] op_sel_hi:[0,1,1]
	v_mov_b32_e32 v14, v15
	s_nop 0
	s_waitcnt vmcnt(0)
	v_lshlrev_b32_e32 v154, 16, v246
	v_and_b32_e32 v155, 0xffff0000, v246
	v_lshlrev_b32_e32 v152, 16, v247
	v_and_b32_e32 v153, 0xffff0000, v247
	v_pk_fma_f32 v[12:13], v[14:15], v[152:153], v[12:13] op_sel_hi:[0,1,1]
	v_pk_fma_f32 v[2:3], v[14:15], v[154:155], v[2:3] op_sel_hi:[0,1,1]
	v_lshl_add_u64 v[236:237], s[0:1], 0, v[146:147]
	global_load_dwordx2 v[236:237], v[236:237], off
	v_lshl_add_u64 v[238:239], s[42:43], 0, v[146:147]
	global_load_dwordx2 v[238:239], v[238:239], off
	v_lshl_add_u64 v[240:241], s[2:3], 0, v[146:147]
	global_load_dwordx2 v[240:241], v[240:241], off
	v_lshl_add_u64 v[242:243], s[36:37], 0, v[146:147]
	global_load_dwordx2 v[242:243], v[242:243], off
	v_lshl_add_u64 v[244:245], s[52:53], 0, v[146:147]
	global_load_dwordx2 v[244:245], v[244:245], off
	v_lshl_add_u64 v[246:247], s[50:51], 0, v[146:147]
	global_load_dwordx2 v[246:247], v[246:247], off
	s_nop 0
	s_nop 0
	s_nop 0
	s_waitcnt vmcnt(5)
	v_lshlrev_b32_e32 v152, 16, v236
	v_and_b32_e32 v153, 0xffff0000, v236
	v_lshlrev_b32_e32 v14, 16, v237
	v_and_b32_e32 v15, 0xffff0000, v237
	s_waitcnt lgkmcnt(1)
	v_pk_fma_f32 v[12:13], v[8:9], v[14:15], v[12:13] op_sel_hi:[0,1,1]
	s_nop 0
	s_nop 0
	v_pk_fma_f32 v[2:3], v[8:9], v[152:153], v[2:3] op_sel_hi:[0,1,1]
	s_nop 0
	s_waitcnt vmcnt(4)
	v_lshlrev_b32_e32 v152, 16, v238
	v_and_b32_e32 v153, 0xffff0000, v238
	v_lshlrev_b32_e32 v14, 16, v239
	v_and_b32_e32 v15, 0xffff0000, v239
	v_pk_fma_f32 v[12:13], v[8:9], v[14:15], v[12:13] op_sel:[1,0,0]
	v_pk_fma_f32 v[2:3], v[8:9], v[152:153], v[2:3] op_sel:[1,0,0]
	s_nop 0
	s_nop 0
	s_nop 0
	s_waitcnt vmcnt(3)
	v_lshlrev_b32_e32 v14, 16, v240
	v_and_b32_e32 v15, 0xffff0000, v240
	v_lshlrev_b32_e32 v8, 16, v241
	v_and_b32_e32 v9, 0xffff0000, v241
	v_pk_fma_f32 v[8:9], v[10:11], v[8:9], v[12:13] op_sel_hi:[0,1,1]
	s_nop 0
	s_nop 0
	v_pk_fma_f32 v[2:3], v[10:11], v[14:15], v[2:3] op_sel_hi:[0,1,1]
	v_mov_b32_e32 v10, v11
	s_nop 0
	s_waitcnt vmcnt(2)
	v_lshlrev_b32_e32 v14, 16, v242
	v_and_b32_e32 v15, 0xffff0000, v242
	v_lshlrev_b32_e32 v12, 16, v243
	v_and_b32_e32 v13, 0xffff0000, v243
	v_pk_fma_f32 v[8:9], v[10:11], v[12:13], v[8:9] op_sel_hi:[0,1,1]
	v_pk_fma_f32 v[2:3], v[10:11], v[14:15], v[2:3] op_sel_hi:[0,1,1]
	s_nop 0
	s_nop 0
	s_nop 0
	s_waitcnt vmcnt(1)
	v_lshlrev_b32_e32 v12, 16, v244
	v_and_b32_e32 v13, 0xffff0000, v244
	v_lshlrev_b32_e32 v10, 16, v245
	v_and_b32_e32 v11, 0xffff0000, v245
	s_waitcnt lgkmcnt(0)
	v_pk_fma_f32 v[8:9], v[4:5], v[10:11], v[8:9] op_sel_hi:[0,1,1]
	s_nop 0
	s_nop 0
	v_pk_fma_f32 v[2:3], v[4:5], v[12:13], v[2:3] op_sel_hi:[0,1,1]
	s_nop 0
	s_waitcnt vmcnt(0)
	v_lshlrev_b32_e32 v12, 16, v246
	v_and_b32_e32 v13, 0xffff0000, v246
	v_lshlrev_b32_e32 v10, 16, v247
	v_and_b32_e32 v11, 0xffff0000, v247
	v_pk_fma_f32 v[8:9], v[4:5], v[10:11], v[8:9] op_sel:[1,0,0]
	v_pk_fma_f32 v[2:3], v[4:5], v[12:13], v[2:3] op_sel:[1,0,0]
	v_lshl_add_u64 v[236:237], s[26:27], 0, v[146:147]
	global_load_dwordx2 v[236:237], v[236:237], off
	v_lshl_add_u64 v[238:239], s[24:25], 0, v[146:147]
	global_load_dwordx2 v[238:239], v[238:239], off
	s_nop 0
	s_nop 0
	s_nop 0
	s_waitcnt vmcnt(1)
	v_lshlrev_b32_e32 v10, 16, v236
	v_and_b32_e32 v11, 0xffff0000, v236
	v_lshlrev_b32_e32 v4, 16, v237
	v_and_b32_e32 v5, 0xffff0000, v237
	v_pk_fma_f32 v[4:5], v[6:7], v[4:5], v[8:9] op_sel_hi:[0,1,1]
	s_nop 0
	s_nop 0
	v_pk_fma_f32 v[2:3], v[6:7], v[10:11], v[2:3] op_sel_hi:[0,1,1]
	v_mov_b32_e32 v6, v7
	s_nop 0
	s_waitcnt vmcnt(0)
	v_lshlrev_b32_e32 v10, 16, v238
	v_and_b32_e32 v11, 0xffff0000, v238
	v_lshlrev_b32_e32 v8, 16, v239
	v_and_b32_e32 v9, 0xffff0000, v239
	v_pk_mul_f32 v[14:15], v[6:7], v[10:11] op_sel_hi:[0,1]
	v_pk_fma_f32 v[2:3], v[6:7], v[10:11], v[2:3] op_sel_hi:[0,1,1]
	v_pk_mul_f32 v[12:13], v[6:7], v[8:9] op_sel_hi:[0,1]
	v_pk_fma_f32 v[8:9], v[6:7], v[8:9], v[4:5] op_sel_hi:[0,1,1]
	v_pk_fma_f32 v[10:11], v[92:93], v[2:3], v[14:15] op_sel_hi:[0,1,1] neg_lo:[0,0,1] neg_hi:[0,0,1]
	v_lshlrev_b64 v[14:15], 1, v[132:133]
	v_pk_fma_f32 v[4:5], v[0:1], v[148:149], v[2:3] op_sel_hi:[0,1,1] neg_lo:[1,0,0] neg_hi:[1,0,0]
	v_pk_fma_f32 v[0:1], v[0:1], v[150:151], v[8:9] op_sel_hi:[0,1,1] neg_lo:[1,0,0] neg_hi:[1,0,0]
	v_pk_fma_f32 v[12:13], v[92:93], v[8:9], v[12:13] op_sel_hi:[0,1,1] neg_lo:[0,0,1] neg_hi:[0,0,1]
	v_lshl_add_u64 v[236:237], s[22:23], 0, v[14:15]
	global_load_dwordx2 v[236:237], v[236:237], off offset:3072
	v_lshl_add_u64 v[238:239], s[20:21], 0, v[14:15]
	global_load_dwordx2 v[238:239], v[238:239], off offset:3072
	v_lshl_add_u64 v[8:9], s[22:23], 0, v[14:15]
	s_nop 0
	v_pk_fma_f32 v[0:1], v[136:137], v[142:143], v[0:1] op_sel_hi:[0,1,1]
	v_pk_fma_f32 v[6:7], v[94:95], v[0:1], v[140:141] op_sel_hi:[0,1,1] neg_lo:[0,0,1] neg_hi:[0,0,1]
	v_lshl_add_u32 v0, v134, 2, s17
	ds_read_b128 v[0:3], v0
	v_pk_fma_f32 v[4:5], v[136:137], v[138:139], v[4:5] op_sel_hi:[0,1,1]
	v_pk_fma_f32 v[4:5], v[94:95], v[4:5], v[144:145] op_sel_hi:[0,1,1] neg_lo:[0,0,1] neg_hi:[0,0,1]
	s_nop 0
	s_waitcnt vmcnt(1)
	v_lshlrev_b32_e32 v134, 16, v236
	v_and_b32_e32 v135, 0xffff0000, v236
	v_lshlrev_b32_e32 v132, 16, v237
	v_and_b32_e32 v133, 0xffff0000, v237
	s_waitcnt lgkmcnt(0)
	v_pk_fma_f32 v[134:135], v[0:1], v[10:11], v[134:135]
	v_lshl_add_u64 v[10:11], s[20:21], 0, v[14:15]
	v_pk_fma_f32 v[132:133], v[2:3], v[12:13], v[132:133]
	s_nop 0
	s_nop 0
	s_waitcnt vmcnt(0)
	v_lshlrev_b32_e32 v14, 16, v238
	v_and_b32_e32 v15, 0xffff0000, v238
	v_lshlrev_b32_e32 v12, 16, v239
	v_and_b32_e32 v13, 0xffff0000, v239
	v_pk_fma_f32 v[138:139], v[0:1], v[4:5], v[14:15]
	v_cvt_pk_bf16_f32 v0, v134, v135
	v_cvt_pk_bf16_f32 v1, v132, v133
	v_pk_fma_f32 v[136:137], v[2:3], v[6:7], v[12:13]
	v_cvt_pk_bf16_f32 v2, v138, v139
	s_nop 0
	v_cvt_pk_bf16_f32 v3, v136, v137
	global_store_dwordx2 v[8:9], v[0:1], off offset:3072
	global_store_dwordx2 v[10:11], v[2:3], off offset:3072
	v_mov_b32_e32 v0, v21
	ds_read_b32 v144, v27 offset:64
	v_lshlrev_b32_e32 v140, 2, v0
	v_add_u32_e32 v142, 0x700, v140
	v_ashrrev_i32_e32 v143, 31, v142
	v_lshlrev_b64 v[154:155], 1, v[142:143]
	v_lshl_add_u64 v[0:1], vcc, 0, v[154:155]
	global_load_dwordx2 v[0:1], v[0:1], off
	v_lshl_add_u64 v[156:157], s[76:77], 0, v[154:155]
	v_lshl_add_u64 v[164:165], s[10:11], 0, v[154:155]
	v_ashrrev_i32_e32 v141, 31, v140
	s_nop 0
	s_waitcnt vmcnt(0)
	v_lshlrev_b32_e32 v146, 16, v0
	v_and_b32_e32 v147, 0xffff0000, v0
	v_lshlrev_b32_e32 v150, 16, v1
	v_and_b32_e32 v151, 0xffff0000, v1
	ds_read_b128 v[0:3], v27
	ds_read_b128 v[12:15], v27 offset:16
	ds_read_b128 v[8:11], v27 offset:32
	ds_read_b128 v[4:7], v27 offset:48
	global_load_dwordx2 v[158:159], v[156:157], off
	s_waitcnt lgkmcnt(4)
	v_pk_mul_f32 v[152:153], v[144:145], v[146:147] op_sel_hi:[0,1]
	global_load_dwordx2 v[164:165], v[164:165], off
	v_pk_mul_f32 v[148:149], v[144:145], v[150:151] op_sel_hi:[0,1]
	s_nop 0
	s_waitcnt vmcnt(1)
	v_lshlrev_b32_e32 v156, 16, v158
	v_and_b32_e32 v157, 0xffff0000, v158
	v_lshlrev_b32_e32 v158, 16, v159
	v_and_b32_e32 v159, 0xffff0000, v159
	s_waitcnt lgkmcnt(3)
	v_pk_fma_f32 v[162:163], v[0:1], v[158:159], 0 op_sel_hi:[0,1,0]
	s_nop 0
	s_waitcnt vmcnt(0)
	v_lshlrev_b32_e32 v166, 16, v164
	v_and_b32_e32 v167, 0xffff0000, v164
	v_lshlrev_b32_e32 v164, 16, v165
	v_and_b32_e32 v165, 0xffff0000, v165
	v_pk_fma_f32 v[162:163], v[0:1], v[164:165], v[162:163] op_sel:[1,0,0]
	v_lshl_add_u64 v[236:237], s[8:9], 0, v[154:155]
	global_load_dwordx2 v[236:237], v[236:237], off
	v_lshl_add_u64 v[238:239], s[44:45], 0, v[154:155]
	global_load_dwordx2 v[238:239], v[238:239], off
	v_lshl_add_u64 v[240:241], s[48:49], 0, v[154:155]
	global_load_dwordx2 v[240:241], v[240:241], off
	v_lshl_add_u64 v[242:243], s[46:47], 0, v[154:155]
	global_load_dwordx2 v[242:243], v[242:243], off
	v_lshl_add_u64 v[244:245], s[30:31], 0, v[154:155]
	global_load_dwordx2 v[244:245], v[244:245], off
	v_lshl_add_u64 v[246:247], s[28:29], 0, v[154:155]
	global_load_dwordx2 v[246:247], v[246:247], off
	s_nop 0
	s_nop 0
	v_pk_fma_f32 v[160:161], v[0:1], v[156:157], 0 op_sel_hi:[0,1,0]
	v_pk_fma_f32 v[160:161], v[0:1], v[166:167], v[160:161] op_sel:[1,0,0]
	s_nop 0
	s_waitcnt vmcnt(5)
	v_lshlrev_b32_e32 v166, 16, v236
	v_and_b32_e32 v167, 0xffff0000, v236
	v_lshlrev_b32_e32 v164, 16, v237
	v_and_b32_e32 v165, 0xffff0000, v237
	v_pk_fma_f32 v[162:163], v[2:3], v[164:165], v[162:163] op_sel_hi:[0,1,1]
	s_nop 0
	s_nop 0
	v_pk_fma_f32 v[160:161], v[2:3], v[166:167], v[160:161] op_sel_hi:[0,1,1]
	v_mov_b32_e32 v2, v3
	s_nop 0
	s_waitcnt vmcnt(4)
	v_lshlrev_b32_e32 v166, 16, v238
	v_and_b32_e32 v167, 0xffff0000, v238
	v_lshlrev_b32_e32 v164, 16, v239
	v_and_b32_e32 v165, 0xffff0000, v239
	v_pk_fma_f32 v[162:163], v[2:3], v[164:165], v[162:163] op_sel_hi:[0,1,1]
	v_pk_fma_f32 v[2:3], v[2:3], v[166:167], v[160:161] op_sel_hi:[0,1,1]
	s_nop 0
	s_nop 0
	s_nop 0
	s_waitcnt vmcnt(3)
	v_lshlrev_b32_e32 v164, 16, v240
	v_and_b32_e32 v165, 0xffff0000, v240
	v_lshlrev_b32_e32 v160, 16, v241
	v_and_b32_e32 v161, 0xffff0000, v241
	s_waitcnt lgkmcnt(2)
	v_pk_fma_f32 v[160:161], v[12:13], v[160:161], v[162:163] op_sel_hi:[0,1,1]
	s_nop 0
	s_nop 0
	v_pk_fma_f32 v[2:3], v[12:13], v[164:165], v[2:3] op_sel_hi:[0,1,1]
	s_nop 0
	s_waitcnt vmcnt(2)
	v_lshlrev_b32_e32 v164, 16, v242
	v_and_b32_e32 v165, 0xffff0000, v242
	v_lshlrev_b32_e32 v162, 16, v243
	v_and_b32_e32 v163, 0xffff0000, v243
	v_pk_fma_f32 v[160:161], v[12:13], v[162:163], v[160:161] op_sel:[1,0,0]
	v_pk_fma_f32 v[2:3], v[12:13], v[164:165], v[2:3] op_sel:[1,0,0]
	s_nop 0
	s_nop 0
	s_nop 0
	s_waitcnt vmcnt(1)
	v_lshlrev_b32_e32 v162, 16, v244
	v_and_b32_e32 v163, 0xffff0000, v244
	v_lshlrev_b32_e32 v12, 16, v245
	v_and_b32_e32 v13, 0xffff0000, v245
	v_pk_fma_f32 v[12:13], v[14:15], v[12:13], v[160:161] op_sel_hi:[0,1,1]
	s_nop 0
	s_nop 0
	v_pk_fma_f32 v[2:3], v[14:15], v[162:163], v[2:3] op_sel_hi:[0,1,1]
	v_mov_b32_e32 v14, v15
	s_nop 0
	s_waitcnt vmcnt(0)
	v_lshlrev_b32_e32 v162, 16, v246
	v_and_b32_e32 v163, 0xffff0000, v246
	v_lshlrev_b32_e32 v160, 16, v247
	v_and_b32_e32 v161, 0xffff0000, v247
	v_pk_fma_f32 v[12:13], v[14:15], v[160:161], v[12:13] op_sel_hi:[0,1,1]
	v_pk_fma_f32 v[2:3], v[14:15], v[162:163], v[2:3] op_sel_hi:[0,1,1]
	v_lshl_add_u64 v[236:237], s[0:1], 0, v[154:155]
	global_load_dwordx2 v[236:237], v[236:237], off
	v_lshl_add_u64 v[238:239], s[42:43], 0, v[154:155]
	global_load_dwordx2 v[238:239], v[238:239], off
	v_lshl_add_u64 v[240:241], s[2:3], 0, v[154:155]
	global_load_dwordx2 v[240:241], v[240:241], off
	v_lshl_add_u64 v[242:243], s[36:37], 0, v[154:155]
	global_load_dwordx2 v[242:243], v[242:243], off
	v_lshl_add_u64 v[244:245], s[52:53], 0, v[154:155]
	global_load_dwordx2 v[244:245], v[244:245], off
	v_lshl_add_u64 v[246:247], s[50:51], 0, v[154:155]
	global_load_dwordx2 v[246:247], v[246:247], off
	s_nop 0
	s_nop 0
	s_nop 0
	s_waitcnt vmcnt(5)
	v_lshlrev_b32_e32 v160, 16, v236
	v_and_b32_e32 v161, 0xffff0000, v236
	v_lshlrev_b32_e32 v14, 16, v237
	v_and_b32_e32 v15, 0xffff0000, v237
	s_waitcnt lgkmcnt(1)
	v_pk_fma_f32 v[12:13], v[8:9], v[14:15], v[12:13] op_sel_hi:[0,1,1]
	s_nop 0
	s_nop 0
	v_pk_fma_f32 v[2:3], v[8:9], v[160:161], v[2:3] op_sel_hi:[0,1,1]
	s_nop 0
	s_waitcnt vmcnt(4)
	v_lshlrev_b32_e32 v160, 16, v238
	v_and_b32_e32 v161, 0xffff0000, v238
	v_lshlrev_b32_e32 v14, 16, v239
	v_and_b32_e32 v15, 0xffff0000, v239
	v_pk_fma_f32 v[12:13], v[8:9], v[14:15], v[12:13] op_sel:[1,0,0]
	v_pk_fma_f32 v[2:3], v[8:9], v[160:161], v[2:3] op_sel:[1,0,0]
	s_nop 0
	s_nop 0
	s_nop 0
	s_waitcnt vmcnt(3)
	v_lshlrev_b32_e32 v14, 16, v240
	v_and_b32_e32 v15, 0xffff0000, v240
	v_lshlrev_b32_e32 v8, 16, v241
	v_and_b32_e32 v9, 0xffff0000, v241
	v_pk_fma_f32 v[8:9], v[10:11], v[8:9], v[12:13] op_sel_hi:[0,1,1]
	s_nop 0
	s_nop 0
	v_pk_fma_f32 v[2:3], v[10:11], v[14:15], v[2:3] op_sel_hi:[0,1,1]
	v_mov_b32_e32 v10, v11
	s_nop 0
	s_waitcnt vmcnt(2)
	v_lshlrev_b32_e32 v14, 16, v242
	v_and_b32_e32 v15, 0xffff0000, v242
	v_lshlrev_b32_e32 v12, 16, v243
	v_and_b32_e32 v13, 0xffff0000, v243
	v_pk_fma_f32 v[8:9], v[10:11], v[12:13], v[8:9] op_sel_hi:[0,1,1]
	v_pk_fma_f32 v[2:3], v[10:11], v[14:15], v[2:3] op_sel_hi:[0,1,1]
	s_nop 0
	s_nop 0
	s_nop 0
	s_waitcnt vmcnt(1)
	v_lshlrev_b32_e32 v12, 16, v244
	v_and_b32_e32 v13, 0xffff0000, v244
	v_lshlrev_b32_e32 v10, 16, v245
	v_and_b32_e32 v11, 0xffff0000, v245
	s_waitcnt lgkmcnt(0)
	v_pk_fma_f32 v[8:9], v[4:5], v[10:11], v[8:9] op_sel_hi:[0,1,1]
	s_nop 0
	s_nop 0
	v_pk_fma_f32 v[2:3], v[4:5], v[12:13], v[2:3] op_sel_hi:[0,1,1]
	s_nop 0
	s_waitcnt vmcnt(0)
	v_lshlrev_b32_e32 v12, 16, v246
	v_and_b32_e32 v13, 0xffff0000, v246
	v_lshlrev_b32_e32 v10, 16, v247
	v_and_b32_e32 v11, 0xffff0000, v247
	v_pk_fma_f32 v[8:9], v[4:5], v[10:11], v[8:9] op_sel:[1,0,0]
	v_pk_fma_f32 v[2:3], v[4:5], v[12:13], v[2:3] op_sel:[1,0,0]
	v_lshl_add_u64 v[236:237], s[26:27], 0, v[154:155]
	global_load_dwordx2 v[236:237], v[236:237], off
	v_lshl_add_u64 v[238:239], s[24:25], 0, v[154:155]
	global_load_dwordx2 v[238:239], v[238:239], off
	s_nop 0
	s_nop 0
	s_nop 0
	s_waitcnt vmcnt(1)
	v_lshlrev_b32_e32 v10, 16, v236
	v_and_b32_e32 v11, 0xffff0000, v236
	v_lshlrev_b32_e32 v4, 16, v237
	v_and_b32_e32 v5, 0xffff0000, v237
	v_pk_fma_f32 v[4:5], v[6:7], v[4:5], v[8:9] op_sel_hi:[0,1,1]
	s_nop 0
	s_nop 0
	v_pk_fma_f32 v[2:3], v[6:7], v[10:11], v[2:3] op_sel_hi:[0,1,1]
	v_mov_b32_e32 v6, v7
	s_nop 0
	s_waitcnt vmcnt(0)
	v_lshlrev_b32_e32 v10, 16, v238
	v_and_b32_e32 v11, 0xffff0000, v238
	v_lshlrev_b32_e32 v8, 16, v239
	v_and_b32_e32 v9, 0xffff0000, v239
	v_pk_fma_f32 v[2:3], v[6:7], v[10:11], v[2:3] op_sel_hi:[0,1,1]
	v_pk_mul_f32 v[12:13], v[6:7], v[8:9] op_sel_hi:[0,1]
	v_pk_mul_f32 v[14:15], v[6:7], v[10:11] op_sel_hi:[0,1]
	v_pk_fma_f32 v[4:5], v[6:7], v[8:9], v[4:5] op_sel_hi:[0,1,1]
	v_pk_fma_f32 v[6:7], v[0:1], v[156:157], v[2:3] op_sel_hi:[0,1,1] neg_lo:[1,0,0] neg_hi:[1,0,0]
	v_pk_fma_f32 v[0:1], v[0:1], v[158:159], v[4:5] op_sel_hi:[0,1,1] neg_lo:[1,0,0] neg_hi:[1,0,0]
	v_pk_fma_f32 v[6:7], v[144:145], v[146:147], v[6:7] op_sel_hi:[0,1,1]
	v_pk_fma_f32 v[4:5], v[92:93], v[4:5], v[12:13] op_sel_hi:[0,1,1] neg_lo:[0,0,1] neg_hi:[0,0,1]
	v_lshlrev_b64 v[12:13], 1, v[140:141]
	v_pk_fma_f32 v[8:9], v[94:95], v[6:7], v[152:153] op_sel_hi:[0,1,1] neg_lo:[0,0,1] neg_hi:[0,0,1]
	v_pk_fma_f32 v[6:7], v[92:93], v[2:3], v[14:15] op_sel_hi:[0,1,1] neg_lo:[0,0,1] neg_hi:[0,0,1]
	v_lshl_add_u64 v[236:237], s[22:23], 0, v[12:13]
	global_load_dwordx2 v[236:237], v[236:237], off offset:3584
	v_lshl_add_u64 v[238:239], s[20:21], 0, v[12:13]
	global_load_dwordx2 v[238:239], v[238:239], off offset:3584
	v_lshl_add_u64 v[14:15], s[22:23], 0, v[12:13]
	s_nop 0
	v_pk_fma_f32 v[0:1], v[144:145], v[150:151], v[0:1] op_sel_hi:[0,1,1]
	v_pk_fma_f32 v[10:11], v[94:95], v[0:1], v[148:149] op_sel_hi:[0,1,1] neg_lo:[0,0,1] neg_hi:[0,0,1]
	v_lshl_add_u32 v0, v142, 2, s17
	ds_read_b128 v[0:3], v0
	s_nop 0
	s_waitcnt vmcnt(1)
	v_lshlrev_b32_e32 v94, 16, v236
	v_and_b32_e32 v95, 0xffff0000, v236
	v_lshlrev_b32_e32 v92, 16, v237
	v_and_b32_e32 v93, 0xffff0000, v237
	s_waitcnt lgkmcnt(0)
	v_pk_fma_f32 v[4:5], v[2:3], v[4:5], v[92:93]
	v_lshl_add_u64 v[92:93], s[20:21], 0, v[12:13]
	s_nop 0
	v_pk_fma_f32 v[6:7], v[0:1], v[6:7], v[94:95]
	s_nop 0
	s_waitcnt vmcnt(0)
	v_lshlrev_b32_e32 v94, 16, v238
	v_and_b32_e32 v95, 0xffff0000, v238
	v_lshlrev_b32_e32 v12, 16, v239
	v_and_b32_e32 v13, 0xffff0000, v239
	v_pk_fma_f32 v[10:11], v[2:3], v[10:11], v[12:13]
	v_pk_fma_f32 v[12:13], v[0:1], v[8:9], v[94:95]
	v_cvt_pk_bf16_f32 v0, v6, v7
	v_cvt_pk_bf16_f32 v1, v4, v5
	s_nop 0
	v_cvt_pk_bf16_f32 v2, v12, v13
	v_cvt_pk_bf16_f32 v3, v10, v11
	global_store_dwordx2 v[14:15], v[0:1], off offset:3584
	global_store_dwordx2 v[92:93], v[2:3], off offset:3584
	v_mul_f32_e32 v0, v87, v87
	v_mul_f32_e32 v1, v85, v85
	v_fmac_f32_e32 v0, v86, v86
	v_fmac_f32_e32 v1, v84, v84
	v_mov_b32_e32 v2, v83
	v_mov_b32_e32 v3, v91
	v_add_f32_e32 v14, v0, v1
	v_mov_b32_e32 v0, v82
	v_mov_b32_e32 v1, v90
	v_pk_mul_f32 v[2:3], v[2:3], v[2:3]
	v_mov_b32_e32 v8, v81
	v_mov_b32_e32 v9, v89
	v_pk_fma_f32 v[0:1], v[0:1], v[0:1], v[2:3]
	v_mov_b32_e32 v2, v80
	v_mov_b32_e32 v3, v88
	v_pk_mul_f32 v[8:9], v[8:9], v[8:9]
	v_mul_f32_e32 v29, v115, v115
	v_pk_fma_f32 v[2:3], v[2:3], v[2:3], v[8:9]
	v_pk_mul_f32 v[8:9], v[102:103], v[102:103]
	v_pk_add_f32 v[0:1], v[0:1], v[2:3]
	v_mul_f32_e32 v2, v99, v99
	v_mul_f32_e32 v3, v97, v97
	v_fmac_f32_e32 v2, v98, v98
	v_fmac_f32_e32 v3, v96, v96
	v_add_f32_e32 v2, v2, v3
	v_add_f32_e32 v27, v14, v2
	v_pk_mul_f32 v[2:3], v[100:101], v[100:101]
	v_pk_add_f32 v[0:1], v[0:1], v[0:1] op_sel:[0,1] op_sel_hi:[1,0]
	v_pk_mov_b32 v[14:15], v[8:9], v[2:3] op_sel:[1,0]
	v_mov_b32_e32 v9, v3
	v_pk_add_f32 v[2:3], v[14:15], v[8:9]
	v_mul_f32_e32 v8, v107, v107
	v_mul_f32_e32 v9, v105, v105
	v_fmac_f32_e32 v8, v106, v106
	v_fmac_f32_e32 v9, v104, v104
	v_add_f32_e32 v8, v8, v9
	v_add_f32_e32 v27, v27, v8
	v_mul_f32_e32 v8, v118, v118
	v_mul_f32_e32 v9, v119, v119
	v_pk_add_f32 v[2:3], v[2:3], v[2:3] op_sel:[0,1] op_sel_hi:[1,0]
	v_mov_b32_e32 v1, v8
	v_mov_b32_e32 v3, v9
	v_pk_add_f32 v[0:1], v[0:1], v[2:3]
	v_mul_f32_e32 v2, v111, v111
	v_mul_f32_e32 v8, v109, v109
	v_mul_f32_e32 v14, v116, v116
	v_mul_f32_e32 v15, v117, v117
	v_pk_fma_f32 v[2:3], v[110:111], v[110:111], v[2:3] op_sel_hi:[1,1,0]
	v_pk_fma_f32 v[8:9], v[108:109], v[108:109], v[8:9] op_sel_hi:[1,1,0]
	v_mov_b32_e32 v3, v14
	v_mov_b32_e32 v9, v15
	v_pk_add_f32 v[2:3], v[2:3], v[8:9]
	v_pk_mul_f32 v[8:9], v[126:127], v[126:127]
	v_pk_add_f32 v[0:1], v[0:1], v[2:3]
	v_pk_mul_f32 v[2:3], v[124:125], v[124:125]
	v_pk_add_f32 v[0:1], v[0:1], v[0:1] op_sel:[0,1] op_sel_hi:[1,0]
	v_pk_mov_b32 v[14:15], v[8:9], v[2:3] op_sel:[1,0]
	v_mov_b32_e32 v9, v3
	v_pk_add_f32 v[2:3], v[14:15], v[8:9]
	v_mul_f32_e32 v8, v6, v6
	v_mul_f32_e32 v9, v7, v7
	v_pk_add_f32 v[2:3], v[2:3], v[2:3] op_sel:[0,1] op_sel_hi:[1,0]
	v_mov_b32_e32 v1, v8
	v_mov_b32_e32 v3, v9
	v_pk_add_f32 v[0:1], v[0:1], v[2:3]
	v_mul_f32_e32 v2, v135, v135
	v_mul_f32_e32 v8, v133, v133
	v_mul_f32_e32 v14, v4, v4
	v_mul_f32_e32 v15, v5, v5
	v_pk_fma_f32 v[2:3], v[134:135], v[134:135], v[2:3] op_sel_hi:[1,1,0]
	v_pk_fma_f32 v[8:9], v[132:133], v[132:133], v[8:9] op_sel_hi:[1,1,0]
	v_mov_b32_e32 v3, v14
	v_mov_b32_e32 v9, v15
	v_pk_add_f32 v[2:3], v[2:3], v[8:9]
	v_mul_f32_e32 v33, v113, v113
	v_pk_add_f32 v[0:1], v[0:1], v[2:3]
	v_xor_b32_e32 v2, 1, v188
	v_add_f32_e32 v0, v0, v1
	v_and_b32_e32 v1, 64, v188
	v_add_u32_e32 v1, 64, v1
	v_cmp_lt_i32_e32 vcc, v2, v1
	v_fmac_f32_e32 v29, v114, v114
	v_fmac_f32_e32 v33, v112, v112
	v_cndmask_b32_e32 v2, v188, v2, vcc
	v_lshlrev_b32_e32 v31, 2, v2
	ds_bpermute_b32 v2, v31, v0
	v_add_f32_e32 v3, v29, v33
	v_mul_f32_e32 v8, v123, v123
	v_mul_f32_e32 v9, v121, v121
	v_fmac_f32_e32 v8, v122, v122
	s_waitcnt lgkmcnt(0)
	v_add_f32_e32 v0, v0, v2
	v_xor_b32_e32 v2, 2, v188
	v_cmp_lt_i32_e32 vcc, v2, v1
	v_fmac_f32_e32 v9, v120, v120
	v_add_f32_e32 v3, v27, v3
	v_cndmask_b32_e32 v2, v188, v2, vcc
	v_lshlrev_b32_e32 v33, 2, v2
	ds_bpermute_b32 v2, v33, v0
	v_add_f32_e32 v8, v8, v9
	v_add_f32_e32 v3, v3, v8
	v_mul_f32_e32 v8, v131, v131
	v_mul_f32_e32 v9, v129, v129
	s_waitcnt lgkmcnt(0)
	v_add_f32_e32 v0, v0, v2
	v_xor_b32_e32 v2, 4, v188
	v_cmp_lt_i32_e32 vcc, v2, v1
	v_fmac_f32_e32 v8, v130, v130
	v_fmac_f32_e32 v9, v128, v128
	v_cndmask_b32_e32 v2, v188, v2, vcc
	v_lshlrev_b32_e32 v35, 2, v2
	ds_bpermute_b32 v2, v35, v0
	v_add_f32_e32 v8, v8, v9
	v_add_f32_e32 v3, v3, v8
	v_mul_f32_e32 v8, v139, v139
	v_mul_f32_e32 v9, v137, v137
	s_waitcnt lgkmcnt(0)
	v_add_f32_e32 v0, v0, v2
	v_xor_b32_e32 v2, 8, v188
	v_cmp_lt_i32_e32 vcc, v2, v1
	v_fmac_f32_e32 v8, v138, v138
	v_fmac_f32_e32 v9, v136, v136
	v_cndmask_b32_e32 v2, v188, v2, vcc
	v_lshlrev_b32_e32 v41, 2, v2
	ds_bpermute_b32 v2, v41, v0
	v_add_f32_e32 v8, v8, v9
	s_waitcnt lgkmcnt(0)
	v_add_f32_e32 v0, v0, v2
	v_xor_b32_e32 v2, 16, v188
	v_cmp_lt_i32_e32 vcc, v2, v1
	s_nop 1
	v_cndmask_b32_e32 v2, v188, v2, vcc
	v_lshlrev_b32_e32 v37, 2, v2
	ds_bpermute_b32 v2, v37, v0
	s_waitcnt lgkmcnt(0)
	v_add_f32_e32 v0, v0, v2
	v_xor_b32_e32 v2, 32, v188
	v_cmp_lt_i32_e32 vcc, v2, v1
	s_nop 1
	v_cndmask_b32_e32 v1, v188, v2, vcc
	v_lshlrev_b32_e32 v39, 2, v1
	ds_bpermute_b32 v1, v39, v0
	v_add_f32_e32 v2, v3, v8
	v_mul_f32_e32 v3, v13, v13
	v_mul_f32_e32 v8, v11, v11
	v_fmac_f32_e32 v3, v12, v12
	s_waitcnt lgkmcnt(0)
	v_add_f32_e32 v0, v0, v1
	v_fmamk_f32 v0, v0, 0x3a000000, v189
	v_mul_f32_e32 v1, 0x4f800000, v0
	v_cmp_gt_f32_e32 vcc, s84, v0
	v_fmac_f32_e32 v8, v10, v10
	v_add_f32_e32 v3, v3, v8
	v_cndmask_b32_e32 v0, v0, v1, vcc
	v_sqrt_f32_e32 v1, v0
	v_add_f32_e32 v2, v2, v3
	v_add_u32_e32 v3, -1, v1
	v_fma_f32 v8, -v3, v1, v0
	v_cmp_ge_f32_e64 s[46:47], 0, v8
	v_add_u32_e32 v8, 1, v1
	s_nop 0
	v_cndmask_b32_e64 v3, v1, v3, s[46:47]
	v_fma_f32 v1, -v8, v1, v0
	v_cmp_lt_f32_e64 s[46:47], 0, v1
	s_nop 1
	v_cndmask_b32_e64 v1, v3, v8, s[46:47]
	v_mul_f32_e32 v3, 0x37800000, v1
	v_cndmask_b32_e32 v1, v1, v3, vcc
	ds_bpermute_b32 v3, v31, v2
	v_cmp_class_f32_e32 vcc, v0, v190
	v_cmp_eq_u32_e64 s[46:47], 1, v20
	s_nop 0
	v_cndmask_b32_e32 v27, v1, v0, vcc
	s_waitcnt lgkmcnt(0)
	v_add_f32_e32 v0, v2, v3
	ds_bpermute_b32 v1, v33, v0
	v_div_scale_f32 v43, s[0:1], v27, v27, 1.0
	v_rcp_f32_e32 v29, v43
	v_div_scale_f32 v47, vcc, 1.0, v27, 1.0
	s_waitcnt lgkmcnt(0)
	v_add_f32_e32 v0, v0, v1
	ds_bpermute_b32 v1, v35, v0
	v_fma_f32 v2, -v43, v29, 1.0
	v_fmac_f32_e32 v29, v2, v29
	v_mul_f32_e32 v45, v47, v29
	v_fma_f32 v51, -v43, v45, v47
	s_waitcnt lgkmcnt(0)
	v_add_f32_e32 v49, v0, v1
	ds_read_b128 v[0:3], v25
	ds_read_b128 v[92:95], v25 offset:1024
	ds_read_b128 v[140:143], v25 offset:2048
	ds_read_b128 v[144:147], v25 offset:3072
	ds_read_b128 v[148:151], v25 offset:4096
	ds_read_b128 v[152:155], v25 offset:5120
	ds_read_b128 v[156:159], v25 offset:6144
	ds_read_b128 v[160:163], v25 offset:7168
	ds_read_b128 v[164:167], v25 offset:8192
	ds_read_b128 v[174:177], v25 offset:9216
	ds_read_b128 v[178:181], v25 offset:10240
	ds_read_b128 v[182:185], v25 offset:11264
	ds_read_b128 v[198:201], v25 offset:12288
	ds_read_b128 v[202:205], v25 offset:13312
	ds_read_b128 v[206:209], v25 offset:14336
	ds_read_b128 v[210:213], v25 offset:15360
	s_waitcnt lgkmcnt(7)
	v_mov_b32_e32 v8, v164
	v_mov_b32_e32 v9, v1
	v_mov_b32_e32 v1, v165
	v_mov_b32_e32 v164, v166
	v_mov_b32_e32 v165, v3
	v_pk_mul_f32 v[14:15], v[82:83], v[8:9]
	v_pk_mul_f32 v[214:215], v[80:81], v[164:165]
	v_mov_b32_e32 v3, v167
	v_pk_fma_f32 v[14:15], v[82:83], v[0:1], v[14:15] op_sel:[0,0,1] op_sel_hi:[1,1,0]
	v_pk_fma_f32 v[166:167], v[80:81], v[2:3], v[214:215] op_sel:[0,0,1] op_sel_hi:[1,1,0]
	v_pk_mul_f32 v[8:9], v[86:87], v[8:9]
	v_pk_add_f32 v[14:15], v[14:15], v[166:167]
	s_waitcnt lgkmcnt(6)
	v_mov_b32_e32 v166, v174
	v_mov_b32_e32 v167, v93
	v_pk_mul_f32 v[214:215], v[90:91], v[166:167]
	v_mov_b32_e32 v93, v175
	v_pk_fma_f32 v[174:175], v[90:91], v[92:93], v[214:215] op_sel:[0,0,1] op_sel_hi:[1,1,0]
	v_mov_b32_e32 v214, v176
	v_mov_b32_e32 v215, v95
	v_pk_mul_f32 v[216:217], v[88:89], v[214:215]
	v_mov_b32_e32 v95, v177
	v_pk_fma_f32 v[176:177], v[88:89], v[94:95], v[216:217] op_sel:[0,0,1] op_sel_hi:[1,1,0]
	v_pk_add_f32 v[14:15], v[14:15], 0 op_sel_hi:[1,0]
	v_pk_add_f32 v[174:175], v[174:175], v[176:177]
	v_pk_fma_f32 v[0:1], v[86:87], v[0:1], v[8:9] op_sel:[0,0,1] op_sel_hi:[1,1,0]
	v_pk_add_f32 v[14:15], v[14:15], v[174:175]
	s_waitcnt lgkmcnt(5)
	v_mov_b32_e32 v174, v178
	v_mov_b32_e32 v175, v141
	v_mov_b32_e32 v141, v179
	v_mov_b32_e32 v178, v180
	v_mov_b32_e32 v179, v143
	v_pk_mul_f32 v[176:177], v[102:103], v[174:175]
	v_pk_mul_f32 v[216:217], v[100:101], v[178:179]
	v_mov_b32_e32 v143, v181
	v_pk_mul_f32 v[8:9], v[84:85], v[164:165]
	v_pk_fma_f32 v[176:177], v[102:103], v[140:141], v[176:177] op_sel:[0,0,1] op_sel_hi:[1,1,0]
	v_pk_fma_f32 v[180:181], v[100:101], v[142:143], v[216:217] op_sel:[0,0,1] op_sel_hi:[1,1,0]
	v_pk_fma_f32 v[2:3], v[84:85], v[2:3], v[8:9] op_sel:[0,0,1] op_sel_hi:[1,1,0]
	v_pk_add_f32 v[176:177], v[176:177], v[180:181]
	v_pk_add_f32 v[0:1], v[0:1], v[2:3]
	v_pk_mul_f32 v[2:3], v[98:99], v[166:167]
	v_pk_mul_f32 v[8:9], v[96:97], v[214:215]
	v_pk_add_f32 v[14:15], v[14:15], v[176:177]
	s_waitcnt lgkmcnt(4)
	v_mov_b32_e32 v176, v182
	v_mov_b32_e32 v177, v145
	v_mov_b32_e32 v145, v183
	v_mov_b32_e32 v182, v184
	v_mov_b32_e32 v183, v147
	v_pk_fma_f32 v[2:3], v[98:99], v[92:93], v[2:3] op_sel:[0,0,1] op_sel_hi:[1,1,0]
	v_pk_fma_f32 v[8:9], v[96:97], v[94:95], v[8:9] op_sel:[0,0,1] op_sel_hi:[1,1,0]
	v_pk_mul_f32 v[180:181], v[110:111], v[176:177]
	v_pk_mul_f32 v[216:217], v[108:109], v[182:183]
	v_mov_b32_e32 v147, v185
	v_pk_add_f32 v[0:1], v[0:1], 0 op_sel_hi:[1,0]
	v_pk_add_f32 v[2:3], v[2:3], v[8:9]
	v_pk_fma_f32 v[180:181], v[110:111], v[144:145], v[180:181] op_sel:[0,0,1] op_sel_hi:[1,1,0]
	v_pk_fma_f32 v[184:185], v[108:109], v[146:147], v[216:217] op_sel:[0,0,1] op_sel_hi:[1,1,0]
	v_pk_add_f32 v[0:1], v[0:1], v[2:3]
	v_pk_mul_f32 v[2:3], v[106:107], v[174:175]
	v_pk_mul_f32 v[8:9], v[104:105], v[178:179]
	v_pk_add_f32 v[180:181], v[180:181], v[184:185]
	v_pk_fma_f32 v[2:3], v[106:107], v[140:141], v[2:3] op_sel:[0,0,1] op_sel_hi:[1,1,0]
	v_pk_fma_f32 v[8:9], v[104:105], v[142:143], v[8:9] op_sel:[0,0,1] op_sel_hi:[1,1,0]
	v_pk_add_f32 v[14:15], v[14:15], v[180:181]
	s_waitcnt lgkmcnt(3)
	v_mov_b32_e32 v180, v198
	v_mov_b32_e32 v181, v149
	v_mov_b32_e32 v149, v199
	v_mov_b32_e32 v198, v200
	v_mov_b32_e32 v199, v151
	v_pk_add_f32 v[2:3], v[2:3], v[8:9]
	v_pk_mul_f32 v[184:185], v[118:119], v[180:181]
	v_pk_mul_f32 v[216:217], v[116:117], v[198:199]
	v_mov_b32_e32 v151, v201
	v_pk_add_f32 v[0:1], v[0:1], v[2:3]
	v_pk_mul_f32 v[2:3], v[114:115], v[176:177]
	v_pk_mul_f32 v[8:9], v[112:113], v[182:183]
	v_pk_fma_f32 v[184:185], v[118:119], v[148:149], v[184:185] op_sel:[0,0,1] op_sel_hi:[1,1,0]
	v_pk_fma_f32 v[200:201], v[116:117], v[150:151], v[216:217] op_sel:[0,0,1] op_sel_hi:[1,1,0]
	v_pk_fma_f32 v[2:3], v[114:115], v[144:145], v[2:3] op_sel:[0,0,1] op_sel_hi:[1,1,0]
	v_pk_fma_f32 v[8:9], v[112:113], v[146:147], v[8:9] op_sel:[0,0,1] op_sel_hi:[1,1,0]
	v_pk_add_f32 v[184:185], v[184:185], v[200:201]
	v_pk_add_f32 v[2:3], v[2:3], v[8:9]
	v_pk_add_f32 v[14:15], v[14:15], v[184:185]
	s_waitcnt lgkmcnt(2)
	v_mov_b32_e32 v184, v202
	v_mov_b32_e32 v185, v153
	v_mov_b32_e32 v153, v203
	v_mov_b32_e32 v202, v204
	v_mov_b32_e32 v203, v155
	v_pk_add_f32 v[0:1], v[0:1], v[2:3]
	v_pk_mul_f32 v[2:3], v[122:123], v[180:181]
	v_pk_mul_f32 v[8:9], v[120:121], v[198:199]
	v_pk_mul_f32 v[200:201], v[126:127], v[184:185]
	v_pk_mul_f32 v[216:217], v[124:125], v[202:203]
	v_mov_b32_e32 v155, v205
	v_pk_fma_f32 v[2:3], v[122:123], v[148:149], v[2:3] op_sel:[0,0,1] op_sel_hi:[1,1,0]
	v_pk_fma_f32 v[8:9], v[120:121], v[150:151], v[8:9] op_sel:[0,0,1] op_sel_hi:[1,1,0]
	v_pk_fma_f32 v[200:201], v[126:127], v[152:153], v[200:201] op_sel:[0,0,1] op_sel_hi:[1,1,0]
	v_pk_fma_f32 v[204:205], v[124:125], v[154:155], v[216:217] op_sel:[0,0,1] op_sel_hi:[1,1,0]
	v_pk_add_f32 v[2:3], v[2:3], v[8:9]
	v_pk_add_f32 v[200:201], v[200:201], v[204:205]
	v_pk_add_f32 v[0:1], v[0:1], v[2:3]
	v_pk_mul_f32 v[2:3], v[130:131], v[184:185]
	v_pk_mul_f32 v[8:9], v[128:129], v[202:203]
	v_pk_add_f32 v[14:15], v[14:15], v[200:201]
	s_waitcnt lgkmcnt(1)
	v_mov_b32_e32 v200, v206
	v_mov_b32_e32 v201, v157
	v_mov_b32_e32 v157, v207
	v_mov_b32_e32 v206, v208
	v_mov_b32_e32 v207, v159
	v_pk_fma_f32 v[2:3], v[130:131], v[152:153], v[2:3] op_sel:[0,0,1] op_sel_hi:[1,1,0]
	v_pk_fma_f32 v[8:9], v[128:129], v[154:155], v[8:9] op_sel:[0,0,1] op_sel_hi:[1,1,0]
	v_pk_mul_f32 v[204:205], v[134:135], v[200:201]
	v_pk_mul_f32 v[216:217], v[132:133], v[206:207]
	v_mov_b32_e32 v159, v209
	v_pk_add_f32 v[2:3], v[2:3], v[8:9]
	v_pk_fma_f32 v[204:205], v[134:135], v[156:157], v[204:205] op_sel:[0,0,1] op_sel_hi:[1,1,0]
	v_pk_fma_f32 v[208:209], v[132:133], v[158:159], v[216:217] op_sel:[0,0,1] op_sel_hi:[1,1,0]
	v_pk_add_f32 v[0:1], v[0:1], v[2:3]
	v_pk_mul_f32 v[2:3], v[138:139], v[200:201]
	v_pk_mul_f32 v[8:9], v[136:137], v[206:207]
	v_pk_add_f32 v[204:205], v[204:205], v[208:209]
	v_pk_fma_f32 v[2:3], v[138:139], v[156:157], v[2:3] op_sel:[0,0,1] op_sel_hi:[1,1,0]
	v_pk_fma_f32 v[8:9], v[136:137], v[158:159], v[8:9] op_sel:[0,0,1] op_sel_hi:[1,1,0]
	v_pk_add_f32 v[14:15], v[14:15], v[204:205]
	s_waitcnt lgkmcnt(0)
	v_mov_b32_e32 v204, v210
	v_mov_b32_e32 v205, v161
	v_mov_b32_e32 v161, v211
	v_mov_b32_e32 v210, v212
	v_mov_b32_e32 v211, v163
	v_pk_add_f32 v[2:3], v[2:3], v[8:9]
	v_pk_mul_f32 v[208:209], v[6:7], v[204:205]
	v_pk_mul_f32 v[216:217], v[4:5], v[210:211]
	v_mov_b32_e32 v163, v213
	v_pk_add_f32 v[0:1], v[0:1], v[2:3]
	v_pk_mul_f32 v[2:3], v[12:13], v[204:205]
	v_pk_mul_f32 v[8:9], v[10:11], v[210:211]
	v_pk_fma_f32 v[208:209], v[6:7], v[160:161], v[208:209] op_sel:[0,0,1] op_sel_hi:[1,1,0]
	v_pk_fma_f32 v[212:213], v[4:5], v[162:163], v[216:217] op_sel:[0,0,1] op_sel_hi:[1,1,0]
	v_pk_fma_f32 v[2:3], v[12:13], v[160:161], v[2:3] op_sel:[0,0,1] op_sel_hi:[1,1,0]
	v_pk_fma_f32 v[8:9], v[10:11], v[162:163], v[8:9] op_sel:[0,0,1] op_sel_hi:[1,1,0]
	v_pk_add_f32 v[208:209], v[208:209], v[212:213]
	v_pk_add_f32 v[2:3], v[2:3], v[8:9]
	v_pk_add_f32 v[14:15], v[14:15], v[208:209]
	v_pk_add_f32 v[0:1], v[0:1], v[2:3]
	ds_read_b128 v[140:143], v25 offset:16384
	ds_read_b128 v[144:147], v25 offset:17408
	ds_read_b128 v[148:151], v25 offset:18432
	ds_read_b128 v[152:155], v25 offset:19456
	ds_read_b128 v[156:159], v25 offset:20480
	ds_read_b128 v[160:163], v25 offset:21504
	ds_read_b128 v[164:167], v25 offset:22528
	ds_read_b128 v[174:177], v25 offset:23552
	ds_read_b128 v[92:95], v25 offset:24576
	ds_read_b128 v[178:181], v25 offset:25600
	ds_read_b128 v[182:185], v25 offset:26624
	ds_read_b128 v[198:201], v25 offset:27648
	ds_read_b128 v[202:205], v25 offset:28672
	ds_read_b128 v[206:209], v25 offset:29696
	ds_read_b128 v[210:213], v25 offset:30720
	ds_read_b128 v[214:217], v25 offset:31744
	s_waitcnt lgkmcnt(7)
	v_mov_b32_e32 v2, v92
	v_mov_b32_e32 v3, v141
	v_mov_b32_e32 v218, v94
	v_mov_b32_e32 v219, v143
	v_pk_mul_f32 v[8:9], v[82:83], v[2:3]
	v_mov_b32_e32 v141, v93
	v_pk_mul_f32 v[92:93], v[80:81], v[218:219]
	v_mov_b32_e32 v143, v95
	v_pk_fma_f32 v[8:9], v[82:83], v[140:141], v[8:9] op_sel:[0,0,1] op_sel_hi:[1,1,0]
	v_pk_fma_f32 v[92:93], v[80:81], v[142:143], v[92:93] op_sel:[0,0,1] op_sel_hi:[1,1,0]
	s_waitcnt lgkmcnt(6)
	v_mov_b32_e32 v94, v178
	v_mov_b32_e32 v95, v145
	v_mov_b32_e32 v145, v179
	v_mov_b32_e32 v178, v180
	v_mov_b32_e32 v179, v147
	v_pk_add_f32 v[8:9], v[8:9], v[92:93]
	v_pk_mul_f32 v[92:93], v[90:91], v[94:95]
	v_pk_mul_f32 v[224:225], v[88:89], v[178:179]
	v_mov_b32_e32 v147, v181
	v_pk_fma_f32 v[92:93], v[90:91], v[144:145], v[92:93] op_sel:[0,0,1] op_sel_hi:[1,1,0]
	v_pk_fma_f32 v[180:181], v[88:89], v[146:147], v[224:225] op_sel:[0,0,1] op_sel_hi:[1,1,0]
	v_pk_add_f32 v[8:9], v[8:9], 0 op_sel_hi:[1,0]
	v_pk_add_f32 v[92:93], v[92:93], v[180:181]
	s_waitcnt lgkmcnt(5)
	v_mov_b32_e32 v180, v182
	v_mov_b32_e32 v181, v149
	v_mov_b32_e32 v149, v183
	v_mov_b32_e32 v182, v184
	v_mov_b32_e32 v183, v151
	v_pk_add_f32 v[8:9], v[8:9], v[92:93]
	v_pk_mul_f32 v[92:93], v[102:103], v[180:181]
	v_pk_mul_f32 v[224:225], v[100:101], v[182:183]
	v_mov_b32_e32 v151, v185
	v_pk_fma_f32 v[92:93], v[102:103], v[148:149], v[92:93] op_sel:[0,0,1] op_sel_hi:[1,1,0]
	v_pk_fma_f32 v[184:185], v[100:101], v[150:151], v[224:225] op_sel:[0,0,1] op_sel_hi:[1,1,0]
	v_pk_mul_f32 v[2:3], v[86:87], v[2:3]
	v_pk_add_f32 v[92:93], v[92:93], v[184:185]
	s_waitcnt lgkmcnt(4)
	v_mov_b32_e32 v184, v198
	v_mov_b32_e32 v185, v153
	v_mov_b32_e32 v153, v199
	v_mov_b32_e32 v198, v200
	v_mov_b32_e32 v199, v155
	v_pk_add_f32 v[8:9], v[8:9], v[92:93]
	v_pk_mul_f32 v[92:93], v[110:111], v[184:185]
	v_pk_mul_f32 v[224:225], v[108:109], v[198:199]
	v_mov_b32_e32 v155, v201
	v_pk_fma_f32 v[92:93], v[110:111], v[152:153], v[92:93] op_sel:[0,0,1] op_sel_hi:[1,1,0]
	v_pk_fma_f32 v[200:201], v[108:109], v[154:155], v[224:225] op_sel:[0,0,1] op_sel_hi:[1,1,0]
	v_pk_fma_f32 v[2:3], v[86:87], v[140:141], v[2:3] op_sel:[0,0,1] op_sel_hi:[1,1,0]
	v_pk_add_f32 v[92:93], v[92:93], v[200:201]
	s_waitcnt lgkmcnt(3)
	v_mov_b32_e32 v200, v202
	v_mov_b32_e32 v201, v157
	v_mov_b32_e32 v157, v203
	v_mov_b32_e32 v202, v204
	v_mov_b32_e32 v203, v159
	v_pk_add_f32 v[8:9], v[8:9], v[92:93]
	v_pk_mul_f32 v[92:93], v[118:119], v[200:201]
	v_pk_mul_f32 v[224:225], v[116:117], v[202:203]
	v_mov_b32_e32 v159, v205
	v_pk_fma_f32 v[92:93], v[118:119], v[156:157], v[92:93] op_sel:[0,0,1] op_sel_hi:[1,1,0]
	v_pk_fma_f32 v[204:205], v[116:117], v[158:159], v[224:225] op_sel:[0,0,1] op_sel_hi:[1,1,0]
	ds_bpermute_b32 v53, v41, v49
	v_pk_add_f32 v[92:93], v[92:93], v[204:205]
	s_waitcnt lgkmcnt(3)
	v_mov_b32_e32 v204, v206
	v_mov_b32_e32 v205, v161
	v_mov_b32_e32 v161, v207
	v_mov_b32_e32 v206, v208
	v_mov_b32_e32 v207, v163
	v_pk_add_f32 v[8:9], v[8:9], v[92:93]
	v_pk_mul_f32 v[92:93], v[126:127], v[204:205]
	v_pk_mul_f32 v[224:225], v[124:125], v[206:207]
	v_mov_b32_e32 v163, v209
	v_pk_fma_f32 v[92:93], v[126:127], v[160:161], v[92:93] op_sel:[0,0,1] op_sel_hi:[1,1,0]
	v_pk_fma_f32 v[208:209], v[124:125], v[162:163], v[224:225] op_sel:[0,0,1] op_sel_hi:[1,1,0]
	v_fmac_f32_e32 v45, v51, v29
	v_pk_add_f32 v[92:93], v[92:93], v[208:209]
	s_waitcnt lgkmcnt(2)
	v_mov_b32_e32 v208, v210
	v_mov_b32_e32 v209, v165
	v_mov_b32_e32 v165, v211
	v_mov_b32_e32 v210, v212
	v_mov_b32_e32 v211, v167
	v_pk_add_f32 v[8:9], v[8:9], v[92:93]
	v_pk_mul_f32 v[92:93], v[134:135], v[208:209]
	v_pk_mul_f32 v[224:225], v[132:133], v[210:211]
	v_mov_b32_e32 v167, v213
	v_pk_fma_f32 v[92:93], v[134:135], v[164:165], v[92:93] op_sel:[0,0,1] op_sel_hi:[1,1,0]
	v_pk_fma_f32 v[212:213], v[132:133], v[166:167], v[224:225] op_sel:[0,0,1] op_sel_hi:[1,1,0]
	s_nop 0
	v_pk_add_f32 v[92:93], v[92:93], v[212:213]
	s_waitcnt lgkmcnt(1)
	v_mov_b32_e32 v212, v214
	v_mov_b32_e32 v213, v175
	v_mov_b32_e32 v175, v215
	v_mov_b32_e32 v214, v216
	v_mov_b32_e32 v215, v177
	v_pk_add_f32 v[8:9], v[8:9], v[92:93]
	v_pk_mul_f32 v[92:93], v[6:7], v[212:213]
	v_pk_mul_f32 v[224:225], v[4:5], v[214:215]
	v_mov_b32_e32 v177, v217
	v_pk_fma_f32 v[92:93], v[6:7], v[174:175], v[92:93] op_sel:[0,0,1] op_sel_hi:[1,1,0]
	v_pk_fma_f32 v[216:217], v[4:5], v[176:177], v[224:225] op_sel:[0,0,1] op_sel_hi:[1,1,0]
	s_nop 0
	v_pk_add_f32 v[92:93], v[92:93], v[216:217]
	s_nop 0
	v_pk_add_f32 v[92:93], v[8:9], v[92:93]
	v_pk_mul_f32 v[8:9], v[84:85], v[218:219]
	s_nop 0
	v_pk_fma_f32 v[8:9], v[84:85], v[142:143], v[8:9] op_sel:[0,0,1] op_sel_hi:[1,1,0]
	s_nop 0
	v_pk_add_f32 v[2:3], v[2:3], v[8:9]
	v_pk_mul_f32 v[8:9], v[98:99], v[94:95]
	v_pk_mul_f32 v[94:95], v[96:97], v[178:179]
	v_pk_fma_f32 v[8:9], v[98:99], v[144:145], v[8:9] op_sel:[0,0,1] op_sel_hi:[1,1,0]
	v_pk_fma_f32 v[94:95], v[96:97], v[146:147], v[94:95] op_sel:[0,0,1] op_sel_hi:[1,1,0]
	v_pk_add_f32 v[2:3], v[2:3], 0 op_sel_hi:[1,0]
	v_pk_add_f32 v[8:9], v[8:9], v[94:95]
	v_pk_mul_f32 v[94:95], v[104:105], v[182:183]
	v_pk_add_f32 v[2:3], v[2:3], v[8:9]
	v_pk_mul_f32 v[8:9], v[106:107], v[180:181]
	v_pk_fma_f32 v[94:95], v[104:105], v[150:151], v[94:95] op_sel:[0,0,1] op_sel_hi:[1,1,0]
	v_pk_fma_f32 v[8:9], v[106:107], v[148:149], v[8:9] op_sel:[0,0,1] op_sel_hi:[1,1,0]
	s_nop 0
	v_pk_add_f32 v[8:9], v[8:9], v[94:95]
	v_pk_mul_f32 v[94:95], v[112:113], v[198:199]
	v_pk_add_f32 v[2:3], v[2:3], v[8:9]
	v_pk_mul_f32 v[8:9], v[114:115], v[184:185]
	v_pk_fma_f32 v[94:95], v[112:113], v[154:155], v[94:95] op_sel:[0,0,1] op_sel_hi:[1,1,0]
	v_pk_fma_f32 v[8:9], v[114:115], v[152:153], v[8:9] op_sel:[0,0,1] op_sel_hi:[1,1,0]
	s_nop 0
	v_pk_add_f32 v[8:9], v[8:9], v[94:95]
	v_pk_mul_f32 v[94:95], v[120:121], v[202:203]
	v_pk_add_f32 v[2:3], v[2:3], v[8:9]
	v_pk_mul_f32 v[8:9], v[122:123], v[200:201]
	v_pk_fma_f32 v[94:95], v[120:121], v[158:159], v[94:95] op_sel:[0,0,1] op_sel_hi:[1,1,0]
	v_pk_fma_f32 v[8:9], v[122:123], v[156:157], v[8:9] op_sel:[0,0,1] op_sel_hi:[1,1,0]
	s_nop 0
	v_pk_add_f32 v[8:9], v[8:9], v[94:95]
	v_pk_mul_f32 v[94:95], v[128:129], v[206:207]
	v_pk_add_f32 v[2:3], v[2:3], v[8:9]
	v_pk_mul_f32 v[8:9], v[130:131], v[204:205]
	v_pk_fma_f32 v[94:95], v[128:129], v[162:163], v[94:95] op_sel:[0,0,1] op_sel_hi:[1,1,0]
	v_pk_fma_f32 v[8:9], v[130:131], v[160:161], v[8:9] op_sel:[0,0,1] op_sel_hi:[1,1,0]
	s_nop 0
	v_pk_add_f32 v[8:9], v[8:9], v[94:95]
	v_pk_mul_f32 v[94:95], v[136:137], v[210:211]
	v_pk_add_f32 v[2:3], v[2:3], v[8:9]
	v_pk_mul_f32 v[8:9], v[138:139], v[208:209]
	v_pk_fma_f32 v[94:95], v[136:137], v[166:167], v[94:95] op_sel:[0,0,1] op_sel_hi:[1,1,0]
	v_pk_fma_f32 v[8:9], v[138:139], v[164:165], v[8:9] op_sel:[0,0,1] op_sel_hi:[1,1,0]
	s_nop 0
	v_pk_add_f32 v[8:9], v[8:9], v[94:95]
	v_pk_mul_f32 v[94:95], v[10:11], v[214:215]
	v_pk_add_f32 v[2:3], v[2:3], v[8:9]
	v_pk_mul_f32 v[8:9], v[12:13], v[212:213]
	v_pk_fma_f32 v[94:95], v[10:11], v[176:177], v[94:95] op_sel:[0,0,1] op_sel_hi:[1,1,0]
	v_pk_fma_f32 v[8:9], v[12:13], v[174:175], v[8:9] op_sel:[0,0,1] op_sel_hi:[1,1,0]
	ds_read_b128 v[140:143], v25 offset:32768
	ds_read_b128 v[144:147], v25 offset:33792
	ds_read_b128 v[148:151], v25 offset:34816
	ds_read_b128 v[152:155], v25 offset:35840
	ds_read_b128 v[156:159], v25 offset:36864
	ds_read_b128 v[160:163], v25 offset:37888
	ds_read_b128 v[164:167], v25 offset:38912
	ds_read_b128 v[174:177], v25 offset:39936
	ds_read_b128 v[178:181], v25 offset:40960
	ds_read_b128 v[182:185], v25 offset:41984
	ds_read_b128 v[198:201], v25 offset:43008
	ds_read_b128 v[202:205], v25 offset:44032
	ds_read_b128 v[206:209], v25 offset:45056
	ds_read_b128 v[210:213], v25 offset:46080
	ds_read_b128 v[214:217], v25 offset:47104
	ds_read_b128 v[224:227], v25 offset:48128
	v_pk_add_f32 v[8:9], v[8:9], v[94:95]
	s_nop 0
	v_pk_add_f32 v[2:3], v[2:3], v[8:9]
	s_waitcnt lgkmcnt(7)
	v_mov_b32_e32 v8, v178
	v_mov_b32_e32 v9, v141
	v_mov_b32_e32 v141, v179
	v_mov_b32_e32 v178, v180
	v_mov_b32_e32 v179, v143
	v_pk_mul_f32 v[94:95], v[82:83], v[8:9]
	v_pk_mul_f32 v[218:219], v[80:81], v[178:179]
	v_mov_b32_e32 v143, v181
	v_pk_fma_f32 v[94:95], v[82:83], v[140:141], v[94:95] op_sel:[0,0,1] op_sel_hi:[1,1,0]
	v_pk_fma_f32 v[180:181], v[80:81], v[142:143], v[218:219] op_sel:[0,0,1] op_sel_hi:[1,1,0]
	v_pk_mul_f32 v[8:9], v[86:87], v[8:9]
	v_pk_add_f32 v[94:95], v[94:95], v[180:181]
	s_waitcnt lgkmcnt(6)
	v_mov_b32_e32 v180, v182
	v_mov_b32_e32 v181, v145
	v_pk_mul_f32 v[218:219], v[90:91], v[180:181]
	v_mov_b32_e32 v145, v183
	v_pk_fma_f32 v[182:183], v[90:91], v[144:145], v[218:219] op_sel:[0,0,1] op_sel_hi:[1,1,0]
	v_mov_b32_e32 v218, v184
	v_mov_b32_e32 v219, v147
	v_pk_mul_f32 v[228:229], v[88:89], v[218:219]
	v_mov_b32_e32 v147, v185
	v_pk_fma_f32 v[184:185], v[88:89], v[146:147], v[228:229] op_sel:[0,0,1] op_sel_hi:[1,1,0]
	v_pk_add_f32 v[94:95], v[94:95], 0 op_sel_hi:[1,0]
	v_pk_add_f32 v[182:183], v[182:183], v[184:185]
	v_pk_fma_f32 v[8:9], v[86:87], v[140:141], v[8:9] op_sel:[0,0,1] op_sel_hi:[1,1,0]
	v_pk_add_f32 v[94:95], v[94:95], v[182:183]
	s_waitcnt lgkmcnt(5)
	v_mov_b32_e32 v182, v198
	v_mov_b32_e32 v183, v149
	v_mov_b32_e32 v149, v199
	v_mov_b32_e32 v198, v200
	v_mov_b32_e32 v199, v151
	v_pk_mul_f32 v[184:185], v[102:103], v[182:183]
	v_pk_mul_f32 v[228:229], v[100:101], v[198:199]
	v_mov_b32_e32 v151, v201
	v_pk_mul_f32 v[140:141], v[84:85], v[178:179]
	v_pk_fma_f32 v[184:185], v[102:103], v[148:149], v[184:185] op_sel:[0,0,1] op_sel_hi:[1,1,0]
	v_pk_fma_f32 v[200:201], v[100:101], v[150:151], v[228:229] op_sel:[0,0,1] op_sel_hi:[1,1,0]
	v_pk_fma_f32 v[140:141], v[84:85], v[142:143], v[140:141] op_sel:[0,0,1] op_sel_hi:[1,1,0]
	v_pk_add_f32 v[184:185], v[184:185], v[200:201]
	v_pk_add_f32 v[8:9], v[8:9], v[140:141]
	v_pk_mul_f32 v[140:141], v[98:99], v[180:181]
	v_pk_mul_f32 v[142:143], v[96:97], v[218:219]
	v_pk_add_f32 v[94:95], v[94:95], v[184:185]
	s_waitcnt lgkmcnt(4)
	v_mov_b32_e32 v184, v202
	v_mov_b32_e32 v185, v153
	v_mov_b32_e32 v153, v203
	v_mov_b32_e32 v202, v204
	v_mov_b32_e32 v203, v155
	v_pk_fma_f32 v[140:141], v[98:99], v[144:145], v[140:141] op_sel:[0,0,1] op_sel_hi:[1,1,0]
	v_pk_fma_f32 v[142:143], v[96:97], v[146:147], v[142:143] op_sel:[0,0,1] op_sel_hi:[1,1,0]
	v_pk_mul_f32 v[200:201], v[110:111], v[184:185]
	v_pk_mul_f32 v[228:229], v[108:109], v[202:203]
	v_mov_b32_e32 v155, v205
	v_pk_add_f32 v[8:9], v[8:9], 0 op_sel_hi:[1,0]
	v_pk_add_f32 v[140:141], v[140:141], v[142:143]
	v_pk_fma_f32 v[200:201], v[110:111], v[152:153], v[200:201] op_sel:[0,0,1] op_sel_hi:[1,1,0]
	v_pk_fma_f32 v[204:205], v[108:109], v[154:155], v[228:229] op_sel:[0,0,1] op_sel_hi:[1,1,0]
	v_pk_add_f32 v[8:9], v[8:9], v[140:141]
	v_pk_mul_f32 v[140:141], v[106:107], v[182:183]
	v_pk_mul_f32 v[142:143], v[104:105], v[198:199]
	v_pk_add_f32 v[200:201], v[200:201], v[204:205]
	v_pk_fma_f32 v[140:141], v[106:107], v[148:149], v[140:141] op_sel:[0,0,1] op_sel_hi:[1,1,0]
	v_pk_fma_f32 v[142:143], v[104:105], v[150:151], v[142:143] op_sel:[0,0,1] op_sel_hi:[1,1,0]
	v_pk_add_f32 v[94:95], v[94:95], v[200:201]
	s_waitcnt lgkmcnt(3)
	v_mov_b32_e32 v200, v206
	v_mov_b32_e32 v201, v157
	v_mov_b32_e32 v157, v207
	v_mov_b32_e32 v206, v208
	v_mov_b32_e32 v207, v159
	v_pk_add_f32 v[140:141], v[140:141], v[142:143]
	v_pk_mul_f32 v[204:205], v[118:119], v[200:201]
	v_pk_mul_f32 v[228:229], v[116:117], v[206:207]
	v_mov_b32_e32 v159, v209
	v_pk_add_f32 v[8:9], v[8:9], v[140:141]
	v_pk_mul_f32 v[140:141], v[114:115], v[184:185]
	v_pk_mul_f32 v[142:143], v[112:113], v[202:203]
	v_pk_fma_f32 v[204:205], v[118:119], v[156:157], v[204:205] op_sel:[0,0,1] op_sel_hi:[1,1,0]
	v_pk_fma_f32 v[208:209], v[116:117], v[158:159], v[228:229] op_sel:[0,0,1] op_sel_hi:[1,1,0]
	v_pk_fma_f32 v[140:141], v[114:115], v[152:153], v[140:141] op_sel:[0,0,1] op_sel_hi:[1,1,0]
	v_pk_fma_f32 v[142:143], v[112:113], v[154:155], v[142:143] op_sel:[0,0,1] op_sel_hi:[1,1,0]
	v_pk_add_f32 v[204:205], v[204:205], v[208:209]
	v_pk_add_f32 v[140:141], v[140:141], v[142:143]
	v_pk_add_f32 v[94:95], v[94:95], v[204:205]
	s_waitcnt lgkmcnt(2)
	v_mov_b32_e32 v204, v210
	v_mov_b32_e32 v205, v161
	v_mov_b32_e32 v161, v211
	v_mov_b32_e32 v210, v212
	v_mov_b32_e32 v211, v163
	v_pk_add_f32 v[8:9], v[8:9], v[140:141]
	v_pk_mul_f32 v[140:141], v[122:123], v[200:201]
	v_pk_mul_f32 v[142:143], v[120:121], v[206:207]
	v_pk_mul_f32 v[208:209], v[126:127], v[204:205]
	v_pk_mul_f32 v[228:229], v[124:125], v[210:211]
	v_mov_b32_e32 v163, v213
	v_pk_fma_f32 v[140:141], v[122:123], v[156:157], v[140:141] op_sel:[0,0,1] op_sel_hi:[1,1,0]
	v_pk_fma_f32 v[142:143], v[120:121], v[158:159], v[142:143] op_sel:[0,0,1] op_sel_hi:[1,1,0]
	v_pk_fma_f32 v[208:209], v[126:127], v[160:161], v[208:209] op_sel:[0,0,1] op_sel_hi:[1,1,0]
	v_pk_fma_f32 v[212:213], v[124:125], v[162:163], v[228:229] op_sel:[0,0,1] op_sel_hi:[1,1,0]
	v_pk_add_f32 v[140:141], v[140:141], v[142:143]
	v_pk_add_f32 v[208:209], v[208:209], v[212:213]
	v_pk_add_f32 v[8:9], v[8:9], v[140:141]
	v_pk_mul_f32 v[140:141], v[130:131], v[204:205]
	v_pk_mul_f32 v[142:143], v[128:129], v[210:211]
	v_pk_add_f32 v[94:95], v[94:95], v[208:209]
	s_waitcnt lgkmcnt(1)
	v_mov_b32_e32 v208, v214
	v_mov_b32_e32 v209, v165
	v_mov_b32_e32 v165, v215
	v_mov_b32_e32 v214, v216
	v_mov_b32_e32 v215, v167
	v_pk_fma_f32 v[140:141], v[130:131], v[160:161], v[140:141] op_sel:[0,0,1] op_sel_hi:[1,1,0]
	v_pk_fma_f32 v[142:143], v[128:129], v[162:163], v[142:143] op_sel:[0,0,1] op_sel_hi:[1,1,0]
	v_pk_mul_f32 v[212:213], v[134:135], v[208:209]
	v_pk_mul_f32 v[228:229], v[132:133], v[214:215]
	v_mov_b32_e32 v167, v217
	v_pk_add_f32 v[140:141], v[140:141], v[142:143]
	v_pk_fma_f32 v[212:213], v[134:135], v[164:165], v[212:213] op_sel:[0,0,1] op_sel_hi:[1,1,0]
	v_pk_fma_f32 v[216:217], v[132:133], v[166:167], v[228:229] op_sel:[0,0,1] op_sel_hi:[1,1,0]
	v_pk_add_f32 v[8:9], v[8:9], v[140:141]
	v_pk_mul_f32 v[140:141], v[138:139], v[208:209]
	v_pk_mul_f32 v[142:143], v[136:137], v[214:215]
	v_pk_add_f32 v[212:213], v[212:213], v[216:217]
	v_pk_fma_f32 v[140:141], v[138:139], v[164:165], v[140:141] op_sel:[0,0,1] op_sel_hi:[1,1,0]
	v_pk_fma_f32 v[142:143], v[136:137], v[166:167], v[142:143] op_sel:[0,0,1] op_sel_hi:[1,1,0]
	v_pk_add_f32 v[94:95], v[94:95], v[212:213]
	s_waitcnt lgkmcnt(0)
	v_mov_b32_e32 v212, v224
	v_mov_b32_e32 v213, v175
	v_mov_b32_e32 v175, v225
	v_mov_b32_e32 v224, v226
	v_mov_b32_e32 v225, v177
	v_pk_add_f32 v[140:141], v[140:141], v[142:143]
	v_pk_mul_f32 v[216:217], v[6:7], v[212:213]
	v_pk_mul_f32 v[228:229], v[4:5], v[224:225]
	v_mov_b32_e32 v177, v227
	v_pk_add_f32 v[8:9], v[8:9], v[140:141]
	v_pk_mul_f32 v[140:141], v[12:13], v[212:213]
	v_pk_mul_f32 v[142:143], v[10:11], v[224:225]
	v_pk_fma_f32 v[216:217], v[6:7], v[174:175], v[216:217] op_sel:[0,0,1] op_sel_hi:[1,1,0]
	v_pk_fma_f32 v[226:227], v[4:5], v[176:177], v[228:229] op_sel:[0,0,1] op_sel_hi:[1,1,0]
	v_pk_fma_f32 v[140:141], v[12:13], v[174:175], v[140:141] op_sel:[0,0,1] op_sel_hi:[1,1,0]
	v_pk_fma_f32 v[142:143], v[10:11], v[176:177], v[142:143] op_sel:[0,0,1] op_sel_hi:[1,1,0]
	v_pk_add_f32 v[216:217], v[216:217], v[226:227]
	v_pk_add_f32 v[140:141], v[140:141], v[142:143]
	v_pk_add_f32 v[94:95], v[94:95], v[216:217]
	v_pk_add_f32 v[8:9], v[8:9], v[140:141]
	ds_read_b128 v[140:143], v25 offset:49152
	ds_read_b128 v[144:147], v25 offset:50176
	ds_read_b128 v[148:151], v25 offset:51200
	ds_read_b128 v[152:155], v25 offset:52224
	ds_read_b128 v[156:159], v25 offset:53248
	ds_read_b128 v[160:163], v25 offset:54272
	ds_read_b128 v[164:167], v25 offset:55296
	ds_read_b128 v[174:177], v25 offset:56320
	ds_read_b128 v[178:181], v25 offset:57344
	ds_read_b128 v[182:185], v25 offset:58368
	ds_read_b128 v[198:201], v25 offset:59392
	ds_read_b128 v[202:205], v25 offset:60416
	ds_read_b128 v[206:209], v25 offset:61440
	ds_read_b128 v[210:213], v25 offset:62464
	ds_read_b128 v[214:217], v25 offset:63488
	ds_read_b128 v[224:227], v25 offset:64512
	s_waitcnt lgkmcnt(7)
	v_mov_b32_e32 v218, v178
	v_mov_b32_e32 v219, v141
	v_pk_mul_f32 v[228:229], v[82:83], v[218:219]
	v_mov_b32_e32 v141, v179
	v_mov_b32_e32 v178, v180
	v_mov_b32_e32 v179, v143
	v_pk_fma_f32 v[82:83], v[82:83], v[140:141], v[228:229] op_sel:[0,0,1] op_sel_hi:[1,1,0]
	v_pk_mul_f32 v[228:229], v[80:81], v[178:179]
	v_mov_b32_e32 v143, v181
	v_pk_fma_f32 v[80:81], v[80:81], v[142:143], v[228:229] op_sel:[0,0,1] op_sel_hi:[1,1,0]
	s_nop 0
	v_pk_add_f32 v[80:81], v[82:83], v[80:81]
	s_waitcnt lgkmcnt(6)
	v_mov_b32_e32 v82, v182
	v_mov_b32_e32 v83, v145
	v_pk_mul_f32 v[180:181], v[90:91], v[82:83]
	v_mov_b32_e32 v145, v183
	v_pk_fma_f32 v[90:91], v[90:91], v[144:145], v[180:181] op_sel:[0,0,1] op_sel_hi:[1,1,0]
	v_mov_b32_e32 v180, v184
	v_mov_b32_e32 v181, v147
	v_pk_mul_f32 v[182:183], v[88:89], v[180:181]
	v_mov_b32_e32 v147, v185
	v_pk_fma_f32 v[88:89], v[88:89], v[146:147], v[182:183] op_sel:[0,0,1] op_sel_hi:[1,1,0]
	v_pk_add_f32 v[80:81], v[80:81], 0 op_sel_hi:[1,0]
	v_pk_add_f32 v[88:89], v[90:91], v[88:89]
	s_nop 0
	v_pk_add_f32 v[80:81], v[80:81], v[88:89]
	s_waitcnt lgkmcnt(5)
	v_mov_b32_e32 v88, v198
	v_mov_b32_e32 v89, v149
	v_pk_mul_f32 v[90:91], v[102:103], v[88:89]
	v_mov_b32_e32 v149, v199
	v_pk_fma_f32 v[90:91], v[102:103], v[148:149], v[90:91] op_sel:[0,0,1] op_sel_hi:[1,1,0]
	v_mov_b32_e32 v102, v200
	v_mov_b32_e32 v103, v151
	v_pk_mul_f32 v[182:183], v[100:101], v[102:103]
	v_mov_b32_e32 v151, v201
	v_pk_fma_f32 v[100:101], v[100:101], v[150:151], v[182:183] op_sel:[0,0,1] op_sel_hi:[1,1,0]
	s_nop 0
	v_pk_add_f32 v[90:91], v[90:91], v[100:101]
	s_nop 0
	v_pk_add_f32 v[80:81], v[80:81], v[90:91]
	s_waitcnt lgkmcnt(4)
	v_mov_b32_e32 v90, v202
	v_mov_b32_e32 v91, v153
	v_pk_mul_f32 v[100:101], v[110:111], v[90:91]
	v_mov_b32_e32 v153, v203
	v_pk_fma_f32 v[100:101], v[110:111], v[152:153], v[100:101] op_sel:[0,0,1] op_sel_hi:[1,1,0]
	v_mov_b32_e32 v110, v204
	v_mov_b32_e32 v111, v155
	v_pk_mul_f32 v[182:183], v[108:109], v[110:111]
	v_mov_b32_e32 v155, v205
	v_pk_fma_f32 v[108:109], v[108:109], v[154:155], v[182:183] op_sel:[0,0,1] op_sel_hi:[1,1,0]
	s_nop 0
	v_pk_add_f32 v[100:101], v[100:101], v[108:109]
	s_nop 0
	v_pk_add_f32 v[80:81], v[80:81], v[100:101]
	s_waitcnt lgkmcnt(3)
	v_mov_b32_e32 v100, v206
	v_mov_b32_e32 v101, v157
	v_pk_mul_f32 v[108:109], v[118:119], v[100:101]
	v_mov_b32_e32 v157, v207
	v_pk_fma_f32 v[108:109], v[118:119], v[156:157], v[108:109] op_sel:[0,0,1] op_sel_hi:[1,1,0]
	v_mov_b32_e32 v118, v208
	v_mov_b32_e32 v119, v159
	v_pk_mul_f32 v[182:183], v[116:117], v[118:119]
	v_mov_b32_e32 v159, v209
	v_pk_fma_f32 v[116:117], v[116:117], v[158:159], v[182:183] op_sel:[0,0,1] op_sel_hi:[1,1,0]
	s_nop 0
	v_pk_add_f32 v[108:109], v[108:109], v[116:117]
	s_nop 0
	v_pk_add_f32 v[80:81], v[80:81], v[108:109]
	s_waitcnt lgkmcnt(2)
	v_mov_b32_e32 v108, v210
	v_mov_b32_e32 v109, v161
	v_pk_mul_f32 v[116:117], v[126:127], v[108:109]
	v_mov_b32_e32 v161, v211
	v_pk_fma_f32 v[116:117], v[126:127], v[160:161], v[116:117] op_sel:[0,0,1] op_sel_hi:[1,1,0]
	v_mov_b32_e32 v126, v212
	v_mov_b32_e32 v127, v163
	v_pk_mul_f32 v[182:183], v[124:125], v[126:127]
	v_mov_b32_e32 v163, v213
	v_pk_fma_f32 v[124:125], v[124:125], v[162:163], v[182:183] op_sel:[0,0,1] op_sel_hi:[1,1,0]
	s_nop 0
	v_pk_add_f32 v[116:117], v[116:117], v[124:125]
	s_nop 0
	v_pk_add_f32 v[80:81], v[80:81], v[116:117]
	s_waitcnt lgkmcnt(1)
	v_mov_b32_e32 v116, v214
	v_mov_b32_e32 v117, v165
	v_pk_mul_f32 v[124:125], v[134:135], v[116:117]
	v_mov_b32_e32 v165, v215
	v_pk_fma_f32 v[124:125], v[134:135], v[164:165], v[124:125] op_sel:[0,0,1] op_sel_hi:[1,1,0]
	v_mov_b32_e32 v134, v216
	v_mov_b32_e32 v135, v167
	v_pk_mul_f32 v[182:183], v[132:133], v[134:135]
	v_mov_b32_e32 v167, v217
	v_pk_fma_f32 v[132:133], v[132:133], v[166:167], v[182:183] op_sel:[0,0,1] op_sel_hi:[1,1,0]
	s_nop 0
	v_pk_add_f32 v[124:125], v[124:125], v[132:133]
	s_nop 0
	v_pk_add_f32 v[80:81], v[80:81], v[124:125]
	s_waitcnt lgkmcnt(0)
	v_mov_b32_e32 v124, v224
	v_mov_b32_e32 v125, v175
	v_pk_mul_f32 v[132:133], v[6:7], v[124:125]
	v_mov_b32_e32 v175, v225
	v_pk_fma_f32 v[6:7], v[6:7], v[174:175], v[132:133] op_sel:[0,0,1] op_sel_hi:[1,1,0]
	v_mov_b32_e32 v132, v226
	v_mov_b32_e32 v133, v177
	v_pk_mul_f32 v[182:183], v[4:5], v[132:133]
	v_mov_b32_e32 v177, v227
	v_pk_fma_f32 v[4:5], v[4:5], v[176:177], v[182:183] op_sel:[0,0,1] op_sel_hi:[1,1,0]
	s_nop 0
	v_pk_add_f32 v[4:5], v[6:7], v[4:5]
	s_nop 0
	v_pk_add_f32 v[6:7], v[80:81], v[4:5]
	v_pk_mul_f32 v[4:5], v[86:87], v[218:219]
	v_pk_mul_f32 v[80:81], v[84:85], v[178:179]
	v_pk_fma_f32 v[4:5], v[86:87], v[140:141], v[4:5] op_sel:[0,0,1] op_sel_hi:[1,1,0]
	v_pk_fma_f32 v[80:81], v[84:85], v[142:143], v[80:81] op_sel:[0,0,1] op_sel_hi:[1,1,0]
	s_nop 0
	v_pk_add_f32 v[4:5], v[4:5], v[80:81]
	v_pk_mul_f32 v[80:81], v[98:99], v[82:83]
	v_pk_mul_f32 v[82:83], v[96:97], v[180:181]
	v_pk_fma_f32 v[80:81], v[98:99], v[144:145], v[80:81] op_sel:[0,0,1] op_sel_hi:[1,1,0]
	v_pk_fma_f32 v[82:83], v[96:97], v[146:147], v[82:83] op_sel:[0,0,1] op_sel_hi:[1,1,0]
	v_pk_add_f32 v[4:5], v[4:5], 0 op_sel_hi:[1,0]
	v_pk_add_f32 v[80:81], v[80:81], v[82:83]
	v_pk_mul_f32 v[82:83], v[104:105], v[102:103]
	v_pk_add_f32 v[4:5], v[4:5], v[80:81]
	v_pk_mul_f32 v[80:81], v[106:107], v[88:89]
	v_pk_fma_f32 v[82:83], v[104:105], v[150:151], v[82:83] op_sel:[0,0,1] op_sel_hi:[1,1,0]
	v_pk_fma_f32 v[80:81], v[106:107], v[148:149], v[80:81] op_sel:[0,0,1] op_sel_hi:[1,1,0]
	s_nop 0
	v_pk_add_f32 v[80:81], v[80:81], v[82:83]
	v_pk_mul_f32 v[82:83], v[112:113], v[110:111]
	v_pk_add_f32 v[4:5], v[4:5], v[80:81]
	v_pk_mul_f32 v[80:81], v[114:115], v[90:91]
	v_pk_fma_f32 v[82:83], v[112:113], v[154:155], v[82:83] op_sel:[0,0,1] op_sel_hi:[1,1,0]
	v_pk_fma_f32 v[80:81], v[114:115], v[152:153], v[80:81] op_sel:[0,0,1] op_sel_hi:[1,1,0]
	s_nop 0
	v_pk_add_f32 v[80:81], v[80:81], v[82:83]
	v_pk_mul_f32 v[82:83], v[120:121], v[118:119]
	v_pk_add_f32 v[4:5], v[4:5], v[80:81]
	v_pk_mul_f32 v[80:81], v[122:123], v[100:101]
	v_pk_fma_f32 v[82:83], v[120:121], v[158:159], v[82:83] op_sel:[0,0,1] op_sel_hi:[1,1,0]
	v_pk_fma_f32 v[80:81], v[122:123], v[156:157], v[80:81] op_sel:[0,0,1] op_sel_hi:[1,1,0]
	s_nop 0
	v_pk_add_f32 v[80:81], v[80:81], v[82:83]
	v_pk_mul_f32 v[82:83], v[128:129], v[126:127]
	v_pk_add_f32 v[4:5], v[4:5], v[80:81]
	v_pk_mul_f32 v[80:81], v[130:131], v[108:109]
	v_pk_fma_f32 v[82:83], v[128:129], v[162:163], v[82:83] op_sel:[0,0,1] op_sel_hi:[1,1,0]
	v_pk_fma_f32 v[80:81], v[130:131], v[160:161], v[80:81] op_sel:[0,0,1] op_sel_hi:[1,1,0]
	s_nop 0
	v_pk_add_f32 v[80:81], v[80:81], v[82:83]
	v_pk_mul_f32 v[82:83], v[136:137], v[134:135]
	v_pk_add_f32 v[4:5], v[4:5], v[80:81]
	v_pk_mul_f32 v[80:81], v[138:139], v[116:117]
	v_pk_fma_f32 v[82:83], v[136:137], v[166:167], v[82:83] op_sel:[0,0,1] op_sel_hi:[1,1,0]
	v_pk_fma_f32 v[80:81], v[138:139], v[164:165], v[80:81] op_sel:[0,0,1] op_sel_hi:[1,1,0]
	s_nop 0
	v_pk_add_f32 v[80:81], v[80:81], v[82:83]
	s_nop 0
	v_pk_add_f32 v[4:5], v[4:5], v[80:81]
	v_pk_mul_f32 v[80:81], v[12:13], v[124:125]
	s_nop 0
	v_pk_fma_f32 v[12:13], v[12:13], v[174:175], v[80:81] op_sel:[0,0,1] op_sel_hi:[1,1,0]
	v_pk_mul_f32 v[80:81], v[10:11], v[132:133]
	s_nop 0
	v_pk_fma_f32 v[10:11], v[10:11], v[176:177], v[80:81] op_sel:[0,0,1] op_sel_hi:[1,1,0]
	s_nop 0
	v_pk_add_f32 v[10:11], v[12:13], v[10:11]
	s_nop 0
	v_pk_add_f32 v[4:5], v[4:5], v[10:11]
	v_cndmask_b32_e64 v10, v14, v15, s[46:47]
	v_cmp_eq_u32_e64 s[46:47], 2, v20
	s_nop 1
	v_cndmask_b32_e64 v10, v10, v92, s[46:47]
	v_cmp_eq_u32_e64 s[46:47], 3, v20
	s_nop 1
	v_cndmask_b32_e64 v10, v10, v93, s[46:47]
	v_cmp_eq_u32_e64 s[46:47], 4, v20
	s_nop 1
	v_cndmask_b32_e64 v10, v10, v94, s[46:47]
	v_cmp_eq_u32_e64 s[46:47], 5, v20
	s_nop 1
	v_cndmask_b32_e64 v10, v10, v95, s[46:47]
	v_cmp_eq_u32_e64 s[46:47], 6, v20
	s_nop 1
	v_cndmask_b32_e64 v10, v10, v6, s[46:47]
	v_cmp_eq_u32_e64 s[46:47], 7, v20
	s_nop 1
	v_cndmask_b32_e64 v10, v10, v7, s[46:47]
	v_cmp_eq_u32_e64 s[46:47], 8, v20
	s_nop 1
	v_cndmask_b32_e64 v10, v10, v0, s[46:47]
	v_cmp_eq_u32_e64 s[46:47], 9, v20
	s_nop 1
	v_cndmask_b32_e64 v10, v10, v1, s[46:47]
	v_cmp_eq_u32_e64 s[46:47], 10, v20
	s_nop 1
	v_cndmask_b32_e64 v10, v10, v2, s[46:47]
	v_cmp_eq_u32_e64 s[46:47], 11, v20
	s_nop 1
	v_cndmask_b32_e64 v10, v10, v3, s[46:47]
	v_cmp_eq_u32_e64 s[46:47], 12, v20
	s_nop 1
	v_cndmask_b32_e64 v10, v10, v8, s[46:47]
	v_cmp_eq_u32_e64 s[46:47], 13, v20
	s_nop 1
	v_cndmask_b32_e64 v10, v10, v9, s[46:47]
	v_cmp_eq_u32_e64 s[46:47], 14, v20
	s_nop 1
	v_cndmask_b32_e64 v10, v10, v4, s[46:47]
	v_cmp_eq_u32_e64 s[46:47], 15, v20
	s_nop 1
	v_cndmask_b32_e64 v10, v10, v5, s[46:47]
	v_cmp_eq_u32_e64 s[46:47], 1, v22
	ds_bpermute_b32 v10, v39, v10
	s_nop 0
	v_cndmask_b32_e64 v11, v14, v15, s[46:47]
	v_cmp_eq_u32_e64 s[46:47], 2, v22
	s_nop 1
	v_cndmask_b32_e64 v11, v11, v92, s[46:47]
	v_cmp_eq_u32_e64 s[46:47], 3, v22
	s_nop 1
	v_cndmask_b32_e64 v11, v11, v93, s[46:47]
	v_cmp_eq_u32_e64 s[46:47], 4, v22
	s_nop 1
	v_cndmask_b32_e64 v11, v11, v94, s[46:47]
	v_cmp_eq_u32_e64 s[46:47], 5, v22
	s_nop 1
	v_cndmask_b32_e64 v11, v11, v95, s[46:47]
	v_cmp_eq_u32_e64 s[46:47], 6, v22
	s_nop 1
	v_cndmask_b32_e64 v11, v11, v6, s[46:47]
	v_cmp_eq_u32_e64 s[46:47], 7, v22
	s_nop 1
	v_cndmask_b32_e64 v11, v11, v7, s[46:47]
	v_cmp_eq_u32_e64 s[46:47], 8, v22
	s_nop 1
	v_cndmask_b32_e64 v11, v11, v0, s[46:47]
	v_cmp_eq_u32_e64 s[46:47], 9, v22
	s_nop 1
	v_cndmask_b32_e64 v11, v11, v1, s[46:47]
	v_cmp_eq_u32_e64 s[46:47], 10, v22
	s_nop 1
	v_cndmask_b32_e64 v11, v11, v2, s[46:47]
	v_cmp_eq_u32_e64 s[46:47], 11, v22
	s_nop 1
	v_cndmask_b32_e64 v11, v11, v3, s[46:47]
	v_cmp_eq_u32_e64 s[46:47], 12, v22
	s_nop 1
	v_cndmask_b32_e64 v11, v11, v8, s[46:47]
	v_cmp_eq_u32_e64 s[46:47], 13, v22
	s_nop 1
	v_cndmask_b32_e64 v11, v11, v9, s[46:47]
	v_cmp_eq_u32_e64 s[46:47], 14, v22
	s_nop 1
	v_cndmask_b32_e64 v11, v11, v4, s[46:47]
	v_cmp_eq_u32_e64 s[46:47], 15, v22
	s_nop 1
	v_cndmask_b32_e64 v11, v11, v5, s[46:47]
	s_waitcnt lgkmcnt(0)
	v_add_f32_e32 v12, v11, v10
	v_cmp_eq_u32_e64 s[46:47], 1, v24
	s_nop 1
	v_cndmask_b32_e64 v10, v12, v15, s[46:47]
	v_cmp_eq_u32_e64 s[46:47], 2, v24
	s_nop 1
	v_cndmask_b32_e64 v10, v10, v92, s[46:47]
	v_cmp_eq_u32_e64 s[46:47], 3, v24
	s_nop 1
	v_cndmask_b32_e64 v10, v10, v93, s[46:47]
	v_cmp_eq_u32_e64 s[46:47], 4, v24
	s_nop 1
	v_cndmask_b32_e64 v10, v10, v94, s[46:47]
	v_cmp_eq_u32_e64 s[46:47], 5, v24
	s_nop 1
	v_cndmask_b32_e64 v10, v10, v95, s[46:47]
	v_cmp_eq_u32_e64 s[46:47], 6, v24
	s_nop 1
	v_cndmask_b32_e64 v10, v10, v6, s[46:47]
	v_cmp_eq_u32_e64 s[46:47], 7, v24
	s_nop 1
	v_cndmask_b32_e64 v10, v10, v7, s[46:47]
	v_cmp_eq_u32_e64 s[46:47], 8, v24
	s_nop 1
	v_cndmask_b32_e64 v10, v10, v0, s[46:47]
	v_cmp_eq_u32_e64 s[46:47], 9, v24
	s_nop 1
	v_cndmask_b32_e64 v10, v10, v1, s[46:47]
	v_cmp_eq_u32_e64 s[46:47], 10, v24
	s_nop 1
	v_cndmask_b32_e64 v10, v10, v2, s[46:47]
	v_cmp_eq_u32_e64 s[46:47], 11, v24
	s_nop 1
	v_cndmask_b32_e64 v10, v10, v3, s[46:47]
	v_cmp_eq_u32_e64 s[46:47], 12, v24
	s_nop 1
	v_cndmask_b32_e64 v10, v10, v8, s[46:47]
	v_cmp_eq_u32_e64 s[46:47], 13, v24
	s_nop 1
	v_cndmask_b32_e64 v10, v10, v9, s[46:47]
	v_cmp_eq_u32_e64 s[46:47], 14, v24
	s_nop 1
	v_cndmask_b32_e64 v10, v10, v4, s[46:47]
	v_cmp_eq_u32_e64 s[46:47], 15, v24
	s_nop 1
	v_cndmask_b32_e64 v10, v10, v5, s[46:47]
	v_cmp_eq_u32_e64 s[46:47], 1, v26
	ds_bpermute_b32 v10, v39, v10
	s_nop 0
	v_cndmask_b32_e64 v11, v12, v15, s[46:47]
	v_cmp_eq_u32_e64 s[46:47], 2, v26
	s_nop 1
	v_cndmask_b32_e64 v11, v11, v92, s[46:47]
	v_cmp_eq_u32_e64 s[46:47], 3, v26
	s_nop 1
	v_cndmask_b32_e64 v11, v11, v93, s[46:47]
	v_cmp_eq_u32_e64 s[46:47], 4, v26
	s_nop 1
	v_cndmask_b32_e64 v11, v11, v94, s[46:47]
	v_cmp_eq_u32_e64 s[46:47], 5, v26
	s_nop 1
	v_cndmask_b32_e64 v11, v11, v95, s[46:47]
	v_cmp_eq_u32_e64 s[46:47], 6, v26
	s_nop 1
	v_cndmask_b32_e64 v11, v11, v6, s[46:47]
	v_cmp_eq_u32_e64 s[46:47], 7, v26
	s_nop 1
	v_cndmask_b32_e64 v11, v11, v7, s[46:47]
	v_cmp_eq_u32_e64 s[46:47], 8, v26
	s_nop 1
	v_cndmask_b32_e64 v11, v11, v0, s[46:47]
	v_cmp_eq_u32_e64 s[46:47], 9, v26
	s_nop 1
	v_cndmask_b32_e64 v11, v11, v1, s[46:47]
	v_cmp_eq_u32_e64 s[46:47], 10, v26
	s_nop 1
	v_cndmask_b32_e64 v11, v11, v2, s[46:47]
	v_cmp_eq_u32_e64 s[46:47], 11, v26
	s_nop 1
	v_cndmask_b32_e64 v11, v11, v3, s[46:47]
	v_cmp_eq_u32_e64 s[46:47], 12, v26
	s_nop 1
	v_cndmask_b32_e64 v11, v11, v8, s[46:47]
	v_cmp_eq_u32_e64 s[46:47], 13, v26
	s_nop 1
	v_cndmask_b32_e64 v11, v11, v9, s[46:47]
	v_cmp_eq_u32_e64 s[46:47], 14, v26
	s_nop 1
	v_cndmask_b32_e64 v11, v11, v4, s[46:47]
	v_cmp_eq_u32_e64 s[46:47], 15, v26
	s_nop 1
	v_cndmask_b32_e64 v11, v11, v5, s[46:47]
	s_waitcnt lgkmcnt(0)
	v_add_f32_e32 v13, v11, v10
	v_cmp_eq_u32_e64 s[46:47], 1, v28
	s_nop 1
	v_cndmask_b32_e64 v10, v12, v13, s[46:47]
	v_cmp_eq_u32_e64 s[46:47], 2, v28
	s_nop 1
	v_cndmask_b32_e64 v10, v10, v92, s[46:47]
	v_cmp_eq_u32_e64 s[46:47], 3, v28
	s_nop 1
	v_cndmask_b32_e64 v10, v10, v93, s[46:47]
	v_cmp_eq_u32_e64 s[46:47], 4, v28
	s_nop 1
	v_cndmask_b32_e64 v10, v10, v94, s[46:47]
	v_cmp_eq_u32_e64 s[46:47], 5, v28
	s_nop 1
	v_cndmask_b32_e64 v10, v10, v95, s[46:47]
	v_cmp_eq_u32_e64 s[46:47], 6, v28
	s_nop 1
	v_cndmask_b32_e64 v10, v10, v6, s[46:47]
	v_cmp_eq_u32_e64 s[46:47], 7, v28
	s_nop 1
	v_cndmask_b32_e64 v10, v10, v7, s[46:47]
	v_cmp_eq_u32_e64 s[46:47], 8, v28
	s_nop 1
	v_cndmask_b32_e64 v10, v10, v0, s[46:47]
	v_cmp_eq_u32_e64 s[46:47], 9, v28
	s_nop 1
	v_cndmask_b32_e64 v10, v10, v1, s[46:47]
	v_cmp_eq_u32_e64 s[46:47], 10, v28
	s_nop 1
	v_cndmask_b32_e64 v10, v10, v2, s[46:47]
	v_cmp_eq_u32_e64 s[46:47], 11, v28
	s_nop 1
	v_cndmask_b32_e64 v10, v10, v3, s[46:47]
	v_cmp_eq_u32_e64 s[46:47], 12, v28
	s_nop 1
	v_cndmask_b32_e64 v10, v10, v8, s[46:47]
	v_cmp_eq_u32_e64 s[46:47], 13, v28
	s_nop 1
	v_cndmask_b32_e64 v10, v10, v9, s[46:47]
	v_cmp_eq_u32_e64 s[46:47], 14, v28
	s_nop 1
	v_cndmask_b32_e64 v10, v10, v4, s[46:47]
	v_cmp_eq_u32_e64 s[46:47], 15, v28
	s_nop 1
	v_cndmask_b32_e64 v10, v10, v5, s[46:47]
	v_cmp_eq_u32_e64 s[46:47], 1, v30
	ds_bpermute_b32 v10, v39, v10
	s_nop 0
	v_cndmask_b32_e64 v11, v12, v13, s[46:47]
	v_cmp_eq_u32_e64 s[46:47], 2, v30
	s_nop 1
	v_cndmask_b32_e64 v11, v11, v92, s[46:47]
	v_cmp_eq_u32_e64 s[46:47], 3, v30
	s_nop 1
	v_cndmask_b32_e64 v11, v11, v93, s[46:47]
	v_cmp_eq_u32_e64 s[46:47], 4, v30
	s_nop 1
	v_cndmask_b32_e64 v11, v11, v94, s[46:47]
	v_cmp_eq_u32_e64 s[46:47], 5, v30
	s_nop 1
	v_cndmask_b32_e64 v11, v11, v95, s[46:47]
	v_cmp_eq_u32_e64 s[46:47], 6, v30
	s_nop 1
	v_cndmask_b32_e64 v11, v11, v6, s[46:47]
	v_cmp_eq_u32_e64 s[46:47], 7, v30
	s_nop 1
	v_cndmask_b32_e64 v11, v11, v7, s[46:47]
	v_cmp_eq_u32_e64 s[46:47], 8, v30
	s_nop 1
	v_cndmask_b32_e64 v11, v11, v0, s[46:47]
	v_cmp_eq_u32_e64 s[46:47], 9, v30
	s_nop 1
	v_cndmask_b32_e64 v11, v11, v1, s[46:47]
	v_cmp_eq_u32_e64 s[46:47], 10, v30
	s_nop 1
	v_cndmask_b32_e64 v11, v11, v2, s[46:47]
	v_cmp_eq_u32_e64 s[46:47], 11, v30
	s_nop 1
	v_cndmask_b32_e64 v11, v11, v3, s[46:47]
	v_cmp_eq_u32_e64 s[46:47], 12, v30
	s_nop 1
	v_cndmask_b32_e64 v11, v11, v8, s[46:47]
	v_cmp_eq_u32_e64 s[46:47], 13, v30
	s_nop 1
	v_cndmask_b32_e64 v11, v11, v9, s[46:47]
	v_cmp_eq_u32_e64 s[46:47], 14, v30
	s_nop 1
	v_cndmask_b32_e64 v11, v11, v4, s[46:47]
	v_cmp_eq_u32_e64 s[46:47], 15, v30
	s_nop 1
	v_cndmask_b32_e64 v11, v11, v5, s[46:47]
	v_cmp_eq_u32_e64 s[46:47], 1, v32
	s_waitcnt lgkmcnt(0)
	v_add_f32_e32 v14, v11, v10
	v_cndmask_b32_e64 v10, v12, v13, s[46:47]
	v_cmp_eq_u32_e64 s[46:47], 2, v32
	s_nop 1
	v_cndmask_b32_e64 v10, v10, v14, s[46:47]
	v_cmp_eq_u32_e64 s[46:47], 3, v32
	s_nop 1
	v_cndmask_b32_e64 v10, v10, v93, s[46:47]
	v_cmp_eq_u32_e64 s[46:47], 4, v32
	s_nop 1
	v_cndmask_b32_e64 v10, v10, v94, s[46:47]
	v_cmp_eq_u32_e64 s[46:47], 5, v32
	s_nop 1
	v_cndmask_b32_e64 v10, v10, v95, s[46:47]
	v_cmp_eq_u32_e64 s[46:47], 6, v32
	s_nop 1
	v_cndmask_b32_e64 v10, v10, v6, s[46:47]
	v_cmp_eq_u32_e64 s[46:47], 7, v32
	s_nop 1
	v_cndmask_b32_e64 v10, v10, v7, s[46:47]
	v_cmp_eq_u32_e64 s[46:47], 8, v32
	s_nop 1
	v_cndmask_b32_e64 v10, v10, v0, s[46:47]
	v_cmp_eq_u32_e64 s[46:47], 9, v32
	s_nop 1
	v_cndmask_b32_e64 v10, v10, v1, s[46:47]
	v_cmp_eq_u32_e64 s[46:47], 10, v32
	s_nop 1
	v_cndmask_b32_e64 v10, v10, v2, s[46:47]
	v_cmp_eq_u32_e64 s[46:47], 11, v32
	s_nop 1
	v_cndmask_b32_e64 v10, v10, v3, s[46:47]
	v_cmp_eq_u32_e64 s[46:47], 12, v32
	s_nop 1
	v_cndmask_b32_e64 v10, v10, v8, s[46:47]
	v_cmp_eq_u32_e64 s[46:47], 13, v32
	s_nop 1
	v_cndmask_b32_e64 v10, v10, v9, s[46:47]
	v_cmp_eq_u32_e64 s[46:47], 14, v32
	s_nop 1
	v_cndmask_b32_e64 v10, v10, v4, s[46:47]
	v_cmp_eq_u32_e64 s[46:47], 15, v32
	s_nop 1
	v_cndmask_b32_e64 v10, v10, v5, s[46:47]
	v_cmp_eq_u32_e64 s[46:47], 1, v34
	ds_bpermute_b32 v10, v39, v10
	s_nop 0
	v_cndmask_b32_e64 v11, v12, v13, s[46:47]
	v_cmp_eq_u32_e64 s[46:47], 2, v34
	s_nop 1
	v_cndmask_b32_e64 v11, v11, v14, s[46:47]
	v_cmp_eq_u32_e64 s[46:47], 3, v34
	s_nop 1
	v_cndmask_b32_e64 v11, v11, v93, s[46:47]
	v_cmp_eq_u32_e64 s[46:47], 4, v34
	s_nop 1
	v_cndmask_b32_e64 v11, v11, v94, s[46:47]
	v_cmp_eq_u32_e64 s[46:47], 5, v34
	s_nop 1
	v_cndmask_b32_e64 v11, v11, v95, s[46:47]
	v_cmp_eq_u32_e64 s[46:47], 6, v34
	s_nop 1
	v_cndmask_b32_e64 v11, v11, v6, s[46:47]
	v_cmp_eq_u32_e64 s[46:47], 7, v34
	s_nop 1
	v_cndmask_b32_e64 v11, v11, v7, s[46:47]
	v_cmp_eq_u32_e64 s[46:47], 8, v34
	s_nop 1
	v_cndmask_b32_e64 v11, v11, v0, s[46:47]
	v_cmp_eq_u32_e64 s[46:47], 9, v34
	s_nop 1
	v_cndmask_b32_e64 v11, v11, v1, s[46:47]
	v_cmp_eq_u32_e64 s[46:47], 10, v34
	s_nop 1
	v_cndmask_b32_e64 v11, v11, v2, s[46:47]
	v_cmp_eq_u32_e64 s[46:47], 11, v34
	s_nop 1
	v_cndmask_b32_e64 v11, v11, v3, s[46:47]
	v_cmp_eq_u32_e64 s[46:47], 12, v34
	s_nop 1
	v_cndmask_b32_e64 v11, v11, v8, s[46:47]
	v_cmp_eq_u32_e64 s[46:47], 13, v34
	s_nop 1
	v_cndmask_b32_e64 v11, v11, v9, s[46:47]
	v_cmp_eq_u32_e64 s[46:47], 14, v34
	s_nop 1
	v_cndmask_b32_e64 v11, v11, v4, s[46:47]
	v_cmp_eq_u32_e64 s[46:47], 15, v34
	s_nop 1
	v_cndmask_b32_e64 v11, v11, v5, s[46:47]
	v_cmp_eq_u32_e64 s[46:47], 1, v36
	s_waitcnt lgkmcnt(0)
	v_add_f32_e32 v15, v11, v10
	v_cndmask_b32_e64 v10, v12, v13, s[46:47]
	v_cmp_eq_u32_e64 s[46:47], 2, v36
	s_nop 1
	v_cndmask_b32_e64 v10, v10, v14, s[46:47]
	v_cmp_eq_u32_e64 s[46:47], 3, v36
	s_nop 1
	v_cndmask_b32_e64 v10, v10, v15, s[46:47]
	v_cmp_eq_u32_e64 s[46:47], 4, v36
	s_nop 1
	v_cndmask_b32_e64 v10, v10, v94, s[46:47]
	v_cmp_eq_u32_e64 s[46:47], 5, v36
	s_nop 1
	v_cndmask_b32_e64 v10, v10, v95, s[46:47]
	v_cmp_eq_u32_e64 s[46:47], 6, v36
	s_nop 1
	v_cndmask_b32_e64 v10, v10, v6, s[46:47]
	v_cmp_eq_u32_e64 s[46:47], 7, v36
	s_nop 1
	v_cndmask_b32_e64 v10, v10, v7, s[46:47]
	v_cmp_eq_u32_e64 s[46:47], 8, v36
	s_nop 1
	v_cndmask_b32_e64 v10, v10, v0, s[46:47]
	v_cmp_eq_u32_e64 s[46:47], 9, v36
	s_nop 1
	v_cndmask_b32_e64 v10, v10, v1, s[46:47]
	v_cmp_eq_u32_e64 s[46:47], 10, v36
	s_nop 1
	v_cndmask_b32_e64 v10, v10, v2, s[46:47]
	v_cmp_eq_u32_e64 s[46:47], 11, v36
	s_nop 1
	v_cndmask_b32_e64 v10, v10, v3, s[46:47]
	v_cmp_eq_u32_e64 s[46:47], 12, v36
	s_nop 1
	v_cndmask_b32_e64 v10, v10, v8, s[46:47]
	v_cmp_eq_u32_e64 s[46:47], 13, v36
	s_nop 1
	v_cndmask_b32_e64 v10, v10, v9, s[46:47]
	v_cmp_eq_u32_e64 s[46:47], 14, v36
	s_nop 1
	v_cndmask_b32_e64 v10, v10, v4, s[46:47]
	v_cmp_eq_u32_e64 s[46:47], 15, v36
	s_nop 1
	v_cndmask_b32_e64 v10, v10, v5, s[46:47]
	v_cmp_eq_u32_e64 s[46:47], 1, v38
	ds_bpermute_b32 v10, v39, v10
	s_nop 0
	v_cndmask_b32_e64 v11, v12, v13, s[46:47]
	v_cmp_eq_u32_e64 s[46:47], 2, v38
	s_nop 1
	v_cndmask_b32_e64 v11, v11, v14, s[46:47]
	v_cmp_eq_u32_e64 s[46:47], 3, v38
	s_nop 1
	v_cndmask_b32_e64 v11, v11, v15, s[46:47]
	v_cmp_eq_u32_e64 s[46:47], 4, v38
	s_nop 1
	v_cndmask_b32_e64 v11, v11, v94, s[46:47]
	v_cmp_eq_u32_e64 s[46:47], 5, v38
	s_nop 1
	v_cndmask_b32_e64 v11, v11, v95, s[46:47]
	v_cmp_eq_u32_e64 s[46:47], 6, v38
	s_nop 1
	v_cndmask_b32_e64 v11, v11, v6, s[46:47]
	v_cmp_eq_u32_e64 s[46:47], 7, v38
	s_nop 1
	v_cndmask_b32_e64 v11, v11, v7, s[46:47]
	v_cmp_eq_u32_e64 s[46:47], 8, v38
	s_nop 1
	v_cndmask_b32_e64 v11, v11, v0, s[46:47]
	v_cmp_eq_u32_e64 s[46:47], 9, v38
	s_nop 1
	v_cndmask_b32_e64 v11, v11, v1, s[46:47]
	v_cmp_eq_u32_e64 s[46:47], 10, v38
	s_nop 1
	v_cndmask_b32_e64 v11, v11, v2, s[46:47]
	v_cmp_eq_u32_e64 s[46:47], 11, v38
	s_nop 1
	v_cndmask_b32_e64 v11, v11, v3, s[46:47]
	v_cmp_eq_u32_e64 s[46:47], 12, v38
	s_nop 1
	v_cndmask_b32_e64 v11, v11, v8, s[46:47]
	v_cmp_eq_u32_e64 s[46:47], 13, v38
	s_nop 1
	v_cndmask_b32_e64 v11, v11, v9, s[46:47]
	v_cmp_eq_u32_e64 s[46:47], 14, v38
	s_nop 1
	v_cndmask_b32_e64 v11, v11, v4, s[46:47]
	v_cmp_eq_u32_e64 s[46:47], 15, v38
	s_nop 1
	v_cndmask_b32_e64 v11, v11, v5, s[46:47]
	v_cmp_eq_u32_e64 s[46:47], 1, v40
	s_waitcnt lgkmcnt(0)
	v_add_f32_e32 v10, v11, v10
	v_cndmask_b32_e64 v11, v12, v13, s[46:47]
	v_cmp_eq_u32_e64 s[46:47], 2, v40
	s_nop 1
	v_cndmask_b32_e64 v11, v11, v14, s[46:47]
	v_cmp_eq_u32_e64 s[46:47], 3, v40
	s_nop 1
	v_cndmask_b32_e64 v11, v11, v15, s[46:47]
	v_cmp_eq_u32_e64 s[46:47], 4, v40
	s_nop 1
	v_cndmask_b32_e64 v11, v11, v10, s[46:47]
	v_cmp_eq_u32_e64 s[46:47], 5, v40
	s_nop 1
	v_cndmask_b32_e64 v11, v11, v95, s[46:47]
	v_cmp_eq_u32_e64 s[46:47], 6, v40
	s_nop 1
	v_cndmask_b32_e64 v11, v11, v6, s[46:47]
	v_cmp_eq_u32_e64 s[46:47], 7, v40
	s_nop 1
	v_cndmask_b32_e64 v11, v11, v7, s[46:47]
	v_cmp_eq_u32_e64 s[46:47], 8, v40
	s_nop 1
	v_cndmask_b32_e64 v11, v11, v0, s[46:47]
	v_cmp_eq_u32_e64 s[46:47], 9, v40
	s_nop 1
	v_cndmask_b32_e64 v11, v11, v1, s[46:47]
	v_cmp_eq_u32_e64 s[46:47], 10, v40
	s_nop 1
	v_cndmask_b32_e64 v11, v11, v2, s[46:47]
	v_cmp_eq_u32_e64 s[46:47], 11, v40
	s_nop 1
	v_cndmask_b32_e64 v11, v11, v3, s[46:47]
	v_cmp_eq_u32_e64 s[46:47], 12, v40
	s_nop 1
	v_cndmask_b32_e64 v11, v11, v8, s[46:47]
	v_cmp_eq_u32_e64 s[46:47], 13, v40
	s_nop 1
	v_cndmask_b32_e64 v11, v11, v9, s[46:47]
	v_cmp_eq_u32_e64 s[46:47], 14, v40
	s_nop 1
	v_cndmask_b32_e64 v11, v11, v4, s[46:47]
	v_cmp_eq_u32_e64 s[46:47], 15, v40
	s_nop 1
	v_cndmask_b32_e64 v11, v11, v5, s[46:47]
	v_cmp_eq_u32_e64 s[46:47], 1, v42
	ds_bpermute_b32 v11, v39, v11
	s_nop 0
	v_cndmask_b32_e64 v55, v12, v13, s[46:47]
	v_cmp_eq_u32_e64 s[46:47], 2, v42
	s_nop 1
	v_cndmask_b32_e64 v55, v55, v14, s[46:47]
	v_cmp_eq_u32_e64 s[46:47], 3, v42
	s_nop 1
	v_cndmask_b32_e64 v55, v55, v15, s[46:47]
	v_cmp_eq_u32_e64 s[46:47], 4, v42
	s_nop 1
	v_cndmask_b32_e64 v55, v55, v10, s[46:47]
	v_cmp_eq_u32_e64 s[46:47], 5, v42
	s_nop 1
	v_cndmask_b32_e64 v55, v55, v95, s[46:47]
	v_cmp_eq_u32_e64 s[46:47], 6, v42
	s_nop 1
	v_cndmask_b32_e64 v55, v55, v6, s[46:47]
	v_cmp_eq_u32_e64 s[46:47], 7, v42
	s_nop 1
	v_cndmask_b32_e64 v55, v55, v7, s[46:47]
	v_cmp_eq_u32_e64 s[46:47], 8, v42
	s_nop 1
	v_cndmask_b32_e64 v55, v55, v0, s[46:47]
	v_cmp_eq_u32_e64 s[46:47], 9, v42
	s_nop 1
	v_cndmask_b32_e64 v55, v55, v1, s[46:47]
	v_cmp_eq_u32_e64 s[46:47], 10, v42
	s_nop 1
	v_cndmask_b32_e64 v55, v55, v2, s[46:47]
	v_cmp_eq_u32_e64 s[46:47], 11, v42
	s_nop 1
	v_cndmask_b32_e64 v55, v55, v3, s[46:47]
	v_cmp_eq_u32_e64 s[46:47], 12, v42
	s_nop 1
	v_cndmask_b32_e64 v55, v55, v8, s[46:47]
	v_cmp_eq_u32_e64 s[46:47], 13, v42
	s_nop 1
	v_cndmask_b32_e64 v55, v55, v9, s[46:47]
	v_cmp_eq_u32_e64 s[46:47], 14, v42
	s_nop 1
	v_cndmask_b32_e64 v55, v55, v4, s[46:47]
	v_cmp_eq_u32_e64 s[46:47], 15, v42
	s_nop 1
	v_cndmask_b32_e64 v55, v55, v5, s[46:47]
	v_cmp_eq_u32_e64 s[46:47], 1, v44
	s_waitcnt lgkmcnt(0)
	v_add_f32_e32 v11, v55, v11
	v_cndmask_b32_e64 v55, v12, v13, s[46:47]
	v_cmp_eq_u32_e64 s[46:47], 2, v44
	s_nop 1
	v_cndmask_b32_e64 v55, v55, v14, s[46:47]
	v_cmp_eq_u32_e64 s[46:47], 3, v44
	s_nop 1
	v_cndmask_b32_e64 v55, v55, v15, s[46:47]
	v_cmp_eq_u32_e64 s[46:47], 4, v44
	s_nop 1
	v_cndmask_b32_e64 v55, v55, v10, s[46:47]
	v_cmp_eq_u32_e64 s[46:47], 5, v44
	s_nop 1
	v_cndmask_b32_e64 v55, v55, v11, s[46:47]
	v_cmp_eq_u32_e64 s[46:47], 6, v44
	s_nop 1
	v_cndmask_b32_e64 v55, v55, v6, s[46:47]
	v_cmp_eq_u32_e64 s[46:47], 7, v44
	s_nop 1
	v_cndmask_b32_e64 v55, v55, v7, s[46:47]
	v_cmp_eq_u32_e64 s[46:47], 8, v44
	s_nop 1
	v_cndmask_b32_e64 v55, v55, v0, s[46:47]
	v_cmp_eq_u32_e64 s[46:47], 9, v44
	s_nop 1
	v_cndmask_b32_e64 v55, v55, v1, s[46:47]
	v_cmp_eq_u32_e64 s[46:47], 10, v44
	s_nop 1
	v_cndmask_b32_e64 v55, v55, v2, s[46:47]
	v_cmp_eq_u32_e64 s[46:47], 11, v44
	s_nop 1
	v_cndmask_b32_e64 v55, v55, v3, s[46:47]
	v_cmp_eq_u32_e64 s[46:47], 12, v44
	s_nop 1
	v_cndmask_b32_e64 v55, v55, v8, s[46:47]
	v_cmp_eq_u32_e64 s[46:47], 13, v44
	s_nop 1
	v_cndmask_b32_e64 v55, v55, v9, s[46:47]
	v_cmp_eq_u32_e64 s[46:47], 14, v44
	s_nop 1
	v_cndmask_b32_e64 v55, v55, v4, s[46:47]
	v_cmp_eq_u32_e64 s[46:47], 15, v44
	s_nop 1
	v_cndmask_b32_e64 v55, v55, v5, s[46:47]
	v_cmp_eq_u32_e64 s[46:47], 1, v46
	ds_bpermute_b32 v55, v39, v55
	s_nop 0
	v_cndmask_b32_e64 v57, v12, v13, s[46:47]
	v_cmp_eq_u32_e64 s[46:47], 2, v46
	s_nop 1
	v_cndmask_b32_e64 v57, v57, v14, s[46:47]
	v_cmp_eq_u32_e64 s[46:47], 3, v46
	s_nop 1
	v_cndmask_b32_e64 v57, v57, v15, s[46:47]
	v_cmp_eq_u32_e64 s[46:47], 4, v46
	s_nop 1
	v_cndmask_b32_e64 v57, v57, v10, s[46:47]
	v_cmp_eq_u32_e64 s[46:47], 5, v46
	s_nop 1
	v_cndmask_b32_e64 v57, v57, v11, s[46:47]
	v_cmp_eq_u32_e64 s[46:47], 6, v46
	s_nop 1
	v_cndmask_b32_e64 v6, v57, v6, s[46:47]
	v_cmp_eq_u32_e64 s[46:47], 7, v46
	s_nop 1
	v_cndmask_b32_e64 v6, v6, v7, s[46:47]
	v_cmp_eq_u32_e64 s[46:47], 8, v46
	s_nop 1
	v_cndmask_b32_e64 v6, v6, v0, s[46:47]
	v_cmp_eq_u32_e64 s[46:47], 9, v46
	s_nop 1
	v_cndmask_b32_e64 v6, v6, v1, s[46:47]
	v_cmp_eq_u32_e64 s[46:47], 10, v46
	s_nop 1
	v_cndmask_b32_e64 v6, v6, v2, s[46:47]
	v_cmp_eq_u32_e64 s[46:47], 11, v46
	s_nop 1
	v_cndmask_b32_e64 v6, v6, v3, s[46:47]
	v_cmp_eq_u32_e64 s[46:47], 12, v46
	s_nop 1
	v_cndmask_b32_e64 v6, v6, v8, s[46:47]
	v_cmp_eq_u32_e64 s[46:47], 13, v46
	s_nop 1
	v_cndmask_b32_e64 v6, v6, v9, s[46:47]
	v_cmp_eq_u32_e64 s[46:47], 14, v46
	s_nop 1
	v_cndmask_b32_e64 v6, v6, v4, s[46:47]
	v_cmp_eq_u32_e64 s[46:47], 15, v46
	s_nop 1
	v_cndmask_b32_e64 v6, v6, v5, s[46:47]
	v_cmp_eq_u32_e64 s[46:47], 1, v48
	s_waitcnt lgkmcnt(0)
	v_add_f32_e32 v6, v6, v55
	v_cndmask_b32_e64 v55, v12, v13, s[46:47]
	v_cmp_eq_u32_e64 s[46:47], 2, v48
	s_nop 1
	v_cndmask_b32_e64 v55, v55, v14, s[46:47]
	v_cmp_eq_u32_e64 s[46:47], 3, v48
	s_nop 1
	v_cndmask_b32_e64 v55, v55, v15, s[46:47]
	v_cmp_eq_u32_e64 s[46:47], 4, v48
	s_nop 1
	v_cndmask_b32_e64 v55, v55, v10, s[46:47]
	v_cmp_eq_u32_e64 s[46:47], 5, v48
	s_nop 1
	v_cndmask_b32_e64 v55, v55, v11, s[46:47]
	v_cmp_eq_u32_e64 s[46:47], 6, v48
	s_nop 1
	v_cndmask_b32_e64 v55, v55, v6, s[46:47]
	v_cmp_eq_u32_e64 s[46:47], 7, v48
	s_nop 1
	v_cndmask_b32_e64 v55, v55, v7, s[46:47]
	v_cmp_eq_u32_e64 s[46:47], 8, v48
	s_nop 1
	v_cndmask_b32_e64 v55, v55, v0, s[46:47]
	v_cmp_eq_u32_e64 s[46:47], 9, v48
	s_nop 1
	v_cndmask_b32_e64 v55, v55, v1, s[46:47]
	v_cmp_eq_u32_e64 s[46:47], 10, v48
	s_nop 1
	v_cndmask_b32_e64 v55, v55, v2, s[46:47]
	v_cmp_eq_u32_e64 s[46:47], 11, v48
	s_nop 1
	v_cndmask_b32_e64 v55, v55, v3, s[46:47]
	v_cmp_eq_u32_e64 s[46:47], 12, v48
	s_nop 1
	v_cndmask_b32_e64 v55, v55, v8, s[46:47]
	v_cmp_eq_u32_e64 s[46:47], 13, v48
	s_nop 1
	v_cndmask_b32_e64 v55, v55, v9, s[46:47]
	v_cmp_eq_u32_e64 s[46:47], 14, v48
	s_nop 1
	v_cndmask_b32_e64 v55, v55, v4, s[46:47]
	v_cmp_eq_u32_e64 s[46:47], 15, v48
	s_nop 1
	v_cndmask_b32_e64 v55, v55, v5, s[46:47]
	v_cmp_eq_u32_e64 s[46:47], 1, v50
	ds_bpermute_b32 v55, v39, v55
	s_nop 0
	v_cndmask_b32_e64 v57, v12, v13, s[46:47]
	v_cmp_eq_u32_e64 s[46:47], 2, v50
	s_nop 1
	v_cndmask_b32_e64 v57, v57, v14, s[46:47]
	v_cmp_eq_u32_e64 s[46:47], 3, v50
	s_nop 1
	v_cndmask_b32_e64 v57, v57, v15, s[46:47]
	v_cmp_eq_u32_e64 s[46:47], 4, v50
	s_nop 1
	v_cndmask_b32_e64 v57, v57, v10, s[46:47]
	v_cmp_eq_u32_e64 s[46:47], 5, v50
	s_nop 1
	v_cndmask_b32_e64 v57, v57, v11, s[46:47]
	v_cmp_eq_u32_e64 s[46:47], 6, v50
	s_nop 1
	v_cndmask_b32_e64 v57, v57, v6, s[46:47]
	v_cmp_eq_u32_e64 s[46:47], 7, v50
	s_nop 1
	v_cndmask_b32_e64 v7, v57, v7, s[46:47]
	v_cmp_eq_u32_e64 s[46:47], 8, v50
	s_nop 1
	v_cndmask_b32_e64 v7, v7, v0, s[46:47]
	v_cmp_eq_u32_e64 s[46:47], 9, v50
	s_nop 1
	v_cndmask_b32_e64 v7, v7, v1, s[46:47]
	v_cmp_eq_u32_e64 s[46:47], 10, v50
	s_nop 1
	v_cndmask_b32_e64 v7, v7, v2, s[46:47]
	v_cmp_eq_u32_e64 s[46:47], 11, v50
	s_nop 1
	v_cndmask_b32_e64 v7, v7, v3, s[46:47]
	v_cmp_eq_u32_e64 s[46:47], 12, v50
	s_nop 1
	v_cndmask_b32_e64 v7, v7, v8, s[46:47]
	v_cmp_eq_u32_e64 s[46:47], 13, v50
	s_nop 1
	v_cndmask_b32_e64 v7, v7, v9, s[46:47]
	v_cmp_eq_u32_e64 s[46:47], 14, v50
	s_nop 1
	v_cndmask_b32_e64 v7, v7, v4, s[46:47]
	v_cmp_eq_u32_e64 s[46:47], 15, v50
	s_nop 1
	v_cndmask_b32_e64 v7, v7, v5, s[46:47]
	v_cmp_eq_u32_e64 s[46:47], 1, v52
	s_waitcnt lgkmcnt(0)
	v_add_f32_e32 v7, v7, v55
	v_cndmask_b32_e64 v55, v12, v13, s[46:47]
	v_cmp_eq_u32_e64 s[46:47], 2, v52
	s_nop 1
	v_cndmask_b32_e64 v55, v55, v14, s[46:47]
	v_cmp_eq_u32_e64 s[46:47], 3, v52
	s_nop 1
	v_cndmask_b32_e64 v55, v55, v15, s[46:47]
	v_cmp_eq_u32_e64 s[46:47], 4, v52
	s_nop 1
	v_cndmask_b32_e64 v55, v55, v10, s[46:47]
	v_cmp_eq_u32_e64 s[46:47], 5, v52
	s_nop 1
	v_cndmask_b32_e64 v55, v55, v11, s[46:47]
	v_cmp_eq_u32_e64 s[46:47], 6, v52
	s_nop 1
	v_cndmask_b32_e64 v55, v55, v6, s[46:47]
	v_cmp_eq_u32_e64 s[46:47], 7, v52
	s_nop 1
	v_cndmask_b32_e64 v55, v55, v7, s[46:47]
	v_cmp_eq_u32_e64 s[46:47], 8, v52
	s_nop 1
	v_cndmask_b32_e64 v55, v55, v0, s[46:47]
	v_cmp_eq_u32_e64 s[46:47], 9, v52
	s_nop 1
	v_cndmask_b32_e64 v55, v55, v1, s[46:47]
	v_cmp_eq_u32_e64 s[46:47], 10, v52
	s_nop 1
	v_cndmask_b32_e64 v55, v55, v2, s[46:47]
	v_cmp_eq_u32_e64 s[46:47], 11, v52
	s_nop 1
	v_cndmask_b32_e64 v55, v55, v3, s[46:47]
	v_cmp_eq_u32_e64 s[46:47], 12, v52
	s_nop 1
	v_cndmask_b32_e64 v55, v55, v8, s[46:47]
	v_cmp_eq_u32_e64 s[46:47], 13, v52
	s_nop 1
	v_cndmask_b32_e64 v55, v55, v9, s[46:47]
	v_cmp_eq_u32_e64 s[46:47], 14, v52
	s_nop 1
	v_cndmask_b32_e64 v55, v55, v4, s[46:47]
	v_cmp_eq_u32_e64 s[46:47], 15, v52
	s_nop 1
	v_cndmask_b32_e64 v55, v55, v5, s[46:47]
	v_cmp_eq_u32_e64 s[46:47], 1, v54
	ds_bpermute_b32 v55, v37, v55
	s_nop 0
	v_cndmask_b32_e64 v12, v12, v13, s[46:47]
	v_cmp_eq_u32_e64 s[46:47], 2, v54
	s_nop 1
	v_cndmask_b32_e64 v12, v12, v14, s[46:47]
	v_cmp_eq_u32_e64 s[46:47], 3, v54
	s_nop 1
	v_cndmask_b32_e64 v12, v12, v15, s[46:47]
	v_cmp_eq_u32_e64 s[46:47], 4, v54
	s_nop 1
	v_cndmask_b32_e64 v12, v12, v10, s[46:47]
	v_cmp_eq_u32_e64 s[46:47], 5, v54
	s_nop 1
	v_cndmask_b32_e64 v12, v12, v11, s[46:47]
	v_cmp_eq_u32_e64 s[46:47], 6, v54
	s_nop 1
	v_cndmask_b32_e64 v12, v12, v6, s[46:47]
	v_cmp_eq_u32_e64 s[46:47], 7, v54
	s_nop 1
	v_cndmask_b32_e64 v12, v12, v7, s[46:47]
	v_cmp_eq_u32_e64 s[46:47], 8, v54
	s_nop 1
	v_cndmask_b32_e64 v12, v12, v0, s[46:47]
	v_cmp_eq_u32_e64 s[46:47], 9, v54
	s_nop 1
	v_cndmask_b32_e64 v12, v12, v1, s[46:47]
	v_cmp_eq_u32_e64 s[46:47], 10, v54
	s_nop 1
	v_cndmask_b32_e64 v12, v12, v2, s[46:47]
	v_cmp_eq_u32_e64 s[46:47], 11, v54
	s_nop 1
	v_cndmask_b32_e64 v12, v12, v3, s[46:47]
	v_cmp_eq_u32_e64 s[46:47], 12, v54
	s_nop 1
	v_cndmask_b32_e64 v12, v12, v8, s[46:47]
	v_cmp_eq_u32_e64 s[46:47], 13, v54
	s_nop 1
	v_cndmask_b32_e64 v12, v12, v9, s[46:47]
	v_cmp_eq_u32_e64 s[46:47], 14, v54
	s_nop 1
	v_cndmask_b32_e64 v12, v12, v4, s[46:47]
	v_cmp_eq_u32_e64 s[46:47], 15, v54
	s_nop 1
	v_cndmask_b32_e64 v12, v12, v5, s[46:47]
	s_waitcnt lgkmcnt(0)
	v_add_f32_e32 v12, v12, v55
	v_cmp_eq_u32_e64 s[46:47], 1, v56
	s_nop 1
	v_cndmask_b32_e64 v55, v12, v13, s[46:47]
	v_cmp_eq_u32_e64 s[46:47], 2, v56
	s_nop 1
	v_cndmask_b32_e64 v55, v55, v14, s[46:47]
	v_cmp_eq_u32_e64 s[46:47], 3, v56
	s_nop 1
	v_cndmask_b32_e64 v55, v55, v15, s[46:47]
	v_cmp_eq_u32_e64 s[46:47], 4, v56
	s_nop 1
	v_cndmask_b32_e64 v55, v55, v10, s[46:47]
	v_cmp_eq_u32_e64 s[46:47], 5, v56
	s_nop 1
	v_cndmask_b32_e64 v55, v55, v11, s[46:47]
	v_cmp_eq_u32_e64 s[46:47], 6, v56
	s_nop 1
	v_cndmask_b32_e64 v55, v55, v6, s[46:47]
	v_cmp_eq_u32_e64 s[46:47], 7, v56
	s_nop 1
	v_cndmask_b32_e64 v55, v55, v7, s[46:47]
	v_cmp_eq_u32_e64 s[46:47], 8, v56
	s_nop 1
	v_cndmask_b32_e64 v55, v55, v0, s[46:47]
	v_cmp_eq_u32_e64 s[46:47], 9, v56
	s_nop 1
	v_cndmask_b32_e64 v55, v55, v1, s[46:47]
	v_cmp_eq_u32_e64 s[46:47], 10, v56
	s_nop 1
	v_cndmask_b32_e64 v55, v55, v2, s[46:47]
	v_cmp_eq_u32_e64 s[46:47], 11, v56
	s_nop 1
	v_cndmask_b32_e64 v55, v55, v3, s[46:47]
	v_cmp_eq_u32_e64 s[46:47], 12, v56
	s_nop 1
	v_cndmask_b32_e64 v55, v55, v8, s[46:47]
	v_cmp_eq_u32_e64 s[46:47], 13, v56
	s_nop 1
	v_cndmask_b32_e64 v55, v55, v9, s[46:47]
	v_cmp_eq_u32_e64 s[46:47], 14, v56
	s_nop 1
	v_cndmask_b32_e64 v55, v55, v4, s[46:47]
	v_cmp_eq_u32_e64 s[46:47], 15, v56
	s_nop 1
	v_cndmask_b32_e64 v55, v55, v5, s[46:47]
	v_cmp_eq_u32_e64 s[46:47], 1, v58
	ds_bpermute_b32 v55, v37, v55
	s_nop 0
	v_cndmask_b32_e64 v13, v12, v13, s[46:47]
	v_cmp_eq_u32_e64 s[46:47], 2, v58
	s_nop 1
	v_cndmask_b32_e64 v13, v13, v14, s[46:47]
	v_cmp_eq_u32_e64 s[46:47], 3, v58
	s_nop 1
	v_cndmask_b32_e64 v13, v13, v15, s[46:47]
	v_cmp_eq_u32_e64 s[46:47], 4, v58
	s_nop 1
	v_cndmask_b32_e64 v13, v13, v10, s[46:47]
	v_cmp_eq_u32_e64 s[46:47], 5, v58
	s_nop 1
	v_cndmask_b32_e64 v13, v13, v11, s[46:47]
	v_cmp_eq_u32_e64 s[46:47], 6, v58
	s_nop 1
	v_cndmask_b32_e64 v13, v13, v6, s[46:47]
	v_cmp_eq_u32_e64 s[46:47], 7, v58
	s_nop 1
	v_cndmask_b32_e64 v13, v13, v7, s[46:47]
	v_cmp_eq_u32_e64 s[46:47], 8, v58
	s_nop 1
	v_cndmask_b32_e64 v13, v13, v0, s[46:47]
	v_cmp_eq_u32_e64 s[46:47], 9, v58
	s_nop 1
	v_cndmask_b32_e64 v13, v13, v1, s[46:47]
	v_cmp_eq_u32_e64 s[46:47], 10, v58
	s_nop 1
	v_cndmask_b32_e64 v13, v13, v2, s[46:47]
	v_cmp_eq_u32_e64 s[46:47], 11, v58
	s_nop 1
	v_cndmask_b32_e64 v13, v13, v3, s[46:47]
	v_cmp_eq_u32_e64 s[46:47], 12, v58
	s_nop 1
	v_cndmask_b32_e64 v13, v13, v8, s[46:47]
	v_cmp_eq_u32_e64 s[46:47], 13, v58
	s_nop 1
	v_cndmask_b32_e64 v13, v13, v9, s[46:47]
	v_cmp_eq_u32_e64 s[46:47], 14, v58
	s_nop 1
	v_cndmask_b32_e64 v13, v13, v4, s[46:47]
	v_cmp_eq_u32_e64 s[46:47], 15, v58
	s_nop 1
	v_cndmask_b32_e64 v13, v13, v5, s[46:47]
	s_waitcnt lgkmcnt(0)
	v_add_f32_e32 v13, v13, v55
	v_cmp_eq_u32_e64 s[46:47], 1, v60
	s_nop 1
	v_cndmask_b32_e64 v55, v12, v13, s[46:47]
	v_cmp_eq_u32_e64 s[46:47], 2, v60
	s_nop 1
	v_cndmask_b32_e64 v55, v55, v14, s[46:47]
	v_cmp_eq_u32_e64 s[46:47], 3, v60
	s_nop 1
	v_cndmask_b32_e64 v55, v55, v15, s[46:47]
	v_cmp_eq_u32_e64 s[46:47], 4, v60
	s_nop 1
	v_cndmask_b32_e64 v55, v55, v10, s[46:47]
	v_cmp_eq_u32_e64 s[46:47], 5, v60
	s_nop 1
	v_cndmask_b32_e64 v55, v55, v11, s[46:47]
	v_cmp_eq_u32_e64 s[46:47], 6, v60
	s_nop 1
	v_cndmask_b32_e64 v55, v55, v6, s[46:47]
	v_cmp_eq_u32_e64 s[46:47], 7, v60
	s_nop 1
	v_cndmask_b32_e64 v55, v55, v7, s[46:47]
	v_cmp_eq_u32_e64 s[46:47], 8, v60
	s_nop 1
	v_cndmask_b32_e64 v55, v55, v0, s[46:47]
	v_cmp_eq_u32_e64 s[46:47], 9, v60
	s_nop 1
	v_cndmask_b32_e64 v55, v55, v1, s[46:47]
	v_cmp_eq_u32_e64 s[46:47], 10, v60
	s_nop 1
	v_cndmask_b32_e64 v55, v55, v2, s[46:47]
	v_cmp_eq_u32_e64 s[46:47], 11, v60
	s_nop 1
	v_cndmask_b32_e64 v55, v55, v3, s[46:47]
	v_cmp_eq_u32_e64 s[46:47], 12, v60
	s_nop 1
	v_cndmask_b32_e64 v55, v55, v8, s[46:47]
	v_cmp_eq_u32_e64 s[46:47], 13, v60
	s_nop 1
	v_cndmask_b32_e64 v55, v55, v9, s[46:47]
	v_cmp_eq_u32_e64 s[46:47], 14, v60
	s_nop 1
	v_cndmask_b32_e64 v55, v55, v4, s[46:47]
	v_cmp_eq_u32_e64 s[46:47], 15, v60
	s_nop 1
	v_cndmask_b32_e64 v55, v55, v5, s[46:47]
	v_cmp_eq_u32_e64 s[46:47], 1, v62
	ds_bpermute_b32 v55, v37, v55
	s_nop 0
	v_cndmask_b32_e64 v57, v12, v13, s[46:47]
	v_cmp_eq_u32_e64 s[46:47], 2, v62
	s_nop 1
	v_cndmask_b32_e64 v14, v57, v14, s[46:47]
	v_cmp_eq_u32_e64 s[46:47], 3, v62
	s_nop 1
	v_cndmask_b32_e64 v14, v14, v15, s[46:47]
	v_cmp_eq_u32_e64 s[46:47], 4, v62
	s_nop 1
	v_cndmask_b32_e64 v14, v14, v10, s[46:47]
	v_cmp_eq_u32_e64 s[46:47], 5, v62
	s_nop 1
	v_cndmask_b32_e64 v14, v14, v11, s[46:47]
	v_cmp_eq_u32_e64 s[46:47], 6, v62
	s_nop 1
	v_cndmask_b32_e64 v14, v14, v6, s[46:47]
	v_cmp_eq_u32_e64 s[46:47], 7, v62
	s_nop 1
	v_cndmask_b32_e64 v14, v14, v7, s[46:47]
	v_cmp_eq_u32_e64 s[46:47], 8, v62
	s_nop 1
	v_cndmask_b32_e64 v14, v14, v0, s[46:47]
	v_cmp_eq_u32_e64 s[46:47], 9, v62
	s_nop 1
	v_cndmask_b32_e64 v14, v14, v1, s[46:47]
	v_cmp_eq_u32_e64 s[46:47], 10, v62
	s_nop 1
	v_cndmask_b32_e64 v14, v14, v2, s[46:47]
	v_cmp_eq_u32_e64 s[46:47], 11, v62
	s_nop 1
	v_cndmask_b32_e64 v14, v14, v3, s[46:47]
	v_cmp_eq_u32_e64 s[46:47], 12, v62
	s_nop 1
	v_cndmask_b32_e64 v14, v14, v8, s[46:47]
	v_cmp_eq_u32_e64 s[46:47], 13, v62
	s_nop 1
	v_cndmask_b32_e64 v14, v14, v9, s[46:47]
	v_cmp_eq_u32_e64 s[46:47], 14, v62
	s_nop 1
	v_cndmask_b32_e64 v14, v14, v4, s[46:47]
	v_cmp_eq_u32_e64 s[46:47], 15, v62
	s_nop 1
	v_cndmask_b32_e64 v14, v14, v5, s[46:47]
	v_cmp_eq_u32_e64 s[46:47], 1, v64
	s_waitcnt lgkmcnt(0)
	v_add_f32_e32 v14, v14, v55
	v_cndmask_b32_e64 v55, v12, v13, s[46:47]
	v_cmp_eq_u32_e64 s[46:47], 2, v64
	s_nop 1
	v_cndmask_b32_e64 v55, v55, v14, s[46:47]
	v_cmp_eq_u32_e64 s[46:47], 3, v64
	s_nop 1
	v_cndmask_b32_e64 v55, v55, v15, s[46:47]
	v_cmp_eq_u32_e64 s[46:47], 4, v64
	s_nop 1
	v_cndmask_b32_e64 v55, v55, v10, s[46:47]
	v_cmp_eq_u32_e64 s[46:47], 5, v64
	s_nop 1
	v_cndmask_b32_e64 v55, v55, v11, s[46:47]
	v_cmp_eq_u32_e64 s[46:47], 6, v64
	s_nop 1
	v_cndmask_b32_e64 v55, v55, v6, s[46:47]
	v_cmp_eq_u32_e64 s[46:47], 7, v64
	s_nop 1
	v_cndmask_b32_e64 v55, v55, v7, s[46:47]
	v_cmp_eq_u32_e64 s[46:47], 8, v64
	s_nop 1
	v_cndmask_b32_e64 v55, v55, v0, s[46:47]
	v_cmp_eq_u32_e64 s[46:47], 9, v64
	s_nop 1
	v_cndmask_b32_e64 v55, v55, v1, s[46:47]
	v_cmp_eq_u32_e64 s[46:47], 10, v64
	s_nop 1
	v_cndmask_b32_e64 v55, v55, v2, s[46:47]
	v_cmp_eq_u32_e64 s[46:47], 11, v64
	s_nop 1
	v_cndmask_b32_e64 v55, v55, v3, s[46:47]
	v_cmp_eq_u32_e64 s[46:47], 12, v64
	s_nop 1
	v_cndmask_b32_e64 v55, v55, v8, s[46:47]
	v_cmp_eq_u32_e64 s[46:47], 13, v64
	s_nop 1
	v_cndmask_b32_e64 v55, v55, v9, s[46:47]
	v_cmp_eq_u32_e64 s[46:47], 14, v64
	s_nop 1
	v_cndmask_b32_e64 v55, v55, v4, s[46:47]
	v_cmp_eq_u32_e64 s[46:47], 15, v64
	s_nop 1
	v_cndmask_b32_e64 v55, v55, v5, s[46:47]
	v_cmp_eq_u32_e64 s[46:47], 1, v66
	ds_bpermute_b32 v55, v37, v55
	s_nop 0
	v_cndmask_b32_e64 v57, v12, v13, s[46:47]
	v_cmp_eq_u32_e64 s[46:47], 2, v66
	s_nop 1
	v_cndmask_b32_e64 v57, v57, v14, s[46:47]
	v_cmp_eq_u32_e64 s[46:47], 3, v66
	s_nop 1
	v_cndmask_b32_e64 v15, v57, v15, s[46:47]
	v_cmp_eq_u32_e64 s[46:47], 4, v66
	s_nop 1
	v_cndmask_b32_e64 v15, v15, v10, s[46:47]
	v_cmp_eq_u32_e64 s[46:47], 5, v66
	s_nop 1
	v_cndmask_b32_e64 v15, v15, v11, s[46:47]
	v_cmp_eq_u32_e64 s[46:47], 6, v66
	s_nop 1
	v_cndmask_b32_e64 v15, v15, v6, s[46:47]
	v_cmp_eq_u32_e64 s[46:47], 7, v66
	s_nop 1
	v_cndmask_b32_e64 v15, v15, v7, s[46:47]
	v_cmp_eq_u32_e64 s[46:47], 8, v66
	s_nop 1
	v_cndmask_b32_e64 v15, v15, v0, s[46:47]
	v_cmp_eq_u32_e64 s[46:47], 9, v66
	s_nop 1
	v_cndmask_b32_e64 v15, v15, v1, s[46:47]
	v_cmp_eq_u32_e64 s[46:47], 10, v66
	s_nop 1
	v_cndmask_b32_e64 v15, v15, v2, s[46:47]
	v_cmp_eq_u32_e64 s[46:47], 11, v66
	s_nop 1
	v_cndmask_b32_e64 v15, v15, v3, s[46:47]
	v_cmp_eq_u32_e64 s[46:47], 12, v66
	s_nop 1
	v_cndmask_b32_e64 v15, v15, v8, s[46:47]
	v_cmp_eq_u32_e64 s[46:47], 13, v66
	s_nop 1
	v_cndmask_b32_e64 v15, v15, v9, s[46:47]
	v_cmp_eq_u32_e64 s[46:47], 14, v66
	s_nop 1
	v_cndmask_b32_e64 v15, v15, v4, s[46:47]
	v_cmp_eq_u32_e64 s[46:47], 15, v66
	s_nop 1
	v_cndmask_b32_e64 v15, v15, v5, s[46:47]
	v_cmp_eq_u32_e64 s[46:47], 1, v68
	s_waitcnt lgkmcnt(0)
	v_add_f32_e32 v15, v15, v55
	v_cndmask_b32_e64 v55, v12, v13, s[46:47]
	v_cmp_eq_u32_e64 s[46:47], 2, v68
	s_nop 1
	v_cndmask_b32_e64 v55, v55, v14, s[46:47]
	v_cmp_eq_u32_e64 s[46:47], 3, v68
	s_nop 1
	v_cndmask_b32_e64 v55, v55, v15, s[46:47]
	v_cmp_eq_u32_e64 s[46:47], 4, v68
	s_nop 1
	v_cndmask_b32_e64 v55, v55, v10, s[46:47]
	v_cmp_eq_u32_e64 s[46:47], 5, v68
	s_nop 1
	v_cndmask_b32_e64 v55, v55, v11, s[46:47]
	v_cmp_eq_u32_e64 s[46:47], 6, v68
	s_nop 1
	v_cndmask_b32_e64 v55, v55, v6, s[46:47]
	v_cmp_eq_u32_e64 s[46:47], 7, v68
	s_nop 1
	v_cndmask_b32_e64 v55, v55, v7, s[46:47]
	v_cmp_eq_u32_e64 s[46:47], 8, v68
	s_nop 1
	v_cndmask_b32_e64 v55, v55, v0, s[46:47]
	v_cmp_eq_u32_e64 s[46:47], 9, v68
	s_nop 1
	v_cndmask_b32_e64 v55, v55, v1, s[46:47]
	v_cmp_eq_u32_e64 s[46:47], 10, v68
	s_nop 1
	v_cndmask_b32_e64 v55, v55, v2, s[46:47]
	v_cmp_eq_u32_e64 s[46:47], 11, v68
	s_nop 1
	v_cndmask_b32_e64 v55, v55, v3, s[46:47]
	v_cmp_eq_u32_e64 s[46:47], 12, v68
	s_nop 1
	v_cndmask_b32_e64 v55, v55, v8, s[46:47]
	v_cmp_eq_u32_e64 s[46:47], 13, v68
	s_nop 1
	v_cndmask_b32_e64 v55, v55, v9, s[46:47]
	v_cmp_eq_u32_e64 s[46:47], 14, v68
	s_nop 1
	v_cndmask_b32_e64 v55, v55, v4, s[46:47]
	v_cmp_eq_u32_e64 s[46:47], 15, v68
	s_nop 1
	v_cndmask_b32_e64 v55, v55, v5, s[46:47]
	v_cmp_eq_u32_e64 s[46:47], 1, v70
	ds_bpermute_b32 v55, v41, v55
	s_nop 0
	v_cndmask_b32_e64 v12, v12, v13, s[46:47]
	v_cmp_eq_u32_e64 s[46:47], 2, v70
	s_nop 1
	v_cndmask_b32_e64 v12, v12, v14, s[46:47]
	v_cmp_eq_u32_e64 s[46:47], 3, v70
	s_nop 1
	v_cndmask_b32_e64 v12, v12, v15, s[46:47]
	v_cmp_eq_u32_e64 s[46:47], 4, v70
	s_nop 1
	v_cndmask_b32_e64 v12, v12, v10, s[46:47]
	v_cmp_eq_u32_e64 s[46:47], 5, v70
	s_nop 1
	v_cndmask_b32_e64 v12, v12, v11, s[46:47]
	v_cmp_eq_u32_e64 s[46:47], 6, v70
	s_nop 1
	v_cndmask_b32_e64 v12, v12, v6, s[46:47]
	v_cmp_eq_u32_e64 s[46:47], 7, v70
	s_nop 1
	v_cndmask_b32_e64 v12, v12, v7, s[46:47]
	v_cmp_eq_u32_e64 s[46:47], 8, v70
	s_nop 1
	v_cndmask_b32_e64 v12, v12, v0, s[46:47]
	v_cmp_eq_u32_e64 s[46:47], 9, v70
	s_nop 1
	v_cndmask_b32_e64 v12, v12, v1, s[46:47]
	v_cmp_eq_u32_e64 s[46:47], 10, v70
	s_nop 1
	v_cndmask_b32_e64 v12, v12, v2, s[46:47]
	v_cmp_eq_u32_e64 s[46:47], 11, v70
	s_nop 1
	v_cndmask_b32_e64 v12, v12, v3, s[46:47]
	v_cmp_eq_u32_e64 s[46:47], 12, v70
	s_nop 1
	v_cndmask_b32_e64 v12, v12, v8, s[46:47]
	v_cmp_eq_u32_e64 s[46:47], 13, v70
	s_nop 1
	v_cndmask_b32_e64 v12, v12, v9, s[46:47]
	v_cmp_eq_u32_e64 s[46:47], 14, v70
	s_nop 1
	v_cndmask_b32_e64 v12, v12, v4, s[46:47]
	v_cmp_eq_u32_e64 s[46:47], 15, v70
	s_nop 1
	v_cndmask_b32_e64 v12, v12, v5, s[46:47]
	s_waitcnt lgkmcnt(0)
	v_add_f32_e32 v12, v12, v55
	v_cmp_eq_u32_e64 s[46:47], 1, v72
	s_nop 1
	v_cndmask_b32_e64 v55, v12, v13, s[46:47]
	v_cmp_eq_u32_e64 s[46:47], 2, v72
	s_nop 1
	v_cndmask_b32_e64 v55, v55, v14, s[46:47]
	v_cmp_eq_u32_e64 s[46:47], 3, v72
	s_nop 1
	v_cndmask_b32_e64 v55, v55, v15, s[46:47]
	v_cmp_eq_u32_e64 s[46:47], 4, v72
	s_nop 1
	v_cndmask_b32_e64 v55, v55, v10, s[46:47]
	v_cmp_eq_u32_e64 s[46:47], 5, v72
	s_nop 1
	v_cndmask_b32_e64 v55, v55, v11, s[46:47]
	v_cmp_eq_u32_e64 s[46:47], 6, v72
	s_nop 1
	v_cndmask_b32_e64 v55, v55, v6, s[46:47]
	v_cmp_eq_u32_e64 s[46:47], 7, v72
	s_nop 1
	v_cndmask_b32_e64 v55, v55, v7, s[46:47]
	v_cmp_eq_u32_e64 s[46:47], 8, v72
	s_nop 1
	v_cndmask_b32_e64 v55, v55, v0, s[46:47]
	v_cmp_eq_u32_e64 s[46:47], 9, v72
	s_nop 1
	v_cndmask_b32_e64 v55, v55, v1, s[46:47]
	v_cmp_eq_u32_e64 s[46:47], 10, v72
	s_nop 1
	v_cndmask_b32_e64 v55, v55, v2, s[46:47]
	v_cmp_eq_u32_e64 s[46:47], 11, v72
	s_nop 1
	v_cndmask_b32_e64 v55, v55, v3, s[46:47]
	v_cmp_eq_u32_e64 s[46:47], 12, v72
	s_nop 1
	v_cndmask_b32_e64 v55, v55, v8, s[46:47]
	v_cmp_eq_u32_e64 s[46:47], 13, v72
	s_nop 1
	v_cndmask_b32_e64 v55, v55, v9, s[46:47]
	v_cmp_eq_u32_e64 s[46:47], 14, v72
	s_nop 1
	v_cndmask_b32_e64 v55, v55, v4, s[46:47]
	v_cmp_eq_u32_e64 s[46:47], 15, v72
	s_nop 1
	v_cndmask_b32_e64 v55, v55, v5, s[46:47]
	v_cmp_eq_u32_e64 s[46:47], 1, v74
	ds_bpermute_b32 v55, v41, v55
	s_nop 0
	v_cndmask_b32_e64 v13, v12, v13, s[46:47]
	v_cmp_eq_u32_e64 s[46:47], 2, v74
	s_nop 1
	v_cndmask_b32_e64 v13, v13, v14, s[46:47]
	v_cmp_eq_u32_e64 s[46:47], 3, v74
	s_nop 1
	v_cndmask_b32_e64 v13, v13, v15, s[46:47]
	v_cmp_eq_u32_e64 s[46:47], 4, v74
	s_nop 1
	v_cndmask_b32_e64 v13, v13, v10, s[46:47]
	v_cmp_eq_u32_e64 s[46:47], 5, v74
	s_nop 1
	v_cndmask_b32_e64 v13, v13, v11, s[46:47]
	v_cmp_eq_u32_e64 s[46:47], 6, v74
	s_nop 1
	v_cndmask_b32_e64 v13, v13, v6, s[46:47]
	v_cmp_eq_u32_e64 s[46:47], 7, v74
	s_nop 1
	v_cndmask_b32_e64 v13, v13, v7, s[46:47]
	v_cmp_eq_u32_e64 s[46:47], 8, v74
	s_nop 1
	v_cndmask_b32_e64 v13, v13, v0, s[46:47]
	v_cmp_eq_u32_e64 s[46:47], 9, v74
	s_nop 1
	v_cndmask_b32_e64 v13, v13, v1, s[46:47]
	v_cmp_eq_u32_e64 s[46:47], 10, v74
	s_nop 1
	v_cndmask_b32_e64 v13, v13, v2, s[46:47]
	v_cmp_eq_u32_e64 s[46:47], 11, v74
	s_nop 1
	v_cndmask_b32_e64 v13, v13, v3, s[46:47]
	v_cmp_eq_u32_e64 s[46:47], 12, v74
	s_nop 1
	v_cndmask_b32_e64 v13, v13, v8, s[46:47]
	v_cmp_eq_u32_e64 s[46:47], 13, v74
	s_nop 1
	v_cndmask_b32_e64 v13, v13, v9, s[46:47]
	v_cmp_eq_u32_e64 s[46:47], 14, v74
	s_nop 1
	v_cndmask_b32_e64 v13, v13, v4, s[46:47]
	v_cmp_eq_u32_e64 s[46:47], 15, v74
	s_nop 1
	v_cndmask_b32_e64 v13, v13, v5, s[46:47]
	s_waitcnt lgkmcnt(0)
	v_add_f32_e32 v13, v13, v55
	v_cmp_ne_u64_e64 s[46:47], 0, v[76:77]
	s_nop 1
	v_cndmask_b32_e64 v55, v12, v13, s[46:47]
	v_cmp_eq_u32_e64 s[46:47], 2, v76
	s_nop 1
	v_cndmask_b32_e64 v55, v55, v14, s[46:47]
	v_cmp_eq_u32_e64 s[46:47], 3, v76
	s_nop 1
	v_cndmask_b32_e64 v55, v55, v15, s[46:47]
	v_cmp_eq_u32_e64 s[46:47], 4, v76
	s_nop 1
	v_cndmask_b32_e64 v55, v55, v10, s[46:47]
	v_cmp_eq_u32_e64 s[46:47], 5, v76
	s_nop 1
	v_cndmask_b32_e64 v55, v55, v11, s[46:47]
	v_cmp_eq_u32_e64 s[46:47], 6, v76
	s_nop 1
	v_cndmask_b32_e64 v55, v55, v6, s[46:47]
	v_cmp_eq_u32_e64 s[46:47], 7, v76
	s_nop 1
	v_cndmask_b32_e64 v55, v55, v7, s[46:47]
	v_cmp_eq_u32_e64 s[46:47], 8, v76
	s_nop 1
	v_cndmask_b32_e64 v55, v55, v0, s[46:47]
	v_cmp_eq_u32_e64 s[46:47], 9, v76
	s_nop 1
	v_cndmask_b32_e64 v55, v55, v1, s[46:47]
	v_cmp_eq_u32_e64 s[46:47], 10, v76
	s_nop 1
	v_cndmask_b32_e64 v55, v55, v2, s[46:47]
	v_cmp_eq_u32_e64 s[46:47], 11, v76
	s_nop 1
	v_cndmask_b32_e64 v55, v55, v3, s[46:47]
	v_cmp_eq_u32_e64 s[46:47], 12, v76
	s_nop 1
	v_cndmask_b32_e64 v55, v55, v8, s[46:47]
	v_cmp_eq_u32_e64 s[46:47], 13, v76
	s_nop 1
	v_cndmask_b32_e64 v55, v55, v9, s[46:47]
	v_cmp_ne_u64_e64 s[46:47], 0, v[78:79]
	s_nop 1
	v_cndmask_b32_e64 v12, v12, v13, s[46:47]
	v_cmp_eq_u32_e64 s[46:47], 2, v78
	s_nop 1
	v_cndmask_b32_e64 v12, v12, v14, s[46:47]
	v_cmp_eq_u32_e64 s[46:47], 3, v78
	s_nop 1
	v_cndmask_b32_e64 v12, v12, v15, s[46:47]
	v_cmp_eq_u32_e64 s[46:47], 4, v78
	s_nop 1
	v_cndmask_b32_e64 v10, v12, v10, s[46:47]
	v_cmp_eq_u32_e64 s[46:47], 5, v78
	s_nop 1
	v_cndmask_b32_e64 v10, v10, v11, s[46:47]
	v_cmp_eq_u32_e64 s[46:47], 6, v78
	s_nop 1
	v_cndmask_b32_e64 v6, v10, v6, s[46:47]
	v_cmp_eq_u32_e64 s[46:47], 7, v78
	s_nop 1
	v_cndmask_b32_e64 v6, v6, v7, s[46:47]
	v_cmp_eq_u32_e64 s[46:47], 8, v78
	s_nop 1
	v_cndmask_b32_e64 v0, v6, v0, s[46:47]
	v_cmp_eq_u32_e64 s[46:47], 9, v78
	s_nop 1
	v_cndmask_b32_e64 v0, v0, v1, s[46:47]
	v_cmp_eq_u32_e64 s[46:47], 10, v78
	s_nop 1
	v_cndmask_b32_e64 v0, v0, v2, s[46:47]
	v_cmp_eq_u32_e64 s[46:47], 11, v78
	v_fma_f32 v2, -v43, v45, v47
	s_nop 0
	v_cndmask_b32_e64 v0, v0, v3, s[46:47]
	v_cmp_eq_u32_e64 s[46:47], 12, v78
	v_add_f32_e32 v3, v49, v53
	s_nop 0
	v_cndmask_b32_e64 v0, v0, v8, s[46:47]
	v_cmp_eq_u32_e64 s[46:47], 13, v78
	s_nop 1
	v_cndmask_b32_e64 v0, v0, v9, s[46:47]
	v_cmp_eq_u32_e64 s[46:47], 14, v78
	s_nop 1
	v_cndmask_b32_e64 v0, v0, v4, s[46:47]
	v_cmp_eq_u32_e64 s[46:47], 15, v78
	s_nop 1
	v_cndmask_b32_e64 v0, v0, v5, s[46:47]
	ds_bpermute_b32 v0, v35, v0
	v_cmp_eq_u32_e64 s[46:47], 14, v76
	s_nop 1
	v_cndmask_b32_e64 v1, v55, v4, s[46:47]
	v_cmp_eq_u32_e64 s[46:47], 15, v76
	ds_bpermute_b32 v4, v37, v3
	s_nop 0
	v_cndmask_b32_e64 v1, v1, v5, s[46:47]
	s_waitcnt lgkmcnt(1)
	v_add_f32_e32 v0, v1, v0
	ds_bpermute_b32 v1, v33, v0
	s_waitcnt lgkmcnt(0)
	v_add_f32_e32 v5, v0, v1
	ds_bpermute_b32 v6, v31, v5
	v_div_fmas_f32 v0, v2, v29, v45
	v_div_fixup_f32 v8, v0, v27, 1.0
	v_add_f32_e32 v0, v3, v4
	ds_bpermute_b32 v1, v39, v0
	s_waitcnt lgkmcnt(1)
	v_add_f32_e32 v2, v5, v6
	s_nop 0
	v_readlane_b32 s1, v2, 0
	v_readlane_b32 s0, v2, 4
	v_readlane_b32 s8, v2, 32
	v_readlane_b32 s9, v2, 36
	v_pk_mul_f32 v[6:7], v[8:9], s[0:1] op_sel_hi:[0,1]
	v_readlane_b32 s0, v2, 8
	v_cmp_gt_f32_e32 vcc, v6, v7
	v_readlane_b32 s10, v2, 40
	v_mul_f32_e32 v3, s0, v8
	v_readlane_b32 s0, v2, 12
	v_readlane_b32 s11, v2, 44
	v_readlane_b32 s12, v2, 48
	v_mul_f32_e32 v4, s0, v8
	v_readlane_b32 s0, v2, 16
	v_readlane_b32 s13, v2, 52
	v_readlane_b32 s14, v2, 56
	v_mul_f32_e32 v9, s0, v8
	v_readlane_b32 s0, v2, 20
	v_readlane_b32 s15, v2, 60
	v_cndmask_b32_e64 v12, 0, 1, vcc
	v_mul_f32_e32 v10, s0, v8
	v_readlane_b32 s0, v2, 24
	v_cmp_lt_f32_e64 s[52:53], s33, v7
	s_nop 0
	v_mul_f32_e32 v11, s0, v8
	v_readlane_b32 s0, v2, 28
	v_cndmask_b32_e32 v2, v7, v6, vcc
	v_cmp_gt_f32_e32 vcc, v3, v2
	v_mul_f32_e32 v5, s0, v8
	s_nop 0
	v_cndmask_b32_e32 v2, v2, v3, vcc
	v_cndmask_b32_e64 v12, v12, 2, vcc
	v_cmp_gt_f32_e32 vcc, v4, v2
	s_nop 1
	v_cndmask_b32_e32 v2, v2, v4, vcc
	v_cndmask_b32_e64 v12, v12, 3, vcc
	v_cmp_gt_f32_e32 vcc, v9, v2
	s_nop 1
	v_cndmask_b32_e32 v2, v2, v9, vcc
	v_cndmask_b32_e64 v12, v12, 4, vcc
	v_cmp_gt_f32_e32 vcc, v10, v2
	s_nop 1
	v_cndmask_b32_e32 v2, v2, v10, vcc
	v_cndmask_b32_e64 v12, v12, 5, vcc
	v_cmp_ngt_f32_e32 vcc, v11, v2
	s_nop 1
	v_cndmask_b32_e32 v2, v11, v2, vcc
	v_cndmask_b32_e32 v12, 6, v12, vcc
	v_cmp_gt_f32_e64 s[48:49], v5, v2
	s_or_b64 s[0:1], vcc, s[48:49]
	v_cmp_ngt_f32_e64 s[46:47], v5, v2
	v_cndmask_b32_e64 v172, v12, 7, s[48:49]
	v_cmp_ne_u32_e64 s[50:51], 0, v172
	s_and_b64 s[50:51], s[50:51], s[52:53]
	s_nop 0
	v_cndmask_b32_e64 v7, v196, v7, s[50:51]
	v_cmp_ne_u32_e64 s[50:51], 1, v172
	v_cmp_gt_f32_e64 s[52:53], v6, v7
	s_and_b64 s[50:51], s[50:51], s[52:53]
	v_cndmask_b32_e64 v6, v7, v6, s[50:51]
	v_cndmask_b32_e64 v7, 0, 1, s[50:51]
	v_cmp_ne_u32_e64 s[50:51], 2, v172
	v_cmp_gt_f32_e64 s[52:53], v3, v6
	s_and_b64 s[50:51], s[50:51], s[52:53]
	v_cndmask_b32_e64 v3, v6, v3, s[50:51]
	v_cndmask_b32_e64 v6, v7, 2, s[50:51]
	v_cmp_ne_u32_e64 s[50:51], 3, v172
	v_cmp_gt_f32_e64 s[52:53], v4, v3
	s_and_b64 s[50:51], s[50:51], s[52:53]
	v_cndmask_b32_e64 v3, v3, v4, s[50:51]
	v_cndmask_b32_e64 v4, v6, 3, s[50:51]
	v_cmp_ne_u32_e64 s[50:51], 4, v172
	v_cmp_gt_f32_e64 s[52:53], v9, v3
	s_and_b64 s[50:51], s[50:51], s[52:53]
	v_cndmask_b32_e64 v3, v3, v9, s[50:51]
	v_cndmask_b32_e64 v4, v4, 4, s[50:51]
	v_cmp_ne_u32_e64 s[50:51], 5, v172
	v_cmp_gt_f32_e64 s[52:53], v10, v3
	s_and_b64 s[50:51], s[50:51], s[52:53]
	v_cndmask_b32_e64 v3, v3, v10, s[50:51]
	v_cmp_gt_f32_e32 vcc, v11, v3
	v_cndmask_b32_e64 v4, v4, 5, s[50:51]
	s_and_b64 vcc, s[0:1], vcc
	v_cndmask_b32_e32 v43, v3, v11, vcc
	v_cndmask_b32_e64 v9, v4, 6, vcc
	s_and_saveexec_b64 s[0:1], s[46:47]
	s_cbranch_execz .LBB0_1340
	v_cmp_gt_f32_e32 vcc, v5, v43
	s_and_saveexec_b64 s[2:3], vcc
	v_mov_b32_e32 v9, 7
	v_mov_b32_e32 v43, v5
	s_or_b64 exec, exec, s[2:3]
	v_mov_b32_e32 v5, v2

.LBB0_1348:
	s_or_b64 exec, exec, s[0:1]
	s_waitcnt lgkmcnt(1)
	v_readfirstlane_b32 s19, v0
	s_waitcnt lgkmcnt(0)
	v_readfirstlane_b32 s54, v1
	s_or_b32 s26, s18, 2
	s_max_i32 s12, s26, 4
	s_add_i32 s12, s12, -4
	s_mov_b32 s13, s60
	s_lshl_b64 s[96:97], s[12:13], 12
	s_max_i32 s12, s26, 3
	s_add_i32 s12, s12, -3
	s_lshl_b64 s[52:53], s[12:13], 12
	s_max_i32 s12, s26, 2
	s_add_i32 s12, s12, -2
	s_lshl_b64 s[50:51], s[12:13], 12
	s_max_i32 s12, s26, 1
	s_add_i32 s12, s12, -1
	s_lshl_b64 s[48:49], s[12:13], 12
	s_max_i32 s12, s26, 0
	s_lshl_b64 s[46:47], s[12:13], 12
	s_max_i32 s12, s26, -1
	s_and_b32 s14, s26, 0x7fe
	s_add_i32 s12, s12, 1
	s_lshl_b64 s[92:93], s[12:13], 12
	s_min_u32 s12, s14, 15
	s_add_i32 s12, s12, 1
	s_min_u32 s13, s14, 14
	v_cvt_f32_ubyte0_e32 v0, s12
	s_add_i32 s15, s13, 2
	v_div_scale_f32 v1, s[12:13], v0, v0, 1.0
	v_rcp_f32_e32 v2, v1
	s_max_i32 s0, s26, 15
	s_add_i32 s0, s0, -15
	s_mov_b32 s1, s60
	v_fma_f32 v3, -v1, v2, 1.0
	v_fmac_f32_e32 v2, v3, v2
	v_div_scale_f32 v3, vcc, 1.0, v0, 1.0
	v_mul_f32_e32 v10, v3, v2
	v_fma_f32 v11, -v1, v10, v3
	v_fmac_f32_e32 v10, v11, v2
	v_fma_f32 v1, -v1, v10, v3
	v_div_fmas_f32 v1, v1, v2, v10
	v_div_fixup_f32 v90, v1, v0, 1.0
	v_cvt_f32_ubyte0_e32 v0, s15
	v_div_scale_f32 v1, s[12:13], v0, v0, 1.0
	v_rcp_f32_e32 v2, v1
	s_min_u32 s12, s14, 7
	s_add_i32 s12, s12, 1
	s_min_u32 s13, s14, 6
	v_fma_f32 v3, -v1, v2, 1.0
	v_fmac_f32_e32 v2, v3, v2
	v_div_scale_f32 v3, vcc, 1.0, v0, 1.0
	v_mul_f32_e32 v10, v3, v2
	v_fma_f32 v11, -v1, v10, v3
	v_fmac_f32_e32 v10, v11, v2
	v_fma_f32 v1, -v1, v10, v3
	v_div_fmas_f32 v1, v1, v2, v10
	v_div_fixup_f32 v92, v1, v0, 1.0
	v_cvt_f32_ubyte0_e32 v0, s12
	s_add_i32 s15, s13, 2
	v_div_scale_f32 v1, s[12:13], v0, v0, 1.0
	v_rcp_f32_e32 v2, v1
	s_lshl_b64 s[42:43], s[0:1], 12
	s_max_i32 s0, s26, 14
	s_add_i32 s0, s0, -14
	v_fma_f32 v3, -v1, v2, 1.0
	v_fmac_f32_e32 v2, v3, v2
	v_div_scale_f32 v3, vcc, 1.0, v0, 1.0
	v_mul_f32_e32 v10, v3, v2
	v_fma_f32 v11, -v1, v10, v3
	v_fmac_f32_e32 v10, v11, v2
	v_fma_f32 v1, -v1, v10, v3
	v_div_fmas_f32 v1, v1, v2, v10
	v_div_fixup_f32 v118, v1, v0, 1.0
	v_cvt_f32_ubyte0_e32 v0, s15
	v_div_scale_f32 v1, s[12:13], v0, v0, 1.0
	v_rcp_f32_e32 v2, v1
	s_lshl_b64 s[88:89], s[0:1], 12
	s_max_i32 s0, s26, 13
	s_add_i32 s0, s0, -13
	s_lshl_b64 s[36:37], s[0:1], 12
	s_max_i32 s0, s26, 12
	v_fma_f32 v3, -v1, v2, 1.0
	s_add_i32 s0, s0, -12
	v_fmac_f32_e32 v2, v3, v2
	v_div_scale_f32 v3, vcc, 1.0, v0, 1.0
	s_lshl_b64 s[78:79], s[0:1], 12
	s_max_i32 s0, s26, 11
	v_mul_f32_e32 v10, v3, v2
	s_add_i32 s0, s0, -11
	v_fma_f32 v11, -v1, v10, v3
	s_lshl_b64 s[76:77], s[0:1], 12
	s_max_i32 s0, s26, 10
	v_fmac_f32_e32 v10, v11, v2
	s_add_i32 s0, s0, -10
	v_fma_f32 v1, -v1, v10, v3
	s_min_u32 s12, s14, 3
	s_lshl_b64 s[10:11], s[0:1], 12
	s_max_i32 s0, s26, 9
	v_div_fmas_f32 v1, v1, v2, v10
	s_add_i32 s12, s12, 1
	s_add_i32 s0, s0, -9
	v_div_fixup_f32 v120, v1, v0, 1.0
	v_cvt_f32_ubyte0_e32 v0, s12
	s_lshl_b64 s[8:9], s[0:1], 12
	s_max_i32 s0, s26, 8
	v_div_scale_f32 v1, s[12:13], v0, v0, 1.0
	s_add_i32 s0, s0, -8
	v_rcp_f32_e32 v2, v1
	s_lshl_b64 s[44:45], s[0:1], 12
	s_max_i32 s0, s26, 7
	s_add_i32 s0, s0, -7
	s_lshl_b64 s[86:87], s[0:1], 12
	s_max_i32 s0, s26, 6
	s_max_i32 s2, s26, 5
	s_add_i32 s0, s0, -6
	s_add_i32 s2, s2, -5
	s_mov_b32 s3, s60
	v_fma_f32 v3, -v1, v2, 1.0
	s_ashr_i32 s27, s26, 31
	s_lshl_b64 s[0:1], s[0:1], 12
	s_lshl_b64 s[2:3], s[2:3], 12
	v_fmac_f32_e32 v2, v3, v2
	v_div_scale_f32 v3, vcc, 1.0, v0, 1.0
	s_lshl_b64 s[12:13], s[26:27], 12
	v_mul_f32_e32 v10, v3, v2
	s_add_u32 s30, s4, s12
	v_fma_f32 v11, -v1, v10, v3
	s_addc_u32 s31, s5, s13
	s_or_b32 s24, s18, 3
	v_fmac_f32_e32 v10, v11, v2
	s_ashr_i32 s25, s24, 31
	v_fma_f32 v1, -v1, v10, v3
	s_lshl_b64 s[12:13], s[24:25], 12
	v_mov_b32_e32 v55, v21
	v_div_fmas_f32 v1, v1, v2, v10
	s_add_u32 s28, s4, s12
	s_addc_u32 s29, s5, s13
	v_lshlrev_b32_e32 v10, 2, v55
	v_ashrrev_i32_e32 v11, 31, v10
	v_readlane_b32 s12, v253, 40
	v_lshlrev_b64 v[82:83], 1, v[10:11]
	v_readlane_b32 s13, v253, 41
	v_mov_b32_e32 v53, s7
	v_div_fixup_f32 v102, v1, v0, 1.0
	v_lshl_add_u64 v[10:11], s[12:13], 0, v[82:83]
	v_lshl_add_u64 v[236:237], v[10:11], 0, s[92:93]
	global_load_dwordx2 v[236:237], v[236:237], off
	v_lshl_add_u64 v[238:239], v[10:11], 0, s[48:49]
	global_load_dwordx2 v[238:239], v[238:239], off
	v_lshl_add_u64 v[240:241], v[10:11], 0, s[46:47]
	global_load_dwordx2 v[240:241], v[240:241], off
	v_lshl_add_u64 v[242:243], s[30:31], 0, v[82:83]
	global_load_dwordx2 v[242:243], v[242:243], off
	s_nop 0
	s_nop 0
	s_nop 0
	s_nop 0
	s_nop 0
	ds_read_b96 v[0:2], v53 offset:64
	s_nop 0
	s_add_u32 vcc_lo, s12, s92
	s_addc_u32 vcc_hi, s13, s93
	s_mov_b64 s[92:93], s[12:13]
	s_add_u32 s48, s92, s48
	s_addc_u32 s49, s93, s49
	s_add_u32 s46, s92, s46
	s_addc_u32 s47, s93, s47
	s_add_u32 s52, s92, s52
	s_addc_u32 s53, s93, s53
	s_add_u32 s50, s92, s50
	s_addc_u32 s51, s93, s51
	s_mov_b32 s12, 0x3e800000
	s_nop 0
	s_waitcnt vmcnt(3)
	v_lshlrev_b32_e32 v14, 16, v236
	v_and_b32_e32 v15, 0xffff0000, v236
	s_nop 0
	s_waitcnt vmcnt(2)
	v_lshlrev_b32_e32 v88, 16, v238
	v_and_b32_e32 v89, 0xffff0000, v238
	v_lshlrev_b32_e32 v86, 16, v239
	v_and_b32_e32 v87, 0xffff0000, v239
	s_waitcnt lgkmcnt(0)
	v_pk_fma_f32 v[94:95], v[0:1], v[88:89], 0 op_sel_hi:[0,1,0]
	v_pk_fma_f32 v[96:97], v[0:1], v[86:87], 0 op_sel_hi:[0,1,0]
	s_nop 0
	s_waitcnt vmcnt(1)
	v_lshlrev_b32_e32 v98, 16, v240
	v_and_b32_e32 v99, 0xffff0000, v240
	v_lshlrev_b32_e32 v10, 16, v241
	v_and_b32_e32 v11, 0xffff0000, v241
	v_pk_mul_f32 v[100:101], v[0:1], v[10:11] op_sel:[1,0]
	v_pk_fma_f32 v[10:11], v[0:1], v[10:11], v[96:97] op_sel:[1,0,0]
	v_pk_fma_f32 v[94:95], v[0:1], v[98:99], v[94:95] op_sel:[1,0,0]
	v_lshlrev_b32_e32 v12, 16, v237
	v_and_b32_e32 v13, 0xffff0000, v237
	v_pk_mul_f32 v[104:105], v[0:1], v[98:99] op_sel:[1,0]
	v_pk_fma_f32 v[88:89], v[0:1], v[88:89], v[94:95] op_sel_hi:[0,1,1] neg_lo:[1,0,0] neg_hi:[1,0,0]
	v_pk_fma_f32 v[0:1], v[0:1], v[86:87], v[10:11] op_sel_hi:[0,1,1] neg_lo:[1,0,0] neg_hi:[1,0,0]
	v_pk_mul_f32 v[84:85], v[2:3], v[12:13] op_sel_hi:[0,1]
	v_pk_fma_f32 v[0:1], v[2:3], v[12:13], v[0:1] op_sel_hi:[0,1,1]
	v_pk_mul_f32 v[80:81], v[2:3], v[14:15] op_sel_hi:[0,1]
	v_pk_fma_f32 v[2:3], v[2:3], v[14:15], v[88:89] op_sel_hi:[0,1,1]
	v_pk_fma_f32 v[14:15], v[0:1], 0.5, v[84:85] op_sel_hi:[1,0,1] neg_lo:[0,0,1] neg_hi:[0,0,1]
	v_lshl_add_u64 v[84:85], s[30:31], 0, v[82:83]
	s_nop 0
	v_lshl_add_u32 v0, v55, 4, s17
	v_pk_fma_f32 v[80:81], v[2:3], 0.5, v[80:81] op_sel_hi:[1,0,1] neg_lo:[0,0,1] neg_hi:[0,0,1]
	ds_read_b128 v[0:3], v0
	v_pk_fma_f32 v[10:11], v[10:11], 0.5, v[100:101] op_sel_hi:[1,0,1] neg_lo:[0,0,1] neg_hi:[0,0,1]
	v_lshl_add_u64 v[82:83], s[28:29], 0, v[82:83]
	v_pk_fma_f32 v[12:13], v[94:95], 0.5, v[104:105] op_sel_hi:[1,0,1] neg_lo:[0,0,1] neg_hi:[0,0,1]
	s_nop 0
	s_waitcnt vmcnt(0)
	v_lshlrev_b32_e32 v88, 16, v242
	v_and_b32_e32 v89, 0xffff0000, v242
	v_lshlrev_b32_e32 v86, 16, v243
	v_and_b32_e32 v87, 0xffff0000, v243
	s_waitcnt lgkmcnt(0)
	v_pk_fma_f32 v[10:11], v[2:3], v[10:11], v[86:87]
	global_load_dwordx2 v[86:87], v[82:83], off
	v_pk_fma_f32 v[12:13], v[0:1], v[12:13], v[88:89]
	s_nop 0
	s_waitcnt vmcnt(0)
	v_lshlrev_b32_e32 v88, 16, v86
	v_and_b32_e32 v89, 0xffff0000, v86
	v_lshlrev_b32_e32 v86, 16, v87
	v_and_b32_e32 v87, 0xffff0000, v87
	v_pk_fma_f32 v[80:81], v[0:1], v[80:81], v[88:89]
	v_cvt_pk_bf16_f32 v0, v12, v13
	v_cvt_pk_bf16_f32 v1, v10, v11
	v_pk_fma_f32 v[14:15], v[2:3], v[14:15], v[86:87]
	v_cvt_pk_bf16_f32 v2, v80, v81
	s_nop 0
	v_cvt_pk_bf16_f32 v3, v14, v15
	global_store_dwordx2 v[84:85], v[0:1], off
	global_store_dwordx2 v[82:83], v[2:3], off
	v_mov_b32_e32 v0, v21
	s_nop 0
	v_lshlrev_b32_e32 v82, 2, v0
	v_add_u32_e32 v84, 0x100, v82
	v_ashrrev_i32_e32 v85, 31, v84
	v_lshlrev_b64 v[86:87], 1, v[84:85]
	v_lshl_add_u64 v[236:237], vcc, 0, v[86:87]
	global_load_dwordx2 v[236:237], v[236:237], off
	v_lshl_add_u64 v[238:239], s[48:49], 0, v[86:87]
	global_load_dwordx2 v[238:239], v[238:239], off
	v_lshl_add_u64 v[240:241], s[46:47], 0, v[86:87]
	global_load_dwordx2 v[240:241], v[240:241], off
	s_nop 0
	s_nop 0
	s_nop 0
	s_nop 0
	s_nop 0
	ds_read_b96 v[0:2], v53 offset:64
	s_nop 0
	v_ashrrev_i32_e32 v83, 31, v82
	s_nop 0
	s_waitcnt vmcnt(2)
	v_lshlrev_b32_e32 v94, 16, v236
	v_and_b32_e32 v95, 0xffff0000, v236
	s_nop 0
	s_waitcnt vmcnt(1)
	v_lshlrev_b32_e32 v104, 16, v238
	v_and_b32_e32 v105, 0xffff0000, v238
	v_lshlrev_b32_e32 v100, 16, v239
	v_and_b32_e32 v101, 0xffff0000, v239
	s_waitcnt lgkmcnt(0)
	v_pk_fma_f32 v[106:107], v[0:1], v[104:105], 0 op_sel_hi:[0,1,0]
	v_pk_fma_f32 v[108:109], v[0:1], v[100:101], 0 op_sel_hi:[0,1,0]
	s_nop 0
	s_waitcnt vmcnt(0)
	v_lshlrev_b32_e32 v110, 16, v240
	v_and_b32_e32 v111, 0xffff0000, v240
	v_lshlrev_b32_e32 v86, 16, v241
	v_and_b32_e32 v87, 0xffff0000, v241
	v_pk_fma_f32 v[108:109], v[0:1], v[86:87], v[108:109] op_sel:[1,0,0]
	v_pk_fma_f32 v[106:107], v[0:1], v[110:111], v[106:107] op_sel:[1,0,0]
	v_lshlrev_b32_e32 v88, 16, v237
	v_and_b32_e32 v89, 0xffff0000, v237
	v_pk_mul_f32 v[112:113], v[0:1], v[86:87] op_sel:[1,0]
	v_pk_mul_f32 v[114:115], v[0:1], v[110:111] op_sel:[1,0]
	v_pk_fma_f32 v[86:87], v[0:1], v[104:105], v[106:107] op_sel_hi:[0,1,1] neg_lo:[1,0,0] neg_hi:[1,0,0]
	v_pk_fma_f32 v[0:1], v[0:1], v[100:101], v[108:109] op_sel_hi:[0,1,1] neg_lo:[1,0,0] neg_hi:[1,0,0]
	v_lshlrev_b64 v[100:101], 1, v[82:83]
	v_pk_mul_f32 v[96:97], v[2:3], v[88:89] op_sel_hi:[0,1]
	v_pk_mul_f32 v[98:99], v[2:3], v[94:95] op_sel_hi:[0,1]
	v_pk_fma_f32 v[0:1], v[2:3], v[88:89], v[0:1] op_sel_hi:[0,1,1]
	v_pk_fma_f32 v[2:3], v[2:3], v[94:95], v[86:87] op_sel_hi:[0,1,1]
	v_lshl_add_u64 v[236:237], s[30:31], 0, v[100:101]
	global_load_dwordx2 v[236:237], v[236:237], off offset:512
	v_lshl_add_u64 v[238:239], s[28:29], 0, v[100:101]
	global_load_dwordx2 v[238:239], v[238:239], off offset:512
	v_lshl_add_u64 v[94:95], s[30:31], 0, v[100:101]
	s_nop 0
	v_pk_fma_f32 v[86:87], v[0:1], 0.5, v[96:97] op_sel_hi:[1,0,1] neg_lo:[0,0,1] neg_hi:[0,0,1]
	v_lshl_add_u32 v0, v84, 2, s17
	v_pk_fma_f32 v[88:89], v[2:3], 0.5, v[98:99] op_sel_hi:[1,0,1] neg_lo:[0,0,1] neg_hi:[0,0,1]
	ds_read_b128 v[0:3], v0
	v_pk_fma_f32 v[96:97], v[106:107], 0.5, v[114:115] op_sel_hi:[1,0,1] neg_lo:[0,0,1] neg_hi:[0,0,1]
	v_pk_fma_f32 v[98:99], v[108:109], 0.5, v[112:113] op_sel_hi:[1,0,1] neg_lo:[0,0,1] neg_hi:[0,0,1]
	s_nop 0
	s_waitcnt vmcnt(1)
	v_lshlrev_b32_e32 v84, 16, v236
	v_and_b32_e32 v85, 0xffff0000, v236
	v_lshlrev_b32_e32 v82, 16, v237
	v_and_b32_e32 v83, 0xffff0000, v237
	s_waitcnt lgkmcnt(0)
	v_pk_fma_f32 v[84:85], v[0:1], v[96:97], v[84:85]
	v_lshl_add_u64 v[96:97], s[28:29], 0, v[100:101]
	v_pk_fma_f32 v[82:83], v[2:3], v[98:99], v[82:83]
	s_nop 0
	s_nop 0
	s_waitcnt vmcnt(0)
	v_lshlrev_b32_e32 v100, 16, v238
	v_and_b32_e32 v101, 0xffff0000, v238
	v_lshlrev_b32_e32 v98, 16, v239
	v_and_b32_e32 v99, 0xffff0000, v239
	v_pk_fma_f32 v[88:89], v[0:1], v[88:89], v[100:101]
	v_cvt_pk_bf16_f32 v0, v84, v85
	v_cvt_pk_bf16_f32 v1, v82, v83
	v_pk_fma_f32 v[86:87], v[2:3], v[86:87], v[98:99]
	v_cvt_pk_bf16_f32 v2, v88, v89
	s_nop 0
	v_cvt_pk_bf16_f32 v3, v86, v87
	global_store_dwordx2 v[94:95], v[0:1], off offset:512
	global_store_dwordx2 v[96:97], v[2:3], off offset:512
	v_mov_b32_e32 v0, v21
	ds_read_b32 v98, v53 offset:72
	v_lshlrev_b32_e32 v94, 2, v0
	v_add_u32_e32 v96, 0x200, v94
	v_ashrrev_i32_e32 v97, 31, v96
	v_lshlrev_b64 v[100:101], 1, v[96:97]
	v_lshl_add_u64 v[236:237], vcc, 0, v[100:101]
	global_load_dwordx2 v[236:237], v[236:237], off
	v_lshl_add_u64 v[238:239], s[52:53], 0, v[100:101]
	global_load_dwordx2 v[238:239], v[238:239], off
	v_lshl_add_u64 v[240:241], s[50:51], 0, v[100:101]
	global_load_dwordx2 v[240:241], v[240:241], off
	v_lshl_add_u64 v[242:243], s[48:49], 0, v[100:101]
	global_load_dwordx2 v[242:243], v[242:243], off
	v_lshl_add_u64 v[244:245], s[46:47], 0, v[100:101]
	global_load_dwordx2 v[244:245], v[244:245], off
	s_nop 0
	s_nop 0
	s_nop 0
	s_nop 0
	s_nop 0
	s_nop 0
	v_ashrrev_i32_e32 v95, 31, v94
	s_nop 0
	s_waitcnt vmcnt(4)
	v_lshlrev_b32_e32 v104, 16, v236
	v_and_b32_e32 v105, 0xffff0000, v236
	v_lshlrev_b32_e32 v106, 16, v237
	v_and_b32_e32 v107, 0xffff0000, v237
	ds_read2_b64 v[0:3], v53 offset0:7 offset1:8
	s_nop 0
	s_waitcnt vmcnt(3)
	v_lshlrev_b32_e32 v114, 16, v238
	v_and_b32_e32 v115, 0xffff0000, v238
	v_lshlrev_b32_e32 v112, 16, v239
	v_and_b32_e32 v113, 0xffff0000, v239
	s_waitcnt lgkmcnt(0)
	v_pk_fma_f32 v[122:123], v[0:1], v[112:113], 0 op_sel_hi:[0,1,0]
	s_nop 0
	s_waitcnt vmcnt(2)
	v_lshlrev_b32_e32 v126, 16, v240
	v_and_b32_e32 v127, 0xffff0000, v240
	v_lshlrev_b32_e32 v124, 16, v241
	v_and_b32_e32 v125, 0xffff0000, v241
	v_pk_fma_f32 v[122:123], v[0:1], v[124:125], v[122:123] op_sel:[1,0,0]
	s_nop 0
	s_nop 0
	s_nop 0
	s_nop 0
	v_pk_fma_f32 v[116:117], v[0:1], v[114:115], 0 op_sel_hi:[0,1,0]
	v_pk_fma_f32 v[116:117], v[0:1], v[126:127], v[116:117] op_sel:[1,0,0]
	v_pk_mul_f32 v[108:109], v[98:99], v[106:107] op_sel_hi:[0,1]
	v_pk_mul_f32 v[110:111], v[98:99], v[104:105] op_sel_hi:[0,1]
	s_nop 0
	s_waitcnt vmcnt(1)
	v_lshlrev_b32_e32 v126, 16, v242
	v_and_b32_e32 v127, 0xffff0000, v242
	v_lshlrev_b32_e32 v124, 16, v243
	v_and_b32_e32 v125, 0xffff0000, v243
	v_pk_fma_f32 v[116:117], v[2:3], v[126:127], v[116:117] op_sel_hi:[0,1,1]
	v_pk_fma_f32 v[122:123], v[2:3], v[124:125], v[122:123] op_sel_hi:[0,1,1]
	s_nop 0
	s_waitcnt vmcnt(0)
	v_lshlrev_b32_e32 v124, 16, v244
	v_and_b32_e32 v125, 0xffff0000, v244
	v_lshlrev_b32_e32 v100, 16, v245
	v_and_b32_e32 v101, 0xffff0000, v245
	v_mov_b32_e32 v2, v3
	v_pk_mul_f32 v[126:127], v[2:3], v[100:101] op_sel_hi:[0,1]
	v_pk_mul_f32 v[128:129], v[2:3], v[124:125] op_sel_hi:[0,1]
	v_pk_fma_f32 v[122:123], v[2:3], v[100:101], v[122:123] op_sel_hi:[0,1,1]
	v_pk_fma_f32 v[2:3], v[2:3], v[124:125], v[116:117] op_sel_hi:[0,1,1]
	v_pk_fma_f32 v[100:101], v[0:1], v[114:115], v[2:3] op_sel_hi:[0,1,1] neg_lo:[1,0,0] neg_hi:[1,0,0]
	v_pk_fma_f32 v[0:1], v[0:1], v[112:113], v[122:123] op_sel_hi:[0,1,1] neg_lo:[1,0,0] neg_hi:[1,0,0]
	v_pk_fma_f32 v[0:1], v[98:99], v[106:107], v[0:1] op_sel_hi:[0,1,1]
	v_pk_fma_f32 v[98:99], v[98:99], v[104:105], v[100:101] op_sel_hi:[0,1,1]
	v_pk_fma_f32 v[100:101], v[98:99], s[12:13], v[110:111] op_sel_hi:[1,0,1] neg_lo:[0,0,1] neg_hi:[0,0,1]
	v_lshlrev_b64 v[110:111], 1, v[94:95]
	v_lshl_add_u64 v[236:237], s[30:31], 0, v[110:111]
	global_load_dwordx2 v[236:237], v[236:237], off offset:1024
	v_lshl_add_u64 v[238:239], s[28:29], 0, v[110:111]
	global_load_dwordx2 v[238:239], v[238:239], off offset:1024
	v_lshl_add_u64 v[104:105], s[30:31], 0, v[110:111]
	s_nop 0
	v_pk_fma_f32 v[98:99], v[0:1], s[12:13], v[108:109] op_sel_hi:[1,0,1] neg_lo:[0,0,1] neg_hi:[0,0,1]
	v_lshl_add_u32 v0, v96, 2, s17
	v_pk_fma_f32 v[106:107], v[102:103], v[2:3], v[128:129] op_sel_hi:[0,1,1] neg_lo:[0,0,1] neg_hi:[0,0,1]
	ds_read_b128 v[0:3], v0
	v_pk_fma_f32 v[108:109], v[102:103], v[122:123], v[126:127] op_sel_hi:[0,1,1] neg_lo:[0,0,1] neg_hi:[0,0,1]
	s_nop 0
	s_waitcnt vmcnt(1)
	v_lshlrev_b32_e32 v96, 16, v236
	v_and_b32_e32 v97, 0xffff0000, v236
	v_lshlrev_b32_e32 v94, 16, v237
	v_and_b32_e32 v95, 0xffff0000, v237
	s_waitcnt lgkmcnt(0)
	v_pk_fma_f32 v[96:97], v[0:1], v[106:107], v[96:97]
	v_lshl_add_u64 v[106:107], s[28:29], 0, v[110:111]
	v_pk_fma_f32 v[94:95], v[2:3], v[108:109], v[94:95]
	s_nop 0
	s_nop 0
	s_waitcnt vmcnt(0)
	v_lshlrev_b32_e32 v110, 16, v238
	v_and_b32_e32 v111, 0xffff0000, v238
	v_lshlrev_b32_e32 v108, 16, v239
	v_and_b32_e32 v109, 0xffff0000, v239
	v_pk_fma_f32 v[100:101], v[0:1], v[100:101], v[110:111]
	v_cvt_pk_bf16_f32 v0, v96, v97
	v_cvt_pk_bf16_f32 v1, v94, v95
	v_pk_fma_f32 v[98:99], v[2:3], v[98:99], v[108:109]
	v_cvt_pk_bf16_f32 v2, v100, v101
	s_nop 0
	v_cvt_pk_bf16_f32 v3, v98, v99
	global_store_dwordx2 v[104:105], v[0:1], off offset:1024
	global_store_dwordx2 v[106:107], v[2:3], off offset:1024
	v_mov_b32_e32 v0, v21
	ds_read_b32 v106, v53 offset:72
	v_lshlrev_b32_e32 v104, 2, v0
	v_add_u32_e32 v110, 0x300, v104
	v_ashrrev_i32_e32 v111, 31, v110
	v_lshlrev_b64 v[108:109], 1, v[110:111]
	v_lshl_add_u64 v[236:237], vcc, 0, v[108:109]
	global_load_dwordx2 v[236:237], v[236:237], off
	v_lshl_add_u64 v[238:239], s[52:53], 0, v[108:109]
	global_load_dwordx2 v[238:239], v[238:239], off
	v_lshl_add_u64 v[240:241], s[50:51], 0, v[108:109]
	global_load_dwordx2 v[240:241], v[240:241], off
	v_lshl_add_u64 v[242:243], s[48:49], 0, v[108:109]
	global_load_dwordx2 v[242:243], v[242:243], off
	v_lshl_add_u64 v[244:245], s[46:47], 0, v[108:109]
	global_load_dwordx2 v[244:245], v[244:245], off
	s_nop 0
	s_nop 0
	s_nop 0
	s_nop 0
	s_nop 0
	s_nop 0
	v_ashrrev_i32_e32 v105, 31, v104
	s_nop 0
	s_waitcnt vmcnt(4)
	v_lshlrev_b32_e32 v112, 16, v236
	v_and_b32_e32 v113, 0xffff0000, v236
	v_lshlrev_b32_e32 v114, 16, v237
	v_and_b32_e32 v115, 0xffff0000, v237
	ds_read2_b64 v[0:3], v53 offset0:7 offset1:8
	s_nop 0
	s_waitcnt vmcnt(3)
	v_lshlrev_b32_e32 v126, 16, v238
	v_and_b32_e32 v127, 0xffff0000, v238
	v_lshlrev_b32_e32 v124, 16, v239
	v_and_b32_e32 v125, 0xffff0000, v239
	s_waitcnt lgkmcnt(0)
	v_pk_fma_f32 v[130:131], v[0:1], v[124:125], 0 op_sel_hi:[0,1,0]
	s_nop 0
	s_waitcnt vmcnt(2)
	v_lshlrev_b32_e32 v134, 16, v240
	v_and_b32_e32 v135, 0xffff0000, v240
	v_lshlrev_b32_e32 v132, 16, v241
	v_and_b32_e32 v133, 0xffff0000, v241
	v_pk_fma_f32 v[130:131], v[0:1], v[132:133], v[130:131] op_sel:[1,0,0]
	s_nop 0
	s_nop 0
	s_nop 0
	s_nop 0
	v_pk_fma_f32 v[128:129], v[0:1], v[126:127], 0 op_sel_hi:[0,1,0]
	v_pk_fma_f32 v[128:129], v[0:1], v[134:135], v[128:129] op_sel:[1,0,0]
	v_pk_mul_f32 v[116:117], v[106:107], v[114:115] op_sel_hi:[0,1]
	v_pk_mul_f32 v[122:123], v[106:107], v[112:113] op_sel_hi:[0,1]
	s_nop 0
	s_waitcnt vmcnt(1)
	v_lshlrev_b32_e32 v134, 16, v242
	v_and_b32_e32 v135, 0xffff0000, v242
	v_lshlrev_b32_e32 v132, 16, v243
	v_and_b32_e32 v133, 0xffff0000, v243
	v_pk_fma_f32 v[128:129], v[2:3], v[134:135], v[128:129] op_sel_hi:[0,1,1]
	v_pk_fma_f32 v[130:131], v[2:3], v[132:133], v[130:131] op_sel_hi:[0,1,1]
	s_nop 0
	s_waitcnt vmcnt(0)
	v_lshlrev_b32_e32 v132, 16, v244
	v_and_b32_e32 v133, 0xffff0000, v244
	v_lshlrev_b32_e32 v108, 16, v245
	v_and_b32_e32 v109, 0xffff0000, v245
	v_mov_b32_e32 v2, v3
	v_pk_mul_f32 v[134:135], v[2:3], v[108:109] op_sel_hi:[0,1]
	v_pk_mul_f32 v[136:137], v[2:3], v[132:133] op_sel_hi:[0,1]
	v_pk_fma_f32 v[130:131], v[2:3], v[108:109], v[130:131] op_sel_hi:[0,1,1]
	v_pk_fma_f32 v[2:3], v[2:3], v[132:133], v[128:129] op_sel_hi:[0,1,1]
	v_pk_fma_f32 v[108:109], v[0:1], v[126:127], v[2:3] op_sel_hi:[0,1,1] neg_lo:[1,0,0] neg_hi:[1,0,0]
	v_pk_fma_f32 v[0:1], v[0:1], v[124:125], v[130:131] op_sel_hi:[0,1,1] neg_lo:[1,0,0] neg_hi:[1,0,0]
	v_pk_fma_f32 v[0:1], v[106:107], v[114:115], v[0:1] op_sel_hi:[0,1,1]
	v_pk_fma_f32 v[106:107], v[106:107], v[112:113], v[108:109] op_sel_hi:[0,1,1]
	v_lshlrev_b64 v[114:115], 1, v[104:105]
	v_pk_fma_f32 v[108:109], v[106:107], s[12:13], v[122:123] op_sel_hi:[1,0,1] neg_lo:[0,0,1] neg_hi:[0,0,1]
	v_pk_fma_f32 v[106:107], v[0:1], s[12:13], v[116:117] op_sel_hi:[1,0,1] neg_lo:[0,0,1] neg_hi:[0,0,1]
	v_lshl_add_u32 v0, v110, 2, s17
	v_lshl_add_u64 v[236:237], s[30:31], 0, v[114:115]
	global_load_dwordx2 v[236:237], v[236:237], off offset:1536
	v_lshl_add_u64 v[238:239], s[28:29], 0, v[114:115]
	global_load_dwordx2 v[238:239], v[238:239], off offset:1536
	v_lshl_add_u64 v[110:111], s[30:31], 0, v[114:115]
	s_nop 0
	v_pk_fma_f32 v[112:113], v[102:103], v[2:3], v[136:137] op_sel_hi:[0,1,1] neg_lo:[0,0,1] neg_hi:[0,0,1]
	ds_read_b128 v[0:3], v0
	v_pk_fma_f32 v[102:103], v[102:103], v[130:131], v[134:135] op_sel_hi:[0,1,1] neg_lo:[0,0,1] neg_hi:[0,0,1]
	s_nop 0
	s_waitcnt vmcnt(1)
	v_lshlrev_b32_e32 v116, 16, v236
	v_and_b32_e32 v117, 0xffff0000, v236
	v_lshlrev_b32_e32 v104, 16, v237
	v_and_b32_e32 v105, 0xffff0000, v237
	s_waitcnt lgkmcnt(0)
	v_pk_fma_f32 v[102:103], v[2:3], v[102:103], v[104:105]
	v_pk_fma_f32 v[104:105], v[0:1], v[112:113], v[116:117]
	v_lshl_add_u64 v[112:113], s[28:29], 0, v[114:115]
	s_nop 0
	s_nop 0
	s_waitcnt vmcnt(0)
	v_lshlrev_b32_e32 v116, 16, v238
	v_and_b32_e32 v117, 0xffff0000, v238
	v_lshlrev_b32_e32 v114, 16, v239
	v_and_b32_e32 v115, 0xffff0000, v239
	v_pk_fma_f32 v[108:109], v[0:1], v[108:109], v[116:117]
	v_cvt_pk_bf16_f32 v0, v104, v105
	v_cvt_pk_bf16_f32 v1, v102, v103
	v_pk_fma_f32 v[106:107], v[2:3], v[106:107], v[114:115]
	v_cvt_pk_bf16_f32 v2, v108, v109
	s_nop 0
	v_cvt_pk_bf16_f32 v3, v106, v107
	global_store_dwordx2 v[110:111], v[0:1], off offset:1536
	global_store_dwordx2 v[112:113], v[2:3], off offset:1536
	v_mov_b32_e32 v0, v21
	s_add_u32 s86, s92, s86
	v_lshlrev_b32_e32 v110, 2, v0
	v_add_u32_e32 v112, 0x400, v110
	v_ashrrev_i32_e32 v113, 31, v112
	v_lshlrev_b64 v[128:129], 1, v[112:113]
	v_lshl_add_u64 v[0:1], vcc, 0, v[128:129]
	global_load_dwordx2 v[0:1], v[0:1], off
	s_addc_u32 s87, s93, s87
	s_add_u32 s0, s92, s0
	v_lshl_add_u64 v[130:131], s[86:87], 0, v[128:129]
	s_addc_u32 s1, s93, s1
	global_load_dwordx2 v[132:133], v[130:131], off
	v_lshl_add_u64 v[138:139], s[0:1], 0, v[128:129]
	global_load_dwordx2 v[138:139], v[138:139], off
	ds_read_b32 v114, v53 offset:72
	s_add_u32 s2, s92, s2
	s_addc_u32 s3, s93, s3
	s_add_u32 s96, s92, s96
	s_addc_u32 s97, s93, s97
	v_ashrrev_i32_e32 v111, 31, v110
	s_add_u32 s42, s92, s42
	s_addc_u32 s43, s93, s43
	s_add_u32 s88, s92, s88
	s_addc_u32 s89, s93, s89
	s_add_u32 s36, s92, s36
	s_addc_u32 s37, s93, s37
	s_add_u32 s78, s92, s78
	s_addc_u32 s79, s93, s79
	s_add_u32 s76, s92, s76
	s_addc_u32 s77, s93, s77
	s_add_u32 s10, s92, s10
	s_addc_u32 s11, s93, s11
	s_add_u32 s8, s92, s8
	s_addc_u32 s9, s93, s9
	s_add_u32 s44, s92, s44
	s_addc_u32 s45, s93, s45
	s_nop 0
	s_waitcnt vmcnt(2)
	v_lshlrev_b32_e32 v116, 16, v0
	v_and_b32_e32 v117, 0xffff0000, v0
	v_lshlrev_b32_e32 v124, 16, v1
	v_and_b32_e32 v125, 0xffff0000, v1
	ds_read2_b64 v[0:3], v53 offset0:5 offset1:6
	s_nop 0
	s_waitcnt vmcnt(1)
	v_lshlrev_b32_e32 v130, 16, v132
	v_and_b32_e32 v131, 0xffff0000, v132
	v_lshlrev_b32_e32 v132, 16, v133
	v_and_b32_e32 v133, 0xffff0000, v133
	s_waitcnt lgkmcnt(0)
	v_pk_fma_f32 v[136:137], v[0:1], v[132:133], 0 op_sel_hi:[0,1,0]
	s_nop 0
	s_waitcnt vmcnt(0)
	v_lshlrev_b32_e32 v140, 16, v138
	v_and_b32_e32 v141, 0xffff0000, v138
	v_lshlrev_b32_e32 v138, 16, v139
	v_and_b32_e32 v139, 0xffff0000, v139
	v_pk_fma_f32 v[136:137], v[0:1], v[138:139], v[136:137] op_sel:[1,0,0]
	v_lshl_add_u64 v[236:237], s[2:3], 0, v[128:129]
	global_load_dwordx2 v[236:237], v[236:237], off
	v_lshl_add_u64 v[238:239], s[96:97], 0, v[128:129]
	global_load_dwordx2 v[238:239], v[238:239], off
	v_lshl_add_u64 v[240:241], s[52:53], 0, v[128:129]
	global_load_dwordx2 v[240:241], v[240:241], off
	v_lshl_add_u64 v[242:243], s[50:51], 0, v[128:129]
	global_load_dwordx2 v[242:243], v[242:243], off
	v_lshl_add_u64 v[244:245], s[48:49], 0, v[128:129]
	global_load_dwordx2 v[244:245], v[244:245], off
	v_lshl_add_u64 v[246:247], s[46:47], 0, v[128:129]
	global_load_dwordx2 v[246:247], v[246:247], off
	s_nop 0
	s_nop 0
	v_pk_fma_f32 v[134:135], v[0:1], v[130:131], 0 op_sel_hi:[0,1,0]
	v_pk_fma_f32 v[134:135], v[0:1], v[140:141], v[134:135] op_sel:[1,0,0]
	v_pk_mul_f32 v[122:123], v[114:115], v[124:125] op_sel_hi:[0,1]
	v_pk_mul_f32 v[126:127], v[114:115], v[116:117] op_sel_hi:[0,1]
	s_nop 0
	s_waitcnt vmcnt(5)
	v_lshlrev_b32_e32 v140, 16, v236
	v_and_b32_e32 v141, 0xffff0000, v236
	v_lshlrev_b32_e32 v138, 16, v237
	v_and_b32_e32 v139, 0xffff0000, v237
	v_pk_fma_f32 v[136:137], v[2:3], v[138:139], v[136:137] op_sel_hi:[0,1,1]
	s_nop 0
	s_nop 0
	v_pk_fma_f32 v[134:135], v[2:3], v[140:141], v[134:135] op_sel_hi:[0,1,1]
	v_mov_b32_e32 v2, v3
	s_nop 0
	s_waitcnt vmcnt(4)
	v_lshlrev_b32_e32 v140, 16, v238
	v_and_b32_e32 v141, 0xffff0000, v238
	v_lshlrev_b32_e32 v138, 16, v239
	v_and_b32_e32 v139, 0xffff0000, v239
	v_pk_fma_f32 v[138:139], v[2:3], v[138:139], v[136:137] op_sel_hi:[0,1,1]
	v_pk_fma_f32 v[2:3], v[2:3], v[140:141], v[134:135] op_sel_hi:[0,1,1]
	s_nop 0
	s_nop 0
	ds_read2_b64 v[134:137], v53 offset0:7 offset1:8
	s_nop 0
	s_waitcnt vmcnt(3)
	v_lshlrev_b32_e32 v142, 16, v240
	v_and_b32_e32 v143, 0xffff0000, v240
	v_lshlrev_b32_e32 v140, 16, v241
	v_and_b32_e32 v141, 0xffff0000, v241
	s_waitcnt lgkmcnt(0)
	v_pk_fma_f32 v[138:139], v[134:135], v[140:141], v[138:139] op_sel_hi:[0,1,1]
	s_nop 0
	s_nop 0
	v_pk_fma_f32 v[2:3], v[134:135], v[142:143], v[2:3] op_sel_hi:[0,1,1]
	s_nop 0
	s_waitcnt vmcnt(2)
	v_lshlrev_b32_e32 v142, 16, v242
	v_and_b32_e32 v143, 0xffff0000, v242
	v_lshlrev_b32_e32 v140, 16, v243
	v_and_b32_e32 v141, 0xffff0000, v243
	v_pk_fma_f32 v[138:139], v[134:135], v[140:141], v[138:139] op_sel:[1,0,0]
	v_pk_fma_f32 v[2:3], v[134:135], v[142:143], v[2:3] op_sel:[1,0,0]
	s_nop 0
	s_nop 0
	s_nop 0
	s_nop 0
	s_nop 0
	s_waitcnt vmcnt(1)
	v_lshlrev_b32_e32 v140, 16, v244
	v_and_b32_e32 v141, 0xffff0000, v244
	v_lshlrev_b32_e32 v134, 16, v245
	v_and_b32_e32 v135, 0xffff0000, v245
	v_pk_fma_f32 v[2:3], v[136:137], v[140:141], v[2:3] op_sel_hi:[0,1,1]
	v_pk_fma_f32 v[134:135], v[136:137], v[134:135], v[138:139] op_sel_hi:[0,1,1]
	s_nop 0
	s_waitcnt vmcnt(0)
	v_lshlrev_b32_e32 v138, 16, v246
	v_and_b32_e32 v139, 0xffff0000, v246
	v_lshlrev_b32_e32 v128, 16, v247
	v_and_b32_e32 v129, 0xffff0000, v247
	v_mov_b32_e32 v136, v137
	v_pk_mul_f32 v[140:141], v[136:137], v[128:129] op_sel_hi:[0,1]
	v_pk_fma_f32 v[128:129], v[136:137], v[128:129], v[134:135] op_sel_hi:[0,1,1]
	v_pk_fma_f32 v[2:3], v[136:137], v[138:139], v[2:3] op_sel_hi:[0,1,1]
	v_pk_fma_f32 v[130:131], v[0:1], v[130:131], v[2:3] op_sel_hi:[0,1,1] neg_lo:[1,0,0] neg_hi:[1,0,0]
	v_pk_fma_f32 v[0:1], v[0:1], v[132:133], v[128:129] op_sel_hi:[0,1,1] neg_lo:[1,0,0] neg_hi:[1,0,0]
	v_pk_fma_f32 v[0:1], v[114:115], v[124:125], v[0:1] op_sel_hi:[0,1,1]
	v_pk_fma_f32 v[114:115], v[114:115], v[116:117], v[130:131] op_sel_hi:[0,1,1]
	v_pk_fma_f32 v[116:117], v[120:121], v[114:115], v[126:127] op_sel_hi:[0,1,1] neg_lo:[0,0,1] neg_hi:[0,0,1]
	v_pk_fma_f32 v[126:127], v[118:119], v[128:129], v[140:141] op_sel_hi:[0,1,1] neg_lo:[0,0,1] neg_hi:[0,0,1]
	v_lshlrev_b64 v[128:129], 1, v[110:111]
	v_pk_fma_f32 v[114:115], v[120:121], v[0:1], v[122:123] op_sel_hi:[0,1,1] neg_lo:[0,0,1] neg_hi:[0,0,1]
	v_lshl_add_u64 v[236:237], s[30:31], 0, v[128:129]
	global_load_dwordx2 v[236:237], v[236:237], off offset:2048
	v_lshl_add_u64 v[238:239], s[28:29], 0, v[128:129]
	global_load_dwordx2 v[238:239], v[238:239], off offset:2048
	v_lshl_add_u64 v[122:123], s[30:31], 0, v[128:129]
	s_nop 0
	v_pk_mul_f32 v[142:143], v[136:137], v[138:139] op_sel_hi:[0,1]
	v_lshl_add_u32 v0, v112, 2, s17
	v_pk_fma_f32 v[124:125], v[118:119], v[2:3], v[142:143] op_sel_hi:[0,1,1] neg_lo:[0,0,1] neg_hi:[0,0,1]
	ds_read_b128 v[0:3], v0
	s_nop 0
	s_waitcnt vmcnt(1)
	v_lshlrev_b32_e32 v112, 16, v236
	v_and_b32_e32 v113, 0xffff0000, v236
	v_lshlrev_b32_e32 v110, 16, v237
	v_and_b32_e32 v111, 0xffff0000, v237
	s_waitcnt lgkmcnt(0)
	v_pk_fma_f32 v[112:113], v[0:1], v[124:125], v[112:113]
	v_lshl_add_u64 v[124:125], s[28:29], 0, v[128:129]
	v_pk_fma_f32 v[110:111], v[2:3], v[126:127], v[110:111]
	s_nop 0
	s_nop 0
	s_waitcnt vmcnt(0)
	v_lshlrev_b32_e32 v128, 16, v238
	v_and_b32_e32 v129, 0xffff0000, v238
	v_lshlrev_b32_e32 v126, 16, v239
	v_and_b32_e32 v127, 0xffff0000, v239
	v_pk_fma_f32 v[116:117], v[0:1], v[116:117], v[128:129]
	v_cvt_pk_bf16_f32 v0, v112, v113
	v_cvt_pk_bf16_f32 v1, v110, v111
	v_pk_fma_f32 v[114:115], v[2:3], v[114:115], v[126:127]
	v_cvt_pk_bf16_f32 v2, v116, v117
	s_nop 0
	v_cvt_pk_bf16_f32 v3, v114, v115
	global_store_dwordx2 v[122:123], v[0:1], off offset:2048
	global_store_dwordx2 v[124:125], v[2:3], off offset:2048
	v_mov_b32_e32 v0, v21
	ds_read_b32 v122, v53 offset:72
	v_lshlrev_b32_e32 v126, 2, v0
	v_add_u32_e32 v128, 0x500, v126
	v_ashrrev_i32_e32 v129, 31, v128
	v_lshlrev_b64 v[136:137], 1, v[128:129]
	v_lshl_add_u64 v[236:237], vcc, 0, v[136:137]
	global_load_dwordx2 v[236:237], v[236:237], off
	v_lshl_add_u64 v[238:239], s[86:87], 0, v[136:137]
	global_load_dwordx2 v[238:239], v[238:239], off
	v_lshl_add_u64 v[240:241], s[0:1], 0, v[136:137]
	global_load_dwordx2 v[240:241], v[240:241], off
	v_lshl_add_u64 v[242:243], s[2:3], 0, v[136:137]
	global_load_dwordx2 v[242:243], v[242:243], off
	v_lshl_add_u64 v[244:245], s[96:97], 0, v[136:137]
	global_load_dwordx2 v[244:245], v[244:245], off
	v_lshl_add_u64 v[246:247], s[52:53], 0, v[136:137]
	global_load_dwordx2 v[246:247], v[246:247], off
	s_nop 0
	s_nop 0
	v_lshl_add_u64 v[138:139], s[86:87], 0, v[136:137]
	s_nop 0
	s_nop 0
	s_nop 0
	v_ashrrev_i32_e32 v127, 31, v126
	s_nop 0
	s_waitcnt vmcnt(5)
	v_lshlrev_b32_e32 v124, 16, v236
	v_and_b32_e32 v125, 0xffff0000, v236
	v_lshlrev_b32_e32 v132, 16, v237
	v_and_b32_e32 v133, 0xffff0000, v237
	ds_read2_b64 v[0:3], v53 offset0:5 offset1:6
	s_nop 0
	s_waitcnt vmcnt(4)
	v_lshlrev_b32_e32 v138, 16, v238
	v_and_b32_e32 v139, 0xffff0000, v238
	v_lshlrev_b32_e32 v140, 16, v239
	v_and_b32_e32 v141, 0xffff0000, v239
	s_waitcnt lgkmcnt(0)
	v_pk_fma_f32 v[144:145], v[0:1], v[140:141], 0 op_sel_hi:[0,1,0]
	s_nop 0
	s_waitcnt vmcnt(3)
	v_lshlrev_b32_e32 v148, 16, v240
	v_and_b32_e32 v149, 0xffff0000, v240
	v_lshlrev_b32_e32 v146, 16, v241
	v_and_b32_e32 v147, 0xffff0000, v241
	v_pk_fma_f32 v[144:145], v[0:1], v[146:147], v[144:145] op_sel:[1,0,0]
	s_nop 0
	s_nop 0
	v_pk_fma_f32 v[142:143], v[0:1], v[138:139], 0 op_sel_hi:[0,1,0]
	v_pk_fma_f32 v[142:143], v[0:1], v[148:149], v[142:143] op_sel:[1,0,0]
	v_pk_mul_f32 v[130:131], v[122:123], v[132:133] op_sel_hi:[0,1]
	v_pk_mul_f32 v[134:135], v[122:123], v[124:125] op_sel_hi:[0,1]
	s_nop 0
	s_waitcnt vmcnt(2)
	v_lshlrev_b32_e32 v148, 16, v242
	v_and_b32_e32 v149, 0xffff0000, v242
	v_lshlrev_b32_e32 v146, 16, v243
	v_and_b32_e32 v147, 0xffff0000, v243
	v_pk_fma_f32 v[144:145], v[2:3], v[146:147], v[144:145] op_sel_hi:[0,1,1]
	s_nop 0
	s_nop 0
	v_pk_fma_f32 v[142:143], v[2:3], v[148:149], v[142:143] op_sel_hi:[0,1,1]
	v_mov_b32_e32 v2, v3
	s_nop 0
	s_waitcnt vmcnt(1)
	v_lshlrev_b32_e32 v148, 16, v244
	v_and_b32_e32 v149, 0xffff0000, v244
	v_lshlrev_b32_e32 v146, 16, v245
	v_and_b32_e32 v147, 0xffff0000, v245
	v_pk_fma_f32 v[146:147], v[2:3], v[146:147], v[144:145] op_sel_hi:[0,1,1]
	v_pk_fma_f32 v[2:3], v[2:3], v[148:149], v[142:143] op_sel_hi:[0,1,1]
	s_nop 0
	s_nop 0
	ds_read2_b64 v[142:145], v53 offset0:7 offset1:8
	s_nop 0
	s_waitcnt vmcnt(0)
	v_lshlrev_b32_e32 v150, 16, v246
	v_and_b32_e32 v151, 0xffff0000, v246
	v_lshlrev_b32_e32 v148, 16, v247
	v_and_b32_e32 v149, 0xffff0000, v247
	s_waitcnt lgkmcnt(0)
	v_pk_fma_f32 v[146:147], v[142:143], v[148:149], v[146:147] op_sel_hi:[0,1,1]
	v_lshl_add_u64 v[236:237], s[50:51], 0, v[136:137]
	global_load_dwordx2 v[236:237], v[236:237], off
	v_lshl_add_u64 v[238:239], s[48:49], 0, v[136:137]
	global_load_dwordx2 v[238:239], v[238:239], off
	v_lshl_add_u64 v[240:241], s[46:47], 0, v[136:137]
	global_load_dwordx2 v[240:241], v[240:241], off
	s_nop 0
	s_nop 0
	v_pk_fma_f32 v[2:3], v[142:143], v[150:151], v[2:3] op_sel_hi:[0,1,1]
	s_nop 0
	s_waitcnt vmcnt(2)
	v_lshlrev_b32_e32 v150, 16, v236
	v_and_b32_e32 v151, 0xffff0000, v236
	v_lshlrev_b32_e32 v148, 16, v237
	v_and_b32_e32 v149, 0xffff0000, v237
	v_pk_fma_f32 v[146:147], v[142:143], v[148:149], v[146:147] op_sel:[1,0,0]
	v_pk_fma_f32 v[2:3], v[142:143], v[150:151], v[2:3] op_sel:[1,0,0]
	s_nop 0
	s_nop 0
	s_nop 0
	s_nop 0
	s_nop 0
	s_waitcnt vmcnt(1)
	v_lshlrev_b32_e32 v148, 16, v238
	v_and_b32_e32 v149, 0xffff0000, v238
	v_lshlrev_b32_e32 v142, 16, v239
	v_and_b32_e32 v143, 0xffff0000, v239
	v_pk_fma_f32 v[2:3], v[144:145], v[148:149], v[2:3] op_sel_hi:[0,1,1]
	v_pk_fma_f32 v[142:143], v[144:145], v[142:143], v[146:147] op_sel_hi:[0,1,1]
	s_nop 0
	s_waitcnt vmcnt(0)
	v_lshlrev_b32_e32 v146, 16, v240
	v_and_b32_e32 v147, 0xffff0000, v240
	v_lshlrev_b32_e32 v136, 16, v241
	v_and_b32_e32 v137, 0xffff0000, v241
	v_mov_b32_e32 v144, v145
	v_pk_mul_f32 v[148:149], v[144:145], v[136:137] op_sel_hi:[0,1]
	v_pk_fma_f32 v[136:137], v[144:145], v[136:137], v[142:143] op_sel_hi:[0,1,1]
	v_pk_fma_f32 v[2:3], v[144:145], v[146:147], v[2:3] op_sel_hi:[0,1,1]
	v_pk_fma_f32 v[138:139], v[0:1], v[138:139], v[2:3] op_sel_hi:[0,1,1] neg_lo:[1,0,0] neg_hi:[1,0,0]
	v_pk_fma_f32 v[0:1], v[0:1], v[140:141], v[136:137] op_sel_hi:[0,1,1] neg_lo:[1,0,0] neg_hi:[1,0,0]
	v_pk_fma_f32 v[0:1], v[122:123], v[132:133], v[0:1] op_sel_hi:[0,1,1]
	v_pk_fma_f32 v[122:123], v[122:123], v[124:125], v[138:139] op_sel_hi:[0,1,1]
	v_pk_fma_f32 v[124:125], v[120:121], v[122:123], v[134:135] op_sel_hi:[0,1,1] neg_lo:[0,0,1] neg_hi:[0,0,1]
	v_pk_fma_f32 v[122:123], v[120:121], v[0:1], v[130:131] op_sel_hi:[0,1,1] neg_lo:[0,0,1] neg_hi:[0,0,1]
	v_lshl_add_u32 v0, v128, 2, s17
	v_lshlrev_b64 v[128:129], 1, v[126:127]
	v_lshl_add_u64 v[126:127], s[30:31], 0, v[128:129]
	global_load_dwordx2 v[130:131], v[126:127], off offset:2560
	v_pk_mul_f32 v[150:151], v[144:145], v[146:147] op_sel_hi:[0,1]
	v_pk_fma_f32 v[120:121], v[118:119], v[2:3], v[150:151] op_sel_hi:[0,1,1] neg_lo:[0,0,1] neg_hi:[0,0,1]
	ds_read_b128 v[0:3], v0
	v_pk_fma_f32 v[118:119], v[118:119], v[136:137], v[148:149] op_sel_hi:[0,1,1] neg_lo:[0,0,1] neg_hi:[0,0,1]
	v_lshl_add_u64 v[128:129], s[28:29], 0, v[128:129]
	s_nop 0
	s_waitcnt vmcnt(0)
	v_lshlrev_b32_e32 v132, 16, v130
	v_and_b32_e32 v133, 0xffff0000, v130
	v_lshlrev_b32_e32 v130, 16, v131
	v_and_b32_e32 v131, 0xffff0000, v131
	s_waitcnt lgkmcnt(0)
	v_pk_fma_f32 v[118:119], v[2:3], v[118:119], v[130:131]
	global_load_dwordx2 v[130:131], v[128:129], off offset:2560
	v_pk_fma_f32 v[120:121], v[0:1], v[120:121], v[132:133]
	s_nop 0
	s_waitcnt vmcnt(0)
	v_lshlrev_b32_e32 v132, 16, v130
	v_and_b32_e32 v133, 0xffff0000, v130
	v_lshlrev_b32_e32 v130, 16, v131
	v_and_b32_e32 v131, 0xffff0000, v131
	v_pk_fma_f32 v[124:125], v[0:1], v[124:125], v[132:133]
	v_cvt_pk_bf16_f32 v0, v120, v121
	v_cvt_pk_bf16_f32 v1, v118, v119
	v_pk_fma_f32 v[122:123], v[2:3], v[122:123], v[130:131]
	v_cvt_pk_bf16_f32 v2, v124, v125
	s_nop 0
	v_cvt_pk_bf16_f32 v3, v122, v123
	global_store_dwordx2 v[126:127], v[0:1], off offset:2560
	global_store_dwordx2 v[128:129], v[2:3], off offset:2560
	v_mov_b32_e32 v0, v21
	ds_read_b32 v130, v53 offset:72
	v_lshlrev_b32_e32 v126, 2, v0
	v_add_u32_e32 v128, 0x600, v126
	v_ashrrev_i32_e32 v129, 31, v128
	v_lshlrev_b64 v[140:141], 1, v[128:129]
	v_lshl_add_u64 v[236:237], vcc, 0, v[140:141]
	global_load_dwordx2 v[236:237], v[236:237], off
	v_lshl_add_u64 v[238:239], s[42:43], 0, v[140:141]
	global_load_dwordx2 v[238:239], v[238:239], off
	v_lshl_add_u64 v[240:241], s[88:89], 0, v[140:141]
	global_load_dwordx2 v[240:241], v[240:241], off
	v_lshl_add_u64 v[242:243], s[36:37], 0, v[140:141]
	global_load_dwordx2 v[242:243], v[242:243], off
	v_lshl_add_u64 v[244:245], s[78:79], 0, v[140:141]
	global_load_dwordx2 v[244:245], v[244:245], off
	v_lshl_add_u64 v[246:247], s[76:77], 0, v[140:141]
	global_load_dwordx2 v[246:247], v[246:247], off
	s_nop 0
	s_nop 0
	v_lshl_add_u64 v[142:143], s[42:43], 0, v[140:141]
	s_nop 0
	s_nop 0
	s_nop 0
	v_ashrrev_i32_e32 v127, 31, v126
	s_nop 0
	s_waitcnt vmcnt(5)
	v_lshlrev_b32_e32 v132, 16, v236
	v_and_b32_e32 v133, 0xffff0000, v236
	v_lshlrev_b32_e32 v136, 16, v237
	v_and_b32_e32 v137, 0xffff0000, v237
	ds_read2_b64 v[0:3], v53 offset0:1 offset1:2
	s_nop 0
	s_waitcnt vmcnt(4)
	v_lshlrev_b32_e32 v142, 16, v238
	v_and_b32_e32 v143, 0xffff0000, v238
	v_lshlrev_b32_e32 v144, 16, v239
	v_and_b32_e32 v145, 0xffff0000, v239
	s_waitcnt lgkmcnt(0)
	v_pk_fma_f32 v[148:149], v[0:1], v[144:145], 0 op_sel_hi:[0,1,0]
	s_nop 0
	s_waitcnt vmcnt(3)
	v_lshlrev_b32_e32 v152, 16, v240
	v_and_b32_e32 v153, 0xffff0000, v240
	v_lshlrev_b32_e32 v150, 16, v241
	v_and_b32_e32 v151, 0xffff0000, v241
	v_pk_fma_f32 v[148:149], v[0:1], v[150:151], v[148:149] op_sel:[1,0,0]
	s_nop 0
	s_nop 0
	v_pk_fma_f32 v[146:147], v[0:1], v[142:143], 0 op_sel_hi:[0,1,0]
	v_pk_fma_f32 v[146:147], v[0:1], v[152:153], v[146:147] op_sel:[1,0,0]
	v_pk_mul_f32 v[134:135], v[130:131], v[136:137] op_sel_hi:[0,1]
	v_pk_mul_f32 v[138:139], v[130:131], v[132:133] op_sel_hi:[0,1]
	s_nop 0
	s_waitcnt vmcnt(2)
	v_lshlrev_b32_e32 v152, 16, v242
	v_and_b32_e32 v153, 0xffff0000, v242
	v_lshlrev_b32_e32 v150, 16, v243
	v_and_b32_e32 v151, 0xffff0000, v243
	v_pk_fma_f32 v[148:149], v[2:3], v[150:151], v[148:149] op_sel_hi:[0,1,1]
	s_nop 0
	s_nop 0
	v_pk_fma_f32 v[146:147], v[2:3], v[152:153], v[146:147] op_sel_hi:[0,1,1]
	v_mov_b32_e32 v2, v3
	s_nop 0
	s_waitcnt vmcnt(1)
	v_lshlrev_b32_e32 v152, 16, v244
	v_and_b32_e32 v153, 0xffff0000, v244
	v_lshlrev_b32_e32 v150, 16, v245
	v_and_b32_e32 v151, 0xffff0000, v245
	v_pk_fma_f32 v[150:151], v[2:3], v[150:151], v[148:149] op_sel_hi:[0,1,1]
	v_pk_fma_f32 v[2:3], v[2:3], v[152:153], v[146:147] op_sel_hi:[0,1,1]
	s_nop 0
	s_nop 0
	ds_read2_b64 v[146:149], v53 offset0:3 offset1:4
	s_nop 0
	s_waitcnt vmcnt(0)
	v_lshlrev_b32_e32 v154, 16, v246
	v_and_b32_e32 v155, 0xffff0000, v246
	v_lshlrev_b32_e32 v152, 16, v247
	v_and_b32_e32 v153, 0xffff0000, v247
	s_waitcnt lgkmcnt(0)
	v_pk_fma_f32 v[150:151], v[146:147], v[152:153], v[150:151] op_sel_hi:[0,1,1]
	v_lshl_add_u64 v[236:237], s[10:11], 0, v[140:141]
	global_load_dwordx2 v[236:237], v[236:237], off
	v_lshl_add_u64 v[238:239], s[8:9], 0, v[140:141]
	global_load_dwordx2 v[238:239], v[238:239], off
	v_lshl_add_u64 v[240:241], s[44:45], 0, v[140:141]
	global_load_dwordx2 v[240:241], v[240:241], off
	v_lshl_add_u64 v[242:243], s[86:87], 0, v[140:141]
	global_load_dwordx2 v[242:243], v[242:243], off
	v_lshl_add_u64 v[244:245], s[0:1], 0, v[140:141]
	global_load_dwordx2 v[244:245], v[244:245], off
	v_lshl_add_u64 v[246:247], s[2:3], 0, v[140:141]
	global_load_dwordx2 v[246:247], v[246:247], off
	s_nop 0
	s_nop 0
	v_pk_fma_f32 v[2:3], v[146:147], v[154:155], v[2:3] op_sel_hi:[0,1,1]
	s_nop 0
	s_waitcnt vmcnt(5)
	v_lshlrev_b32_e32 v154, 16, v236
	v_and_b32_e32 v155, 0xffff0000, v236
	v_lshlrev_b32_e32 v152, 16, v237
	v_and_b32_e32 v153, 0xffff0000, v237
	v_pk_fma_f32 v[150:151], v[146:147], v[152:153], v[150:151] op_sel:[1,0,0]
	v_pk_fma_f32 v[2:3], v[146:147], v[154:155], v[2:3] op_sel:[1,0,0]
	s_nop 0
	s_nop 0
	s_nop 0
	s_waitcnt vmcnt(4)
	v_lshlrev_b32_e32 v152, 16, v238
	v_and_b32_e32 v153, 0xffff0000, v238
	v_lshlrev_b32_e32 v146, 16, v239
	v_and_b32_e32 v147, 0xffff0000, v239
	v_pk_fma_f32 v[146:147], v[148:149], v[146:147], v[150:151] op_sel_hi:[0,1,1]
	s_nop 0
	s_nop 0
	v_pk_fma_f32 v[2:3], v[148:149], v[152:153], v[2:3] op_sel_hi:[0,1,1]
	v_mov_b32_e32 v148, v149
	s_nop 0
	s_waitcnt vmcnt(3)
	v_lshlrev_b32_e32 v152, 16, v240
	v_and_b32_e32 v153, 0xffff0000, v240
	v_pk_fma_f32 v[2:3], v[148:149], v[152:153], v[2:3] op_sel_hi:[0,1,1]
	s_nop 0
	s_nop 0
	v_lshlrev_b32_e32 v150, 16, v241
	v_and_b32_e32 v151, 0xffff0000, v241
	v_pk_fma_f32 v[150:151], v[148:149], v[150:151], v[146:147] op_sel_hi:[0,1,1]
	ds_read2_b64 v[146:149], v53 offset0:5 offset1:6
	s_nop 0
	s_waitcnt vmcnt(2)
	v_lshlrev_b32_e32 v154, 16, v242
	v_and_b32_e32 v155, 0xffff0000, v242
	v_lshlrev_b32_e32 v152, 16, v243
	v_and_b32_e32 v153, 0xffff0000, v243
	s_waitcnt lgkmcnt(0)
	v_pk_fma_f32 v[150:151], v[146:147], v[152:153], v[150:151] op_sel_hi:[0,1,1]
	s_nop 0
	s_nop 0
	v_pk_fma_f32 v[2:3], v[146:147], v[154:155], v[2:3] op_sel_hi:[0,1,1]
	s_nop 0
	s_waitcnt vmcnt(1)
	v_lshlrev_b32_e32 v154, 16, v244
	v_and_b32_e32 v155, 0xffff0000, v244
	v_lshlrev_b32_e32 v152, 16, v245
	v_and_b32_e32 v153, 0xffff0000, v245
	v_pk_fma_f32 v[150:151], v[146:147], v[152:153], v[150:151] op_sel:[1,0,0]
	v_pk_fma_f32 v[2:3], v[146:147], v[154:155], v[2:3] op_sel:[1,0,0]
	s_nop 0
	s_nop 0
	s_nop 0
	s_waitcnt vmcnt(0)
	v_lshlrev_b32_e32 v152, 16, v246
	v_and_b32_e32 v153, 0xffff0000, v246
	v_lshlrev_b32_e32 v146, 16, v247
	v_and_b32_e32 v147, 0xffff0000, v247
	v_pk_fma_f32 v[146:147], v[148:149], v[146:147], v[150:151] op_sel_hi:[0,1,1]
	v_lshl_add_u64 v[236:237], s[96:97], 0, v[140:141]
	global_load_dwordx2 v[236:237], v[236:237], off
	v_lshl_add_u64 v[238:239], s[52:53], 0, v[140:141]
	global_load_dwordx2 v[238:239], v[238:239], off
	v_lshl_add_u64 v[240:241], s[50:51], 0, v[140:141]
	global_load_dwordx2 v[240:241], v[240:241], off
	v_lshl_add_u64 v[242:243], s[48:49], 0, v[140:141]
	global_load_dwordx2 v[242:243], v[242:243], off
	v_lshl_add_u64 v[244:245], s[46:47], 0, v[140:141]
	global_load_dwordx2 v[244:245], v[244:245], off
	s_nop 0
	s_nop 0
	v_pk_fma_f32 v[2:3], v[148:149], v[152:153], v[2:3] op_sel_hi:[0,1,1]
	v_mov_b32_e32 v148, v149
	s_nop 0
	s_waitcnt vmcnt(4)
	v_lshlrev_b32_e32 v152, 16, v236
	v_and_b32_e32 v153, 0xffff0000, v236
	v_pk_fma_f32 v[2:3], v[148:149], v[152:153], v[2:3] op_sel_hi:[0,1,1]
	s_nop 0
	s_nop 0
	v_lshlrev_b32_e32 v150, 16, v237
	v_and_b32_e32 v151, 0xffff0000, v237
	v_pk_fma_f32 v[150:151], v[148:149], v[150:151], v[146:147] op_sel_hi:[0,1,1]
	ds_read2_b64 v[146:149], v53 offset0:7 offset1:8
	s_nop 0
	s_waitcnt vmcnt(3)
	v_lshlrev_b32_e32 v154, 16, v238
	v_and_b32_e32 v155, 0xffff0000, v238
	v_lshlrev_b32_e32 v152, 16, v239
	v_and_b32_e32 v153, 0xffff0000, v239
	s_waitcnt lgkmcnt(0)
	v_pk_fma_f32 v[150:151], v[146:147], v[152:153], v[150:151] op_sel_hi:[0,1,1]
	s_nop 0
	s_nop 0
	v_pk_fma_f32 v[2:3], v[146:147], v[154:155], v[2:3] op_sel_hi:[0,1,1]
	s_nop 0
	s_waitcnt vmcnt(2)
	v_lshlrev_b32_e32 v154, 16, v240
	v_and_b32_e32 v155, 0xffff0000, v240
	v_lshlrev_b32_e32 v152, 16, v241
	v_and_b32_e32 v153, 0xffff0000, v241
	v_pk_fma_f32 v[150:151], v[146:147], v[152:153], v[150:151] op_sel:[1,0,0]
	v_pk_fma_f32 v[2:3], v[146:147], v[154:155], v[2:3] op_sel:[1,0,0]
	s_nop 0
	s_nop 0
	s_nop 0
	s_nop 0
	s_nop 0
	s_waitcnt vmcnt(1)
	v_lshlrev_b32_e32 v152, 16, v242
	v_and_b32_e32 v153, 0xffff0000, v242
	v_lshlrev_b32_e32 v146, 16, v243
	v_and_b32_e32 v147, 0xffff0000, v243
	v_pk_fma_f32 v[2:3], v[148:149], v[152:153], v[2:3] op_sel_hi:[0,1,1]
	v_pk_fma_f32 v[146:147], v[148:149], v[146:147], v[150:151] op_sel_hi:[0,1,1]
	s_nop 0
	s_waitcnt vmcnt(0)
	v_lshlrev_b32_e32 v150, 16, v244
	v_and_b32_e32 v151, 0xffff0000, v244
	v_lshlrev_b32_e32 v140, 16, v245
	v_and_b32_e32 v141, 0xffff0000, v245
	v_mov_b32_e32 v148, v149
	v_pk_mul_f32 v[152:153], v[148:149], v[140:141] op_sel_hi:[0,1]
	v_pk_fma_f32 v[140:141], v[148:149], v[140:141], v[146:147] op_sel_hi:[0,1,1]
	v_pk_fma_f32 v[2:3], v[148:149], v[150:151], v[2:3] op_sel_hi:[0,1,1]
	v_pk_fma_f32 v[142:143], v[0:1], v[142:143], v[2:3] op_sel_hi:[0,1,1] neg_lo:[1,0,0] neg_hi:[1,0,0]
	v_pk_fma_f32 v[0:1], v[0:1], v[144:145], v[140:141] op_sel_hi:[0,1,1] neg_lo:[1,0,0] neg_hi:[1,0,0]
	v_pk_fma_f32 v[0:1], v[130:131], v[136:137], v[0:1] op_sel_hi:[0,1,1]
	v_pk_fma_f32 v[130:131], v[130:131], v[132:133], v[142:143] op_sel_hi:[0,1,1]
	v_pk_fma_f32 v[132:133], v[92:93], v[130:131], v[138:139] op_sel_hi:[0,1,1] neg_lo:[0,0,1] neg_hi:[0,0,1]
	v_pk_fma_f32 v[138:139], v[90:91], v[140:141], v[152:153] op_sel_hi:[0,1,1] neg_lo:[0,0,1] neg_hi:[0,0,1]
	v_lshlrev_b64 v[140:141], 1, v[126:127]
	v_pk_fma_f32 v[130:131], v[92:93], v[0:1], v[134:135] op_sel_hi:[0,1,1] neg_lo:[0,0,1] neg_hi:[0,0,1]
	v_lshl_add_u64 v[236:237], s[30:31], 0, v[140:141]
	global_load_dwordx2 v[236:237], v[236:237], off offset:3072
	v_lshl_add_u64 v[238:239], s[28:29], 0, v[140:141]
	global_load_dwordx2 v[238:239], v[238:239], off offset:3072
	v_lshl_add_u64 v[134:135], s[30:31], 0, v[140:141]
	s_nop 0
	v_pk_mul_f32 v[154:155], v[148:149], v[150:151] op_sel_hi:[0,1]
	v_lshl_add_u32 v0, v128, 2, s17
	v_pk_fma_f32 v[136:137], v[90:91], v[2:3], v[154:155] op_sel_hi:[0,1,1] neg_lo:[0,0,1] neg_hi:[0,0,1]
	ds_read_b128 v[0:3], v0
	s_nop 0
	s_waitcnt vmcnt(1)
	v_lshlrev_b32_e32 v128, 16, v236
	v_and_b32_e32 v129, 0xffff0000, v236
	v_lshlrev_b32_e32 v126, 16, v237
	v_and_b32_e32 v127, 0xffff0000, v237
	s_waitcnt lgkmcnt(0)
	v_pk_fma_f32 v[128:129], v[0:1], v[136:137], v[128:129]
	v_lshl_add_u64 v[136:137], s[28:29], 0, v[140:141]
	v_pk_fma_f32 v[126:127], v[2:3], v[138:139], v[126:127]
	s_nop 0
	s_nop 0
	s_waitcnt vmcnt(0)
	v_lshlrev_b32_e32 v140, 16, v238
	v_and_b32_e32 v141, 0xffff0000, v238
	v_lshlrev_b32_e32 v138, 16, v239
	v_and_b32_e32 v139, 0xffff0000, v239
	v_pk_fma_f32 v[132:133], v[0:1], v[132:133], v[140:141]
	v_cvt_pk_bf16_f32 v0, v128, v129
	v_cvt_pk_bf16_f32 v1, v126, v127
	v_pk_fma_f32 v[130:131], v[2:3], v[130:131], v[138:139]
	v_cvt_pk_bf16_f32 v2, v132, v133
	s_nop 0
	v_cvt_pk_bf16_f32 v3, v130, v131
	global_store_dwordx2 v[134:135], v[0:1], off offset:3072
	global_store_dwordx2 v[136:137], v[2:3], off offset:3072
	v_mov_b32_e32 v0, v21
	ds_read_b32 v138, v53 offset:72
	v_lshlrev_b32_e32 v134, 2, v0
	v_add_u32_e32 v136, 0x700, v134
	v_ashrrev_i32_e32 v137, 31, v136
	v_lshlrev_b64 v[148:149], 1, v[136:137]
	v_lshl_add_u64 v[236:237], vcc, 0, v[148:149]
	global_load_dwordx2 v[236:237], v[236:237], off
	v_lshl_add_u64 v[238:239], s[42:43], 0, v[148:149]
	global_load_dwordx2 v[238:239], v[238:239], off
	v_lshl_add_u64 v[240:241], s[88:89], 0, v[148:149]
	global_load_dwordx2 v[240:241], v[240:241], off
	v_lshl_add_u64 v[242:243], s[36:37], 0, v[148:149]
	global_load_dwordx2 v[242:243], v[242:243], off
	v_lshl_add_u64 v[244:245], s[78:79], 0, v[148:149]
	global_load_dwordx2 v[244:245], v[244:245], off
	v_lshl_add_u64 v[246:247], s[76:77], 0, v[148:149]
	global_load_dwordx2 v[246:247], v[246:247], off
	s_nop 0
	s_nop 0
	v_lshl_add_u64 v[150:151], s[42:43], 0, v[148:149]
	s_nop 0
	s_nop 0
	s_nop 0
	v_ashrrev_i32_e32 v135, 31, v134
	s_nop 0
	s_waitcnt vmcnt(5)
	v_lshlrev_b32_e32 v140, 16, v236
	v_and_b32_e32 v141, 0xffff0000, v236
	v_lshlrev_b32_e32 v144, 16, v237
	v_and_b32_e32 v145, 0xffff0000, v237
	ds_read2_b64 v[0:3], v53 offset0:1 offset1:2
	s_nop 0
	s_waitcnt vmcnt(4)
	v_lshlrev_b32_e32 v150, 16, v238
	v_and_b32_e32 v151, 0xffff0000, v238
	v_lshlrev_b32_e32 v152, 16, v239
	v_and_b32_e32 v153, 0xffff0000, v239
	s_waitcnt lgkmcnt(0)
	v_pk_fma_f32 v[156:157], v[0:1], v[152:153], 0 op_sel_hi:[0,1,0]
	s_nop 0
	s_waitcnt vmcnt(3)
	v_lshlrev_b32_e32 v160, 16, v240
	v_and_b32_e32 v161, 0xffff0000, v240
	v_lshlrev_b32_e32 v158, 16, v241
	v_and_b32_e32 v159, 0xffff0000, v241
	v_pk_fma_f32 v[156:157], v[0:1], v[158:159], v[156:157] op_sel:[1,0,0]
	s_nop 0
	s_nop 0
	v_pk_fma_f32 v[154:155], v[0:1], v[150:151], 0 op_sel_hi:[0,1,0]
	v_pk_fma_f32 v[154:155], v[0:1], v[160:161], v[154:155] op_sel:[1,0,0]
	v_pk_mul_f32 v[142:143], v[138:139], v[144:145] op_sel_hi:[0,1]
	v_pk_mul_f32 v[146:147], v[138:139], v[140:141] op_sel_hi:[0,1]
	s_nop 0
	s_waitcnt vmcnt(2)
	v_lshlrev_b32_e32 v160, 16, v242
	v_and_b32_e32 v161, 0xffff0000, v242
	v_lshlrev_b32_e32 v158, 16, v243
	v_and_b32_e32 v159, 0xffff0000, v243
	v_pk_fma_f32 v[156:157], v[2:3], v[158:159], v[156:157] op_sel_hi:[0,1,1]
	s_nop 0
	s_nop 0
	v_pk_fma_f32 v[154:155], v[2:3], v[160:161], v[154:155] op_sel_hi:[0,1,1]
	v_mov_b32_e32 v2, v3
	s_nop 0
	s_waitcnt vmcnt(1)
	v_lshlrev_b32_e32 v160, 16, v244
	v_and_b32_e32 v161, 0xffff0000, v244
	v_lshlrev_b32_e32 v158, 16, v245
	v_and_b32_e32 v159, 0xffff0000, v245
	v_pk_fma_f32 v[158:159], v[2:3], v[158:159], v[156:157] op_sel_hi:[0,1,1]
	v_pk_fma_f32 v[2:3], v[2:3], v[160:161], v[154:155] op_sel_hi:[0,1,1]
	s_nop 0
	s_nop 0
	ds_read2_b64 v[154:157], v53 offset0:3 offset1:4
	s_nop 0
	s_waitcnt vmcnt(0)
	v_lshlrev_b32_e32 v162, 16, v246
	v_and_b32_e32 v163, 0xffff0000, v246
	v_lshlrev_b32_e32 v160, 16, v247
	v_and_b32_e32 v161, 0xffff0000, v247
	s_waitcnt lgkmcnt(0)
	v_pk_fma_f32 v[158:159], v[154:155], v[160:161], v[158:159] op_sel_hi:[0,1,1]
	v_lshl_add_u64 v[236:237], s[10:11], 0, v[148:149]
	global_load_dwordx2 v[236:237], v[236:237], off
	v_lshl_add_u64 v[238:239], s[8:9], 0, v[148:149]
	global_load_dwordx2 v[238:239], v[238:239], off
	v_lshl_add_u64 v[240:241], s[44:45], 0, v[148:149]
	global_load_dwordx2 v[240:241], v[240:241], off
	v_lshl_add_u64 v[242:243], s[86:87], 0, v[148:149]
	global_load_dwordx2 v[242:243], v[242:243], off
	v_lshl_add_u64 v[244:245], s[0:1], 0, v[148:149]
	global_load_dwordx2 v[244:245], v[244:245], off
	v_lshl_add_u64 v[246:247], s[2:3], 0, v[148:149]
	global_load_dwordx2 v[246:247], v[246:247], off
	s_nop 0
	s_nop 0
	v_pk_fma_f32 v[2:3], v[154:155], v[162:163], v[2:3] op_sel_hi:[0,1,1]
	s_nop 0
	s_waitcnt vmcnt(5)
	v_lshlrev_b32_e32 v162, 16, v236
	v_and_b32_e32 v163, 0xffff0000, v236
	v_lshlrev_b32_e32 v160, 16, v237
	v_and_b32_e32 v161, 0xffff0000, v237
	v_pk_fma_f32 v[158:159], v[154:155], v[160:161], v[158:159] op_sel:[1,0,0]
	v_pk_fma_f32 v[2:3], v[154:155], v[162:163], v[2:3] op_sel:[1,0,0]
	s_nop 0
	s_nop 0
	s_nop 0
	s_waitcnt vmcnt(4)
	v_lshlrev_b32_e32 v160, 16, v238
	v_and_b32_e32 v161, 0xffff0000, v238
	v_lshlrev_b32_e32 v154, 16, v239
	v_and_b32_e32 v155, 0xffff0000, v239
	v_pk_fma_f32 v[154:155], v[156:157], v[154:155], v[158:159] op_sel_hi:[0,1,1]
	s_nop 0
	s_nop 0
	v_pk_fma_f32 v[2:3], v[156:157], v[160:161], v[2:3] op_sel_hi:[0,1,1]
	v_mov_b32_e32 v156, v157
	s_nop 0
	s_waitcnt vmcnt(3)
	v_lshlrev_b32_e32 v160, 16, v240
	v_and_b32_e32 v161, 0xffff0000, v240
	v_pk_fma_f32 v[2:3], v[156:157], v[160:161], v[2:3] op_sel_hi:[0,1,1]
	s_nop 0
	s_nop 0
	v_lshlrev_b32_e32 v158, 16, v241
	v_and_b32_e32 v159, 0xffff0000, v241
	v_pk_fma_f32 v[158:159], v[156:157], v[158:159], v[154:155] op_sel_hi:[0,1,1]
	ds_read2_b64 v[154:157], v53 offset0:5 offset1:6
	s_nop 0
	s_waitcnt vmcnt(2)
	v_lshlrev_b32_e32 v162, 16, v242
	v_and_b32_e32 v163, 0xffff0000, v242
	v_lshlrev_b32_e32 v160, 16, v243
	v_and_b32_e32 v161, 0xffff0000, v243
	s_waitcnt lgkmcnt(0)
	v_pk_fma_f32 v[158:159], v[154:155], v[160:161], v[158:159] op_sel_hi:[0,1,1]
	s_nop 0
	s_nop 0
	v_pk_fma_f32 v[2:3], v[154:155], v[162:163], v[2:3] op_sel_hi:[0,1,1]
	s_nop 0
	s_waitcnt vmcnt(1)
	v_lshlrev_b32_e32 v162, 16, v244
	v_and_b32_e32 v163, 0xffff0000, v244
	v_lshlrev_b32_e32 v160, 16, v245
	v_and_b32_e32 v161, 0xffff0000, v245
	v_pk_fma_f32 v[158:159], v[154:155], v[160:161], v[158:159] op_sel:[1,0,0]
	v_pk_fma_f32 v[2:3], v[154:155], v[162:163], v[2:3] op_sel:[1,0,0]
	s_nop 0
	s_nop 0
	s_nop 0
	s_waitcnt vmcnt(0)
	v_lshlrev_b32_e32 v160, 16, v246
	v_and_b32_e32 v161, 0xffff0000, v246
	v_lshlrev_b32_e32 v154, 16, v247
	v_and_b32_e32 v155, 0xffff0000, v247
	v_pk_fma_f32 v[154:155], v[156:157], v[154:155], v[158:159] op_sel_hi:[0,1,1]
	v_lshl_add_u64 v[236:237], s[96:97], 0, v[148:149]
	global_load_dwordx2 v[236:237], v[236:237], off
	v_lshl_add_u64 v[238:239], s[52:53], 0, v[148:149]
	global_load_dwordx2 v[238:239], v[238:239], off
	v_lshl_add_u64 v[240:241], s[50:51], 0, v[148:149]
	global_load_dwordx2 v[240:241], v[240:241], off
	v_lshl_add_u64 v[242:243], s[48:49], 0, v[148:149]
	global_load_dwordx2 v[242:243], v[242:243], off
	v_lshl_add_u64 v[244:245], s[46:47], 0, v[148:149]
	global_load_dwordx2 v[244:245], v[244:245], off
	s_nop 0
	s_nop 0
	v_pk_fma_f32 v[2:3], v[156:157], v[160:161], v[2:3] op_sel_hi:[0,1,1]
	v_mov_b32_e32 v156, v157
	s_nop 0
	s_waitcnt vmcnt(4)
	v_lshlrev_b32_e32 v160, 16, v236
	v_and_b32_e32 v161, 0xffff0000, v236
	v_pk_fma_f32 v[2:3], v[156:157], v[160:161], v[2:3] op_sel_hi:[0,1,1]
	s_nop 0
	s_nop 0
	v_lshlrev_b32_e32 v158, 16, v237
	v_and_b32_e32 v159, 0xffff0000, v237
	v_pk_fma_f32 v[158:159], v[156:157], v[158:159], v[154:155] op_sel_hi:[0,1,1]
	ds_read2_b64 v[154:157], v53 offset0:7 offset1:8
	s_nop 0
	s_waitcnt vmcnt(3)
	v_lshlrev_b32_e32 v162, 16, v238
	v_and_b32_e32 v163, 0xffff0000, v238
	v_lshlrev_b32_e32 v160, 16, v239
	v_and_b32_e32 v161, 0xffff0000, v239
	s_waitcnt lgkmcnt(0)
	v_pk_fma_f32 v[158:159], v[154:155], v[160:161], v[158:159] op_sel_hi:[0,1,1]
	s_nop 0
	s_nop 0
	v_pk_fma_f32 v[2:3], v[154:155], v[162:163], v[2:3] op_sel_hi:[0,1,1]
	s_nop 0
	s_waitcnt vmcnt(2)
	v_lshlrev_b32_e32 v162, 16, v240
	v_and_b32_e32 v163, 0xffff0000, v240
	v_lshlrev_b32_e32 v160, 16, v241
	v_and_b32_e32 v161, 0xffff0000, v241
	v_pk_fma_f32 v[158:159], v[154:155], v[160:161], v[158:159] op_sel:[1,0,0]
	v_pk_fma_f32 v[2:3], v[154:155], v[162:163], v[2:3] op_sel:[1,0,0]
	s_nop 0
	s_nop 0
	s_nop 0
	s_nop 0
	s_nop 0
	s_waitcnt vmcnt(1)
	v_lshlrev_b32_e32 v160, 16, v242
	v_and_b32_e32 v161, 0xffff0000, v242
	v_lshlrev_b32_e32 v154, 16, v243
	v_and_b32_e32 v155, 0xffff0000, v243
	v_pk_fma_f32 v[2:3], v[156:157], v[160:161], v[2:3] op_sel_hi:[0,1,1]
	v_pk_fma_f32 v[154:155], v[156:157], v[154:155], v[158:159] op_sel_hi:[0,1,1]
	s_nop 0
	s_waitcnt vmcnt(0)
	v_lshlrev_b32_e32 v158, 16, v244
	v_and_b32_e32 v159, 0xffff0000, v244
	v_lshlrev_b32_e32 v148, 16, v245
	v_and_b32_e32 v149, 0xffff0000, v245
	v_mov_b32_e32 v156, v157
	v_pk_mul_f32 v[160:161], v[156:157], v[148:149] op_sel_hi:[0,1]
	v_pk_fma_f32 v[148:149], v[156:157], v[148:149], v[154:155] op_sel_hi:[0,1,1]
	v_pk_fma_f32 v[2:3], v[156:157], v[158:159], v[2:3] op_sel_hi:[0,1,1]
	v_pk_fma_f32 v[150:151], v[0:1], v[150:151], v[2:3] op_sel_hi:[0,1,1] neg_lo:[1,0,0] neg_hi:[1,0,0]
	v_pk_fma_f32 v[0:1], v[0:1], v[152:153], v[148:149] op_sel_hi:[0,1,1] neg_lo:[1,0,0] neg_hi:[1,0,0]
	v_pk_fma_f32 v[0:1], v[138:139], v[144:145], v[0:1] op_sel_hi:[0,1,1]
	v_pk_fma_f32 v[138:139], v[138:139], v[140:141], v[150:151] op_sel_hi:[0,1,1]
	v_pk_fma_f32 v[140:141], v[92:93], v[0:1], v[142:143] op_sel_hi:[0,1,1] neg_lo:[0,0,1] neg_hi:[0,0,1]
	v_lshl_add_u32 v0, v136, 2, s17
	v_lshlrev_b64 v[136:137], 1, v[134:135]
	v_lshl_add_u64 v[236:237], s[30:31], 0, v[136:137]
	global_load_dwordx2 v[236:237], v[236:237], off offset:3584
	v_lshl_add_u64 v[238:239], s[28:29], 0, v[136:137]
	global_load_dwordx2 v[238:239], v[238:239], off offset:3584
	v_lshl_add_u64 v[134:135], s[30:31], 0, v[136:137]
	s_nop 0
	v_pk_mul_f32 v[162:163], v[156:157], v[158:159] op_sel_hi:[0,1]
	v_pk_fma_f32 v[138:139], v[92:93], v[138:139], v[146:147] op_sel_hi:[0,1,1] neg_lo:[0,0,1] neg_hi:[0,0,1]
	v_pk_fma_f32 v[92:93], v[90:91], v[2:3], v[162:163] op_sel_hi:[0,1,1] neg_lo:[0,0,1] neg_hi:[0,0,1]
	ds_read_b128 v[0:3], v0
	v_pk_fma_f32 v[90:91], v[90:91], v[148:149], v[160:161] op_sel_hi:[0,1,1] neg_lo:[0,0,1] neg_hi:[0,0,1]
	s_nop 0
	s_waitcnt vmcnt(1)
	v_lshlrev_b32_e32 v144, 16, v236
	v_and_b32_e32 v145, 0xffff0000, v236
	v_lshlrev_b32_e32 v142, 16, v237
	v_and_b32_e32 v143, 0xffff0000, v237
	s_waitcnt lgkmcnt(0)
	v_pk_fma_f32 v[90:91], v[2:3], v[90:91], v[142:143]
	v_lshl_add_u64 v[142:143], s[28:29], 0, v[136:137]
	s_nop 0
	v_pk_fma_f32 v[92:93], v[0:1], v[92:93], v[144:145]
	s_nop 0
	s_waitcnt vmcnt(0)
	v_lshlrev_b32_e32 v144, 16, v238
	v_and_b32_e32 v145, 0xffff0000, v238
	v_lshlrev_b32_e32 v136, 16, v239
	v_and_b32_e32 v137, 0xffff0000, v239
	v_pk_fma_f32 v[138:139], v[0:1], v[138:139], v[144:145]
	v_cvt_pk_bf16_f32 v0, v92, v93
	v_cvt_pk_bf16_f32 v1, v90, v91
	v_pk_fma_f32 v[136:137], v[2:3], v[140:141], v[136:137]
	v_cvt_pk_bf16_f32 v2, v138, v139
	s_nop 0
	v_cvt_pk_bf16_f32 v3, v136, v137
	global_store_dwordx2 v[134:135], v[0:1], off offset:3584
	global_store_dwordx2 v[142:143], v[2:3], off offset:3584
	v_mul_f32_e32 v0, v81, v81
	v_mul_f32_e32 v1, v15, v15
	v_fmac_f32_e32 v0, v80, v80
	v_fmac_f32_e32 v1, v14, v14
	v_mov_b32_e32 v2, v13
	v_mov_b32_e32 v3, v85
	v_add_f32_e32 v53, v0, v1
	v_mov_b32_e32 v0, v12
	v_mov_b32_e32 v1, v84
	v_pk_mul_f32 v[2:3], v[2:3], v[2:3]
	v_mov_b32_e32 v134, v11
	v_mov_b32_e32 v135, v83
	v_pk_fma_f32 v[0:1], v[0:1], v[0:1], v[2:3]
	v_mov_b32_e32 v2, v10
	v_mov_b32_e32 v3, v82
	v_pk_mul_f32 v[134:135], v[134:135], v[134:135]
	v_mul_f32_e32 v59, v112, v112
	v_pk_fma_f32 v[2:3], v[2:3], v[2:3], v[134:135]
	v_pk_mul_f32 v[134:135], v[96:97], v[96:97]
	v_pk_add_f32 v[0:1], v[0:1], v[2:3]
	v_mul_f32_e32 v2, v89, v89
	v_mul_f32_e32 v3, v87, v87
	v_fmac_f32_e32 v2, v88, v88
	v_fmac_f32_e32 v3, v86, v86
	v_add_f32_e32 v2, v2, v3
	v_add_f32_e32 v53, v53, v2
	v_pk_mul_f32 v[2:3], v[94:95], v[94:95]
	v_mul_f32_e32 v61, v113, v113
	v_pk_mov_b32 v[140:141], v[134:135], v[2:3] op_sel:[1,0]
	v_mov_b32_e32 v135, v3
	v_pk_add_f32 v[2:3], v[140:141], v[134:135]
	v_pk_add_f32 v[0:1], v[0:1], v[0:1] op_sel:[0,1] op_sel_hi:[1,0]
	v_pk_add_f32 v[2:3], v[2:3], v[2:3] op_sel:[0,1] op_sel_hi:[1,0]
	v_mov_b32_e32 v1, v59
	v_mov_b32_e32 v3, v61
	v_pk_add_f32 v[0:1], v[0:1], v[2:3]
	v_mul_f32_e32 v2, v105, v105
	v_mul_f32_e32 v134, v103, v103
	v_mul_f32_e32 v63, v110, v110
	v_mul_f32_e32 v65, v111, v111
	v_pk_fma_f32 v[2:3], v[104:105], v[104:105], v[2:3] op_sel_hi:[1,1,0]
	v_pk_fma_f32 v[134:135], v[102:103], v[102:103], v[134:135] op_sel_hi:[1,1,0]
	v_mov_b32_e32 v3, v63
	v_mov_b32_e32 v135, v65
	v_pk_add_f32 v[2:3], v[2:3], v[134:135]
	v_pk_mul_f32 v[134:135], v[120:121], v[120:121]
	v_pk_add_f32 v[0:1], v[0:1], v[2:3]
	v_pk_mul_f32 v[2:3], v[118:119], v[118:119]
	v_mul_f32_e32 v59, v92, v92
	v_pk_mov_b32 v[140:141], v[134:135], v[2:3] op_sel:[1,0]
	v_mov_b32_e32 v135, v3
	v_pk_add_f32 v[2:3], v[140:141], v[134:135]
	v_mul_f32_e32 v61, v93, v93
	v_pk_add_f32 v[0:1], v[0:1], v[0:1] op_sel:[0,1] op_sel_hi:[1,0]
	v_pk_add_f32 v[2:3], v[2:3], v[2:3] op_sel:[0,1] op_sel_hi:[1,0]
	v_mov_b32_e32 v1, v59
	v_mov_b32_e32 v3, v61
	v_pk_add_f32 v[0:1], v[0:1], v[2:3]
	v_mul_f32_e32 v2, v129, v129
	v_mul_f32_e32 v134, v127, v127
	v_mul_f32_e32 v63, v90, v90
	v_mul_f32_e32 v65, v91, v91
	v_pk_fma_f32 v[2:3], v[128:129], v[128:129], v[2:3] op_sel_hi:[1,1,0]
	v_pk_fma_f32 v[134:135], v[126:127], v[126:127], v[134:135] op_sel_hi:[1,1,0]
	v_mov_b32_e32 v3, v63
	v_mov_b32_e32 v135, v65
	v_pk_add_f32 v[2:3], v[2:3], v[134:135]
	v_mul_f32_e32 v55, v101, v101
	v_pk_add_f32 v[0:1], v[0:1], v[2:3]
	v_mul_f32_e32 v57, v99, v99
	v_add_f32_e32 v0, v0, v1
	ds_bpermute_b32 v1, v31, v0
	v_fmac_f32_e32 v55, v100, v100
	v_fmac_f32_e32 v57, v98, v98
	v_add_f32_e32 v55, v55, v57
	v_add_f32_e32 v53, v53, v55
	s_waitcnt lgkmcnt(0)
	v_add_f32_e32 v0, v0, v1
	ds_bpermute_b32 v1, v33, v0
	v_mul_f32_e32 v55, v109, v109
	v_mul_f32_e32 v57, v107, v107
	v_fmac_f32_e32 v55, v108, v108
	v_fmac_f32_e32 v57, v106, v106
	s_waitcnt lgkmcnt(0)
	v_add_f32_e32 v0, v0, v1
	ds_bpermute_b32 v1, v35, v0
	v_add_f32_e32 v2, v55, v57
	v_add_f32_e32 v2, v53, v2
	v_mul_f32_e32 v3, v117, v117
	v_mul_f32_e32 v53, v115, v115
	s_waitcnt lgkmcnt(0)
	v_add_f32_e32 v0, v0, v1
	ds_bpermute_b32 v1, v41, v0
	v_fmac_f32_e32 v3, v116, v116
	v_fmac_f32_e32 v53, v114, v114
	v_add_f32_e32 v3, v3, v53
	v_add_f32_e32 v2, v2, v3
	s_waitcnt lgkmcnt(0)
	v_add_f32_e32 v0, v0, v1
	ds_bpermute_b32 v1, v37, v0
	v_mul_f32_e32 v3, v125, v125
	v_mul_f32_e32 v53, v123, v123
	v_fmac_f32_e32 v3, v124, v124
	v_fmac_f32_e32 v53, v122, v122
	s_waitcnt lgkmcnt(0)
	v_add_f32_e32 v0, v0, v1
	ds_bpermute_b32 v1, v39, v0
	v_add_f32_e32 v3, v3, v53
	v_add_f32_e32 v2, v2, v3
	v_mul_f32_e32 v3, v133, v133
	v_mul_f32_e32 v53, v131, v131
	s_waitcnt lgkmcnt(0)
	v_add_f32_e32 v0, v0, v1
	v_fmamk_f32 v0, v0, 0x3a000000, v189
	v_mul_f32_e32 v1, 0x4f800000, v0
	v_cmp_gt_f32_e32 vcc, s84, v0
	v_fmac_f32_e32 v3, v132, v132
	v_fmac_f32_e32 v53, v130, v130
	v_cndmask_b32_e32 v0, v0, v1, vcc
	v_add_f32_e32 v3, v3, v53
	v_sqrt_f32_e32 v1, v0
	v_add_f32_e32 v2, v2, v3
	v_mul_f32_e32 v3, v139, v139
	v_mul_f32_e32 v53, v137, v137
	v_fmac_f32_e32 v3, v138, v138
	v_fmac_f32_e32 v53, v136, v136
	v_add_f32_e32 v3, v3, v53
	v_add_f32_e32 v2, v2, v3
	v_add_u32_e32 v3, -1, v1
	v_fma_f32 v53, -v3, v1, v0
	v_cmp_ge_f32_e64 s[46:47], 0, v53
	v_add_u32_e32 v53, 1, v1
	s_mov_b32 s33, 0xff61b1e6
	v_cndmask_b32_e64 v3, v1, v3, s[46:47]
	v_fma_f32 v1, -v53, v1, v0
	v_cmp_lt_f32_e64 s[46:47], 0, v1
	s_nop 1
	v_cndmask_b32_e64 v1, v3, v53, s[46:47]
	v_mul_f32_e32 v3, 0x37800000, v1
	v_cndmask_b32_e32 v1, v1, v3, vcc
	ds_bpermute_b32 v3, v31, v2
	v_cmp_class_f32_e32 vcc, v0, v190
	v_cmp_eq_u32_e64 s[46:47], 1, v20
	s_nop 0
	v_cndmask_b32_e32 v53, v1, v0, vcc
	s_waitcnt lgkmcnt(0)
	v_add_f32_e32 v0, v2, v3
	ds_bpermute_b32 v1, v33, v0
	v_div_scale_f32 v57, s[0:1], v53, v53, 1.0
	v_rcp_f32_e32 v55, v57
	v_div_scale_f32 v61, vcc, 1.0, v53, 1.0
	s_waitcnt lgkmcnt(0)
	v_add_f32_e32 v0, v0, v1
	ds_bpermute_b32 v1, v35, v0
	v_fma_f32 v2, -v57, v55, 1.0
	v_fmac_f32_e32 v55, v2, v55
	v_mul_f32_e32 v59, v61, v55
	v_fma_f32 v65, -v57, v59, v61
	s_waitcnt lgkmcnt(0)
	v_add_f32_e32 v63, v0, v1
	ds_read_b128 v[0:3], v25
	ds_read_b128 v[142:145], v25 offset:1024
	ds_read_b128 v[146:149], v25 offset:2048
	ds_read_b128 v[150:153], v25 offset:3072
	ds_read_b128 v[154:157], v25 offset:4096
	ds_read_b128 v[158:161], v25 offset:5120
	ds_read_b128 v[162:165], v25 offset:6144
	ds_read_b128 v[174:177], v25 offset:7168
	ds_read_b128 v[178:181], v25 offset:8192
	ds_read_b128 v[182:185], v25 offset:9216
	ds_read_b128 v[198:201], v25 offset:10240
	ds_read_b128 v[202:205], v25 offset:11264
	ds_read_b128 v[206:209], v25 offset:12288
	ds_read_b128 v[210:213], v25 offset:13312
	ds_read_b128 v[214:217], v25 offset:14336
	ds_read_b128 v[224:227], v25 offset:15360
	s_waitcnt lgkmcnt(7)
	v_mov_b32_e32 v134, v178
	v_mov_b32_e32 v135, v1
	v_mov_b32_e32 v166, v180
	v_mov_b32_e32 v167, v3
	v_pk_mul_f32 v[140:141], v[12:13], v[134:135]
	v_mov_b32_e32 v1, v179
	v_pk_mul_f32 v[178:179], v[10:11], v[166:167]
	v_mov_b32_e32 v3, v181
	v_pk_fma_f32 v[140:141], v[12:13], v[0:1], v[140:141] op_sel:[0,0,1] op_sel_hi:[1,1,0]
	v_pk_fma_f32 v[178:179], v[10:11], v[2:3], v[178:179] op_sel:[0,0,1] op_sel_hi:[1,1,0]
	v_pk_mul_f32 v[134:135], v[80:81], v[134:135]
	v_pk_add_f32 v[140:141], v[140:141], v[178:179]
	s_waitcnt lgkmcnt(6)
	v_mov_b32_e32 v178, v182
	v_mov_b32_e32 v179, v143
	v_mov_b32_e32 v143, v183
	v_mov_b32_e32 v182, v184
	v_mov_b32_e32 v183, v145
	v_pk_mul_f32 v[180:181], v[84:85], v[178:179]
	v_pk_mul_f32 v[218:219], v[82:83], v[182:183]
	v_mov_b32_e32 v145, v185
	v_pk_fma_f32 v[180:181], v[84:85], v[142:143], v[180:181] op_sel:[0,0,1] op_sel_hi:[1,1,0]
	v_pk_fma_f32 v[184:185], v[82:83], v[144:145], v[218:219] op_sel:[0,0,1] op_sel_hi:[1,1,0]
	v_pk_add_f32 v[140:141], v[140:141], 0 op_sel_hi:[1,0]
	v_pk_add_f32 v[180:181], v[180:181], v[184:185]
	v_pk_fma_f32 v[0:1], v[80:81], v[0:1], v[134:135] op_sel:[0,0,1] op_sel_hi:[1,1,0]
	v_pk_add_f32 v[140:141], v[140:141], v[180:181]
	s_waitcnt lgkmcnt(5)
	v_mov_b32_e32 v180, v198
	v_mov_b32_e32 v181, v147
	v_mov_b32_e32 v147, v199
	v_mov_b32_e32 v198, v200
	v_mov_b32_e32 v199, v149
	v_pk_mul_f32 v[184:185], v[96:97], v[180:181]
	v_pk_mul_f32 v[218:219], v[94:95], v[198:199]
	v_mov_b32_e32 v149, v201
	v_pk_fma_f32 v[184:185], v[96:97], v[146:147], v[184:185] op_sel:[0,0,1] op_sel_hi:[1,1,0]
	v_pk_fma_f32 v[200:201], v[94:95], v[148:149], v[218:219] op_sel:[0,0,1] op_sel_hi:[1,1,0]
	v_pk_mul_f32 v[134:135], v[14:15], v[166:167]
	v_pk_add_f32 v[184:185], v[184:185], v[200:201]
	v_pk_fma_f32 v[2:3], v[14:15], v[2:3], v[134:135] op_sel:[0,0,1] op_sel_hi:[1,1,0]
	v_pk_add_f32 v[140:141], v[140:141], v[184:185]
	s_waitcnt lgkmcnt(4)
	v_mov_b32_e32 v184, v202
	v_mov_b32_e32 v185, v151
	v_mov_b32_e32 v151, v203
	v_mov_b32_e32 v202, v204
	v_mov_b32_e32 v203, v153
	v_pk_add_f32 v[0:1], v[0:1], v[2:3]
	v_pk_mul_f32 v[2:3], v[88:89], v[178:179]
	v_pk_mul_f32 v[134:135], v[86:87], v[182:183]
	v_pk_mul_f32 v[200:201], v[104:105], v[184:185]
	v_pk_mul_f32 v[218:219], v[102:103], v[202:203]
	v_mov_b32_e32 v153, v205
	v_pk_fma_f32 v[2:3], v[88:89], v[142:143], v[2:3] op_sel:[0,0,1] op_sel_hi:[1,1,0]
	v_pk_fma_f32 v[134:135], v[86:87], v[144:145], v[134:135] op_sel:[0,0,1] op_sel_hi:[1,1,0]
	v_pk_fma_f32 v[200:201], v[104:105], v[150:151], v[200:201] op_sel:[0,0,1] op_sel_hi:[1,1,0]
	v_pk_fma_f32 v[204:205], v[102:103], v[152:153], v[218:219] op_sel:[0,0,1] op_sel_hi:[1,1,0]
	v_pk_add_f32 v[0:1], v[0:1], 0 op_sel_hi:[1,0]
	v_pk_add_f32 v[2:3], v[2:3], v[134:135]
	v_pk_add_f32 v[200:201], v[200:201], v[204:205]
	v_pk_add_f32 v[0:1], v[0:1], v[2:3]
	v_pk_mul_f32 v[2:3], v[100:101], v[180:181]
	v_pk_mul_f32 v[134:135], v[98:99], v[198:199]
	v_pk_add_f32 v[140:141], v[140:141], v[200:201]
	s_waitcnt lgkmcnt(3)
	v_mov_b32_e32 v200, v206
	v_mov_b32_e32 v201, v155
	v_mov_b32_e32 v155, v207
	v_mov_b32_e32 v206, v208
	v_mov_b32_e32 v207, v157
	v_pk_fma_f32 v[2:3], v[100:101], v[146:147], v[2:3] op_sel:[0,0,1] op_sel_hi:[1,1,0]
	v_pk_fma_f32 v[134:135], v[98:99], v[148:149], v[134:135] op_sel:[0,0,1] op_sel_hi:[1,1,0]
	v_pk_mul_f32 v[204:205], v[112:113], v[200:201]
	v_pk_mul_f32 v[218:219], v[110:111], v[206:207]
	v_mov_b32_e32 v157, v209
	v_pk_add_f32 v[2:3], v[2:3], v[134:135]
	v_pk_fma_f32 v[204:205], v[112:113], v[154:155], v[204:205] op_sel:[0,0,1] op_sel_hi:[1,1,0]
	v_pk_fma_f32 v[208:209], v[110:111], v[156:157], v[218:219] op_sel:[0,0,1] op_sel_hi:[1,1,0]
	v_pk_add_f32 v[0:1], v[0:1], v[2:3]
	v_pk_mul_f32 v[2:3], v[108:109], v[184:185]
	v_pk_mul_f32 v[134:135], v[106:107], v[202:203]
	v_pk_add_f32 v[204:205], v[204:205], v[208:209]
	v_pk_fma_f32 v[2:3], v[108:109], v[150:151], v[2:3] op_sel:[0,0,1] op_sel_hi:[1,1,0]
	v_pk_fma_f32 v[134:135], v[106:107], v[152:153], v[134:135] op_sel:[0,0,1] op_sel_hi:[1,1,0]
	v_pk_add_f32 v[140:141], v[140:141], v[204:205]
	s_waitcnt lgkmcnt(2)
	v_mov_b32_e32 v204, v210
	v_mov_b32_e32 v205, v159
	v_mov_b32_e32 v159, v211
	v_mov_b32_e32 v210, v212
	v_mov_b32_e32 v211, v161
	v_pk_add_f32 v[2:3], v[2:3], v[134:135]
	v_pk_mul_f32 v[208:209], v[120:121], v[204:205]
	v_pk_mul_f32 v[218:219], v[118:119], v[210:211]
	v_mov_b32_e32 v161, v213
	v_pk_add_f32 v[0:1], v[0:1], v[2:3]
	v_pk_mul_f32 v[2:3], v[116:117], v[200:201]
	v_pk_mul_f32 v[134:135], v[114:115], v[206:207]
	v_pk_fma_f32 v[208:209], v[120:121], v[158:159], v[208:209] op_sel:[0,0,1] op_sel_hi:[1,1,0]
	v_pk_fma_f32 v[212:213], v[118:119], v[160:161], v[218:219] op_sel:[0,0,1] op_sel_hi:[1,1,0]
	v_pk_fma_f32 v[2:3], v[116:117], v[154:155], v[2:3] op_sel:[0,0,1] op_sel_hi:[1,1,0]
	v_pk_fma_f32 v[134:135], v[114:115], v[156:157], v[134:135] op_sel:[0,0,1] op_sel_hi:[1,1,0]
	v_pk_add_f32 v[208:209], v[208:209], v[212:213]
	v_pk_add_f32 v[2:3], v[2:3], v[134:135]
	v_pk_add_f32 v[140:141], v[140:141], v[208:209]
	s_waitcnt lgkmcnt(1)
	v_mov_b32_e32 v208, v214
	v_mov_b32_e32 v209, v163
	v_mov_b32_e32 v163, v215
	v_mov_b32_e32 v214, v216
	v_mov_b32_e32 v215, v165
	v_pk_add_f32 v[0:1], v[0:1], v[2:3]
	v_pk_mul_f32 v[2:3], v[124:125], v[204:205]
	v_pk_mul_f32 v[134:135], v[122:123], v[210:211]
	v_pk_mul_f32 v[212:213], v[128:129], v[208:209]
	v_pk_mul_f32 v[218:219], v[126:127], v[214:215]
	v_mov_b32_e32 v165, v217
	v_pk_fma_f32 v[2:3], v[124:125], v[158:159], v[2:3] op_sel:[0,0,1] op_sel_hi:[1,1,0]
	v_pk_fma_f32 v[134:135], v[122:123], v[160:161], v[134:135] op_sel:[0,0,1] op_sel_hi:[1,1,0]
	v_pk_fma_f32 v[212:213], v[128:129], v[162:163], v[212:213] op_sel:[0,0,1] op_sel_hi:[1,1,0]
	v_pk_fma_f32 v[216:217], v[126:127], v[164:165], v[218:219] op_sel:[0,0,1] op_sel_hi:[1,1,0]
	v_pk_add_f32 v[2:3], v[2:3], v[134:135]
	v_pk_add_f32 v[212:213], v[212:213], v[216:217]
	v_pk_add_f32 v[0:1], v[0:1], v[2:3]
	v_pk_mul_f32 v[2:3], v[132:133], v[208:209]
	v_pk_mul_f32 v[134:135], v[130:131], v[214:215]
	v_pk_add_f32 v[140:141], v[140:141], v[212:213]
	s_waitcnt lgkmcnt(0)
	v_mov_b32_e32 v212, v224
	v_mov_b32_e32 v213, v175
	v_mov_b32_e32 v218, v226
	v_mov_b32_e32 v219, v177
	v_pk_fma_f32 v[2:3], v[132:133], v[162:163], v[2:3] op_sel:[0,0,1] op_sel_hi:[1,1,0]
	v_pk_fma_f32 v[134:135], v[130:131], v[164:165], v[134:135] op_sel:[0,0,1] op_sel_hi:[1,1,0]
	v_pk_mul_f32 v[216:217], v[92:93], v[212:213]
	v_mov_b32_e32 v175, v225
	v_pk_mul_f32 v[224:225], v[90:91], v[218:219]
	v_mov_b32_e32 v177, v227
	v_pk_add_f32 v[2:3], v[2:3], v[134:135]
	v_pk_fma_f32 v[216:217], v[92:93], v[174:175], v[216:217] op_sel:[0,0,1] op_sel_hi:[1,1,0]
	v_pk_fma_f32 v[224:225], v[90:91], v[176:177], v[224:225] op_sel:[0,0,1] op_sel_hi:[1,1,0]
	v_pk_add_f32 v[0:1], v[0:1], v[2:3]
	v_pk_mul_f32 v[2:3], v[138:139], v[212:213]
	v_pk_mul_f32 v[134:135], v[136:137], v[218:219]
	v_pk_add_f32 v[216:217], v[216:217], v[224:225]
	v_pk_fma_f32 v[2:3], v[138:139], v[174:175], v[2:3] op_sel:[0,0,1] op_sel_hi:[1,1,0]
	v_pk_fma_f32 v[134:135], v[136:137], v[176:177], v[134:135] op_sel:[0,0,1] op_sel_hi:[1,1,0]
	v_pk_add_f32 v[140:141], v[140:141], v[216:217]
	v_pk_add_f32 v[2:3], v[2:3], v[134:135]
	ds_read_b128 v[144:147], v25 offset:16384
	ds_read_b128 v[148:151], v25 offset:17408
	ds_read_b128 v[152:155], v25 offset:18432
	ds_read_b128 v[156:159], v25 offset:19456
	ds_read_b128 v[160:163], v25 offset:20480
	ds_read_b128 v[164:167], v25 offset:21504
	ds_read_b128 v[174:177], v25 offset:22528
	ds_read_b128 v[178:181], v25 offset:23552
	ds_read_b128 v[182:185], v25 offset:24576
	ds_read_b128 v[198:201], v25 offset:25600
	ds_read_b128 v[202:205], v25 offset:26624
	ds_read_b128 v[206:209], v25 offset:27648
	ds_read_b128 v[210:213], v25 offset:28672
	ds_read_b128 v[214:217], v25 offset:29696
	ds_read_b128 v[224:227], v25 offset:30720
	ds_read_b128 v[228:231], v25 offset:31744
	v_pk_add_f32 v[0:1], v[0:1], v[2:3]
	s_waitcnt lgkmcnt(7)
	v_mov_b32_e32 v2, v182
	v_mov_b32_e32 v3, v145
	v_mov_b32_e32 v145, v183
	v_mov_b32_e32 v182, v184
	v_mov_b32_e32 v183, v147
	v_pk_mul_f32 v[134:135], v[12:13], v[2:3]
	v_pk_mul_f32 v[142:143], v[10:11], v[182:183]
	v_mov_b32_e32 v147, v185
	v_pk_fma_f32 v[134:135], v[12:13], v[144:145], v[134:135] op_sel:[0,0,1] op_sel_hi:[1,1,0]
	v_pk_fma_f32 v[142:143], v[10:11], v[146:147], v[142:143] op_sel:[0,0,1] op_sel_hi:[1,1,0]
	s_waitcnt lgkmcnt(6)
	v_mov_b32_e32 v184, v198
	v_mov_b32_e32 v185, v149
	v_mov_b32_e32 v149, v199
	v_mov_b32_e32 v198, v200
	v_mov_b32_e32 v199, v151
	v_pk_add_f32 v[134:135], v[134:135], v[142:143]
	v_pk_mul_f32 v[142:143], v[84:85], v[184:185]
	v_pk_mul_f32 v[218:219], v[82:83], v[198:199]
	v_mov_b32_e32 v151, v201
	v_pk_fma_f32 v[142:143], v[84:85], v[148:149], v[142:143] op_sel:[0,0,1] op_sel_hi:[1,1,0]
	v_pk_fma_f32 v[200:201], v[82:83], v[150:151], v[218:219] op_sel:[0,0,1] op_sel_hi:[1,1,0]
	v_pk_add_f32 v[134:135], v[134:135], 0 op_sel_hi:[1,0]
	v_pk_add_f32 v[142:143], v[142:143], v[200:201]
	s_waitcnt lgkmcnt(5)
	v_mov_b32_e32 v200, v202
	v_mov_b32_e32 v201, v153
	v_mov_b32_e32 v153, v203
	v_mov_b32_e32 v202, v204
	v_mov_b32_e32 v203, v155
	v_pk_add_f32 v[134:135], v[134:135], v[142:143]
	v_pk_mul_f32 v[142:143], v[96:97], v[200:201]
	v_pk_mul_f32 v[218:219], v[94:95], v[202:203]
	v_mov_b32_e32 v155, v205
	v_pk_fma_f32 v[142:143], v[96:97], v[152:153], v[142:143] op_sel:[0,0,1] op_sel_hi:[1,1,0]
	v_pk_fma_f32 v[204:205], v[94:95], v[154:155], v[218:219] op_sel:[0,0,1] op_sel_hi:[1,1,0]
	v_pk_mul_f32 v[2:3], v[80:81], v[2:3]
	v_pk_add_f32 v[142:143], v[142:143], v[204:205]
	s_waitcnt lgkmcnt(4)
	v_mov_b32_e32 v204, v206
	v_mov_b32_e32 v205, v157
	v_mov_b32_e32 v157, v207
	v_mov_b32_e32 v206, v208
	v_mov_b32_e32 v207, v159
	v_pk_add_f32 v[134:135], v[134:135], v[142:143]
	v_pk_mul_f32 v[142:143], v[104:105], v[204:205]
	v_pk_mul_f32 v[218:219], v[102:103], v[206:207]
	v_mov_b32_e32 v159, v209
	v_pk_fma_f32 v[142:143], v[104:105], v[156:157], v[142:143] op_sel:[0,0,1] op_sel_hi:[1,1,0]
	v_pk_fma_f32 v[208:209], v[102:103], v[158:159], v[218:219] op_sel:[0,0,1] op_sel_hi:[1,1,0]
	v_pk_fma_f32 v[2:3], v[80:81], v[144:145], v[2:3] op_sel:[0,0,1] op_sel_hi:[1,1,0]
	v_pk_add_f32 v[142:143], v[142:143], v[208:209]
	s_waitcnt lgkmcnt(3)
	v_mov_b32_e32 v208, v210
	v_mov_b32_e32 v209, v161
	v_mov_b32_e32 v161, v211
	v_mov_b32_e32 v210, v212
	v_mov_b32_e32 v211, v163
	v_pk_add_f32 v[134:135], v[134:135], v[142:143]
	v_pk_mul_f32 v[142:143], v[112:113], v[208:209]
	v_pk_mul_f32 v[218:219], v[110:111], v[210:211]
	v_mov_b32_e32 v163, v213
	v_pk_fma_f32 v[142:143], v[112:113], v[160:161], v[142:143] op_sel:[0,0,1] op_sel_hi:[1,1,0]
	v_pk_fma_f32 v[212:213], v[110:111], v[162:163], v[218:219] op_sel:[0,0,1] op_sel_hi:[1,1,0]
	v_pk_mul_f32 v[144:145], v[86:87], v[198:199]
	v_pk_add_f32 v[142:143], v[142:143], v[212:213]
	s_waitcnt lgkmcnt(2)
	v_mov_b32_e32 v212, v214
	v_mov_b32_e32 v213, v165
	v_mov_b32_e32 v165, v215
	v_mov_b32_e32 v214, v216
	v_mov_b32_e32 v215, v167
	v_pk_add_f32 v[134:135], v[134:135], v[142:143]
	v_pk_mul_f32 v[142:143], v[120:121], v[212:213]
	v_pk_mul_f32 v[218:219], v[118:119], v[214:215]
	v_mov_b32_e32 v167, v217
	v_pk_fma_f32 v[142:143], v[120:121], v[164:165], v[142:143] op_sel:[0,0,1] op_sel_hi:[1,1,0]
	v_pk_fma_f32 v[216:217], v[118:119], v[166:167], v[218:219] op_sel:[0,0,1] op_sel_hi:[1,1,0]
	s_waitcnt lgkmcnt(1)
	v_mov_b32_e32 v218, v226
	v_pk_add_f32 v[142:143], v[142:143], v[216:217]
	v_mov_b32_e32 v216, v224
	v_mov_b32_e32 v217, v175
	v_mov_b32_e32 v219, v177
	v_pk_add_f32 v[134:135], v[134:135], v[142:143]
	v_pk_mul_f32 v[142:143], v[128:129], v[216:217]
	v_mov_b32_e32 v175, v225
	v_pk_mul_f32 v[224:225], v[126:127], v[218:219]
	v_mov_b32_e32 v177, v227
	v_pk_fma_f32 v[142:143], v[128:129], v[174:175], v[142:143] op_sel:[0,0,1] op_sel_hi:[1,1,0]
	v_pk_fma_f32 v[224:225], v[126:127], v[176:177], v[224:225] op_sel:[0,0,1] op_sel_hi:[1,1,0]
	s_waitcnt lgkmcnt(0)
	v_mov_b32_e32 v226, v230
	v_pk_add_f32 v[142:143], v[142:143], v[224:225]
	v_mov_b32_e32 v224, v228
	v_mov_b32_e32 v225, v179
	v_mov_b32_e32 v227, v181
	v_pk_add_f32 v[134:135], v[134:135], v[142:143]
	v_pk_mul_f32 v[142:143], v[92:93], v[224:225]
	v_mov_b32_e32 v179, v229
	v_pk_mul_f32 v[228:229], v[90:91], v[226:227]
	v_mov_b32_e32 v181, v231
	v_pk_fma_f32 v[142:143], v[92:93], v[178:179], v[142:143] op_sel:[0,0,1] op_sel_hi:[1,1,0]
	v_pk_fma_f32 v[228:229], v[90:91], v[180:181], v[228:229] op_sel:[0,0,1] op_sel_hi:[1,1,0]
	v_pk_fma_f32 v[144:145], v[86:87], v[150:151], v[144:145] op_sel:[0,0,1] op_sel_hi:[1,1,0]
	v_pk_add_f32 v[142:143], v[142:143], v[228:229]
	ds_bpermute_b32 v67, v41, v63
	v_pk_add_f32 v[142:143], v[134:135], v[142:143]
	v_pk_mul_f32 v[134:135], v[14:15], v[182:183]
	v_fmac_f32_e32 v59, v65, v55
	v_pk_fma_f32 v[134:135], v[14:15], v[146:147], v[134:135] op_sel:[0,0,1] op_sel_hi:[1,1,0]
	s_nop 0
	v_pk_add_f32 v[2:3], v[2:3], v[134:135]
	v_pk_mul_f32 v[134:135], v[88:89], v[184:185]
	v_pk_add_f32 v[2:3], v[2:3], 0 op_sel_hi:[1,0]
	v_pk_fma_f32 v[134:135], v[88:89], v[148:149], v[134:135] op_sel:[0,0,1] op_sel_hi:[1,1,0]
	s_nop 0
	v_pk_add_f32 v[134:135], v[134:135], v[144:145]
	v_pk_mul_f32 v[144:145], v[98:99], v[202:203]
	v_pk_add_f32 v[2:3], v[2:3], v[134:135]
	v_pk_mul_f32 v[134:135], v[100:101], v[200:201]
	v_pk_fma_f32 v[144:145], v[98:99], v[154:155], v[144:145] op_sel:[0,0,1] op_sel_hi:[1,1,0]
	v_pk_fma_f32 v[134:135], v[100:101], v[152:153], v[134:135] op_sel:[0,0,1] op_sel_hi:[1,1,0]
	s_nop 0
	v_pk_add_f32 v[134:135], v[134:135], v[144:145]
	v_pk_mul_f32 v[144:145], v[106:107], v[206:207]
	v_pk_add_f32 v[2:3], v[2:3], v[134:135]
	v_pk_mul_f32 v[134:135], v[108:109], v[204:205]
	v_pk_fma_f32 v[144:145], v[106:107], v[158:159], v[144:145] op_sel:[0,0,1] op_sel_hi:[1,1,0]
	v_pk_fma_f32 v[134:135], v[108:109], v[156:157], v[134:135] op_sel:[0,0,1] op_sel_hi:[1,1,0]
	s_nop 0
	v_pk_add_f32 v[134:135], v[134:135], v[144:145]
	v_pk_mul_f32 v[144:145], v[114:115], v[210:211]
	v_pk_add_f32 v[2:3], v[2:3], v[134:135]
	v_pk_mul_f32 v[134:135], v[116:117], v[208:209]
	v_pk_fma_f32 v[144:145], v[114:115], v[162:163], v[144:145] op_sel:[0,0,1] op_sel_hi:[1,1,0]
	v_pk_fma_f32 v[134:135], v[116:117], v[160:161], v[134:135] op_sel:[0,0,1] op_sel_hi:[1,1,0]
	s_nop 0
	v_pk_add_f32 v[134:135], v[134:135], v[144:145]
	v_pk_mul_f32 v[144:145], v[122:123], v[214:215]
	v_pk_add_f32 v[2:3], v[2:3], v[134:135]
	v_pk_mul_f32 v[134:135], v[124:125], v[212:213]
	v_pk_fma_f32 v[144:145], v[122:123], v[166:167], v[144:145] op_sel:[0,0,1] op_sel_hi:[1,1,0]
	v_pk_fma_f32 v[134:135], v[124:125], v[164:165], v[134:135] op_sel:[0,0,1] op_sel_hi:[1,1,0]
	s_nop 0
	v_pk_add_f32 v[134:135], v[134:135], v[144:145]
	v_pk_mul_f32 v[144:145], v[130:131], v[218:219]
	v_pk_add_f32 v[2:3], v[2:3], v[134:135]
	v_pk_mul_f32 v[134:135], v[132:133], v[216:217]
	v_pk_fma_f32 v[144:145], v[130:131], v[176:177], v[144:145] op_sel:[0,0,1] op_sel_hi:[1,1,0]
	v_pk_fma_f32 v[134:135], v[132:133], v[174:175], v[134:135] op_sel:[0,0,1] op_sel_hi:[1,1,0]
	s_nop 0
	v_pk_add_f32 v[134:135], v[134:135], v[144:145]
	v_pk_mul_f32 v[144:145], v[136:137], v[226:227]
	v_pk_add_f32 v[2:3], v[2:3], v[134:135]
	v_pk_mul_f32 v[134:135], v[138:139], v[224:225]
	v_pk_fma_f32 v[144:145], v[136:137], v[180:181], v[144:145] op_sel:[0,0,1] op_sel_hi:[1,1,0]
	v_pk_fma_f32 v[134:135], v[138:139], v[178:179], v[134:135] op_sel:[0,0,1] op_sel_hi:[1,1,0]
	ds_read_b128 v[146:149], v25 offset:32768
	ds_read_b128 v[150:153], v25 offset:33792
	ds_read_b128 v[154:157], v25 offset:34816
	ds_read_b128 v[158:161], v25 offset:35840
	ds_read_b128 v[162:165], v25 offset:36864
	ds_read_b128 v[174:177], v25 offset:37888
	ds_read_b128 v[178:181], v25 offset:38912
	ds_read_b128 v[182:185], v25 offset:39936
	ds_read_b128 v[198:201], v25 offset:40960
	ds_read_b128 v[202:205], v25 offset:41984
	ds_read_b128 v[206:209], v25 offset:43008
	ds_read_b128 v[210:213], v25 offset:44032
	ds_read_b128 v[214:217], v25 offset:45056
	ds_read_b128 v[224:227], v25 offset:46080
	ds_read_b128 v[228:231], v25 offset:47104
	ds_read_b128 v[232:235], v25 offset:48128
	v_pk_add_f32 v[134:135], v[134:135], v[144:145]
	s_waitcnt lgkmcnt(7)
	v_mov_b32_e32 v166, v200
	v_pk_add_f32 v[2:3], v[2:3], v[134:135]
	v_mov_b32_e32 v134, v198
	v_mov_b32_e32 v135, v147
	v_mov_b32_e32 v167, v149
	v_pk_mul_f32 v[144:145], v[12:13], v[134:135]
	v_mov_b32_e32 v147, v199
	v_pk_mul_f32 v[198:199], v[10:11], v[166:167]
	v_mov_b32_e32 v149, v201
	v_pk_fma_f32 v[144:145], v[12:13], v[146:147], v[144:145] op_sel:[0,0,1] op_sel_hi:[1,1,0]
	v_pk_fma_f32 v[198:199], v[10:11], v[148:149], v[198:199] op_sel:[0,0,1] op_sel_hi:[1,1,0]
	v_pk_mul_f32 v[134:135], v[80:81], v[134:135]
	v_pk_add_f32 v[144:145], v[144:145], v[198:199]
	s_waitcnt lgkmcnt(6)
	v_mov_b32_e32 v198, v202
	v_mov_b32_e32 v199, v151
	v_mov_b32_e32 v151, v203
	v_mov_b32_e32 v202, v204
	v_mov_b32_e32 v203, v153
	v_pk_mul_f32 v[200:201], v[84:85], v[198:199]
	v_pk_mul_f32 v[218:219], v[82:83], v[202:203]
	v_mov_b32_e32 v153, v205
	v_pk_fma_f32 v[200:201], v[84:85], v[150:151], v[200:201] op_sel:[0,0,1] op_sel_hi:[1,1,0]
	v_pk_fma_f32 v[204:205], v[82:83], v[152:153], v[218:219] op_sel:[0,0,1] op_sel_hi:[1,1,0]
	v_pk_add_f32 v[144:145], v[144:145], 0 op_sel_hi:[1,0]
	v_pk_add_f32 v[200:201], v[200:201], v[204:205]
	v_pk_fma_f32 v[134:135], v[80:81], v[146:147], v[134:135] op_sel:[0,0,1] op_sel_hi:[1,1,0]
	v_pk_add_f32 v[144:145], v[144:145], v[200:201]
	s_waitcnt lgkmcnt(5)
	v_mov_b32_e32 v200, v206
	v_mov_b32_e32 v201, v155
	v_mov_b32_e32 v155, v207
	v_mov_b32_e32 v206, v208
	v_mov_b32_e32 v207, v157
	v_pk_mul_f32 v[204:205], v[96:97], v[200:201]
	v_pk_mul_f32 v[218:219], v[94:95], v[206:207]
	v_mov_b32_e32 v157, v209
	v_pk_mul_f32 v[146:147], v[14:15], v[166:167]
	v_pk_fma_f32 v[204:205], v[96:97], v[154:155], v[204:205] op_sel:[0,0,1] op_sel_hi:[1,1,0]
	v_pk_fma_f32 v[208:209], v[94:95], v[156:157], v[218:219] op_sel:[0,0,1] op_sel_hi:[1,1,0]
	v_pk_fma_f32 v[146:147], v[14:15], v[148:149], v[146:147] op_sel:[0,0,1] op_sel_hi:[1,1,0]
	v_pk_add_f32 v[204:205], v[204:205], v[208:209]
	v_pk_add_f32 v[134:135], v[134:135], v[146:147]
	v_pk_mul_f32 v[146:147], v[88:89], v[198:199]
	v_pk_mul_f32 v[148:149], v[86:87], v[202:203]
	v_pk_add_f32 v[144:145], v[144:145], v[204:205]
	s_waitcnt lgkmcnt(4)
	v_mov_b32_e32 v204, v210
	v_mov_b32_e32 v205, v159
	v_mov_b32_e32 v159, v211
	v_mov_b32_e32 v210, v212
	v_mov_b32_e32 v211, v161
	v_pk_fma_f32 v[146:147], v[88:89], v[150:151], v[146:147] op_sel:[0,0,1] op_sel_hi:[1,1,0]
	v_pk_fma_f32 v[148:149], v[86:87], v[152:153], v[148:149] op_sel:[0,0,1] op_sel_hi:[1,1,0]
	v_pk_mul_f32 v[208:209], v[104:105], v[204:205]
	v_pk_mul_f32 v[218:219], v[102:103], v[210:211]
	v_mov_b32_e32 v161, v213
	v_pk_add_f32 v[134:135], v[134:135], 0 op_sel_hi:[1,0]
	v_pk_add_f32 v[146:147], v[146:147], v[148:149]
	v_pk_fma_f32 v[208:209], v[104:105], v[158:159], v[208:209] op_sel:[0,0,1] op_sel_hi:[1,1,0]
	v_pk_fma_f32 v[212:213], v[102:103], v[160:161], v[218:219] op_sel:[0,0,1] op_sel_hi:[1,1,0]
	v_pk_add_f32 v[134:135], v[134:135], v[146:147]
	v_pk_mul_f32 v[146:147], v[100:101], v[200:201]
	v_pk_mul_f32 v[148:149], v[98:99], v[206:207]
	v_pk_add_f32 v[208:209], v[208:209], v[212:213]
	v_pk_fma_f32 v[146:147], v[100:101], v[154:155], v[146:147] op_sel:[0,0,1] op_sel_hi:[1,1,0]
	v_pk_fma_f32 v[148:149], v[98:99], v[156:157], v[148:149] op_sel:[0,0,1] op_sel_hi:[1,1,0]
	v_pk_add_f32 v[144:145], v[144:145], v[208:209]
	s_waitcnt lgkmcnt(3)
	v_mov_b32_e32 v208, v214
	v_mov_b32_e32 v209, v163
	v_mov_b32_e32 v163, v215
	v_mov_b32_e32 v214, v216
	v_mov_b32_e32 v215, v165
	v_pk_add_f32 v[146:147], v[146:147], v[148:149]
	v_pk_mul_f32 v[212:213], v[112:113], v[208:209]
	v_pk_mul_f32 v[218:219], v[110:111], v[214:215]
	v_mov_b32_e32 v165, v217
	v_pk_add_f32 v[134:135], v[134:135], v[146:147]
	v_pk_mul_f32 v[146:147], v[108:109], v[204:205]
	v_pk_mul_f32 v[148:149], v[106:107], v[210:211]
	v_pk_fma_f32 v[212:213], v[112:113], v[162:163], v[212:213] op_sel:[0,0,1] op_sel_hi:[1,1,0]
	v_pk_fma_f32 v[216:217], v[110:111], v[164:165], v[218:219] op_sel:[0,0,1] op_sel_hi:[1,1,0]
	v_pk_fma_f32 v[146:147], v[108:109], v[158:159], v[146:147] op_sel:[0,0,1] op_sel_hi:[1,1,0]
	v_pk_fma_f32 v[148:149], v[106:107], v[160:161], v[148:149] op_sel:[0,0,1] op_sel_hi:[1,1,0]
	v_pk_add_f32 v[212:213], v[212:213], v[216:217]
	v_pk_add_f32 v[146:147], v[146:147], v[148:149]
	v_pk_add_f32 v[144:145], v[144:145], v[212:213]
	s_waitcnt lgkmcnt(2)
	v_mov_b32_e32 v212, v224
	v_mov_b32_e32 v213, v175
	v_mov_b32_e32 v218, v226
	v_mov_b32_e32 v219, v177
	v_pk_add_f32 v[134:135], v[134:135], v[146:147]
	v_pk_mul_f32 v[146:147], v[116:117], v[208:209]
	v_pk_mul_f32 v[148:149], v[114:115], v[214:215]
	v_pk_mul_f32 v[216:217], v[120:121], v[212:213]
	v_mov_b32_e32 v175, v225
	v_pk_mul_f32 v[224:225], v[118:119], v[218:219]
	v_mov_b32_e32 v177, v227
	v_pk_fma_f32 v[146:147], v[116:117], v[162:163], v[146:147] op_sel:[0,0,1] op_sel_hi:[1,1,0]
	v_pk_fma_f32 v[148:149], v[114:115], v[164:165], v[148:149] op_sel:[0,0,1] op_sel_hi:[1,1,0]
	v_pk_fma_f32 v[216:217], v[120:121], v[174:175], v[216:217] op_sel:[0,0,1] op_sel_hi:[1,1,0]
	v_pk_fma_f32 v[224:225], v[118:119], v[176:177], v[224:225] op_sel:[0,0,1] op_sel_hi:[1,1,0]
	v_pk_add_f32 v[146:147], v[146:147], v[148:149]
	v_pk_add_f32 v[216:217], v[216:217], v[224:225]
	v_pk_add_f32 v[134:135], v[134:135], v[146:147]
	v_pk_mul_f32 v[146:147], v[124:125], v[212:213]
	v_pk_mul_f32 v[148:149], v[122:123], v[218:219]
	v_pk_add_f32 v[144:145], v[144:145], v[216:217]
	s_waitcnt lgkmcnt(1)
	v_mov_b32_e32 v216, v228
	v_mov_b32_e32 v217, v179
	v_mov_b32_e32 v226, v230
	v_mov_b32_e32 v227, v181
	v_pk_fma_f32 v[146:147], v[124:125], v[174:175], v[146:147] op_sel:[0,0,1] op_sel_hi:[1,1,0]
	v_pk_fma_f32 v[148:149], v[122:123], v[176:177], v[148:149] op_sel:[0,0,1] op_sel_hi:[1,1,0]
	v_pk_mul_f32 v[224:225], v[128:129], v[216:217]
	v_mov_b32_e32 v179, v229
	v_pk_mul_f32 v[228:229], v[126:127], v[226:227]
	v_mov_b32_e32 v181, v231
	v_pk_add_f32 v[146:147], v[146:147], v[148:149]
	v_pk_fma_f32 v[224:225], v[128:129], v[178:179], v[224:225] op_sel:[0,0,1] op_sel_hi:[1,1,0]
	v_pk_fma_f32 v[228:229], v[126:127], v[180:181], v[228:229] op_sel:[0,0,1] op_sel_hi:[1,1,0]
	v_pk_add_f32 v[134:135], v[134:135], v[146:147]
	v_pk_mul_f32 v[146:147], v[132:133], v[216:217]
	v_pk_mul_f32 v[148:149], v[130:131], v[226:227]
	v_pk_add_f32 v[224:225], v[224:225], v[228:229]
	v_pk_fma_f32 v[146:147], v[132:133], v[178:179], v[146:147] op_sel:[0,0,1] op_sel_hi:[1,1,0]
	v_pk_fma_f32 v[148:149], v[130:131], v[180:181], v[148:149] op_sel:[0,0,1] op_sel_hi:[1,1,0]
	v_pk_add_f32 v[144:145], v[144:145], v[224:225]
	s_waitcnt lgkmcnt(0)
	v_mov_b32_e32 v224, v232
	v_mov_b32_e32 v225, v183
	v_mov_b32_e32 v230, v234
	v_mov_b32_e32 v231, v185
	v_pk_add_f32 v[146:147], v[146:147], v[148:149]
	v_pk_mul_f32 v[228:229], v[92:93], v[224:225]
	v_mov_b32_e32 v183, v233
	v_pk_mul_f32 v[232:233], v[90:91], v[230:231]
	v_mov_b32_e32 v185, v235
	v_pk_add_f32 v[134:135], v[134:135], v[146:147]
	v_pk_mul_f32 v[146:147], v[138:139], v[224:225]
	v_pk_mul_f32 v[148:149], v[136:137], v[230:231]
	v_pk_fma_f32 v[228:229], v[92:93], v[182:183], v[228:229] op_sel:[0,0,1] op_sel_hi:[1,1,0]
	v_pk_fma_f32 v[232:233], v[90:91], v[184:185], v[232:233] op_sel:[0,0,1] op_sel_hi:[1,1,0]
	v_pk_fma_f32 v[146:147], v[138:139], v[182:183], v[146:147] op_sel:[0,0,1] op_sel_hi:[1,1,0]
	v_pk_fma_f32 v[148:149], v[136:137], v[184:185], v[148:149] op_sel:[0,0,1] op_sel_hi:[1,1,0]
	v_pk_add_f32 v[228:229], v[228:229], v[232:233]
	v_pk_add_f32 v[146:147], v[146:147], v[148:149]
	v_pk_add_f32 v[144:145], v[144:145], v[228:229]
	v_pk_add_f32 v[134:135], v[134:135], v[146:147]
	ds_read_b128 v[146:149], v25 offset:49152
	ds_read_b128 v[150:153], v25 offset:50176
	ds_read_b128 v[154:157], v25 offset:51200
	ds_read_b128 v[158:161], v25 offset:52224
	ds_read_b128 v[162:165], v25 offset:53248
	ds_read_b128 v[174:177], v25 offset:54272
	ds_read_b128 v[178:181], v25 offset:55296
	ds_read_b128 v[182:185], v25 offset:56320
	ds_read_b128 v[198:201], v25 offset:57344
	ds_read_b128 v[202:205], v25 offset:58368
	ds_read_b128 v[206:209], v25 offset:59392
	ds_read_b128 v[210:213], v25 offset:60416
	ds_read_b128 v[214:217], v25 offset:61440
	ds_read_b128 v[224:227], v25 offset:62464
	ds_read_b128 v[228:231], v25 offset:63488
	ds_read_b128 v[232:235], v25 offset:64512
	s_waitcnt lgkmcnt(7)
	v_mov_b32_e32 v166, v198
	v_mov_b32_e32 v167, v147
	v_pk_mul_f32 v[218:219], v[12:13], v[166:167]
	v_mov_b32_e32 v147, v199
	v_mov_b32_e32 v198, v200
	v_mov_b32_e32 v199, v149
	v_pk_fma_f32 v[12:13], v[12:13], v[146:147], v[218:219] op_sel:[0,0,1] op_sel_hi:[1,1,0]
	v_pk_mul_f32 v[218:219], v[10:11], v[198:199]
	v_mov_b32_e32 v149, v201
	v_pk_fma_f32 v[10:11], v[10:11], v[148:149], v[218:219] op_sel:[0,0,1] op_sel_hi:[1,1,0]
	s_waitcnt lgkmcnt(6)
	v_mov_b32_e32 v200, v202
	v_mov_b32_e32 v201, v151
	v_pk_add_f32 v[10:11], v[12:13], v[10:11]
	v_pk_mul_f32 v[12:13], v[84:85], v[200:201]
	v_mov_b32_e32 v151, v203
	v_pk_fma_f32 v[12:13], v[84:85], v[150:151], v[12:13] op_sel:[0,0,1] op_sel_hi:[1,1,0]
	v_mov_b32_e32 v84, v204
	v_mov_b32_e32 v85, v153
	v_pk_mul_f32 v[202:203], v[82:83], v[84:85]
	v_mov_b32_e32 v153, v205
	v_pk_fma_f32 v[82:83], v[82:83], v[152:153], v[202:203] op_sel:[0,0,1] op_sel_hi:[1,1,0]
	v_pk_add_f32 v[10:11], v[10:11], 0 op_sel_hi:[1,0]
	v_pk_add_f32 v[12:13], v[12:13], v[82:83]
	s_waitcnt lgkmcnt(5)
	v_mov_b32_e32 v82, v206
	v_mov_b32_e32 v83, v155
	v_pk_add_f32 v[10:11], v[10:11], v[12:13]
	v_pk_mul_f32 v[12:13], v[96:97], v[82:83]
	v_mov_b32_e32 v155, v207
	v_pk_fma_f32 v[12:13], v[96:97], v[154:155], v[12:13] op_sel:[0,0,1] op_sel_hi:[1,1,0]
	v_mov_b32_e32 v96, v208
	v_mov_b32_e32 v97, v157
	v_pk_mul_f32 v[202:203], v[94:95], v[96:97]
	v_mov_b32_e32 v157, v209
	v_pk_fma_f32 v[94:95], v[94:95], v[156:157], v[202:203] op_sel:[0,0,1] op_sel_hi:[1,1,0]
	s_nop 0
	v_pk_add_f32 v[12:13], v[12:13], v[94:95]
	s_waitcnt lgkmcnt(4)
	v_mov_b32_e32 v94, v210
	v_mov_b32_e32 v95, v159
	v_pk_add_f32 v[10:11], v[10:11], v[12:13]
	v_pk_mul_f32 v[12:13], v[104:105], v[94:95]
	v_mov_b32_e32 v159, v211
	v_pk_fma_f32 v[12:13], v[104:105], v[158:159], v[12:13] op_sel:[0,0,1] op_sel_hi:[1,1,0]
	v_mov_b32_e32 v104, v212
	v_mov_b32_e32 v105, v161
	v_pk_mul_f32 v[202:203], v[102:103], v[104:105]
	v_mov_b32_e32 v161, v213
	v_pk_fma_f32 v[102:103], v[102:103], v[160:161], v[202:203] op_sel:[0,0,1] op_sel_hi:[1,1,0]
	s_nop 0
	v_pk_add_f32 v[12:13], v[12:13], v[102:103]
	s_waitcnt lgkmcnt(3)
	v_mov_b32_e32 v102, v214
	v_mov_b32_e32 v103, v163
	v_pk_add_f32 v[10:11], v[10:11], v[12:13]
	v_pk_mul_f32 v[12:13], v[112:113], v[102:103]
	v_mov_b32_e32 v163, v215
	v_pk_fma_f32 v[12:13], v[112:113], v[162:163], v[12:13] op_sel:[0,0,1] op_sel_hi:[1,1,0]
	v_mov_b32_e32 v112, v216
	v_mov_b32_e32 v113, v165
	v_pk_mul_f32 v[202:203], v[110:111], v[112:113]
	v_mov_b32_e32 v165, v217
	v_pk_fma_f32 v[110:111], v[110:111], v[164:165], v[202:203] op_sel:[0,0,1] op_sel_hi:[1,1,0]
	s_nop 0
	v_pk_add_f32 v[12:13], v[12:13], v[110:111]
	s_waitcnt lgkmcnt(2)
	v_mov_b32_e32 v110, v224
	v_mov_b32_e32 v111, v175
	v_pk_add_f32 v[10:11], v[10:11], v[12:13]
	v_pk_mul_f32 v[12:13], v[120:121], v[110:111]
	v_mov_b32_e32 v175, v225
	v_pk_fma_f32 v[12:13], v[120:121], v[174:175], v[12:13] op_sel:[0,0,1] op_sel_hi:[1,1,0]
	v_mov_b32_e32 v120, v226
	v_mov_b32_e32 v121, v177
	v_pk_mul_f32 v[202:203], v[118:119], v[120:121]
	v_mov_b32_e32 v177, v227
	v_pk_fma_f32 v[118:119], v[118:119], v[176:177], v[202:203] op_sel:[0,0,1] op_sel_hi:[1,1,0]
	s_nop 0
	v_pk_add_f32 v[12:13], v[12:13], v[118:119]
	s_waitcnt lgkmcnt(1)
	v_mov_b32_e32 v118, v228
	v_mov_b32_e32 v119, v179
	v_pk_add_f32 v[10:11], v[10:11], v[12:13]
	v_pk_mul_f32 v[12:13], v[128:129], v[118:119]
	v_mov_b32_e32 v179, v229
	v_pk_fma_f32 v[12:13], v[128:129], v[178:179], v[12:13] op_sel:[0,0,1] op_sel_hi:[1,1,0]
	v_mov_b32_e32 v128, v230
	v_mov_b32_e32 v129, v181
	v_pk_mul_f32 v[202:203], v[126:127], v[128:129]
	v_mov_b32_e32 v181, v231
	v_pk_fma_f32 v[126:127], v[126:127], v[180:181], v[202:203] op_sel:[0,0,1] op_sel_hi:[1,1,0]
	s_nop 0
	v_pk_add_f32 v[12:13], v[12:13], v[126:127]
	s_waitcnt lgkmcnt(0)
	v_mov_b32_e32 v126, v232
	v_mov_b32_e32 v127, v183
	v_pk_add_f32 v[10:11], v[10:11], v[12:13]
	v_pk_mul_f32 v[12:13], v[92:93], v[126:127]
	v_mov_b32_e32 v183, v233
	v_pk_fma_f32 v[12:13], v[92:93], v[182:183], v[12:13] op_sel:[0,0,1] op_sel_hi:[1,1,0]
	v_mov_b32_e32 v92, v234
	v_mov_b32_e32 v93, v185
	v_pk_mul_f32 v[202:203], v[90:91], v[92:93]
	v_mov_b32_e32 v185, v235
	v_pk_fma_f32 v[90:91], v[90:91], v[184:185], v[202:203] op_sel:[0,0,1] op_sel_hi:[1,1,0]
	s_nop 0
	v_pk_add_f32 v[12:13], v[12:13], v[90:91]
	s_nop 0
	v_pk_add_f32 v[12:13], v[10:11], v[12:13]
	v_pk_mul_f32 v[10:11], v[80:81], v[166:167]
	s_nop 0
	v_pk_fma_f32 v[10:11], v[80:81], v[146:147], v[10:11] op_sel:[0,0,1] op_sel_hi:[1,1,0]
	v_pk_mul_f32 v[80:81], v[14:15], v[198:199]
	s_nop 0
	v_pk_fma_f32 v[14:15], v[14:15], v[148:149], v[80:81] op_sel:[0,0,1] op_sel_hi:[1,1,0]
	v_pk_mul_f32 v[80:81], v[86:87], v[84:85]
	v_pk_add_f32 v[10:11], v[10:11], v[14:15]
	v_pk_mul_f32 v[14:15], v[88:89], v[200:201]
	v_pk_fma_f32 v[80:81], v[86:87], v[152:153], v[80:81] op_sel:[0,0,1] op_sel_hi:[1,1,0]
	v_pk_fma_f32 v[14:15], v[88:89], v[150:151], v[14:15] op_sel:[0,0,1] op_sel_hi:[1,1,0]
	v_pk_add_f32 v[10:11], v[10:11], 0 op_sel_hi:[1,0]
	v_pk_add_f32 v[14:15], v[14:15], v[80:81]
	v_pk_mul_f32 v[80:81], v[98:99], v[96:97]
	v_pk_add_f32 v[10:11], v[10:11], v[14:15]
	v_pk_mul_f32 v[14:15], v[100:101], v[82:83]
	v_pk_fma_f32 v[80:81], v[98:99], v[156:157], v[80:81] op_sel:[0,0,1] op_sel_hi:[1,1,0]
	v_pk_fma_f32 v[14:15], v[100:101], v[154:155], v[14:15] op_sel:[0,0,1] op_sel_hi:[1,1,0]
	s_nop 0
	v_pk_add_f32 v[14:15], v[14:15], v[80:81]
	v_pk_mul_f32 v[80:81], v[106:107], v[104:105]
	v_pk_add_f32 v[10:11], v[10:11], v[14:15]
	v_pk_mul_f32 v[14:15], v[108:109], v[94:95]
	v_pk_fma_f32 v[80:81], v[106:107], v[160:161], v[80:81] op_sel:[0,0,1] op_sel_hi:[1,1,0]
	v_pk_fma_f32 v[14:15], v[108:109], v[158:159], v[14:15] op_sel:[0,0,1] op_sel_hi:[1,1,0]
	s_nop 0
	v_pk_add_f32 v[14:15], v[14:15], v[80:81]
	v_pk_mul_f32 v[80:81], v[114:115], v[112:113]
	v_pk_add_f32 v[10:11], v[10:11], v[14:15]
	v_pk_mul_f32 v[14:15], v[116:117], v[102:103]
	v_pk_fma_f32 v[80:81], v[114:115], v[164:165], v[80:81] op_sel:[0,0,1] op_sel_hi:[1,1,0]
	v_pk_fma_f32 v[14:15], v[116:117], v[162:163], v[14:15] op_sel:[0,0,1] op_sel_hi:[1,1,0]
	s_nop 0
	v_pk_add_f32 v[14:15], v[14:15], v[80:81]
	v_pk_mul_f32 v[80:81], v[122:123], v[120:121]
	v_pk_add_f32 v[10:11], v[10:11], v[14:15]
	v_pk_mul_f32 v[14:15], v[124:125], v[110:111]
	v_pk_fma_f32 v[80:81], v[122:123], v[176:177], v[80:81] op_sel:[0,0,1] op_sel_hi:[1,1,0]
	v_pk_fma_f32 v[14:15], v[124:125], v[174:175], v[14:15] op_sel:[0,0,1] op_sel_hi:[1,1,0]
	s_nop 0
	v_pk_add_f32 v[14:15], v[14:15], v[80:81]
	v_pk_mul_f32 v[80:81], v[130:131], v[128:129]
	v_pk_add_f32 v[10:11], v[10:11], v[14:15]
	v_pk_mul_f32 v[14:15], v[132:133], v[118:119]
	v_pk_fma_f32 v[80:81], v[130:131], v[180:181], v[80:81] op_sel:[0,0,1] op_sel_hi:[1,1,0]
	v_pk_fma_f32 v[14:15], v[132:133], v[178:179], v[14:15] op_sel:[0,0,1] op_sel_hi:[1,1,0]
	s_nop 0
	v_pk_add_f32 v[14:15], v[14:15], v[80:81]
	v_pk_mul_f32 v[80:81], v[136:137], v[92:93]
	v_pk_add_f32 v[10:11], v[10:11], v[14:15]
	v_pk_mul_f32 v[14:15], v[138:139], v[126:127]
	v_pk_fma_f32 v[80:81], v[136:137], v[184:185], v[80:81] op_sel:[0,0,1] op_sel_hi:[1,1,0]
	v_pk_fma_f32 v[14:15], v[138:139], v[182:183], v[14:15] op_sel:[0,0,1] op_sel_hi:[1,1,0]
	s_nop 0
	v_pk_add_f32 v[14:15], v[14:15], v[80:81]
	s_nop 0
	v_pk_add_f32 v[10:11], v[10:11], v[14:15]
	v_cndmask_b32_e64 v14, v140, v141, s[46:47]
	v_cmp_eq_u32_e64 s[46:47], 2, v20
	s_nop 1
	v_cndmask_b32_e64 v14, v14, v142, s[46:47]
	v_cmp_eq_u32_e64 s[46:47], 3, v20
	s_nop 1
	v_cndmask_b32_e64 v14, v14, v143, s[46:47]
	v_cmp_eq_u32_e64 s[46:47], 4, v20
	s_nop 1
	v_cndmask_b32_e64 v14, v14, v144, s[46:47]
	v_cmp_eq_u32_e64 s[46:47], 5, v20
	s_nop 1
	v_cndmask_b32_e64 v14, v14, v145, s[46:47]
	v_cmp_eq_u32_e64 s[46:47], 6, v20
	s_nop 1
	v_cndmask_b32_e64 v14, v14, v12, s[46:47]
	v_cmp_eq_u32_e64 s[46:47], 7, v20
	s_nop 1
	v_cndmask_b32_e64 v14, v14, v13, s[46:47]
	v_cmp_eq_u32_e64 s[46:47], 8, v20
	s_nop 1
	v_cndmask_b32_e64 v14, v14, v0, s[46:47]
	v_cmp_eq_u32_e64 s[46:47], 9, v20
	s_nop 1
	v_cndmask_b32_e64 v14, v14, v1, s[46:47]
	v_cmp_eq_u32_e64 s[46:47], 10, v20
	s_nop 1
	v_cndmask_b32_e64 v14, v14, v2, s[46:47]
	v_cmp_eq_u32_e64 s[46:47], 11, v20
	s_nop 1
	v_cndmask_b32_e64 v14, v14, v3, s[46:47]
	v_cmp_eq_u32_e64 s[46:47], 12, v20
	s_nop 1
	v_cndmask_b32_e64 v14, v14, v134, s[46:47]
	v_cmp_eq_u32_e64 s[46:47], 13, v20
	s_nop 1
	v_cndmask_b32_e64 v14, v14, v135, s[46:47]
	v_cmp_eq_u32_e64 s[46:47], 14, v20
	s_nop 1
	v_cndmask_b32_e64 v14, v14, v10, s[46:47]
	v_cmp_eq_u32_e64 s[46:47], 15, v20
	s_nop 1
	v_cndmask_b32_e64 v14, v14, v11, s[46:47]
	v_cmp_eq_u32_e64 s[46:47], 1, v22
	ds_bpermute_b32 v14, v39, v14
	s_nop 0
	v_cndmask_b32_e64 v15, v140, v141, s[46:47]
	v_cmp_eq_u32_e64 s[46:47], 2, v22
	s_nop 1
	v_cndmask_b32_e64 v15, v15, v142, s[46:47]
	v_cmp_eq_u32_e64 s[46:47], 3, v22
	s_nop 1
	v_cndmask_b32_e64 v15, v15, v143, s[46:47]
	v_cmp_eq_u32_e64 s[46:47], 4, v22
	s_nop 1
	v_cndmask_b32_e64 v15, v15, v144, s[46:47]
	v_cmp_eq_u32_e64 s[46:47], 5, v22
	s_nop 1
	v_cndmask_b32_e64 v15, v15, v145, s[46:47]
	v_cmp_eq_u32_e64 s[46:47], 6, v22
	s_nop 1
	v_cndmask_b32_e64 v15, v15, v12, s[46:47]
	v_cmp_eq_u32_e64 s[46:47], 7, v22
	s_nop 1
	v_cndmask_b32_e64 v15, v15, v13, s[46:47]
	v_cmp_eq_u32_e64 s[46:47], 8, v22
	s_nop 1
	v_cndmask_b32_e64 v15, v15, v0, s[46:47]
	v_cmp_eq_u32_e64 s[46:47], 9, v22
	s_nop 1
	v_cndmask_b32_e64 v15, v15, v1, s[46:47]
	v_cmp_eq_u32_e64 s[46:47], 10, v22
	s_nop 1
	v_cndmask_b32_e64 v15, v15, v2, s[46:47]
	v_cmp_eq_u32_e64 s[46:47], 11, v22
	s_nop 1
	v_cndmask_b32_e64 v15, v15, v3, s[46:47]
	v_cmp_eq_u32_e64 s[46:47], 12, v22
	s_nop 1
	v_cndmask_b32_e64 v15, v15, v134, s[46:47]
	v_cmp_eq_u32_e64 s[46:47], 13, v22
	s_nop 1
	v_cndmask_b32_e64 v15, v15, v135, s[46:47]
	v_cmp_eq_u32_e64 s[46:47], 14, v22
	s_nop 1
	v_cndmask_b32_e64 v15, v15, v10, s[46:47]
	v_cmp_eq_u32_e64 s[46:47], 15, v22
	s_nop 1
	v_cndmask_b32_e64 v15, v15, v11, s[46:47]
	s_waitcnt lgkmcnt(0)
	v_add_f32_e32 v69, v15, v14
	v_cmp_eq_u32_e64 s[46:47], 1, v24
	s_nop 1
	v_cndmask_b32_e64 v14, v69, v141, s[46:47]
	v_cmp_eq_u32_e64 s[46:47], 2, v24
	s_nop 1
	v_cndmask_b32_e64 v14, v14, v142, s[46:47]
	v_cmp_eq_u32_e64 s[46:47], 3, v24
	s_nop 1
	v_cndmask_b32_e64 v14, v14, v143, s[46:47]
	v_cmp_eq_u32_e64 s[46:47], 4, v24
	s_nop 1
	v_cndmask_b32_e64 v14, v14, v144, s[46:47]
	v_cmp_eq_u32_e64 s[46:47], 5, v24
	s_nop 1
	v_cndmask_b32_e64 v14, v14, v145, s[46:47]
	v_cmp_eq_u32_e64 s[46:47], 6, v24
	s_nop 1
	v_cndmask_b32_e64 v14, v14, v12, s[46:47]
	v_cmp_eq_u32_e64 s[46:47], 7, v24
	s_nop 1
	v_cndmask_b32_e64 v14, v14, v13, s[46:47]
	v_cmp_eq_u32_e64 s[46:47], 8, v24
	s_nop 1
	v_cndmask_b32_e64 v14, v14, v0, s[46:47]
	v_cmp_eq_u32_e64 s[46:47], 9, v24
	s_nop 1
	v_cndmask_b32_e64 v14, v14, v1, s[46:47]
	v_cmp_eq_u32_e64 s[46:47], 10, v24
	s_nop 1
	v_cndmask_b32_e64 v14, v14, v2, s[46:47]
	v_cmp_eq_u32_e64 s[46:47], 11, v24
	s_nop 1
	v_cndmask_b32_e64 v14, v14, v3, s[46:47]
	v_cmp_eq_u32_e64 s[46:47], 12, v24
	s_nop 1
	v_cndmask_b32_e64 v14, v14, v134, s[46:47]
	v_cmp_eq_u32_e64 s[46:47], 13, v24
	s_nop 1
	v_cndmask_b32_e64 v14, v14, v135, s[46:47]
	v_cmp_eq_u32_e64 s[46:47], 14, v24
	s_nop 1
	v_cndmask_b32_e64 v14, v14, v10, s[46:47]
	v_cmp_eq_u32_e64 s[46:47], 15, v24
	s_nop 1
	v_cndmask_b32_e64 v14, v14, v11, s[46:47]
	v_cmp_eq_u32_e64 s[46:47], 1, v26
	ds_bpermute_b32 v14, v39, v14
	s_nop 0
	v_cndmask_b32_e64 v15, v69, v141, s[46:47]
	v_cmp_eq_u32_e64 s[46:47], 2, v26
	s_nop 1
	v_cndmask_b32_e64 v15, v15, v142, s[46:47]
	v_cmp_eq_u32_e64 s[46:47], 3, v26
	s_nop 1
	v_cndmask_b32_e64 v15, v15, v143, s[46:47]
	v_cmp_eq_u32_e64 s[46:47], 4, v26
	s_nop 1
	v_cndmask_b32_e64 v15, v15, v144, s[46:47]
	v_cmp_eq_u32_e64 s[46:47], 5, v26
	s_nop 1
	v_cndmask_b32_e64 v15, v15, v145, s[46:47]
	v_cmp_eq_u32_e64 s[46:47], 6, v26
	s_nop 1
	v_cndmask_b32_e64 v15, v15, v12, s[46:47]
	v_cmp_eq_u32_e64 s[46:47], 7, v26
	s_nop 1
	v_cndmask_b32_e64 v15, v15, v13, s[46:47]
	v_cmp_eq_u32_e64 s[46:47], 8, v26
	s_nop 1
	v_cndmask_b32_e64 v15, v15, v0, s[46:47]
	v_cmp_eq_u32_e64 s[46:47], 9, v26
	s_nop 1
	v_cndmask_b32_e64 v15, v15, v1, s[46:47]
	v_cmp_eq_u32_e64 s[46:47], 10, v26
	s_nop 1
	v_cndmask_b32_e64 v15, v15, v2, s[46:47]
	v_cmp_eq_u32_e64 s[46:47], 11, v26
	s_nop 1
	v_cndmask_b32_e64 v15, v15, v3, s[46:47]
	v_cmp_eq_u32_e64 s[46:47], 12, v26
	s_nop 1
	v_cndmask_b32_e64 v15, v15, v134, s[46:47]
	v_cmp_eq_u32_e64 s[46:47], 13, v26
	s_nop 1
	v_cndmask_b32_e64 v15, v15, v135, s[46:47]
	v_cmp_eq_u32_e64 s[46:47], 14, v26
	s_nop 1
	v_cndmask_b32_e64 v15, v15, v10, s[46:47]
	v_cmp_eq_u32_e64 s[46:47], 15, v26
	s_nop 1
	v_cndmask_b32_e64 v15, v15, v11, s[46:47]
	s_waitcnt lgkmcnt(0)
	v_add_f32_e32 v71, v15, v14
	v_cmp_eq_u32_e64 s[46:47], 1, v28
	s_nop 1
	v_cndmask_b32_e64 v14, v69, v71, s[46:47]
	v_cmp_eq_u32_e64 s[46:47], 2, v28
	s_nop 1
	v_cndmask_b32_e64 v14, v14, v142, s[46:47]
	v_cmp_eq_u32_e64 s[46:47], 3, v28
	s_nop 1
	v_cndmask_b32_e64 v14, v14, v143, s[46:47]
	v_cmp_eq_u32_e64 s[46:47], 4, v28
	s_nop 1
	v_cndmask_b32_e64 v14, v14, v144, s[46:47]
	v_cmp_eq_u32_e64 s[46:47], 5, v28
	s_nop 1
	v_cndmask_b32_e64 v14, v14, v145, s[46:47]
	v_cmp_eq_u32_e64 s[46:47], 6, v28
	s_nop 1
	v_cndmask_b32_e64 v14, v14, v12, s[46:47]
	v_cmp_eq_u32_e64 s[46:47], 7, v28
	s_nop 1
	v_cndmask_b32_e64 v14, v14, v13, s[46:47]
	v_cmp_eq_u32_e64 s[46:47], 8, v28
	s_nop 1
	v_cndmask_b32_e64 v14, v14, v0, s[46:47]
	v_cmp_eq_u32_e64 s[46:47], 9, v28
	s_nop 1
	v_cndmask_b32_e64 v14, v14, v1, s[46:47]
	v_cmp_eq_u32_e64 s[46:47], 10, v28
	s_nop 1
	v_cndmask_b32_e64 v14, v14, v2, s[46:47]
	v_cmp_eq_u32_e64 s[46:47], 11, v28
	s_nop 1
	v_cndmask_b32_e64 v14, v14, v3, s[46:47]
	v_cmp_eq_u32_e64 s[46:47], 12, v28
	s_nop 1
	v_cndmask_b32_e64 v14, v14, v134, s[46:47]
	v_cmp_eq_u32_e64 s[46:47], 13, v28
	s_nop 1
	v_cndmask_b32_e64 v14, v14, v135, s[46:47]
	v_cmp_eq_u32_e64 s[46:47], 14, v28
	s_nop 1
	v_cndmask_b32_e64 v14, v14, v10, s[46:47]
	v_cmp_eq_u32_e64 s[46:47], 15, v28
	s_nop 1
	v_cndmask_b32_e64 v14, v14, v11, s[46:47]
	v_cmp_eq_u32_e64 s[46:47], 1, v30
	ds_bpermute_b32 v14, v39, v14
	s_nop 0
	v_cndmask_b32_e64 v15, v69, v71, s[46:47]
	v_cmp_eq_u32_e64 s[46:47], 2, v30
	s_nop 1
	v_cndmask_b32_e64 v15, v15, v142, s[46:47]
	v_cmp_eq_u32_e64 s[46:47], 3, v30
	s_nop 1
	v_cndmask_b32_e64 v15, v15, v143, s[46:47]
	v_cmp_eq_u32_e64 s[46:47], 4, v30
	s_nop 1
	v_cndmask_b32_e64 v15, v15, v144, s[46:47]
	v_cmp_eq_u32_e64 s[46:47], 5, v30
	s_nop 1
	v_cndmask_b32_e64 v15, v15, v145, s[46:47]
	v_cmp_eq_u32_e64 s[46:47], 6, v30
	s_nop 1
	v_cndmask_b32_e64 v15, v15, v12, s[46:47]
	v_cmp_eq_u32_e64 s[46:47], 7, v30
	s_nop 1
	v_cndmask_b32_e64 v15, v15, v13, s[46:47]
	v_cmp_eq_u32_e64 s[46:47], 8, v30
	s_nop 1
	v_cndmask_b32_e64 v15, v15, v0, s[46:47]
	v_cmp_eq_u32_e64 s[46:47], 9, v30
	s_nop 1
	v_cndmask_b32_e64 v15, v15, v1, s[46:47]
	v_cmp_eq_u32_e64 s[46:47], 10, v30
	s_nop 1
	v_cndmask_b32_e64 v15, v15, v2, s[46:47]
	v_cmp_eq_u32_e64 s[46:47], 11, v30
	s_nop 1
	v_cndmask_b32_e64 v15, v15, v3, s[46:47]
	v_cmp_eq_u32_e64 s[46:47], 12, v30
	s_nop 1
	v_cndmask_b32_e64 v15, v15, v134, s[46:47]
	v_cmp_eq_u32_e64 s[46:47], 13, v30
	s_nop 1
	v_cndmask_b32_e64 v15, v15, v135, s[46:47]
	v_cmp_eq_u32_e64 s[46:47], 14, v30
	s_nop 1
	v_cndmask_b32_e64 v15, v15, v10, s[46:47]
	v_cmp_eq_u32_e64 s[46:47], 15, v30
	s_nop 1
	v_cndmask_b32_e64 v15, v15, v11, s[46:47]
	v_cmp_eq_u32_e64 s[46:47], 1, v32
	s_waitcnt lgkmcnt(0)
	v_add_f32_e32 v73, v15, v14
	v_cndmask_b32_e64 v14, v69, v71, s[46:47]
	v_cmp_eq_u32_e64 s[46:47], 2, v32
	s_nop 1
	v_cndmask_b32_e64 v14, v14, v73, s[46:47]
	v_cmp_eq_u32_e64 s[46:47], 3, v32
	s_nop 1
	v_cndmask_b32_e64 v14, v14, v143, s[46:47]
	v_cmp_eq_u32_e64 s[46:47], 4, v32
	s_nop 1
	v_cndmask_b32_e64 v14, v14, v144, s[46:47]
	v_cmp_eq_u32_e64 s[46:47], 5, v32
	s_nop 1
	v_cndmask_b32_e64 v14, v14, v145, s[46:47]
	v_cmp_eq_u32_e64 s[46:47], 6, v32
	s_nop 1
	v_cndmask_b32_e64 v14, v14, v12, s[46:47]
	v_cmp_eq_u32_e64 s[46:47], 7, v32
	s_nop 1
	v_cndmask_b32_e64 v14, v14, v13, s[46:47]
	v_cmp_eq_u32_e64 s[46:47], 8, v32
	s_nop 1
	v_cndmask_b32_e64 v14, v14, v0, s[46:47]
	v_cmp_eq_u32_e64 s[46:47], 9, v32
	s_nop 1
	v_cndmask_b32_e64 v14, v14, v1, s[46:47]
	v_cmp_eq_u32_e64 s[46:47], 10, v32
	s_nop 1
	v_cndmask_b32_e64 v14, v14, v2, s[46:47]
	v_cmp_eq_u32_e64 s[46:47], 11, v32
	s_nop 1
	v_cndmask_b32_e64 v14, v14, v3, s[46:47]
	v_cmp_eq_u32_e64 s[46:47], 12, v32
	s_nop 1
	v_cndmask_b32_e64 v14, v14, v134, s[46:47]
	v_cmp_eq_u32_e64 s[46:47], 13, v32
	s_nop 1
	v_cndmask_b32_e64 v14, v14, v135, s[46:47]
	v_cmp_eq_u32_e64 s[46:47], 14, v32
	s_nop 1
	v_cndmask_b32_e64 v14, v14, v10, s[46:47]
	v_cmp_eq_u32_e64 s[46:47], 15, v32
	s_nop 1
	v_cndmask_b32_e64 v14, v14, v11, s[46:47]
	v_cmp_eq_u32_e64 s[46:47], 1, v34
	ds_bpermute_b32 v14, v39, v14
	s_nop 0
	v_cndmask_b32_e64 v15, v69, v71, s[46:47]
	v_cmp_eq_u32_e64 s[46:47], 2, v34
	s_nop 1
	v_cndmask_b32_e64 v15, v15, v73, s[46:47]
	v_cmp_eq_u32_e64 s[46:47], 3, v34
	s_nop 1
	v_cndmask_b32_e64 v15, v15, v143, s[46:47]
	v_cmp_eq_u32_e64 s[46:47], 4, v34
	s_nop 1
	v_cndmask_b32_e64 v15, v15, v144, s[46:47]
	v_cmp_eq_u32_e64 s[46:47], 5, v34
	s_nop 1
	v_cndmask_b32_e64 v15, v15, v145, s[46:47]
	v_cmp_eq_u32_e64 s[46:47], 6, v34
	s_nop 1
	v_cndmask_b32_e64 v15, v15, v12, s[46:47]
	v_cmp_eq_u32_e64 s[46:47], 7, v34
	s_nop 1
	v_cndmask_b32_e64 v15, v15, v13, s[46:47]
	v_cmp_eq_u32_e64 s[46:47], 8, v34
	s_nop 1
	v_cndmask_b32_e64 v15, v15, v0, s[46:47]
	v_cmp_eq_u32_e64 s[46:47], 9, v34
	s_nop 1
	v_cndmask_b32_e64 v15, v15, v1, s[46:47]
	v_cmp_eq_u32_e64 s[46:47], 10, v34
	s_nop 1
	v_cndmask_b32_e64 v15, v15, v2, s[46:47]
	v_cmp_eq_u32_e64 s[46:47], 11, v34
	s_nop 1
	v_cndmask_b32_e64 v15, v15, v3, s[46:47]
	v_cmp_eq_u32_e64 s[46:47], 12, v34
	s_nop 1
	v_cndmask_b32_e64 v15, v15, v134, s[46:47]
	v_cmp_eq_u32_e64 s[46:47], 13, v34
	s_nop 1
	v_cndmask_b32_e64 v15, v15, v135, s[46:47]
	v_cmp_eq_u32_e64 s[46:47], 14, v34
	s_nop 1
	v_cndmask_b32_e64 v15, v15, v10, s[46:47]
	v_cmp_eq_u32_e64 s[46:47], 15, v34
	s_nop 1
	v_cndmask_b32_e64 v15, v15, v11, s[46:47]
	v_cmp_eq_u32_e64 s[46:47], 1, v36
	s_waitcnt lgkmcnt(0)
	v_add_f32_e32 v75, v15, v14
	v_cndmask_b32_e64 v14, v69, v71, s[46:47]
	v_cmp_eq_u32_e64 s[46:47], 2, v36
	s_nop 1
	v_cndmask_b32_e64 v14, v14, v73, s[46:47]
	v_cmp_eq_u32_e64 s[46:47], 3, v36
	s_nop 1
	v_cndmask_b32_e64 v14, v14, v75, s[46:47]
	v_cmp_eq_u32_e64 s[46:47], 4, v36
	s_nop 1
	v_cndmask_b32_e64 v14, v14, v144, s[46:47]
	v_cmp_eq_u32_e64 s[46:47], 5, v36
	s_nop 1
	v_cndmask_b32_e64 v14, v14, v145, s[46:47]
	v_cmp_eq_u32_e64 s[46:47], 6, v36
	s_nop 1
	v_cndmask_b32_e64 v14, v14, v12, s[46:47]
	v_cmp_eq_u32_e64 s[46:47], 7, v36
	s_nop 1
	v_cndmask_b32_e64 v14, v14, v13, s[46:47]
	v_cmp_eq_u32_e64 s[46:47], 8, v36
	s_nop 1
	v_cndmask_b32_e64 v14, v14, v0, s[46:47]
	v_cmp_eq_u32_e64 s[46:47], 9, v36
	s_nop 1
	v_cndmask_b32_e64 v14, v14, v1, s[46:47]
	v_cmp_eq_u32_e64 s[46:47], 10, v36
	s_nop 1
	v_cndmask_b32_e64 v14, v14, v2, s[46:47]
	v_cmp_eq_u32_e64 s[46:47], 11, v36
	s_nop 1
	v_cndmask_b32_e64 v14, v14, v3, s[46:47]
	v_cmp_eq_u32_e64 s[46:47], 12, v36
	s_nop 1
	v_cndmask_b32_e64 v14, v14, v134, s[46:47]
	v_cmp_eq_u32_e64 s[46:47], 13, v36
	s_nop 1
	v_cndmask_b32_e64 v14, v14, v135, s[46:47]
	v_cmp_eq_u32_e64 s[46:47], 14, v36
	s_nop 1
	v_cndmask_b32_e64 v14, v14, v10, s[46:47]
	v_cmp_eq_u32_e64 s[46:47], 15, v36
	s_nop 1
	v_cndmask_b32_e64 v14, v14, v11, s[46:47]
	v_cmp_eq_u32_e64 s[46:47], 1, v38
	ds_bpermute_b32 v14, v39, v14
	s_nop 0
	v_cndmask_b32_e64 v15, v69, v71, s[46:47]
	v_cmp_eq_u32_e64 s[46:47], 2, v38
	s_nop 1
	v_cndmask_b32_e64 v15, v15, v73, s[46:47]
	v_cmp_eq_u32_e64 s[46:47], 3, v38
	s_nop 1
	v_cndmask_b32_e64 v15, v15, v75, s[46:47]
	v_cmp_eq_u32_e64 s[46:47], 4, v38
	s_nop 1
	v_cndmask_b32_e64 v15, v15, v144, s[46:47]
	v_cmp_eq_u32_e64 s[46:47], 5, v38
	s_nop 1
	v_cndmask_b32_e64 v15, v15, v145, s[46:47]
	v_cmp_eq_u32_e64 s[46:47], 6, v38
	s_nop 1
	v_cndmask_b32_e64 v15, v15, v12, s[46:47]
	v_cmp_eq_u32_e64 s[46:47], 7, v38
	s_nop 1
	v_cndmask_b32_e64 v15, v15, v13, s[46:47]
	v_cmp_eq_u32_e64 s[46:47], 8, v38
	s_nop 1
	v_cndmask_b32_e64 v15, v15, v0, s[46:47]
	v_cmp_eq_u32_e64 s[46:47], 9, v38
	s_nop 1
	v_cndmask_b32_e64 v15, v15, v1, s[46:47]
	v_cmp_eq_u32_e64 s[46:47], 10, v38
	s_nop 1
	v_cndmask_b32_e64 v15, v15, v2, s[46:47]
	v_cmp_eq_u32_e64 s[46:47], 11, v38
	s_nop 1
	v_cndmask_b32_e64 v15, v15, v3, s[46:47]
	v_cmp_eq_u32_e64 s[46:47], 12, v38
	s_nop 1
	v_cndmask_b32_e64 v15, v15, v134, s[46:47]
	v_cmp_eq_u32_e64 s[46:47], 13, v38
	s_nop 1
	v_cndmask_b32_e64 v15, v15, v135, s[46:47]
	v_cmp_eq_u32_e64 s[46:47], 14, v38
	s_nop 1
	v_cndmask_b32_e64 v15, v15, v10, s[46:47]
	v_cmp_eq_u32_e64 s[46:47], 15, v38
	s_nop 1
	v_cndmask_b32_e64 v15, v15, v11, s[46:47]
	v_cmp_eq_u32_e64 s[46:47], 1, v40
	s_waitcnt lgkmcnt(0)
	v_add_f32_e32 v14, v15, v14
	v_cndmask_b32_e64 v15, v69, v71, s[46:47]
	v_cmp_eq_u32_e64 s[46:47], 2, v40
	s_nop 1
	v_cndmask_b32_e64 v15, v15, v73, s[46:47]
	v_cmp_eq_u32_e64 s[46:47], 3, v40
	s_nop 1
	v_cndmask_b32_e64 v15, v15, v75, s[46:47]
	v_cmp_eq_u32_e64 s[46:47], 4, v40
	s_nop 1
	v_cndmask_b32_e64 v15, v15, v14, s[46:47]
	v_cmp_eq_u32_e64 s[46:47], 5, v40
	s_nop 1
	v_cndmask_b32_e64 v15, v15, v145, s[46:47]
	v_cmp_eq_u32_e64 s[46:47], 6, v40
	s_nop 1
	v_cndmask_b32_e64 v15, v15, v12, s[46:47]
	v_cmp_eq_u32_e64 s[46:47], 7, v40
	s_nop 1
	v_cndmask_b32_e64 v15, v15, v13, s[46:47]
	v_cmp_eq_u32_e64 s[46:47], 8, v40
	s_nop 1
	v_cndmask_b32_e64 v15, v15, v0, s[46:47]
	v_cmp_eq_u32_e64 s[46:47], 9, v40
	s_nop 1
	v_cndmask_b32_e64 v15, v15, v1, s[46:47]
	v_cmp_eq_u32_e64 s[46:47], 10, v40
	s_nop 1
	v_cndmask_b32_e64 v15, v15, v2, s[46:47]
	v_cmp_eq_u32_e64 s[46:47], 11, v40
	s_nop 1
	v_cndmask_b32_e64 v15, v15, v3, s[46:47]
	v_cmp_eq_u32_e64 s[46:47], 12, v40
	s_nop 1
	v_cndmask_b32_e64 v15, v15, v134, s[46:47]
	v_cmp_eq_u32_e64 s[46:47], 13, v40
	s_nop 1
	v_cndmask_b32_e64 v15, v15, v135, s[46:47]
	v_cmp_eq_u32_e64 s[46:47], 14, v40
	s_nop 1
	v_cndmask_b32_e64 v15, v15, v10, s[46:47]
	v_cmp_eq_u32_e64 s[46:47], 15, v40
	s_nop 1
	v_cndmask_b32_e64 v15, v15, v11, s[46:47]
	v_cmp_eq_u32_e64 s[46:47], 1, v42
	ds_bpermute_b32 v15, v39, v15
	s_nop 0
	v_cndmask_b32_e64 v80, v69, v71, s[46:47]
	v_cmp_eq_u32_e64 s[46:47], 2, v42
	s_nop 1
	v_cndmask_b32_e64 v80, v80, v73, s[46:47]
	v_cmp_eq_u32_e64 s[46:47], 3, v42
	s_nop 1
	v_cndmask_b32_e64 v80, v80, v75, s[46:47]
	v_cmp_eq_u32_e64 s[46:47], 4, v42
	s_nop 1
	v_cndmask_b32_e64 v80, v80, v14, s[46:47]
	v_cmp_eq_u32_e64 s[46:47], 5, v42
	s_nop 1
	v_cndmask_b32_e64 v80, v80, v145, s[46:47]
	v_cmp_eq_u32_e64 s[46:47], 6, v42
	s_nop 1
	v_cndmask_b32_e64 v80, v80, v12, s[46:47]
	v_cmp_eq_u32_e64 s[46:47], 7, v42
	s_nop 1
	v_cndmask_b32_e64 v80, v80, v13, s[46:47]
	v_cmp_eq_u32_e64 s[46:47], 8, v42
	s_nop 1
	v_cndmask_b32_e64 v80, v80, v0, s[46:47]
	v_cmp_eq_u32_e64 s[46:47], 9, v42
	s_nop 1
	v_cndmask_b32_e64 v80, v80, v1, s[46:47]
	v_cmp_eq_u32_e64 s[46:47], 10, v42
	s_nop 1
	v_cndmask_b32_e64 v80, v80, v2, s[46:47]
	v_cmp_eq_u32_e64 s[46:47], 11, v42
	s_nop 1
	v_cndmask_b32_e64 v80, v80, v3, s[46:47]
	v_cmp_eq_u32_e64 s[46:47], 12, v42
	s_nop 1
	v_cndmask_b32_e64 v80, v80, v134, s[46:47]
	v_cmp_eq_u32_e64 s[46:47], 13, v42
	s_nop 1
	v_cndmask_b32_e64 v80, v80, v135, s[46:47]
	v_cmp_eq_u32_e64 s[46:47], 14, v42
	s_nop 1
	v_cndmask_b32_e64 v80, v80, v10, s[46:47]
	v_cmp_eq_u32_e64 s[46:47], 15, v42
	s_nop 1
	v_cndmask_b32_e64 v80, v80, v11, s[46:47]
	v_cmp_eq_u32_e64 s[46:47], 1, v44
	s_waitcnt lgkmcnt(0)
	v_add_f32_e32 v15, v80, v15
	v_cndmask_b32_e64 v80, v69, v71, s[46:47]
	v_cmp_eq_u32_e64 s[46:47], 2, v44
	s_nop 1
	v_cndmask_b32_e64 v80, v80, v73, s[46:47]
	v_cmp_eq_u32_e64 s[46:47], 3, v44
	s_nop 1
	v_cndmask_b32_e64 v80, v80, v75, s[46:47]
	v_cmp_eq_u32_e64 s[46:47], 4, v44
	s_nop 1
	v_cndmask_b32_e64 v80, v80, v14, s[46:47]
	v_cmp_eq_u32_e64 s[46:47], 5, v44
	s_nop 1
	v_cndmask_b32_e64 v80, v80, v15, s[46:47]
	v_cmp_eq_u32_e64 s[46:47], 6, v44
	s_nop 1
	v_cndmask_b32_e64 v80, v80, v12, s[46:47]
	v_cmp_eq_u32_e64 s[46:47], 7, v44
	s_nop 1
	v_cndmask_b32_e64 v80, v80, v13, s[46:47]
	v_cmp_eq_u32_e64 s[46:47], 8, v44
	s_nop 1
	v_cndmask_b32_e64 v80, v80, v0, s[46:47]
	v_cmp_eq_u32_e64 s[46:47], 9, v44
	s_nop 1
	v_cndmask_b32_e64 v80, v80, v1, s[46:47]
	v_cmp_eq_u32_e64 s[46:47], 10, v44
	s_nop 1
	v_cndmask_b32_e64 v80, v80, v2, s[46:47]
	v_cmp_eq_u32_e64 s[46:47], 11, v44
	s_nop 1
	v_cndmask_b32_e64 v80, v80, v3, s[46:47]
	v_cmp_eq_u32_e64 s[46:47], 12, v44
	s_nop 1
	v_cndmask_b32_e64 v80, v80, v134, s[46:47]
	v_cmp_eq_u32_e64 s[46:47], 13, v44
	s_nop 1
	v_cndmask_b32_e64 v80, v80, v135, s[46:47]
	v_cmp_eq_u32_e64 s[46:47], 14, v44
	s_nop 1
	v_cndmask_b32_e64 v80, v80, v10, s[46:47]
	v_cmp_eq_u32_e64 s[46:47], 15, v44
	s_nop 1
	v_cndmask_b32_e64 v80, v80, v11, s[46:47]
	v_cmp_eq_u32_e64 s[46:47], 1, v46
	ds_bpermute_b32 v80, v39, v80
	s_nop 0
	v_cndmask_b32_e64 v81, v69, v71, s[46:47]
	v_cmp_eq_u32_e64 s[46:47], 2, v46
	s_nop 1
	v_cndmask_b32_e64 v81, v81, v73, s[46:47]
	v_cmp_eq_u32_e64 s[46:47], 3, v46
	s_nop 1
	v_cndmask_b32_e64 v81, v81, v75, s[46:47]
	v_cmp_eq_u32_e64 s[46:47], 4, v46
	s_nop 1
	v_cndmask_b32_e64 v81, v81, v14, s[46:47]
	v_cmp_eq_u32_e64 s[46:47], 5, v46
	s_nop 1
	v_cndmask_b32_e64 v81, v81, v15, s[46:47]
	v_cmp_eq_u32_e64 s[46:47], 6, v46
	s_nop 1
	v_cndmask_b32_e64 v12, v81, v12, s[46:47]
	v_cmp_eq_u32_e64 s[46:47], 7, v46
	s_nop 1
	v_cndmask_b32_e64 v12, v12, v13, s[46:47]
	v_cmp_eq_u32_e64 s[46:47], 8, v46
	s_nop 1
	v_cndmask_b32_e64 v12, v12, v0, s[46:47]
	v_cmp_eq_u32_e64 s[46:47], 9, v46
	s_nop 1
	v_cndmask_b32_e64 v12, v12, v1, s[46:47]
	v_cmp_eq_u32_e64 s[46:47], 10, v46
	s_nop 1
	v_cndmask_b32_e64 v12, v12, v2, s[46:47]
	v_cmp_eq_u32_e64 s[46:47], 11, v46
	s_nop 1
	v_cndmask_b32_e64 v12, v12, v3, s[46:47]
	v_cmp_eq_u32_e64 s[46:47], 12, v46
	s_nop 1
	v_cndmask_b32_e64 v12, v12, v134, s[46:47]
	v_cmp_eq_u32_e64 s[46:47], 13, v46
	s_nop 1
	v_cndmask_b32_e64 v12, v12, v135, s[46:47]
	v_cmp_eq_u32_e64 s[46:47], 14, v46
	s_nop 1
	v_cndmask_b32_e64 v12, v12, v10, s[46:47]
	v_cmp_eq_u32_e64 s[46:47], 15, v46
	s_nop 1
	v_cndmask_b32_e64 v12, v12, v11, s[46:47]
	v_cmp_eq_u32_e64 s[46:47], 1, v48
	s_waitcnt lgkmcnt(0)
	v_add_f32_e32 v12, v12, v80
	v_cndmask_b32_e64 v80, v69, v71, s[46:47]
	v_cmp_eq_u32_e64 s[46:47], 2, v48
	s_nop 1
	v_cndmask_b32_e64 v80, v80, v73, s[46:47]
	v_cmp_eq_u32_e64 s[46:47], 3, v48
	s_nop 1
	v_cndmask_b32_e64 v80, v80, v75, s[46:47]
	v_cmp_eq_u32_e64 s[46:47], 4, v48
	s_nop 1
	v_cndmask_b32_e64 v80, v80, v14, s[46:47]
	v_cmp_eq_u32_e64 s[46:47], 5, v48
	s_nop 1
	v_cndmask_b32_e64 v80, v80, v15, s[46:47]
	v_cmp_eq_u32_e64 s[46:47], 6, v48
	s_nop 1
	v_cndmask_b32_e64 v80, v80, v12, s[46:47]
	v_cmp_eq_u32_e64 s[46:47], 7, v48
	s_nop 1
	v_cndmask_b32_e64 v80, v80, v13, s[46:47]
	v_cmp_eq_u32_e64 s[46:47], 8, v48
	s_nop 1
	v_cndmask_b32_e64 v80, v80, v0, s[46:47]
	v_cmp_eq_u32_e64 s[46:47], 9, v48
	s_nop 1
	v_cndmask_b32_e64 v80, v80, v1, s[46:47]
	v_cmp_eq_u32_e64 s[46:47], 10, v48
	s_nop 1
	v_cndmask_b32_e64 v80, v80, v2, s[46:47]
	v_cmp_eq_u32_e64 s[46:47], 11, v48
	s_nop 1
	v_cndmask_b32_e64 v80, v80, v3, s[46:47]
	v_cmp_eq_u32_e64 s[46:47], 12, v48
	s_nop 1
	v_cndmask_b32_e64 v80, v80, v134, s[46:47]
	v_cmp_eq_u32_e64 s[46:47], 13, v48
	s_nop 1
	v_cndmask_b32_e64 v80, v80, v135, s[46:47]
	v_cmp_eq_u32_e64 s[46:47], 14, v48
	s_nop 1
	v_cndmask_b32_e64 v80, v80, v10, s[46:47]
	v_cmp_eq_u32_e64 s[46:47], 15, v48
	s_nop 1
	v_cndmask_b32_e64 v80, v80, v11, s[46:47]
	v_cmp_eq_u32_e64 s[46:47], 1, v50
	ds_bpermute_b32 v80, v39, v80
	s_nop 0
	v_cndmask_b32_e64 v81, v69, v71, s[46:47]
	v_cmp_eq_u32_e64 s[46:47], 2, v50
	s_nop 1
	v_cndmask_b32_e64 v81, v81, v73, s[46:47]
	v_cmp_eq_u32_e64 s[46:47], 3, v50
	s_nop 1
	v_cndmask_b32_e64 v81, v81, v75, s[46:47]
	v_cmp_eq_u32_e64 s[46:47], 4, v50
	s_nop 1
	v_cndmask_b32_e64 v81, v81, v14, s[46:47]
	v_cmp_eq_u32_e64 s[46:47], 5, v50
	s_nop 1
	v_cndmask_b32_e64 v81, v81, v15, s[46:47]
	v_cmp_eq_u32_e64 s[46:47], 6, v50
	s_nop 1
	v_cndmask_b32_e64 v81, v81, v12, s[46:47]
	v_cmp_eq_u32_e64 s[46:47], 7, v50
	s_nop 1
	v_cndmask_b32_e64 v13, v81, v13, s[46:47]
	v_cmp_eq_u32_e64 s[46:47], 8, v50
	s_nop 1
	v_cndmask_b32_e64 v13, v13, v0, s[46:47]
	v_cmp_eq_u32_e64 s[46:47], 9, v50
	s_nop 1
	v_cndmask_b32_e64 v13, v13, v1, s[46:47]
	v_cmp_eq_u32_e64 s[46:47], 10, v50
	s_nop 1
	v_cndmask_b32_e64 v13, v13, v2, s[46:47]
	v_cmp_eq_u32_e64 s[46:47], 11, v50
	s_nop 1
	v_cndmask_b32_e64 v13, v13, v3, s[46:47]
	v_cmp_eq_u32_e64 s[46:47], 12, v50
	s_nop 1
	v_cndmask_b32_e64 v13, v13, v134, s[46:47]
	v_cmp_eq_u32_e64 s[46:47], 13, v50
	s_nop 1
	v_cndmask_b32_e64 v13, v13, v135, s[46:47]
	v_cmp_eq_u32_e64 s[46:47], 14, v50
	s_nop 1
	v_cndmask_b32_e64 v13, v13, v10, s[46:47]
	v_cmp_eq_u32_e64 s[46:47], 15, v50
	s_nop 1
	v_cndmask_b32_e64 v13, v13, v11, s[46:47]
	v_cmp_eq_u32_e64 s[46:47], 1, v52
	s_waitcnt lgkmcnt(0)
	v_add_f32_e32 v13, v13, v80
	v_cndmask_b32_e64 v80, v69, v71, s[46:47]
	v_cmp_eq_u32_e64 s[46:47], 2, v52
	s_nop 1
	v_cndmask_b32_e64 v80, v80, v73, s[46:47]
	v_cmp_eq_u32_e64 s[46:47], 3, v52
	s_nop 1
	v_cndmask_b32_e64 v80, v80, v75, s[46:47]
	v_cmp_eq_u32_e64 s[46:47], 4, v52
	s_nop 1
	v_cndmask_b32_e64 v80, v80, v14, s[46:47]
	v_cmp_eq_u32_e64 s[46:47], 5, v52
	s_nop 1
	v_cndmask_b32_e64 v80, v80, v15, s[46:47]
	v_cmp_eq_u32_e64 s[46:47], 6, v52
	s_nop 1
	v_cndmask_b32_e64 v80, v80, v12, s[46:47]
	v_cmp_eq_u32_e64 s[46:47], 7, v52
	s_nop 1
	v_cndmask_b32_e64 v80, v80, v13, s[46:47]
	v_cmp_eq_u32_e64 s[46:47], 8, v52
	s_nop 1
	v_cndmask_b32_e64 v80, v80, v0, s[46:47]
	v_cmp_eq_u32_e64 s[46:47], 9, v52
	s_nop 1
	v_cndmask_b32_e64 v80, v80, v1, s[46:47]
	v_cmp_eq_u32_e64 s[46:47], 10, v52
	s_nop 1
	v_cndmask_b32_e64 v80, v80, v2, s[46:47]
	v_cmp_eq_u32_e64 s[46:47], 11, v52
	s_nop 1
	v_cndmask_b32_e64 v80, v80, v3, s[46:47]
	v_cmp_eq_u32_e64 s[46:47], 12, v52
	s_nop 1
	v_cndmask_b32_e64 v80, v80, v134, s[46:47]
	v_cmp_eq_u32_e64 s[46:47], 13, v52
	s_nop 1
	v_cndmask_b32_e64 v80, v80, v135, s[46:47]
	v_cmp_eq_u32_e64 s[46:47], 14, v52
	s_nop 1
	v_cndmask_b32_e64 v80, v80, v10, s[46:47]
	v_cmp_eq_u32_e64 s[46:47], 15, v52
	s_nop 1
	v_cndmask_b32_e64 v80, v80, v11, s[46:47]
	v_cmp_eq_u32_e64 s[46:47], 1, v54
	ds_bpermute_b32 v80, v37, v80
	s_nop 0
	v_cndmask_b32_e64 v69, v69, v71, s[46:47]
	v_cmp_eq_u32_e64 s[46:47], 2, v54
	s_nop 1
	v_cndmask_b32_e64 v69, v69, v73, s[46:47]
	v_cmp_eq_u32_e64 s[46:47], 3, v54
	s_nop 1
	v_cndmask_b32_e64 v69, v69, v75, s[46:47]
	v_cmp_eq_u32_e64 s[46:47], 4, v54
	s_nop 1
	v_cndmask_b32_e64 v69, v69, v14, s[46:47]
	v_cmp_eq_u32_e64 s[46:47], 5, v54
	s_nop 1
	v_cndmask_b32_e64 v69, v69, v15, s[46:47]
	v_cmp_eq_u32_e64 s[46:47], 6, v54
	s_nop 1
	v_cndmask_b32_e64 v69, v69, v12, s[46:47]
	v_cmp_eq_u32_e64 s[46:47], 7, v54
	s_nop 1
	v_cndmask_b32_e64 v69, v69, v13, s[46:47]
	v_cmp_eq_u32_e64 s[46:47], 8, v54
	s_nop 1
	v_cndmask_b32_e64 v69, v69, v0, s[46:47]
	v_cmp_eq_u32_e64 s[46:47], 9, v54
	s_nop 1
	v_cndmask_b32_e64 v69, v69, v1, s[46:47]
	v_cmp_eq_u32_e64 s[46:47], 10, v54
	s_nop 1
	v_cndmask_b32_e64 v69, v69, v2, s[46:47]
	v_cmp_eq_u32_e64 s[46:47], 11, v54
	s_nop 1
	v_cndmask_b32_e64 v69, v69, v3, s[46:47]
	v_cmp_eq_u32_e64 s[46:47], 12, v54
	s_nop 1
	v_cndmask_b32_e64 v69, v69, v134, s[46:47]
	v_cmp_eq_u32_e64 s[46:47], 13, v54
	s_nop 1
	v_cndmask_b32_e64 v69, v69, v135, s[46:47]
	v_cmp_eq_u32_e64 s[46:47], 14, v54
	s_nop 1
	v_cndmask_b32_e64 v69, v69, v10, s[46:47]
	v_cmp_eq_u32_e64 s[46:47], 15, v54
	s_nop 1
	v_cndmask_b32_e64 v69, v69, v11, s[46:47]
	s_waitcnt lgkmcnt(0)
	v_add_f32_e32 v69, v69, v80
	v_cmp_eq_u32_e64 s[46:47], 1, v56
	s_nop 1
	v_cndmask_b32_e64 v80, v69, v71, s[46:47]
	v_cmp_eq_u32_e64 s[46:47], 2, v56
	s_nop 1
	v_cndmask_b32_e64 v80, v80, v73, s[46:47]
	v_cmp_eq_u32_e64 s[46:47], 3, v56
	s_nop 1
	v_cndmask_b32_e64 v80, v80, v75, s[46:47]
	v_cmp_eq_u32_e64 s[46:47], 4, v56
	s_nop 1
	v_cndmask_b32_e64 v80, v80, v14, s[46:47]
	v_cmp_eq_u32_e64 s[46:47], 5, v56
	s_nop 1
	v_cndmask_b32_e64 v80, v80, v15, s[46:47]
	v_cmp_eq_u32_e64 s[46:47], 6, v56
	s_nop 1
	v_cndmask_b32_e64 v80, v80, v12, s[46:47]
	v_cmp_eq_u32_e64 s[46:47], 7, v56
	s_nop 1
	v_cndmask_b32_e64 v80, v80, v13, s[46:47]
	v_cmp_eq_u32_e64 s[46:47], 8, v56
	s_nop 1
	v_cndmask_b32_e64 v80, v80, v0, s[46:47]
	v_cmp_eq_u32_e64 s[46:47], 9, v56
	s_nop 1
	v_cndmask_b32_e64 v80, v80, v1, s[46:47]
	v_cmp_eq_u32_e64 s[46:47], 10, v56
	s_nop 1
	v_cndmask_b32_e64 v80, v80, v2, s[46:47]
	v_cmp_eq_u32_e64 s[46:47], 11, v56
	s_nop 1
	v_cndmask_b32_e64 v80, v80, v3, s[46:47]
	v_cmp_eq_u32_e64 s[46:47], 12, v56
	s_nop 1
	v_cndmask_b32_e64 v80, v80, v134, s[46:47]
	v_cmp_eq_u32_e64 s[46:47], 13, v56
	s_nop 1
	v_cndmask_b32_e64 v80, v80, v135, s[46:47]
	v_cmp_eq_u32_e64 s[46:47], 14, v56
	s_nop 1
	v_cndmask_b32_e64 v80, v80, v10, s[46:47]
	v_cmp_eq_u32_e64 s[46:47], 15, v56
	s_nop 1
	v_cndmask_b32_e64 v80, v80, v11, s[46:47]
	v_cmp_eq_u32_e64 s[46:47], 1, v58
	ds_bpermute_b32 v80, v37, v80
	s_nop 0
	v_cndmask_b32_e64 v71, v69, v71, s[46:47]
	v_cmp_eq_u32_e64 s[46:47], 2, v58
	s_nop 1
	v_cndmask_b32_e64 v71, v71, v73, s[46:47]
	v_cmp_eq_u32_e64 s[46:47], 3, v58
	s_nop 1
	v_cndmask_b32_e64 v71, v71, v75, s[46:47]
	v_cmp_eq_u32_e64 s[46:47], 4, v58
	s_nop 1
	v_cndmask_b32_e64 v71, v71, v14, s[46:47]
	v_cmp_eq_u32_e64 s[46:47], 5, v58
	s_nop 1
	v_cndmask_b32_e64 v71, v71, v15, s[46:47]
	v_cmp_eq_u32_e64 s[46:47], 6, v58
	s_nop 1
	v_cndmask_b32_e64 v71, v71, v12, s[46:47]
	v_cmp_eq_u32_e64 s[46:47], 7, v58
	s_nop 1
	v_cndmask_b32_e64 v71, v71, v13, s[46:47]
	v_cmp_eq_u32_e64 s[46:47], 8, v58
	s_nop 1
	v_cndmask_b32_e64 v71, v71, v0, s[46:47]
	v_cmp_eq_u32_e64 s[46:47], 9, v58
	s_nop 1
	v_cndmask_b32_e64 v71, v71, v1, s[46:47]
	v_cmp_eq_u32_e64 s[46:47], 10, v58
	s_nop 1
	v_cndmask_b32_e64 v71, v71, v2, s[46:47]
	v_cmp_eq_u32_e64 s[46:47], 11, v58
	s_nop 1
	v_cndmask_b32_e64 v71, v71, v3, s[46:47]
	v_cmp_eq_u32_e64 s[46:47], 12, v58
	s_nop 1
	v_cndmask_b32_e64 v71, v71, v134, s[46:47]
	v_cmp_eq_u32_e64 s[46:47], 13, v58
	s_nop 1
	v_cndmask_b32_e64 v71, v71, v135, s[46:47]
	v_cmp_eq_u32_e64 s[46:47], 14, v58
	s_nop 1
	v_cndmask_b32_e64 v71, v71, v10, s[46:47]
	v_cmp_eq_u32_e64 s[46:47], 15, v58
	s_nop 1
	v_cndmask_b32_e64 v71, v71, v11, s[46:47]
	s_waitcnt lgkmcnt(0)
	v_add_f32_e32 v71, v71, v80
	v_cmp_eq_u32_e64 s[46:47], 1, v60
	s_nop 1
	v_cndmask_b32_e64 v80, v69, v71, s[46:47]
	v_cmp_eq_u32_e64 s[46:47], 2, v60
	s_nop 1
	v_cndmask_b32_e64 v80, v80, v73, s[46:47]
	v_cmp_eq_u32_e64 s[46:47], 3, v60
	s_nop 1
	v_cndmask_b32_e64 v80, v80, v75, s[46:47]
	v_cmp_eq_u32_e64 s[46:47], 4, v60
	s_nop 1
	v_cndmask_b32_e64 v80, v80, v14, s[46:47]
	v_cmp_eq_u32_e64 s[46:47], 5, v60
	s_nop 1
	v_cndmask_b32_e64 v80, v80, v15, s[46:47]
	v_cmp_eq_u32_e64 s[46:47], 6, v60
	s_nop 1
	v_cndmask_b32_e64 v80, v80, v12, s[46:47]
	v_cmp_eq_u32_e64 s[46:47], 7, v60
	s_nop 1
	v_cndmask_b32_e64 v80, v80, v13, s[46:47]
	v_cmp_eq_u32_e64 s[46:47], 8, v60
	s_nop 1
	v_cndmask_b32_e64 v80, v80, v0, s[46:47]
	v_cmp_eq_u32_e64 s[46:47], 9, v60
	s_nop 1
	v_cndmask_b32_e64 v80, v80, v1, s[46:47]
	v_cmp_eq_u32_e64 s[46:47], 10, v60
	s_nop 1
	v_cndmask_b32_e64 v80, v80, v2, s[46:47]
	v_cmp_eq_u32_e64 s[46:47], 11, v60
	s_nop 1
	v_cndmask_b32_e64 v80, v80, v3, s[46:47]
	v_cmp_eq_u32_e64 s[46:47], 12, v60
	s_nop 1
	v_cndmask_b32_e64 v80, v80, v134, s[46:47]
	v_cmp_eq_u32_e64 s[46:47], 13, v60
	s_nop 1
	v_cndmask_b32_e64 v80, v80, v135, s[46:47]
	v_cmp_eq_u32_e64 s[46:47], 14, v60
	s_nop 1
	v_cndmask_b32_e64 v80, v80, v10, s[46:47]
	v_cmp_eq_u32_e64 s[46:47], 15, v60
	s_nop 1
	v_cndmask_b32_e64 v80, v80, v11, s[46:47]
	v_cmp_eq_u32_e64 s[46:47], 1, v62
	ds_bpermute_b32 v80, v37, v80
	s_nop 0
	v_cndmask_b32_e64 v81, v69, v71, s[46:47]
	v_cmp_eq_u32_e64 s[46:47], 2, v62
	s_nop 1
	v_cndmask_b32_e64 v73, v81, v73, s[46:47]
	v_cmp_eq_u32_e64 s[46:47], 3, v62
	s_nop 1
	v_cndmask_b32_e64 v73, v73, v75, s[46:47]
	v_cmp_eq_u32_e64 s[46:47], 4, v62
	s_nop 1
	v_cndmask_b32_e64 v73, v73, v14, s[46:47]
	v_cmp_eq_u32_e64 s[46:47], 5, v62
	s_nop 1
	v_cndmask_b32_e64 v73, v73, v15, s[46:47]
	v_cmp_eq_u32_e64 s[46:47], 6, v62
	s_nop 1
	v_cndmask_b32_e64 v73, v73, v12, s[46:47]
	v_cmp_eq_u32_e64 s[46:47], 7, v62
	s_nop 1
	v_cndmask_b32_e64 v73, v73, v13, s[46:47]
	v_cmp_eq_u32_e64 s[46:47], 8, v62
	s_nop 1
	v_cndmask_b32_e64 v73, v73, v0, s[46:47]
	v_cmp_eq_u32_e64 s[46:47], 9, v62
	s_nop 1
	v_cndmask_b32_e64 v73, v73, v1, s[46:47]
	v_cmp_eq_u32_e64 s[46:47], 10, v62
	s_nop 1
	v_cndmask_b32_e64 v73, v73, v2, s[46:47]
	v_cmp_eq_u32_e64 s[46:47], 11, v62
	s_nop 1
	v_cndmask_b32_e64 v73, v73, v3, s[46:47]
	v_cmp_eq_u32_e64 s[46:47], 12, v62
	s_nop 1
	v_cndmask_b32_e64 v73, v73, v134, s[46:47]
	v_cmp_eq_u32_e64 s[46:47], 13, v62
	s_nop 1
	v_cndmask_b32_e64 v73, v73, v135, s[46:47]
	v_cmp_eq_u32_e64 s[46:47], 14, v62
	s_nop 1
	v_cndmask_b32_e64 v73, v73, v10, s[46:47]
	v_cmp_eq_u32_e64 s[46:47], 15, v62
	s_nop 1
	v_cndmask_b32_e64 v73, v73, v11, s[46:47]
	v_cmp_eq_u32_e64 s[46:47], 1, v64
	s_waitcnt lgkmcnt(0)
	v_add_f32_e32 v73, v73, v80
	v_cndmask_b32_e64 v80, v69, v71, s[46:47]
	v_cmp_eq_u32_e64 s[46:47], 2, v64
	s_nop 1
	v_cndmask_b32_e64 v80, v80, v73, s[46:47]
	v_cmp_eq_u32_e64 s[46:47], 3, v64
	s_nop 1
	v_cndmask_b32_e64 v80, v80, v75, s[46:47]
	v_cmp_eq_u32_e64 s[46:47], 4, v64
	s_nop 1
	v_cndmask_b32_e64 v80, v80, v14, s[46:47]
	v_cmp_eq_u32_e64 s[46:47], 5, v64
	s_nop 1
	v_cndmask_b32_e64 v80, v80, v15, s[46:47]
	v_cmp_eq_u32_e64 s[46:47], 6, v64
	s_nop 1
	v_cndmask_b32_e64 v80, v80, v12, s[46:47]
	v_cmp_eq_u32_e64 s[46:47], 7, v64
	s_nop 1
	v_cndmask_b32_e64 v80, v80, v13, s[46:47]
	v_cmp_eq_u32_e64 s[46:47], 8, v64
	s_nop 1
	v_cndmask_b32_e64 v80, v80, v0, s[46:47]
	v_cmp_eq_u32_e64 s[46:47], 9, v64
	s_nop 1
	v_cndmask_b32_e64 v80, v80, v1, s[46:47]
	v_cmp_eq_u32_e64 s[46:47], 10, v64
	s_nop 1
	v_cndmask_b32_e64 v80, v80, v2, s[46:47]
	v_cmp_eq_u32_e64 s[46:47], 11, v64
	s_nop 1
	v_cndmask_b32_e64 v80, v80, v3, s[46:47]
	v_cmp_eq_u32_e64 s[46:47], 12, v64
	s_nop 1
	v_cndmask_b32_e64 v80, v80, v134, s[46:47]
	v_cmp_eq_u32_e64 s[46:47], 13, v64
	s_nop 1
	v_cndmask_b32_e64 v80, v80, v135, s[46:47]
	v_cmp_eq_u32_e64 s[46:47], 14, v64
	s_nop 1
	v_cndmask_b32_e64 v80, v80, v10, s[46:47]
	v_cmp_eq_u32_e64 s[46:47], 15, v64
	s_nop 1
	v_cndmask_b32_e64 v80, v80, v11, s[46:47]
	v_cmp_eq_u32_e64 s[46:47], 1, v66
	ds_bpermute_b32 v80, v37, v80
	s_nop 0
	v_cndmask_b32_e64 v81, v69, v71, s[46:47]
	v_cmp_eq_u32_e64 s[46:47], 2, v66
	s_nop 1
	v_cndmask_b32_e64 v81, v81, v73, s[46:47]
	v_cmp_eq_u32_e64 s[46:47], 3, v66
	s_nop 1
	v_cndmask_b32_e64 v75, v81, v75, s[46:47]
	v_cmp_eq_u32_e64 s[46:47], 4, v66
	s_nop 1
	v_cndmask_b32_e64 v75, v75, v14, s[46:47]
	v_cmp_eq_u32_e64 s[46:47], 5, v66
	s_nop 1
	v_cndmask_b32_e64 v75, v75, v15, s[46:47]
	v_cmp_eq_u32_e64 s[46:47], 6, v66
	s_nop 1
	v_cndmask_b32_e64 v75, v75, v12, s[46:47]
	v_cmp_eq_u32_e64 s[46:47], 7, v66
	s_nop 1
	v_cndmask_b32_e64 v75, v75, v13, s[46:47]
	v_cmp_eq_u32_e64 s[46:47], 8, v66
	s_nop 1
	v_cndmask_b32_e64 v75, v75, v0, s[46:47]
	v_cmp_eq_u32_e64 s[46:47], 9, v66
	s_nop 1
	v_cndmask_b32_e64 v75, v75, v1, s[46:47]
	v_cmp_eq_u32_e64 s[46:47], 10, v66
	s_nop 1
	v_cndmask_b32_e64 v75, v75, v2, s[46:47]
	v_cmp_eq_u32_e64 s[46:47], 11, v66
	s_nop 1
	v_cndmask_b32_e64 v75, v75, v3, s[46:47]
	v_cmp_eq_u32_e64 s[46:47], 12, v66
	s_nop 1
	v_cndmask_b32_e64 v75, v75, v134, s[46:47]
	v_cmp_eq_u32_e64 s[46:47], 13, v66
	s_nop 1
	v_cndmask_b32_e64 v75, v75, v135, s[46:47]
	v_cmp_eq_u32_e64 s[46:47], 14, v66
	s_nop 1
	v_cndmask_b32_e64 v75, v75, v10, s[46:47]
	v_cmp_eq_u32_e64 s[46:47], 15, v66
	s_nop 1
	v_cndmask_b32_e64 v75, v75, v11, s[46:47]
	v_cmp_eq_u32_e64 s[46:47], 1, v68
	s_waitcnt lgkmcnt(0)
	v_add_f32_e32 v75, v75, v80
	v_cndmask_b32_e64 v80, v69, v71, s[46:47]
	v_cmp_eq_u32_e64 s[46:47], 2, v68
	s_nop 1
	v_cndmask_b32_e64 v80, v80, v73, s[46:47]
	v_cmp_eq_u32_e64 s[46:47], 3, v68
	s_nop 1
	v_cndmask_b32_e64 v80, v80, v75, s[46:47]
	v_cmp_eq_u32_e64 s[46:47], 4, v68
	s_nop 1
	v_cndmask_b32_e64 v80, v80, v14, s[46:47]
	v_cmp_eq_u32_e64 s[46:47], 5, v68
	s_nop 1
	v_cndmask_b32_e64 v80, v80, v15, s[46:47]
	v_cmp_eq_u32_e64 s[46:47], 6, v68
	s_nop 1
	v_cndmask_b32_e64 v80, v80, v12, s[46:47]
	v_cmp_eq_u32_e64 s[46:47], 7, v68
	s_nop 1
	v_cndmask_b32_e64 v80, v80, v13, s[46:47]
	v_cmp_eq_u32_e64 s[46:47], 8, v68
	s_nop 1
	v_cndmask_b32_e64 v80, v80, v0, s[46:47]
	v_cmp_eq_u32_e64 s[46:47], 9, v68
	s_nop 1
	v_cndmask_b32_e64 v80, v80, v1, s[46:47]
	v_cmp_eq_u32_e64 s[46:47], 10, v68
	s_nop 1
	v_cndmask_b32_e64 v80, v80, v2, s[46:47]
	v_cmp_eq_u32_e64 s[46:47], 11, v68
	s_nop 1
	v_cndmask_b32_e64 v80, v80, v3, s[46:47]
	v_cmp_eq_u32_e64 s[46:47], 12, v68
	s_nop 1
	v_cndmask_b32_e64 v80, v80, v134, s[46:47]
	v_cmp_eq_u32_e64 s[46:47], 13, v68
	s_nop 1
	v_cndmask_b32_e64 v80, v80, v135, s[46:47]
	v_cmp_eq_u32_e64 s[46:47], 14, v68
	s_nop 1
	v_cndmask_b32_e64 v80, v80, v10, s[46:47]
	v_cmp_eq_u32_e64 s[46:47], 15, v68
	s_nop 1
	v_cndmask_b32_e64 v80, v80, v11, s[46:47]
	v_cmp_eq_u32_e64 s[46:47], 1, v70
	ds_bpermute_b32 v80, v41, v80
	s_nop 0
	v_cndmask_b32_e64 v69, v69, v71, s[46:47]
	v_cmp_eq_u32_e64 s[46:47], 2, v70
	s_nop 1
	v_cndmask_b32_e64 v69, v69, v73, s[46:47]
	v_cmp_eq_u32_e64 s[46:47], 3, v70
	s_nop 1
	v_cndmask_b32_e64 v69, v69, v75, s[46:47]
	v_cmp_eq_u32_e64 s[46:47], 4, v70
	s_nop 1
	v_cndmask_b32_e64 v69, v69, v14, s[46:47]
	v_cmp_eq_u32_e64 s[46:47], 5, v70
	s_nop 1
	v_cndmask_b32_e64 v69, v69, v15, s[46:47]
	v_cmp_eq_u32_e64 s[46:47], 6, v70
	s_nop 1
	v_cndmask_b32_e64 v69, v69, v12, s[46:47]
	v_cmp_eq_u32_e64 s[46:47], 7, v70
	s_nop 1
	v_cndmask_b32_e64 v69, v69, v13, s[46:47]
	v_cmp_eq_u32_e64 s[46:47], 8, v70
	s_nop 1
	v_cndmask_b32_e64 v69, v69, v0, s[46:47]
	v_cmp_eq_u32_e64 s[46:47], 9, v70
	s_nop 1
	v_cndmask_b32_e64 v69, v69, v1, s[46:47]
	v_cmp_eq_u32_e64 s[46:47], 10, v70
	s_nop 1
	v_cndmask_b32_e64 v69, v69, v2, s[46:47]
	v_cmp_eq_u32_e64 s[46:47], 11, v70
	s_nop 1
	v_cndmask_b32_e64 v69, v69, v3, s[46:47]
	v_cmp_eq_u32_e64 s[46:47], 12, v70
	s_nop 1
	v_cndmask_b32_e64 v69, v69, v134, s[46:47]
	v_cmp_eq_u32_e64 s[46:47], 13, v70
	s_nop 1
	v_cndmask_b32_e64 v69, v69, v135, s[46:47]
	v_cmp_eq_u32_e64 s[46:47], 14, v70
	s_nop 1
	v_cndmask_b32_e64 v69, v69, v10, s[46:47]
	v_cmp_eq_u32_e64 s[46:47], 15, v70
	s_nop 1
	v_cndmask_b32_e64 v69, v69, v11, s[46:47]
	s_waitcnt lgkmcnt(0)
	v_add_f32_e32 v69, v69, v80
	v_cmp_eq_u32_e64 s[46:47], 1, v72
	s_nop 1
	v_cndmask_b32_e64 v80, v69, v71, s[46:47]
	v_cmp_eq_u32_e64 s[46:47], 2, v72
	s_nop 1
	v_cndmask_b32_e64 v80, v80, v73, s[46:47]
	v_cmp_eq_u32_e64 s[46:47], 3, v72
	s_nop 1
	v_cndmask_b32_e64 v80, v80, v75, s[46:47]
	v_cmp_eq_u32_e64 s[46:47], 4, v72
	s_nop 1
	v_cndmask_b32_e64 v80, v80, v14, s[46:47]
	v_cmp_eq_u32_e64 s[46:47], 5, v72
	s_nop 1
	v_cndmask_b32_e64 v80, v80, v15, s[46:47]
	v_cmp_eq_u32_e64 s[46:47], 6, v72
	s_nop 1
	v_cndmask_b32_e64 v80, v80, v12, s[46:47]
	v_cmp_eq_u32_e64 s[46:47], 7, v72
	s_nop 1
	v_cndmask_b32_e64 v80, v80, v13, s[46:47]
	v_cmp_eq_u32_e64 s[46:47], 8, v72
	s_nop 1
	v_cndmask_b32_e64 v80, v80, v0, s[46:47]
	v_cmp_eq_u32_e64 s[46:47], 9, v72
	s_nop 1
	v_cndmask_b32_e64 v80, v80, v1, s[46:47]
	v_cmp_eq_u32_e64 s[46:47], 10, v72
	s_nop 1
	v_cndmask_b32_e64 v80, v80, v2, s[46:47]
	v_cmp_eq_u32_e64 s[46:47], 11, v72
	s_nop 1
	v_cndmask_b32_e64 v80, v80, v3, s[46:47]
	v_cmp_eq_u32_e64 s[46:47], 12, v72
	s_nop 1
	v_cndmask_b32_e64 v80, v80, v134, s[46:47]
	v_cmp_eq_u32_e64 s[46:47], 13, v72
	s_nop 1
	v_cndmask_b32_e64 v80, v80, v135, s[46:47]
	v_cmp_eq_u32_e64 s[46:47], 14, v72
	s_nop 1
	v_cndmask_b32_e64 v80, v80, v10, s[46:47]
	v_cmp_eq_u32_e64 s[46:47], 15, v72
	s_nop 1
	v_cndmask_b32_e64 v80, v80, v11, s[46:47]
	v_cmp_eq_u32_e64 s[46:47], 1, v74
	ds_bpermute_b32 v41, v41, v80
	s_nop 0
	v_cndmask_b32_e64 v71, v69, v71, s[46:47]
	v_cmp_eq_u32_e64 s[46:47], 2, v74
	s_nop 1
	v_cndmask_b32_e64 v71, v71, v73, s[46:47]
	v_cmp_eq_u32_e64 s[46:47], 3, v74
	s_nop 1
	v_cndmask_b32_e64 v71, v71, v75, s[46:47]
	v_cmp_eq_u32_e64 s[46:47], 4, v74
	s_nop 1
	v_cndmask_b32_e64 v71, v71, v14, s[46:47]
	v_cmp_eq_u32_e64 s[46:47], 5, v74
	s_nop 1
	v_cndmask_b32_e64 v71, v71, v15, s[46:47]
	v_cmp_eq_u32_e64 s[46:47], 6, v74
	s_nop 1
	v_cndmask_b32_e64 v71, v71, v12, s[46:47]
	v_cmp_eq_u32_e64 s[46:47], 7, v74
	s_nop 1
	v_cndmask_b32_e64 v71, v71, v13, s[46:47]
	v_cmp_eq_u32_e64 s[46:47], 8, v74
	s_nop 1
	v_cndmask_b32_e64 v71, v71, v0, s[46:47]
	v_cmp_eq_u32_e64 s[46:47], 9, v74
	s_nop 1
	v_cndmask_b32_e64 v71, v71, v1, s[46:47]
	v_cmp_eq_u32_e64 s[46:47], 10, v74
	s_nop 1
	v_cndmask_b32_e64 v71, v71, v2, s[46:47]
	v_cmp_eq_u32_e64 s[46:47], 11, v74
	s_nop 1
	v_cndmask_b32_e64 v71, v71, v3, s[46:47]
	v_cmp_eq_u32_e64 s[46:47], 12, v74
	s_nop 1
	v_cndmask_b32_e64 v71, v71, v134, s[46:47]
	v_cmp_eq_u32_e64 s[46:47], 13, v74
	s_nop 1
	v_cndmask_b32_e64 v71, v71, v135, s[46:47]
	v_cmp_eq_u32_e64 s[46:47], 14, v74
	s_nop 1
	v_cndmask_b32_e64 v71, v71, v10, s[46:47]
	v_cmp_eq_u32_e64 s[46:47], 15, v74
	s_nop 1
	v_cndmask_b32_e64 v71, v71, v11, s[46:47]
	s_waitcnt lgkmcnt(0)
	v_add_f32_e32 v41, v71, v41
	v_cmp_ne_u64_e64 s[46:47], 0, v[76:77]
	s_nop 1
	v_cndmask_b32_e64 v71, v69, v41, s[46:47]
	v_cmp_eq_u32_e64 s[46:47], 2, v76
	s_nop 1
	v_cndmask_b32_e64 v71, v71, v73, s[46:47]
	v_cmp_eq_u32_e64 s[46:47], 3, v76
	s_nop 1
	v_cndmask_b32_e64 v71, v71, v75, s[46:47]
	v_cmp_eq_u32_e64 s[46:47], 4, v76
	s_nop 1
	v_cndmask_b32_e64 v71, v71, v14, s[46:47]
	v_cmp_eq_u32_e64 s[46:47], 5, v76
	s_nop 1
	v_cndmask_b32_e64 v71, v71, v15, s[46:47]
	v_cmp_eq_u32_e64 s[46:47], 6, v76
	s_nop 1
	v_cndmask_b32_e64 v71, v71, v12, s[46:47]
	v_cmp_eq_u32_e64 s[46:47], 7, v76
	s_nop 1
	v_cndmask_b32_e64 v71, v71, v13, s[46:47]
	v_cmp_eq_u32_e64 s[46:47], 8, v76
	s_nop 1
	v_cndmask_b32_e64 v71, v71, v0, s[46:47]
	v_cmp_eq_u32_e64 s[46:47], 9, v76
	s_nop 1
	v_cndmask_b32_e64 v71, v71, v1, s[46:47]
	v_cmp_eq_u32_e64 s[46:47], 10, v76
	s_nop 1
	v_cndmask_b32_e64 v71, v71, v2, s[46:47]
	v_cmp_eq_u32_e64 s[46:47], 11, v76
	s_nop 1
	v_cndmask_b32_e64 v71, v71, v3, s[46:47]
	v_cmp_eq_u32_e64 s[46:47], 12, v76
	s_nop 1
	v_cndmask_b32_e64 v71, v71, v134, s[46:47]
	v_cmp_eq_u32_e64 s[46:47], 13, v76
	s_nop 1
	v_cndmask_b32_e64 v71, v71, v135, s[46:47]
	v_cmp_ne_u64_e64 s[46:47], 0, v[78:79]
	s_nop 1
	v_cndmask_b32_e64 v41, v69, v41, s[46:47]
	v_cmp_eq_u32_e64 s[46:47], 2, v78
	s_nop 1
	v_cndmask_b32_e64 v41, v41, v73, s[46:47]
	v_cmp_eq_u32_e64 s[46:47], 3, v78
	s_nop 1
	v_cndmask_b32_e64 v41, v41, v75, s[46:47]
	v_cmp_eq_u32_e64 s[46:47], 4, v78
	s_nop 1
	v_cndmask_b32_e64 v14, v41, v14, s[46:47]
	v_cmp_eq_u32_e64 s[46:47], 5, v78
	s_nop 1
	v_cndmask_b32_e64 v14, v14, v15, s[46:47]
	v_cmp_eq_u32_e64 s[46:47], 6, v78
	s_nop 1
	v_cndmask_b32_e64 v12, v14, v12, s[46:47]
	v_cmp_eq_u32_e64 s[46:47], 7, v78
	s_nop 1
	v_cndmask_b32_e64 v12, v12, v13, s[46:47]
	v_cmp_eq_u32_e64 s[46:47], 8, v78
	s_nop 1
	v_cndmask_b32_e64 v0, v12, v0, s[46:47]
	v_cmp_eq_u32_e64 s[46:47], 9, v78
	s_nop 1
	v_cndmask_b32_e64 v0, v0, v1, s[46:47]
	v_cmp_eq_u32_e64 s[46:47], 10, v78
	s_nop 1
	v_cndmask_b32_e64 v0, v0, v2, s[46:47]
	v_cmp_eq_u32_e64 s[46:47], 11, v78
	v_fma_f32 v2, -v57, v59, v61
	s_nop 0
	v_cndmask_b32_e64 v0, v0, v3, s[46:47]
	v_cmp_eq_u32_e64 s[46:47], 12, v78
	v_add_f32_e32 v3, v63, v67
	s_nop 0
	v_cndmask_b32_e64 v0, v0, v134, s[46:47]
	v_cmp_eq_u32_e64 s[46:47], 13, v78
	s_nop 1
	v_cndmask_b32_e64 v0, v0, v135, s[46:47]
	v_cmp_eq_u32_e64 s[46:47], 14, v78
	s_nop 1
	v_cndmask_b32_e64 v0, v0, v10, s[46:47]
	v_cmp_eq_u32_e64 s[46:47], 15, v78
	s_nop 1
	v_cndmask_b32_e64 v0, v0, v11, s[46:47]
	ds_bpermute_b32 v0, v35, v0
	v_cmp_eq_u32_e64 s[46:47], 14, v76
	s_nop 1
	v_cndmask_b32_e64 v1, v71, v10, s[46:47]
	v_cmp_eq_u32_e64 s[46:47], 15, v76
	ds_bpermute_b32 v10, v37, v3
	s_nop 0
	v_cndmask_b32_e64 v1, v1, v11, s[46:47]
	s_waitcnt lgkmcnt(1)
	v_add_f32_e32 v0, v1, v0
	ds_bpermute_b32 v1, v33, v0
	s_waitcnt lgkmcnt(0)
	v_add_f32_e32 v1, v0, v1
	ds_bpermute_b32 v11, v31, v1
	v_div_fmas_f32 v0, v2, v55, v59
	v_div_fixup_f32 v12, v0, v53, 1.0
	v_add_f32_e32 v0, v3, v10
	ds_bpermute_b32 v2, v39, v0
	s_waitcnt lgkmcnt(1)
	v_add_f32_e32 v3, v1, v11
	s_nop 0
	v_readlane_b32 s1, v3, 0
	v_readlane_b32 s0, v3, 4
	v_readlane_b32 s8, v3, 32
	v_readlane_b32 s9, v3, 36
	v_pk_mul_f32 v[14:15], v[12:13], s[0:1] op_sel_hi:[0,1]
	v_readlane_b32 s0, v3, 8
	v_cmp_gt_f32_e32 vcc, v14, v15
	v_readlane_b32 s10, v3, 40
	v_mul_f32_e32 v11, s0, v12
	v_readlane_b32 s0, v3, 12
	v_readlane_b32 s11, v3, 44
	v_readlane_b32 s12, v3, 48
	v_mul_f32_e32 v13, s0, v12
	v_readlane_b32 s0, v3, 16
	v_readlane_b32 s13, v3, 52
	v_readlane_b32 s14, v3, 56
	v_mul_f32_e32 v31, s0, v12
	v_readlane_b32 s0, v3, 20
	v_readlane_b32 s15, v3, 60
	v_cndmask_b32_e64 v10, 0, 1, vcc
	v_mul_f32_e32 v33, s0, v12
	v_readlane_b32 s0, v3, 24
	v_cmp_lt_f32_e64 s[52:53], s33, v15
	s_nop 0
	v_mul_f32_e32 v35, s0, v12
	v_readlane_b32 s0, v3, 28
	v_cndmask_b32_e32 v3, v15, v14, vcc
	v_cmp_gt_f32_e32 vcc, v11, v3
	v_mul_f32_e32 v1, s0, v12
	s_nop 0
	v_cndmask_b32_e32 v3, v3, v11, vcc
	v_cndmask_b32_e64 v10, v10, 2, vcc
	v_cmp_gt_f32_e32 vcc, v13, v3
	s_nop 1
	v_cndmask_b32_e32 v3, v3, v13, vcc
	v_cndmask_b32_e64 v10, v10, 3, vcc
	v_cmp_gt_f32_e32 vcc, v31, v3
	s_nop 1
	v_cndmask_b32_e32 v3, v3, v31, vcc
	v_cndmask_b32_e64 v10, v10, 4, vcc
	v_cmp_gt_f32_e32 vcc, v33, v3
	s_nop 1
	v_cndmask_b32_e32 v3, v3, v33, vcc
	v_cndmask_b32_e64 v10, v10, 5, vcc
	v_cmp_ngt_f32_e32 vcc, v35, v3
	s_nop 1
	v_cndmask_b32_e32 v3, v35, v3, vcc
	v_cndmask_b32_e32 v10, 6, v10, vcc
	v_cmp_gt_f32_e64 s[48:49], v1, v3
	s_or_b64 s[0:1], vcc, s[48:49]
	v_cmp_ngt_f32_e64 s[46:47], v1, v3
	v_cndmask_b32_e64 v10, v10, 7, s[48:49]
	v_cmp_ne_u32_e64 s[50:51], 0, v10
	s_and_b64 s[50:51], s[50:51], s[52:53]
	s_nop 0
	v_cndmask_b32_e64 v15, v196, v15, s[50:51]
	v_cmp_ne_u32_e64 s[50:51], 1, v10
	v_cmp_gt_f32_e64 s[52:53], v14, v15
	s_and_b64 s[50:51], s[50:51], s[52:53]
	v_cndmask_b32_e64 v14, v15, v14, s[50:51]
	v_cndmask_b32_e64 v15, 0, 1, s[50:51]
	v_cmp_ne_u32_e64 s[50:51], 2, v10
	v_cmp_gt_f32_e64 s[52:53], v11, v14
	s_and_b64 s[50:51], s[50:51], s[52:53]
	v_cndmask_b32_e64 v11, v14, v11, s[50:51]
	v_cndmask_b32_e64 v14, v15, 2, s[50:51]
	v_cmp_ne_u32_e64 s[50:51], 3, v10
	v_cmp_gt_f32_e64 s[52:53], v13, v11
	s_and_b64 s[50:51], s[50:51], s[52:53]
	v_cndmask_b32_e64 v11, v11, v13, s[50:51]
	v_cndmask_b32_e64 v13, v14, 3, s[50:51]
	v_cmp_ne_u32_e64 s[50:51], 4, v10
	v_cmp_gt_f32_e64 s[52:53], v31, v11
	s_and_b64 s[50:51], s[50:51], s[52:53]
	v_cndmask_b32_e64 v11, v11, v31, s[50:51]
	v_cndmask_b32_e64 v13, v13, 4, s[50:51]
	v_cmp_ne_u32_e64 s[50:51], 5, v10
	v_cmp_gt_f32_e64 s[52:53], v33, v11
	s_and_b64 s[50:51], s[50:51], s[52:53]
	v_cndmask_b32_e64 v11, v11, v33, s[50:51]
	v_cmp_gt_f32_e32 vcc, v35, v11
	v_cndmask_b32_e64 v13, v13, 5, s[50:51]
	s_and_b64 vcc, s[0:1], vcc
	v_cndmask_b32_e32 v35, v11, v35, vcc
	v_cndmask_b32_e64 v13, v13, 6, vcc
	s_and_saveexec_b64 s[0:1], s[46:47]
	s_cbranch_execz .LBB0_1352
	v_cmp_gt_f32_e32 vcc, v1, v35
	s_and_saveexec_b64 s[2:3], vcc
	v_mov_b32_e32 v13, 7
	v_mov_b32_e32 v35, v1
	s_or_b64 exec, exec, s[2:3]
	v_mov_b32_e32 v1, v3

.LBB0_1419:
	v_writelane_b32 v253, s62, 40
	s_nop 1
	v_writelane_b32 v253, s63, 41
	v_writelane_b32 v253, s61, 62
	s_or_b64 exec, exec, s[0:1]
	v_readlane_b32 s8, v253, 31
	v_readlane_b32 s9, v253, 32
	s_waitcnt lgkmcnt(0)
	s_barrier
	v_readlane_b32 s10, v253, 12
	v_readlane_b32 s11, v253, 13
	s_nop 0
	global_load_dword v0, v173, s[8:9] sc1
	global_load_dword v1, v173, s[8:9] offset:256 sc1
	global_load_dword v2, v173, s[8:9] offset:512 sc1
	global_load_dword v3, v173, s[8:9] offset:768 sc1
	global_load_dword v4, v173, s[8:9] offset:1024 sc1
	global_load_dword v5, v173, s[8:9] offset:1280 sc1
	global_load_dword v6, v173, s[8:9] offset:1536 sc1
	global_load_dword v7, v173, s[8:9] offset:1792 sc1
	v_readlane_b32 s30, v253, 9
	s_waitcnt vmcnt(0)
	v_readfirstlane_b32 s0, v0
	s_nop 0
	s_min_i32 s0, s0, 0x2000
	s_addk_i32 s0, 0xff
	s_ashr_i32 s2, s0, 8
	s_nop 0
	v_readfirstlane_b32 s0, v1
	s_nop 0
	s_min_i32 s0, s0, 0x2000
	s_addk_i32 s0, 0xff
	s_ashr_i32 s3, s0, 8
	s_add_i32 s7, s3, s2
	s_nop 0
	v_readfirstlane_b32 s0, v2
	s_nop 0
	s_min_i32 s0, s0, 0x2000
	s_addk_i32 s0, 0xff
	s_ashr_i32 s73, s0, 8
	s_add_i32 s61, s73, s7
	s_nop 0
	v_readfirstlane_b32 s0, v3
	s_nop 0
	s_min_i32 s0, s0, 0x2000
	s_addk_i32 s0, 0xff
	s_ashr_i32 s74, s0, 8
	s_add_i32 s62, s74, s61
	s_nop 0
	v_readfirstlane_b32 s0, v4
	s_nop 0
	s_min_i32 s0, s0, 0x2000
	s_addk_i32 s0, 0xff
	s_ashr_i32 s75, s0, 8
	s_add_i32 s63, s75, s62
	s_nop 0
	v_readfirstlane_b32 s0, v5
	s_nop 0
	s_min_i32 s0, s0, 0x2000
	s_addk_i32 s0, 0xff
	s_ashr_i32 s84, s0, 8
	s_add_i32 s64, s84, s63
	s_nop 0
	v_readfirstlane_b32 s0, v6
	s_nop 0
	s_min_i32 s0, s0, 0x2000
	s_addk_i32 s0, 0xff
	s_ashr_i32 s65, s0, 8
	s_add_i32 s43, s65, s64
	s_nop 0
	v_readfirstlane_b32 s0, v7
	s_min_i32 s0, s0, 0x2000
	s_addk_i32 s0, 0xff
	s_ashr_i32 s66, s0, 8
	s_add_i32 s0, s66, s43
	s_cmp_lt_i32 s0, 1
	s_mul_i32 s8, s0, 11
	s_cselect_b64 s[0:1], -1, 0
	s_or_b64 s[0:1], s[10:11], s[0:1]
	s_and_b64 vcc, exec, s[0:1]
	s_cbranch_vccnz .LBB0_1421
	s_add_i32 s0, s8, -1
	v_readlane_b32 s13, v253, 9
	s_add_i32 s1, s0, s13
	s_ashr_i32 s9, s1, 31
	v_readlane_b32 s10, v253, 29
	s_xor_b32 s9, s9, s10
	s_abs_i32 s1, s1
	v_readlane_b32 s10, v253, 49
	s_mul_hi_u32 s10, s1, s10
	v_readlane_b32 s14, v253, 50
	s_mul_i32 s11, s10, s14
	s_sub_i32 s1, s1, s11
	s_add_i32 s11, s10, 1
	s_sub_i32 s12, s1, s14
	s_cmp_ge_u32 s1, s14
	s_cselect_b32 s10, s11, s10
	s_cselect_b32 s1, s12, s1
	s_add_i32 s11, s10, 1
	s_cmp_ge_u32 s1, s14
	s_cselect_b32 s1, s11, s10
	s_xor_b32 s1, s1, s9
	s_sub_i32 s1, s1, s9
	s_abs_i32 s9, s1
	v_cvt_f32_u32_e32 v0, s9
	s_sub_i32 s10, 0, s9
	s_add_i32 s0, s1, s0
	s_xor_b32 s1, s0, s1
	v_rcp_iflag_f32_e32 v0, v0
	s_abs_i32 s0, s0
	s_ashr_i32 s1, s1, 31
	v_mul_f32_e32 v0, 0x4f7ffffe, v0
	v_cvt_u32_f32_e32 v0, v0
	s_nop 0
	v_readfirstlane_b32 s11, v0
	s_mul_i32 s10, s10, s11
	s_mul_hi_u32 s10, s11, s10
	s_add_i32 s11, s11, s10
	s_mul_hi_u32 s10, s0, s11
	s_mul_i32 s11, s10, s9
	s_sub_i32 s0, s0, s11
	s_add_i32 s11, s10, 1
	s_sub_i32 s12, s0, s9
	s_cmp_ge_u32 s0, s9
	s_cselect_b32 s10, s11, s10
	s_cselect_b32 s0, s12, s0
	s_add_i32 s11, s10, 1
	s_cmp_ge_u32 s0, s9
	s_cselect_b32 s0, s11, s10
	s_xor_b32 s0, s0, s1
	s_sub_i32 s0, s0, s1
	s_add_i32 s0, s0, 7
	s_and_b32 s0, s0, -8
	s_min_i32 s30, s0, s13

.LBB0_1649:
	s_or_b64 exec, exec, s[0:1]
	v_readlane_b32 s8, v253, 31
	v_readlane_b32 s9, v253, 32
	s_waitcnt lgkmcnt(0)
	s_barrier
	s_nop 2
	global_load_dword v0, v173, s[8:9] sc1
	global_load_dword v1, v173, s[8:9] offset:256 sc1
	global_load_dword v2, v173, s[8:9] offset:512 sc1
	global_load_dword v3, v173, s[8:9] offset:768 sc1
	global_load_dword v4, v173, s[8:9] offset:1024 sc1
	global_load_dword v5, v173, s[8:9] offset:1280 sc1
	global_load_dword v6, v173, s[8:9] offset:1536 sc1
	global_load_dword v7, v173, s[8:9] offset:1792 sc1
	s_waitcnt vmcnt(0)
	v_readfirstlane_b32 s0, v0
	s_nop 0
	s_min_i32 s0, s0, 0x2000
	v_writelane_b32 v253, s0, 58
	s_addk_i32 s0, 0xff
	s_ashr_i32 s3, s0, 8
	s_nop 0
	v_readfirstlane_b32 s0, v1
	s_nop 0
	s_min_i32 s0, s0, 0x2000
	v_writelane_b32 v253, s0, 59
	s_addk_i32 s0, 0xff
	s_ashr_i32 s0, s0, 8
	v_writelane_b32 v253, s0, 54
	s_add_i32 s27, s0, s3
	s_nop 0
	v_readfirstlane_b32 s0, v2
	s_nop 0
	s_min_i32 s0, s0, 0x2000
	v_writelane_b32 v253, s0, 55
	s_addk_i32 s0, 0xff
	s_ashr_i32 s0, s0, 8
	v_writelane_b32 v253, s0, 56
	s_add_i32 s30, s0, s27
	s_nop 0
	v_readfirstlane_b32 s0, v3
	s_nop 0
	s_min_i32 s0, s0, 0x2000
	v_writelane_b32 v253, s0, 57
	s_addk_i32 s0, 0xff
	s_ashr_i32 s0, s0, 8
	v_writelane_b32 v253, s0, 60
	s_add_i32 s39, s0, s30
	s_nop 0
	v_readfirstlane_b32 s0, v4
	s_nop 0
	s_min_i32 s0, s0, 0x2000
	v_writelane_b32 v253, s0, 61
	s_addk_i32 s0, 0xff
	s_ashr_i32 s0, s0, 8
	v_writelane_b32 v255, s0, 3
	s_add_i32 s42, s0, s39
	v_readlane_b32 s10, v253, 12
	v_readlane_b32 s11, v253, 13
	v_readlane_b32 s51, v253, 9
	s_nop 0
	v_readfirstlane_b32 s0, v5
	s_nop 0
	s_min_i32 s43, s0, 0x2000
	s_add_i32 s0, s43, 0xff
	s_ashr_i32 s44, s0, 8
	s_add_i32 s45, s44, s42
	s_nop 0
	v_readfirstlane_b32 s0, v6
	s_nop 0
	s_min_i32 s46, s0, 0x2000
	s_add_i32 s0, s46, 0xff
	s_ashr_i32 s47, s0, 8
	s_add_i32 s7, s47, s45
	s_nop 0
	v_readfirstlane_b32 s0, v7
	s_min_i32 s48, s0, 0x2000
	s_add_i32 s0, s48, 0xff
	s_ashr_i32 s49, s0, 8
	s_add_i32 s50, s49, s7
	s_lshl_b32 s8, s50, 3
	s_cmp_lt_i32 s50, 1
	s_cselect_b64 s[0:1], -1, 0
	s_or_b64 s[0:1], s[10:11], s[0:1]
	s_and_b64 vcc, exec, s[0:1]
	s_cbranch_vccnz .LBB0_1651
	s_add_i32 s0, s8, -1
	v_readlane_b32 s12, v253, 9
	s_add_i32 s1, s0, s12
	s_ashr_i32 s2, s1, 31
	v_readlane_b32 s9, v253, 29
	s_xor_b32 s2, s2, s9
	s_abs_i32 s1, s1
	v_readlane_b32 s9, v253, 49
	s_mul_hi_u32 s9, s1, s9
	v_readlane_b32 s13, v253, 50
	s_mul_i32 s10, s9, s13
	s_sub_i32 s1, s1, s10
	s_add_i32 s10, s9, 1
	s_sub_i32 s11, s1, s13
	s_cmp_ge_u32 s1, s13
	s_cselect_b32 s9, s10, s9
	s_cselect_b32 s1, s11, s1
	s_add_i32 s10, s9, 1
	s_cmp_ge_u32 s1, s13
	s_cselect_b32 s1, s10, s9
	s_xor_b32 s1, s1, s2
	s_sub_i32 s1, s1, s2
	s_abs_i32 s2, s1
	v_cvt_f32_u32_e32 v0, s2
	s_sub_i32 s9, 0, s2
	s_add_i32 s0, s1, s0
	s_xor_b32 s1, s0, s1
	v_rcp_iflag_f32_e32 v0, v0
	s_abs_i32 s0, s0
	s_ashr_i32 s1, s1, 31
	v_mul_f32_e32 v0, 0x4f7ffffe, v0
	v_cvt_u32_f32_e32 v0, v0
	s_nop 0
	v_readfirstlane_b32 s10, v0
	s_mul_i32 s9, s9, s10
	s_mul_hi_u32 s9, s10, s9
	s_add_i32 s10, s10, s9
	s_mul_hi_u32 s9, s0, s10
	s_mul_i32 s10, s9, s2
	s_sub_i32 s0, s0, s10
	s_add_i32 s10, s9, 1
	s_sub_i32 s11, s0, s2
	s_cmp_ge_u32 s0, s2
	s_cselect_b32 s9, s10, s9
	s_cselect_b32 s0, s11, s0
	s_add_i32 s10, s9, 1
	s_cmp_ge_u32 s0, s2
	s_cselect_b32 s0, s10, s9
	s_xor_b32 s0, s0, s1
	s_sub_i32 s0, s0, s1
	s_add_i32 s0, s0, 7
	s_and_b32 s0, s0, -8
	s_min_i32 s51, s0, s12
